# expert scale exponents also kept as a compact byte table; the GEMM3 routing epilogue stages the layer's 32 KiB table into a dead part of the LDS tile region and reads the 16 scales of a row from LDS i
# baseline (speedup 1.0000x reference)
; __device__ __forceinline__ void row_to_fp8_2(int lane, const float* xrow0, const float* xrow1, unsigned (&ow0)[4], unsigned (&ow1)[4], float& isc0, float& isc1) {
;     const GAS f32x4* xr0 = (const GAS f32x4*)xrow0 + lane; const GAS f32x4* xr1 = (const GAS f32x4*)xrow1 + lane;
;     f32x4 v0[4], v1[4];
; #pragma unroll
;     for (int j = 0; j < 4; ++j) { v0[j] = __builtin_nontemporal_load(xr0 + 64 * j); v1[j] = __builtin_nontemporal_load(xr1 + 64 * j); }
;     float m0 = 0.f, m1 = 0.f;
; #pragma unroll
;     for (int j = 0; j < 4; ++j) { m0 = fmaxf(m0, fmaxf(fmaxf(fabsf(v0[j].x), fabsf(v0[j].y)), fmaxf(fabsf(v0[j].z), fabsf(v0[j].w)))); m1 = fmaxf(m1, fmaxf(fmaxf(fabsf(v1[j].x), fabsf(v1[j].y)), fmaxf(fabsf(v1[j].z), fabsf(v1[j].w)))); }
; #pragma unroll
;     for (int o = 1; o < 64; o <<= 1) { m0 = fmaxf(m0, __shfl_xor(m0, o)); m1 = fmaxf(m1, __shfl_xor(m1, o)); }
;     int b0 = (int)((__float_as_uint(m0) >> 23) & 255u); b0 = b0 < 16 ? 16 : (b0 > 240 ? 240 : b0);
;     int b1 = (int)((__float_as_uint(m1) >> 23) & 255u); b1 = b1 < 16 ? 16 : (b1 > 240 ? 240 : b1);
;     const float s0 = __uint_as_float((unsigned)(261 - b0) << 23), s1 = __uint_as_float((unsigned)(261 - b1) << 23);
;     isc0 = __uint_as_float((unsigned)(b0 - 7) << 23); isc1 = __uint_as_float((unsigned)(b1 - 7) << 23);
; #pragma unroll
;     for (int j = 0; j < 4; ++j) { int p = __builtin_amdgcn_cvt_pk_fp8_f32(v0[j].x * s0, v0[j].y * s0, 0, false); p = __builtin_amdgcn_cvt_pk_fp8_f32(v0[j].z * s0, v0[j].w * s0, p, true); ow0[j] = (unsigned)p;
;         int q = __builtin_amdgcn_cvt_pk_fp8_f32(v1[j].x * s1, v1[j].y * s1, 0, false); q = __builtin_amdgcn_cvt_pk_fp8_f32(v1[j].z * s1, v1[j].w * s1, q, true); ow1[j] = (unsigned)q; }
; }
; __device__ __forceinline__ void tables_part(LAS unsigned char* lds, int wave, int lane, const float* pu, const float* pv, unsigned char* ws, int gw, int ngw, int wg, int nwg, int r0, int r1, int i0, int i1) {
;     for (int m = r0 + gw; m < r1; m += 2 * ngw) {
;         const int m1 = (m + ngw < r1) ? m + ngw : m;
;         float isc0, isc1; unsigned ow0[4], ow1[4];
;         row_to_fp8_2(lane, pu + (size_t)m * D, pu + (size_t)m1 * D, ow0, ow1, isc0, isc1);
; #pragma unroll
;         for (int j = 0; j < 4; ++j) { *((GAS unsigned*)(ws + WS_UT + (size_t)m * D + j * 256) + lane) = ow0[j]; *((GAS unsigned*)(ws + WS_UT + (size_t)m1 * D + j * 256) + lane) = ow1[j]; }
.LBB0_179:
	global_load_dwordx4 v[14:17], v[8:9], off offset:-2048 nt
	global_load_dwordx4 v[18:21], v[8:9], off offset:-1024 nt
	global_load_dwordx4 v[22:25], v[8:9], off nt
	global_load_dwordx4 v[26:29], v[8:9], off offset:1024 nt
	s_add_i32 s7, s6, 0x400
	s_cmpk_lt_i32 s6, 0x3c00
	s_cselect_b32 s18, s7, s6
	s_ashr_i32 s19, s18, 31
	s_lshl_b64 s[20:21], s[18:19], 12
	v_lshl_add_u64 v[46:47], v[2:3], 0, s[20:21]
	global_load_dwordx4 v[30:33], v[46:47], off nt
	global_load_dwordx4 v[34:37], v[46:47], off offset:1024 nt
	global_load_dwordx4 v[38:41], v[46:47], off offset:2048 nt
	global_load_dwordx4 v[42:45], v[46:47], off offset:3072 nt
	v_mov_b32_e32 v55, 0
	s_lshl_b64 s[20:21], s[18:19], 10
	s_waitcnt vmcnt(0)
	v_max_f32_e64 v13, |v17|, |v17|
	v_max_f32_e64 v46, |v16|, |v16|
	v_max_f32_e64 v47, |v21|, |v21|
	v_max_f32_e64 v48, |v20|, |v20|
	v_max_f32_e64 v49, |v25|, |v25|
	v_max_f32_e64 v50, |v24|, |v24|
	v_max_f32_e64 v51, |v29|, |v29|
	v_max_f32_e64 v52, |v28|, |v28|
	v_max_f32_e32 v13, v46, v13
	v_max_f32_e32 v46, v48, v47
	v_max_f32_e32 v47, v50, v49
	v_max_f32_e32 v48, v52, v51
	v_max3_f32 v13, |v14|, |v15|, v13
	v_max3_f32 v46, |v18|, |v19|, v46
	v_max3_f32 v47, |v22|, |v23|, v47
	v_max3_f32 v48, |v26|, |v27|, v48
	v_max3_f32 v13, v13, 0, v46
	v_max3_f32 v13, v13, v47, v48
	ds_bpermute_b32 v46, v173, v13
	v_max_f32_e64 v47, |v33|, |v33|
	v_max_f32_e64 v48, |v32|, |v32|
	v_max_f32_e64 v49, |v37|, |v37|
	v_max_f32_e64 v50, |v36|, |v36|
	v_max_f32_e64 v51, |v41|, |v41|
	v_max_f32_e64 v52, |v40|, |v40|
	v_max_f32_e64 v53, |v45|, |v45|
	v_max_f32_e64 v54, |v44|, |v44|
	v_max_f32_e32 v47, v48, v47
	v_max_f32_e32 v48, v50, v49
	v_max_f32_e32 v49, v52, v51
	v_max_f32_e32 v50, v54, v53
	v_max3_f32 v47, |v30|, |v31|, v47
	v_max3_f32 v48, |v34|, |v35|, v48
	v_max3_f32 v49, |v38|, |v39|, v49
	v_max3_f32 v50, |v42|, |v43|, v50
	v_max3_f32 v47, v47, 0, v48
	v_max3_f32 v47, v47, v49, v50
	s_waitcnt lgkmcnt(0)
	v_max_f32_e32 v46, v46, v46
	ds_bpermute_b32 v48, v173, v47
	v_max_f32_e32 v13, v13, v46
	ds_bpermute_b32 v46, v174, v13
	v_mov_b32_e32 v49, 0
	v_mov_b32_e32 v53, 0
	s_waitcnt lgkmcnt(1)
	v_max_f32_e32 v48, v48, v48
	v_max_f32_e32 v47, v47, v48
	s_waitcnt lgkmcnt(0)
	v_max_f32_e32 v46, v46, v46
	ds_bpermute_b32 v48, v174, v47
	v_max_f32_e32 v13, v13, v46
	ds_bpermute_b32 v46, v175, v13
	v_mov_b32_e32 v51, 0
	v_mov_b32_e32 v54, 0
	s_waitcnt lgkmcnt(1)
	v_max_f32_e32 v48, v48, v48
	v_max_f32_e32 v47, v47, v48
	s_waitcnt lgkmcnt(0)
	v_max_f32_e32 v46, v46, v46
	ds_bpermute_b32 v48, v175, v47
	v_max_f32_e32 v13, v13, v46
	ds_bpermute_b32 v46, v176, v13
	v_mov_b32_e32 v50, 0
	v_mov_b32_e32 v52, 0
	s_waitcnt lgkmcnt(1)
	v_max_f32_e32 v48, v48, v48
	v_max_f32_e32 v47, v47, v48
	s_waitcnt lgkmcnt(0)
	v_max_f32_e32 v46, v46, v46
	ds_bpermute_b32 v48, v176, v47
	v_max_f32_e32 v13, v13, v46
	ds_bpermute_b32 v46, v10, v13
	s_waitcnt lgkmcnt(1)
	v_max_f32_e32 v48, v48, v48
	v_max_f32_e32 v47, v47, v48
	s_waitcnt lgkmcnt(0)
	v_max_f32_e32 v46, v46, v46
	ds_bpermute_b32 v48, v10, v47
	v_max_f32_e32 v13, v13, v46
	ds_bpermute_b32 v46, v11, v13
	s_waitcnt lgkmcnt(1)
	v_max_f32_e32 v48, v48, v48
	v_max_f32_e32 v47, v47, v48
	s_waitcnt lgkmcnt(0)
	v_max_f32_e32 v46, v46, v46
	v_max_f32_e32 v13, v13, v46
	ds_bpermute_b32 v46, v11, v47
	v_bfe_u32 v13, v13, 23, 8
	v_med3_u32 v13, v13, 16, v1
	v_lshlrev_b32_e32 v13, 23, v13
	v_sub_u32_e32 v48, 0x82800000, v13
	s_waitcnt lgkmcnt(0)
	v_max_f32_e32 v46, v46, v46
	v_mul_f32_e32 v14, v14, v48
	v_mul_f32_e32 v15, v15, v48
	v_mul_f32_e32 v22, v22, v48
	v_mul_f32_e32 v23, v23, v48
	v_max_f32_e32 v46, v47, v46
	v_cvt_pk_fp8_f32 v49, v14, v15
	v_cvt_pk_fp8_f32 v53, v22, v23
	v_bfe_u32 v14, v46, 23, 8
	v_med3_u32 v14, v14, 16, v1
	v_lshlrev_b32_e32 v14, 23, v14
	v_mul_f32_e32 v18, v18, v48
	v_mul_f32_e32 v19, v19, v48
	v_mul_f32_e32 v24, v24, v48
	v_mul_f32_e32 v25, v25, v48
	v_sub_u32_e32 v15, 0x82800000, v14
	v_cvt_pk_fp8_f32 v51, v18, v19
	v_cvt_pk_fp8_f32 v53, v24, v25 op_sel:[0,0,1]
	v_mul_f32_e32 v24, v38, v15
	v_mul_f32_e32 v25, v39, v15
	v_cvt_pk_fp8_f32 v54, v24, v25
	v_mul_f32_e32 v16, v16, v48
	v_mul_f32_e32 v17, v17, v48
	v_mul_f32_e32 v20, v20, v48
	v_mul_f32_e32 v21, v21, v48
	v_mul_f32_e32 v26, v26, v48
	v_mul_f32_e32 v27, v27, v48
	v_cvt_pk_fp8_f32 v49, v16, v17 op_sel:[0,0,1]
	v_mul_f32_e32 v16, v30, v15
	v_mul_f32_e32 v17, v31, v15
	v_cvt_pk_fp8_f32 v55, v26, v27
	v_cvt_pk_fp8_f32 v51, v20, v21 op_sel:[0,0,1]
	v_mul_f32_e32 v20, v34, v15
	v_mul_f32_e32 v21, v35, v15
	v_mul_f32_e32 v26, v40, v15
	v_cvt_pk_fp8_f32 v50, v16, v17
	v_mul_f32_e32 v16, v41, v15
	v_cvt_pk_fp8_f32 v52, v20, v21
	v_cvt_pk_fp8_f32 v54, v26, v16 op_sel:[0,0,1]
	v_mul_f32_e32 v16, v42, v15
	v_mul_f32_e32 v17, v43, v15
	v_mov_b32_e32 v20, 0
	v_cvt_pk_fp8_f32 v20, v16, v17
	v_mul_f32_e32 v18, v32, v15
	v_mul_f32_e32 v19, v33, v15
	v_mul_f32_e32 v22, v36, v15
	v_mul_f32_e32 v23, v37, v15
	v_cvt_pk_fp8_f32 v50, v18, v19 op_sel:[0,0,1]
	v_mul_f32_e32 v16, v44, v15
	v_mul_f32_e32 v15, v45, v15
	v_cvt_pk_fp8_f32 v20, v16, v15 op_sel:[0,0,1]
	v_lshl_add_u64 v[16:17], s[10:11], 0, v[6:7]
	v_cvt_pk_fp8_f32 v52, v22, v23 op_sel:[0,0,1]
	v_add_co_u32_e32 v16, vcc, 0x15000000, v16
	v_mul_f32_e32 v28, v28, v48
	v_mul_f32_e32 v29, v29, v48
	v_addc_co_u32_e32 v17, vcc, 0, v17, vcc
	v_lshl_add_u64 v[18:19], v[4:5], 0, s[20:21]
	v_cvt_pk_fp8_f32 v55, v28, v29 op_sel:[0,0,1]
	global_store_dword v[16:17], v49, off
	global_store_dword v[18:19], v50, off
	global_store_dword v[16:17], v51, off offset:256
	global_store_dword v[18:19], v52, off offset:256
	global_store_dword v[16:17], v53, off offset:512
	global_store_dword v[18:19], v54, off offset:512
	global_store_dword v[16:17], v55, off offset:768
	global_store_dword v[18:19], v20, off offset:768
	s_and_saveexec_b64 s[20:21], s[4:5]
	s_cbranch_execz .LBB0_178
	v_mov_b32_e32 v56, s6
	v_mov_b32_e32 v57, s18
	v_lshlrev_b32_e32 v56, 1, v56
	v_lshlrev_b32_e32 v57, 1, v57
	v_add_u32_e32 v56, 0x19100000, v56
	v_add_u32_e32 v57, 0x19100000, v57
	s_lshl_b64 s[18:19], s[18:19], 3
	s_add_u32 s18, s9, s18
	s_addc_u32 s19, s22, s19
	s_add_u32 s26, s10, s23
	v_add_u32_e32 v13, 0xfc800000, v13
	s_addc_u32 s27, s11, s24
	v_add_u32_e32 v14, 0xfc800000, v14
	global_store_dword v12, v13, s[26:27]
	global_store_dword v12, v14, s[18:19]
	v_lshrrev_b32_e32 v58, 23, v13
	v_lshrrev_b32_e32 v59, 23, v14
	global_store_byte v56, v58, s[10:11]
	global_store_byte v57, v59, s[10:11]
	s_branch .LBB0_178

; #define GAS __attribute__((address_space(1)))
; #define LAS __attribute__((address_space(3)))
; __device__ __forceinline__ void row_to_fp8_2(int lane, const float* xrow0, const float* xrow1, unsigned (&ow0)[4], unsigned (&ow1)[4], float& isc0, float& isc1) {
;     const GAS f32x4* xr0 = (const GAS f32x4*)xrow0 + lane; const GAS f32x4* xr1 = (const GAS f32x4*)xrow1 + lane;
;     f32x4 v0[4], v1[4];
; #pragma unroll
;     for (int j = 0; j < 4; ++j) { v0[j] = __builtin_nontemporal_load(xr0 + 64 * j); v1[j] = __builtin_nontemporal_load(xr1 + 64 * j); }
;     float m0 = 0.f, m1 = 0.f;
; #pragma unroll
;     for (int j = 0; j < 4; ++j) { m0 = fmaxf(m0, fmaxf(fmaxf(fabsf(v0[j].x), fabsf(v0[j].y)), fmaxf(fabsf(v0[j].z), fabsf(v0[j].w)))); m1 = fmaxf(m1, fmaxf(fmaxf(fabsf(v1[j].x), fabsf(v1[j].y)), fmaxf(fabsf(v1[j].z), fabsf(v1[j].w)))); }
; #pragma unroll
;     for (int o = 1; o < 64; o <<= 1) { m0 = fmaxf(m0, __shfl_xor(m0, o)); m1 = fmaxf(m1, __shfl_xor(m1, o)); }
;     int b0 = (int)((__float_as_uint(m0) >> 23) & 255u); b0 = b0 < 16 ? 16 : (b0 > 240 ? 240 : b0);
;     int b1 = (int)((__float_as_uint(m1) >> 23) & 255u); b1 = b1 < 16 ? 16 : (b1 > 240 ? 240 : b1);
;     const float s0 = __uint_as_float((unsigned)(261 - b0) << 23), s1 = __uint_as_float((unsigned)(261 - b1) << 23);
;     isc0 = __uint_as_float((unsigned)(b0 - 7) << 23); isc1 = __uint_as_float((unsigned)(b1 - 7) << 23);
; #pragma unroll
;     for (int j = 0; j < 4; ++j) { int p = __builtin_amdgcn_cvt_pk_fp8_f32(v0[j].x * s0, v0[j].y * s0, 0, false); p = __builtin_amdgcn_cvt_pk_fp8_f32(v0[j].z * s0, v0[j].w * s0, p, true); ow0[j] = (unsigned)p;
;         int q = __builtin_amdgcn_cvt_pk_fp8_f32(v1[j].x * s1, v1[j].y * s1, 0, false); q = __builtin_amdgcn_cvt_pk_fp8_f32(v1[j].z * s1, v1[j].w * s1, q, true); ow1[j] = (unsigned)q; }
; }
; __device__ __forceinline__ void p0_vslice_item(LAS unsigned char* lds, int wave, int tid, const float* vt_l, unsigned char* VS_l, float* vsc_l, int item) {
;     const int lane = tid & 63, e0 = item * 64;
;     __syncthreads();
; #pragma unroll 1
;     for (int i = 0; i < 8; i += 2) { const int er = wave * 8 + i; float isc0, isc1; unsigned ow0[4], ow1[4];
;         row_to_fp8_2(lane, vt_l + (size_t)(e0 + er) * 1024, vt_l + (size_t)(e0 + er + 1) * 1024, ow0, ow1, isc0, isc1);
; #pragma unroll
.LBB0_186:
	global_load_dwordx4 v[14:17], v[4:5], off offset:-3072 nt
	global_load_dwordx4 v[18:21], v[4:5], off offset:-2048 nt
	global_load_dwordx4 v[22:25], v[4:5], off offset:-1024 nt
	global_load_dwordx4 v[26:29], v[4:5], off nt
	v_add_co_u32_e32 v12, vcc, 0xfffff000, v4
	s_waitcnt vmcnt(2)
	v_max_f32_e64 v46, |v21|, |v21|
	v_addc_co_u32_e32 v13, vcc, -1, v5, vcc
	global_load_dwordx4 v[30:33], v[12:13], off offset:-3072 nt
	global_load_dwordx4 v[34:37], v[12:13], off offset:-2048 nt
	global_load_dwordx4 v[38:41], v[12:13], off offset:-1024 nt
	global_load_dwordx4 v[42:45], v[4:5], off offset:-4096 nt
	v_max_f32_e64 v12, |v17|, |v17|
	v_max_f32_e64 v13, |v16|, |v16|
	v_max_f32_e64 v47, |v20|, |v20|
	s_waitcnt vmcnt(5)
	v_max_f32_e64 v48, |v25|, |v25|
	v_max_f32_e64 v49, |v24|, |v24|
	s_waitcnt vmcnt(4)
	v_max_f32_e64 v50, |v29|, |v29|
	v_max_f32_e64 v51, |v28|, |v28|
	v_max_f32_e32 v12, v13, v12
	v_max_f32_e32 v13, v47, v46
	v_max_f32_e32 v46, v49, v48
	v_max_f32_e32 v47, v51, v50
	v_max3_f32 v12, |v14|, |v15|, v12
	v_max3_f32 v13, |v18|, |v19|, v13
	v_max3_f32 v46, |v22|, |v23|, v46
	v_max3_f32 v47, |v26|, |v27|, v47
	v_max3_f32 v12, v12, 0, v13
	v_max3_f32 v12, v12, v46, v47
	ds_bpermute_b32 v47, v173, v12
	s_waitcnt lgkmcnt(0)
	v_max_f32_e32 v47, v47, v47
	v_max_f32_e32 v12, v12, v47
	ds_bpermute_b32 v47, v174, v12
	s_waitcnt lgkmcnt(0)
	v_max_f32_e32 v47, v47, v47
	v_max_f32_e32 v12, v12, v47
	ds_bpermute_b32 v47, v175, v12
	s_waitcnt lgkmcnt(0)
	v_max_f32_e32 v47, v47, v47
	v_max_f32_e32 v12, v12, v47
	ds_bpermute_b32 v47, v176, v12
	s_waitcnt lgkmcnt(0)
	v_max_f32_e32 v47, v47, v47
	v_max_f32_e32 v12, v12, v47
	ds_bpermute_b32 v47, v10, v12
	s_waitcnt lgkmcnt(0)
	v_max_f32_e32 v47, v47, v47
	v_max_f32_e32 v12, v12, v47
	ds_bpermute_b32 v47, v11, v12
	s_waitcnt lgkmcnt(0)
	v_max_f32_e32 v47, v47, v47
	v_max_f32_e32 v12, v12, v47
	v_bfe_u32 v12, v12, 23, 8
	v_med3_u32 v12, v12, 16, v8
	v_lshlrev_b32_e32 v12, 23, v12
	s_waitcnt vmcnt(3)
	v_max_f32_e64 v48, |v33|, |v33|
	v_max_f32_e64 v49, |v32|, |v32|
	s_waitcnt vmcnt(2)
	v_max_f32_e64 v50, |v37|, |v37|
	v_max_f32_e64 v51, |v36|, |v36|
	s_waitcnt vmcnt(1)
	v_max_f32_e64 v52, |v41|, |v41|
	v_max_f32_e64 v53, |v40|, |v40|
	s_waitcnt vmcnt(0)
	v_max_f32_e64 v54, |v45|, |v45|
	v_max_f32_e64 v55, |v44|, |v44|
	v_max_f32_e32 v48, v49, v48
	v_max_f32_e32 v49, v51, v50
	v_max_f32_e32 v13, v53, v52
	v_max_f32_e32 v50, v55, v54
	v_max3_f32 v48, |v30|, |v31|, v48
	v_max3_f32 v49, |v34|, |v35|, v49
	v_max3_f32 v13, |v38|, |v39|, v13
	v_max3_f32 v50, |v42|, |v43|, v50
	v_max3_f32 v46, v48, 0, v49
	v_max3_f32 v13, v46, v13, v50
	ds_bpermute_b32 v46, v173, v13
	v_mov_b32_e32 v49, 0
	v_mov_b32_e32 v48, 0
	v_mov_b32_e32 v53, 0
	v_mov_b32_e32 v50, 0
	s_waitcnt lgkmcnt(0)
	v_max_f32_e32 v46, v46, v46
	v_max_f32_e32 v13, v13, v46
	ds_bpermute_b32 v46, v174, v13
	v_mov_b32_e32 v51, 0
	v_mov_b32_e32 v52, 0
	v_mov_b32_e32 v54, 0
	s_waitcnt lgkmcnt(0)
	v_max_f32_e32 v46, v46, v46
	v_max_f32_e32 v13, v13, v46
	ds_bpermute_b32 v46, v175, v13
	s_waitcnt lgkmcnt(0)
	v_max_f32_e32 v46, v46, v46
	v_max_f32_e32 v13, v13, v46
	ds_bpermute_b32 v46, v176, v13
	s_waitcnt lgkmcnt(0)
	v_max_f32_e32 v46, v46, v46
	v_max_f32_e32 v13, v13, v46
	ds_bpermute_b32 v46, v10, v13
	s_waitcnt lgkmcnt(0)
	v_max_f32_e32 v46, v46, v46
	v_max_f32_e32 v13, v13, v46
	ds_bpermute_b32 v46, v11, v13
	s_waitcnt lgkmcnt(0)
	v_max_f32_e32 v46, v46, v46
	v_max_f32_e32 v13, v13, v46
	v_bfe_u32 v13, v13, 23, 8
	v_med3_u32 v13, v13, 16, v8
	v_sub_u32_e32 v46, 0x82800000, v12
	v_lshlrev_b32_e32 v13, 23, v13
	v_mul_f32_e32 v14, v14, v46
	v_mul_f32_e32 v15, v15, v46
	v_sub_u32_e32 v47, 0x82800000, v13
	v_cvt_pk_fp8_f32 v49, v14, v15
	v_mul_f32_e32 v14, v30, v47
	v_mul_f32_e32 v15, v31, v47
	v_cvt_pk_fp8_f32 v48, v14, v15
	v_mul_f32_e32 v22, v22, v46
	v_mul_f32_e32 v23, v23, v46
	v_mul_f32_e32 v18, v18, v46
	v_mul_f32_e32 v19, v19, v46
	v_cvt_pk_fp8_f32 v53, v22, v23
	v_mul_f32_e32 v22, v34, v47
	v_mul_f32_e32 v23, v35, v47
	v_mul_f32_e32 v16, v16, v46
	v_mul_f32_e32 v17, v17, v46
	v_cvt_pk_fp8_f32 v51, v18, v19
	v_mul_f32_e32 v18, v32, v47
	v_mul_f32_e32 v19, v33, v47
	v_mul_f32_e32 v30, v36, v47
	v_mul_f32_e32 v31, v37, v47
	v_mul_f32_e32 v32, v38, v47
	v_mul_f32_e32 v33, v39, v47
	v_mul_f32_e32 v36, v42, v47
	v_mul_f32_e32 v37, v43, v47
	v_cvt_pk_fp8_f32 v50, v22, v23
	v_cvt_pk_fp8_f32 v52, v32, v33
	v_cvt_pk_fp8_f32 v54, v36, v37
	v_cvt_pk_fp8_f32 v49, v16, v17 op_sel:[0,0,1]
	v_cvt_pk_fp8_f32 v48, v18, v19 op_sel:[0,0,1]
	v_mul_f32_e32 v16, v26, v46
	v_mul_f32_e32 v17, v27, v46
	v_mov_b32_e32 v18, 0
	v_cvt_pk_fp8_f32 v18, v16, v17
	v_mul_f32_e32 v20, v20, v46
	v_mul_f32_e32 v21, v21, v46
	v_mul_f32_e32 v34, v40, v47
	v_mul_f32_e32 v35, v41, v47
	v_cvt_pk_fp8_f32 v51, v20, v21 op_sel:[0,0,1]
	v_cvt_pk_fp8_f32 v50, v30, v31 op_sel:[0,0,1]
	v_mul_f32_e32 v14, v44, v47
	v_mul_f32_e32 v15, v45, v47
	v_mul_f32_e32 v24, v24, v46
	v_mul_f32_e32 v25, v25, v46
	v_cvt_pk_fp8_f32 v52, v34, v35 op_sel:[0,0,1]
	v_cvt_pk_fp8_f32 v54, v14, v15 op_sel:[0,0,1]
	v_mul_f32_e32 v14, v28, v46
	v_mul_f32_e32 v15, v29, v46
	v_cvt_pk_fp8_f32 v53, v24, v25 op_sel:[0,0,1]
	v_cvt_pk_fp8_f32 v18, v14, v15 op_sel:[0,0,1]
	v_add_u32_e32 v14, 8, v9
	ds_write2st64_b32 v9, v48, v50 offset1:1
	ds_write2st64_b32 v14, v49, v51 offset0:4 offset1:5
	ds_write2st64_b32 v9, v52, v54 offset0:2 offset1:3
	ds_write2st64_b32 v14, v53, v18 offset0:6 offset1:7
	s_and_saveexec_b64 s[20:21], s[4:5]
	s_cbranch_execz .LBB0_185
	v_add_u32_e32 v14, 0xfc800000, v13
	v_add_u32_e32 v15, 0xfc800000, v12
	global_store_dword v1, v14, s[18:19] offset:-4
	global_store_dword v1, v15, s[18:19] offset:4
	s_sub_u32 s98, s18, s22
	s_sub_u32 s98, s98, 0x2000008
	s_lshr_b32 s98, s98, 2
	s_add_u32 s98, s98, 0x2100001
	v_mov_b32_e32 v56, s98
	v_lshrrev_b32_e32 v58, 23, v14
	v_lshrrev_b32_e32 v59, 23, v15
	global_store_byte v56, v58, s[22:23]
	global_store_byte v56, v59, s[22:23] offset:2
	s_branch .LBB0_185

; __device__ __forceinline__ void sort16_desc(float (&v)[16]) {
;     CE(v[0], v[1]); CE(v[2], v[3]); CE(v[0], v[2]); CE(v[1], v[3]);
;     CE(v[1], v[2]); CE(v[4], v[5]); CE(v[6], v[7]); CE(v[4], v[6]);
;     CE(v[5], v[7]); CE(v[5], v[6]); CE(v[0], v[4]); CE(v[2], v[6]);
;     CE(v[2], v[4]); CE(v[1], v[5]); CE(v[3], v[7]); CE(v[3], v[5]);
;     CE(v[1], v[2]); CE(v[3], v[4]); CE(v[5], v[6]); CE(v[8], v[9]);
;     CE(v[10], v[11]); CE(v[8], v[10]); CE(v[9], v[11]); CE(v[9], v[10]);
;     CE(v[12], v[13]); CE(v[14], v[15]); CE(v[12], v[14]); CE(v[13], v[15]);
;     CE(v[13], v[14]); CE(v[8], v[12]); CE(v[10], v[14]); CE(v[10], v[12]);
;     CE(v[9], v[13]); CE(v[11], v[15]); CE(v[11], v[13]); CE(v[9], v[10]);
;     CE(v[11], v[12]); CE(v[13], v[14]); CE(v[0], v[8]); CE(v[4], v[12]);
;     CE(v[4], v[8]); CE(v[2], v[10]); CE(v[6], v[14]); CE(v[6], v[10]);
;     CE(v[2], v[4]); CE(v[6], v[8]); CE(v[10], v[12]); CE(v[1], v[9]);
;     CE(v[5], v[13]); CE(v[5], v[9]); CE(v[3], v[11]); CE(v[7], v[15]);
;     __device__ __forceinline__ void fused(f32x4 (&acc)[2][2][4][2], const Unit& u, int wr, int wc, int fr, int fq, PG8_LAS unsigned char* lds, int wid, int lane) const {
;     ...
; #pragma unroll
;                     for (int n = 0; n < 2; ++n) {
;                         const int rw = ai * HALF + wr * 64 + m * 16 + fr, g = 8 * wc + 4 * n + fq, col = 32 * wc + 16 * n + 4 * fq;
;                         const f32x4 v = acc[ai][bj][m][n]; f32x4 p;
; #pragma unroll
;                         for (int e = 0; e < 4; ++e) p[e] = __uint_as_float((__float_as_uint(v[e]) & ~127u) | (unsigned)(col + e));
;                         *(PG8_LAS f32x4*)(tile + rw * 128 + ((g ^ fr) << 2)) = p;
;                     }
;             RT_BAR();
;             float run[16];
; #pragma unroll
;             for (int grp = 0; grp < 4; ++grp) {
;                 float nw[16];
; #pragma unroll
;                 for (int i = 0; i < 4; ++i) { const int g = half * 16 + grp * 4 + i; const f32x4 v = *(const PG8_LAS f32x4*)(tile + row * 128 + ((g ^ (row & 15)) << 2));
;                     nw[4 * i] = v[0]; nw[4 * i + 1] = v[1]; nw[4 * i + 2] = v[2]; nw[4 * i + 3] = v[3]; }
;                 sort16_desc(nw);
;                 if (grp == 0) {
; #pragma unroll
;                     for (int q = 0; q < 16; ++q) run[q] = nw[q];
;                 } else merge_top16(run, nw);
.LBB0_584:
	s_movk_i32 s19, 0xff80
	v_and_or_b32 v60, v60, s19, v129
	v_and_or_b32 v61, v61, s98, v218
	v_and_or_b32 v62, v62, s98, v219
	v_and_or_b32 v63, v63, s98, v220
	v_and_or_b32 v56, v56, s19, v124
	v_and_or_b32 v57, v57, s98, v221
	v_and_or_b32 v58, v58, s98, v222
	v_and_or_b32 v59, v59, s98, v223
	v_and_or_b32 v52, v52, s19, v129
	v_and_or_b32 v53, v53, s98, v218
	v_and_or_b32 v54, v54, s98, v219
	v_and_or_b32 v55, v55, s98, v220
	v_and_or_b32 v48, v48, s19, v124
	v_and_or_b32 v49, v49, s98, v221
	v_and_or_b32 v50, v50, s98, v222
	v_and_or_b32 v51, v51, s98, v223
	v_and_or_b32 v44, v44, s19, v129
	v_and_or_b32 v45, v45, s98, v218
	v_and_or_b32 v46, v46, s98, v219
	v_and_or_b32 v47, v47, s98, v220
	v_and_or_b32 v40, v40, s19, v124
	v_and_or_b32 v41, v41, s98, v221
	v_and_or_b32 v42, v42, s98, v222
	v_and_or_b32 v43, v43, s98, v223
	v_and_or_b32 v36, v36, s19, v129
	v_and_or_b32 v37, v37, s98, v218
	v_and_or_b32 v38, v38, s98, v219
	v_and_or_b32 v39, v39, s98, v220
	v_and_or_b32 v32, v32, s19, v124
	v_and_or_b32 v33, v33, s98, v221
	v_and_or_b32 v34, v34, s98, v222
	v_and_or_b32 v35, v35, s98, v223
	v_and_or_b32 v28, v28, s19, v129
	v_and_or_b32 v29, v29, s98, v218
	v_and_or_b32 v30, v30, s98, v219
	v_and_or_b32 v31, v31, s98, v220
	v_and_or_b32 v24, v24, s19, v124
	v_and_or_b32 v25, v25, s98, v221
	v_and_or_b32 v26, v26, s98, v222
	v_and_or_b32 v27, v27, s98, v223
	v_and_or_b32 v20, v20, s19, v129
	v_and_or_b32 v21, v21, s98, v218
	v_and_or_b32 v22, v22, s98, v219
	v_and_or_b32 v23, v23, s98, v220
	v_and_or_b32 v16, v16, s19, v124
	v_and_or_b32 v17, v17, s98, v221
	v_and_or_b32 v18, v18, s98, v222
	v_and_or_b32 v19, v19, s98, v223
	v_and_or_b32 v12, v12, s19, v129
	v_and_or_b32 v13, v13, s98, v218
	v_and_or_b32 v14, v14, s98, v219
	v_and_or_b32 v15, v15, s98, v220
	v_and_or_b32 v8, v8, s19, v124
	v_and_or_b32 v9, v9, s98, v221
	v_and_or_b32 v10, v10, s98, v222
	v_and_or_b32 v11, v11, s98, v223
	v_and_or_b32 v4, v4, s19, v129
	v_and_or_b32 v5, v5, s98, v218
	v_and_or_b32 v6, v6, s98, v219
	v_and_or_b32 v7, v7, s98, v220
	v_and_or_b32 v0, v0, s19, v124
	v_and_or_b32 v1, v1, s98, v221
	v_and_or_b32 v2, v2, s98, v222
	v_and_or_b32 v3, v3, s98, v223
	s_waitcnt lgkmcnt(0)
	s_barrier
	ds_write_b128 v125, v[60:63]
	ds_write_b128 v120, v[56:59]
	ds_write_b128 v125, v[52:55] offset:8192
	ds_write_b128 v120, v[48:51] offset:8192
	ds_write_b128 v125, v[44:47] offset:16384
	ds_write_b128 v120, v[40:43] offset:16384
	ds_write_b128 v125, v[36:39] offset:24576
	ds_write_b128 v120, v[32:35] offset:24576
	ds_write_b128 v92, v[28:31]
	ds_write_b128 v88, v[24:27]
	ds_write_b128 v84, v[20:23]
	ds_write_b128 v82, v[16:19]
	ds_write_b128 v85, v[12:15]
	ds_write_b128 v86, v[8:11]
	ds_write_b128 v90, v[4:7]
	ds_write_b128 v91, v[0:3]
	s_waitcnt lgkmcnt(0)
	s_barrier
	s_lshr_b32 s98, s61, 2
	v_lshlrev_b32_e32 v240, 6, v128
	s_lshl_b32 s98, s98, 14
	v_add_u32_e32 v240, s98, v240
	v_add_u32_e32 v241, 0x18000, v240
	v_add_u32_e32 v240, 0x19100000, v240
	global_load_dwordx4 v[224:227], v240, s[30:31]
	global_load_dwordx4 v[228:231], v240, s[30:31] offset:16
	global_load_dwordx4 v[232:235], v240, s[30:31] offset:32
	global_load_dwordx4 v[236:239], v240, s[30:31] offset:48
	ds_read_b128 v[0:3], v93
	ds_read_b128 v[4:7], v89
	s_and_b64 vcc, exec, s[4:5]
	s_waitcnt lgkmcnt(0)
	v_min_f32_e32 v10, v0, v1
	v_max_f32_e32 v8, v0, v1
	v_min_f32_e32 v13, v2, v3
	v_max_f32_e32 v9, v2, v3
	v_min_f32_e32 v17, v4, v5
	v_max_f32_e32 v15, v4, v5
	v_min_f32_e32 v20, v6, v7
	v_max_f32_e32 v16, v6, v7
	ds_read_b128 v[0:3], v81
	ds_read_b128 v[4:7], v80
	s_waitcnt lgkmcnt(0)
	v_min_f32_e32 v23, v0, v1
	v_min_f32_e32 v24, v2, v3
	v_min_f32_e32 v26, v4, v5
	v_min_f32_e32 v27, v6, v7
	v_max_f32_e32 v0, v0, v1
	v_max_f32_e32 v1, v2, v3
	v_max_f32_e32 v4, v4, v5
	v_max_f32_e32 v5, v6, v7
	v_min_f32_e32 v14, v10, v13
	v_min_f32_e32 v21, v17, v20
	v_min_f32_e32 v25, v23, v24
	v_max_f32_e32 v10, v10, v13
	v_min_f32_e32 v11, v8, v9
	v_max_f32_e32 v13, v17, v20
	v_min_f32_e32 v17, v15, v16
	v_max_f32_e32 v23, v23, v24
	v_min_f32_e32 v2, v0, v1
	v_max_f32_e32 v24, v26, v27
	v_min_f32_e32 v6, v4, v5
	v_min_f32_e32 v28, v26, v27
	v_max_f32_e32 v12, v10, v11
	v_max_f32_e32 v18, v13, v17
	v_max_f32_e32 v3, v23, v2
	v_max_f32_e32 v7, v24, v6
	v_min_f32_e32 v22, v14, v21
	v_min_f32_e32 v29, v25, v28
	v_max_f32_e32 v14, v14, v21
	v_min_f32_e32 v19, v12, v18
	v_min_f32_e32 v10, v10, v11
	v_min_f32_e32 v11, v13, v17
	v_max_f32_e32 v21, v25, v28
	v_min_f32_e32 v25, v3, v7
	v_min_f32_e32 v2, v23, v2
	v_min_f32_e32 v6, v24, v6
	v_max_f32_e32 v20, v14, v19
	v_max_f32_e32 v13, v10, v11
	v_max_f32_e32 v8, v8, v9
	v_max_f32_e32 v9, v15, v16
	v_max_f32_e32 v23, v2, v6
	v_max_f32_e32 v0, v0, v1
	v_max_f32_e32 v1, v4, v5
	v_min_f32_e32 v14, v14, v19
	v_min_f32_e32 v10, v10, v11
	v_min_f32_e32 v19, v21, v25
	v_min_f32_e32 v2, v2, v6
	v_min_f32_e32 v15, v8, v9
	v_min_f32_e32 v4, v0, v1
	v_max_f32_e32 v11, v14, v10
	v_max_f32_e32 v6, v19, v2
	v_min_f32_e32 v10, v14, v10
	v_min_f32_e32 v2, v19, v2
	v_min_f32_e32 v5, v23, v4
	v_min_f32_e32 v14, v10, v2
	v_max_f32_e32 v2, v10, v2
	v_max_f32_e32 v10, v12, v18
	v_max_f32_e32 v12, v13, v15
	v_max_f32_e32 v3, v3, v7
	v_max_f32_e32 v4, v23, v4
	v_min_f32_e32 v16, v13, v15
	v_max_f32_e32 v26, v21, v25
	v_min_f32_e32 v13, v10, v12
	v_min_f32_e32 v7, v3, v4
	v_max_f32_e32 v10, v10, v12
	v_max_f32_e32 v3, v3, v4
	v_max_f32_e32 v17, v20, v16
	v_max_f32_e32 v24, v26, v5
	v_min_f32_e32 v21, v11, v6
	v_min_f32_e32 v16, v20, v16
	v_min_f32_e32 v5, v26, v5
	v_max_f32_e32 v6, v11, v6
	v_min_f32_e32 v4, v10, v3
	v_max_f32_e32 v8, v8, v9
	v_max_f32_e32 v9, v0, v1
	v_max_f32_e32 v30, v22, v29
	v_min_f32_e32 v27, v17, v24
	v_min_f32_e32 v15, v13, v7
	v_min_f32_e32 v20, v16, v5
	v_min_f32_e32 v11, v6, v4
	v_max_f32_e32 v5, v16, v5
	v_min_f32_e32 v0, v8, v9
	v_max_f32_e32 v17, v17, v24
	v_max_f32_e32 v4, v6, v4
	v_min_f32_e32 v28, v30, v27
	v_min_f32_e32 v18, v2, v15
	v_max_f32_e32 v27, v30, v27
	v_max_f32_e32 v2, v2, v15
	v_min_f32_e32 v1, v5, v0
	v_min_f32_e32 v24, v17, v4
	v_max_f32_e32 v17, v17, v4
	v_max_f32_e32 v4, v13, v7
	v_max_f32_e32 v5, v5, v0
	v_min_f32_e32 v12, v27, v11
	v_max_f32_e32 v11, v27, v11
	v_min_f32_e32 v15, v2, v1
	v_max_f32_e32 v27, v2, v1
	v_min_f32_e32 v13, v4, v5
	v_max_f32_e32 v10, v10, v3
	ds_read_b128 v[0:3], v99
	v_max_f32_e32 v31, v4, v5
	ds_read_b128 v[4:7], v96
	v_min_f32_e32 v22, v22, v29
	v_min_f32_e32 v25, v28, v21
	s_waitcnt lgkmcnt(0)
; __device__ __forceinline__ void sort16_desc(float (&v)[16]) {
;     CE(v[0], v[1]); CE(v[2], v[3]); CE(v[0], v[2]); CE(v[1], v[3]);
;     CE(v[1], v[2]); CE(v[4], v[5]); CE(v[6], v[7]); CE(v[4], v[6]);
;     CE(v[5], v[7]); CE(v[5], v[6]); CE(v[0], v[4]); CE(v[2], v[6]);
;     CE(v[2], v[4]); CE(v[1], v[5]); CE(v[3], v[7]); CE(v[3], v[5]);
;     CE(v[1], v[2]); CE(v[3], v[4]); CE(v[5], v[6]); CE(v[8], v[9]);
;     CE(v[10], v[11]); CE(v[8], v[10]); CE(v[9], v[11]); CE(v[9], v[10]);
;     CE(v[12], v[13]); CE(v[14], v[15]); CE(v[12], v[14]); CE(v[13], v[15]);
;     CE(v[13], v[14]); CE(v[8], v[12]); CE(v[10], v[14]); CE(v[10], v[12]);
;     CE(v[9], v[13]); CE(v[11], v[15]); CE(v[11], v[13]); CE(v[9], v[10]);
;     CE(v[11], v[12]); CE(v[13], v[14]); CE(v[0], v[8]); CE(v[4], v[12]);
;     CE(v[4], v[8]); CE(v[2], v[10]); CE(v[6], v[14]); CE(v[6], v[10]);
;     CE(v[2], v[4]); CE(v[6], v[8]); CE(v[10], v[12]); CE(v[1], v[9]);
;     CE(v[5], v[13]); CE(v[5], v[9]); CE(v[3], v[11]); CE(v[7], v[15]);
;     CE(v[7], v[11]); CE(v[3], v[5]); CE(v[7], v[9]); CE(v[11], v[13]);
;     CE(v[1], v[2]); CE(v[3], v[4]); CE(v[5], v[6]); CE(v[7], v[8]);
;     CE(v[9], v[10]); CE(v[11], v[12]); CE(v[13], v[14]);
; }
; __device__ __forceinline__ void merge_top16(float (&v)[16], const float (&nw)[16]) {
;     v[0] = fmaxf(v[0], nw[15]); v[1] = fmaxf(v[1], nw[14]); v[2] = fmaxf(v[2], nw[13]); v[3] = fmaxf(v[3], nw[12]); v[4] = fmaxf(v[4], nw[11]); v[5] = fmaxf(v[5], nw[10]); v[6] = fmaxf(v[6], nw[9]); v[7] = fmaxf(v[7], nw[8]); v[8] = fmaxf(v[8], nw[7]); v[9] = fmaxf(v[9], nw[6]); v[10] = fmaxf(v[10], nw[5]); v[11] = fmaxf(v[11], nw[4]); v[12] = fmaxf(v[12], nw[3]); v[13] = fmaxf(v[13], nw[2]); v[14] = fmaxf(v[14], nw[1]); v[15] = fmaxf(v[15], nw[0]);
;     CE(v[0], v[8]); CE(v[1], v[9]); CE(v[2], v[10]); CE(v[3], v[11]);
;     CE(v[4], v[12]); CE(v[5], v[13]); CE(v[6], v[14]); CE(v[7], v[15]);
;     CE(v[0], v[4]); CE(v[1], v[5]); CE(v[2], v[6]); CE(v[3], v[7]);
;     CE(v[8], v[12]); CE(v[9], v[13]); CE(v[10], v[14]); CE(v[11], v[15]);
;     CE(v[0], v[2]); CE(v[1], v[3]); CE(v[4], v[6]); CE(v[5], v[7]);
;     CE(v[8], v[10]); CE(v[9], v[11]); CE(v[12], v[14]); CE(v[13], v[15]);
;     CE(v[0], v[1]); CE(v[2], v[3]); CE(v[4], v[5]); CE(v[6], v[7]);
;     CE(v[8], v[9]); CE(v[10], v[11]); CE(v[12], v[13]); CE(v[14], v[15]);
; }
	v_min_f32_e32 v34, v0, v1
	v_max_f32_e32 v29, v0, v1
	v_min_f32_e32 v37, v2, v3
	v_max_f32_e32 v33, v2, v3
	v_min_f32_e32 v41, v4, v5
	v_max_f32_e32 v39, v4, v5
	v_min_f32_e32 v44, v6, v7
	v_max_f32_e32 v40, v6, v7
	ds_read_b128 v[0:3], v87
	ds_read_b128 v[4:7], v83
	s_waitcnt lgkmcnt(0)
	v_min_f32_e32 v47, v0, v1
	v_min_f32_e32 v48, v2, v3
	v_min_f32_e32 v50, v4, v5
	v_min_f32_e32 v51, v6, v7
	v_max_f32_e32 v0, v0, v1
	v_max_f32_e32 v1, v2, v3
	v_max_f32_e32 v4, v4, v5
	v_max_f32_e32 v5, v6, v7
	v_min_f32_e32 v38, v34, v37
	v_min_f32_e32 v45, v41, v44
	v_min_f32_e32 v49, v47, v48
	v_max_f32_e32 v34, v34, v37
	v_min_f32_e32 v35, v29, v33
	v_max_f32_e32 v37, v41, v44
	v_min_f32_e32 v41, v39, v40
	v_max_f32_e32 v47, v47, v48
	v_min_f32_e32 v2, v0, v1
	v_max_f32_e32 v48, v50, v51
	v_min_f32_e32 v6, v4, v5
	v_min_f32_e32 v52, v50, v51
	v_max_f32_e32 v36, v34, v35
	v_max_f32_e32 v42, v37, v41
	v_max_f32_e32 v3, v47, v2
	v_max_f32_e32 v7, v48, v6
	v_min_f32_e32 v46, v38, v45
	v_min_f32_e32 v53, v49, v52
	v_max_f32_e32 v38, v38, v45
	v_min_f32_e32 v43, v36, v42
	v_min_f32_e32 v34, v34, v35
	v_min_f32_e32 v35, v37, v41
	v_max_f32_e32 v45, v49, v52
	v_min_f32_e32 v49, v3, v7
	v_min_f32_e32 v2, v47, v2
	v_min_f32_e32 v6, v48, v6
	v_max_f32_e32 v44, v38, v43
	v_max_f32_e32 v37, v34, v35
	v_max_f32_e32 v29, v29, v33
	v_max_f32_e32 v33, v39, v40
	v_max_f32_e32 v47, v2, v6
	v_max_f32_e32 v0, v0, v1
	v_max_f32_e32 v1, v4, v5
	v_min_f32_e32 v38, v38, v43
	v_min_f32_e32 v34, v34, v35
	v_min_f32_e32 v43, v45, v49
	v_min_f32_e32 v2, v2, v6
	v_min_f32_e32 v39, v29, v33
	v_min_f32_e32 v4, v0, v1
	v_max_f32_e32 v35, v38, v34
	v_max_f32_e32 v6, v43, v2
	v_min_f32_e32 v34, v38, v34
	v_min_f32_e32 v2, v43, v2
	v_min_f32_e32 v40, v37, v39
	v_max_f32_e32 v50, v45, v49
	v_min_f32_e32 v5, v47, v4
	v_min_f32_e32 v38, v34, v2
	v_max_f32_e32 v2, v34, v2
	v_max_f32_e32 v34, v36, v42
	v_max_f32_e32 v36, v37, v39
	v_max_f32_e32 v3, v3, v7
	v_max_f32_e32 v4, v47, v4
	v_max_f32_e32 v41, v44, v40
	v_max_f32_e32 v48, v50, v5
	v_min_f32_e32 v37, v34, v36
	v_min_f32_e32 v7, v3, v4
	v_min_f32_e32 v40, v44, v40
	v_min_f32_e32 v5, v50, v5
	v_max_f32_e32 v34, v34, v36
	v_max_f32_e32 v3, v3, v4
	v_max_f32_e32 v29, v29, v33
	v_max_f32_e32 v0, v0, v1
	v_max_f32_e32 v54, v46, v53
	v_min_f32_e32 v51, v41, v48
	v_min_f32_e32 v45, v35, v6
	v_min_f32_e32 v39, v37, v7
	v_min_f32_e32 v44, v40, v5
	v_max_f32_e32 v6, v35, v6
	v_min_f32_e32 v4, v34, v3
	v_max_f32_e32 v5, v40, v5
	v_min_f32_e32 v1, v29, v0
	v_min_f32_e32 v52, v54, v51
	v_min_f32_e32 v42, v2, v39
	v_max_f32_e32 v51, v54, v51
	v_min_f32_e32 v35, v6, v4
	v_max_f32_e32 v2, v2, v39
	v_min_f32_e32 v33, v5, v1
	v_max_f32_e32 v41, v41, v48
	v_max_f32_e32 v4, v6, v4
	v_max_f32_e32 v7, v37, v7
	v_max_f32_e32 v1, v5, v1
	v_max_f32_e32 v21, v28, v21
	v_min_f32_e32 v23, v18, v20
	v_max_f32_e32 v18, v18, v20
	v_min_f32_e32 v49, v52, v45
	v_max_f32_e32 v45, v52, v45
	v_min_f32_e32 v47, v42, v44
	v_min_f32_e32 v36, v51, v35
	v_max_f32_e32 v42, v42, v44
	v_max_f32_e32 v35, v51, v35
	v_min_f32_e32 v39, v2, v33
	v_min_f32_e32 v6, v41, v4
	v_max_f32_e32 v2, v2, v33
	v_max_f32_e32 v4, v41, v4
	v_min_f32_e32 v5, v7, v1
	v_max_f32_e32 v3, v34, v3
	v_max_f32_e32 v1, v7, v1
	v_min_f32_e32 v19, v25, v14
	v_min_f32_e32 v26, v21, v23
	v_min_f32_e32 v20, v12, v18
	v_min_f32_e32 v16, v11, v15
	v_min_f32_e32 v28, v24, v27
	v_min_f32_e32 v30, v17, v13
	v_min_f32_e32 v32, v10, v31
	v_min_f32_e32 v43, v49, v38
	v_min_f32_e32 v50, v45, v47
	v_min_f32_e32 v44, v36, v42
	v_min_f32_e32 v40, v35, v39
	v_min_f32_e32 v33, v6, v2
	v_min_f32_e32 v37, v4, v5
	v_min_f32_e32 v7, v3, v1
	v_min_f32_e32 v34, v46, v53
	v_max3_f32 v8, v8, v9, v34
	v_max3_f32 v9, v10, v31, v43
	v_max3_f32 v10, v32, v49, v38
	v_max3_f32 v13, v17, v13, v50
	v_max3_f32 v17, v30, v45, v47
	v_max3_f32 v24, v24, v27, v44
	v_max3_f32 v27, v28, v36, v42
	v_max3_f32 v11, v11, v15, v40
	v_max3_f32 v15, v16, v35, v39
	v_max3_f32 v12, v12, v18, v33
	v_max3_f32 v2, v20, v6, v2
	v_max3_f32 v6, v21, v23, v37
	v_max3_f32 v4, v26, v4, v5
	v_max3_f32 v5, v25, v14, v7
	v_max3_f32 v1, v19, v3, v1
	v_max3_f32 v0, v22, v29, v0
	v_max_f32_e32 v3, v8, v15
	v_min_f32_e32 v7, v8, v15
	v_max_f32_e32 v8, v9, v12
	v_min_f32_e32 v9, v9, v12
	v_max_f32_e32 v12, v10, v2
	v_min_f32_e32 v2, v10, v2
	v_max_f32_e32 v10, v13, v6
	v_min_f32_e32 v6, v13, v6
	v_max_f32_e32 v13, v17, v4
	v_min_f32_e32 v4, v17, v4
	v_max_f32_e32 v14, v24, v5
	v_min_f32_e32 v5, v24, v5
	v_max_f32_e32 v15, v27, v1
	v_min_f32_e32 v1, v27, v1
	v_max_f32_e32 v16, v11, v0
	v_min_f32_e32 v0, v11, v0
	v_max_f32_e32 v11, v3, v13
	v_min_f32_e32 v3, v3, v13
	v_max_f32_e32 v13, v8, v14
	v_min_f32_e32 v8, v8, v14
	v_max_f32_e32 v14, v12, v15
	v_min_f32_e32 v12, v12, v15
	v_max_f32_e32 v15, v10, v16
	v_min_f32_e32 v10, v10, v16
	v_max_f32_e32 v16, v7, v4
	v_min_f32_e32 v4, v7, v4
	v_max_f32_e32 v7, v9, v5
	v_min_f32_e32 v5, v9, v5
	v_max_f32_e32 v9, v2, v1
	v_min_f32_e32 v1, v2, v1
	v_max_f32_e32 v2, v6, v0
	v_min_f32_e32 v0, v6, v0
	v_max_f32_e32 v17, v11, v14
	v_min_f32_e32 v11, v11, v14
	v_max_f32_e32 v14, v13, v15
	v_min_f32_e32 v13, v13, v15
	v_max_f32_e32 v15, v3, v12
	v_min_f32_e32 v12, v3, v12
	v_max_f32_e32 v18, v8, v10
	v_min_f32_e32 v8, v8, v10
	v_max_f32_e32 v10, v16, v9
	v_min_f32_e32 v9, v16, v9
	v_max_f32_e32 v16, v7, v2
	v_min_f32_e32 v19, v7, v2
	v_max_f32_e32 v20, v4, v1
	v_min_f32_e32 v21, v4, v1
	v_max_f32_e32 v22, v5, v0
	v_min_f32_e32 v23, v5, v0
	ds_read_b128 v[0:3], v102
	ds_read_b128 v[4:7], v101
	v_min_f32_e32 v24, v17, v14
	v_min_f32_e32 v25, v11, v13
	v_min_f32_e32 v26, v15, v18
	s_waitcnt lgkmcnt(0)
; __device__ __forceinline__ void sort16_desc(float (&v)[16]) {
;     CE(v[0], v[1]); CE(v[2], v[3]); CE(v[0], v[2]); CE(v[1], v[3]);
;     CE(v[1], v[2]); CE(v[4], v[5]); CE(v[6], v[7]); CE(v[4], v[6]);
;     CE(v[5], v[7]); CE(v[5], v[6]); CE(v[0], v[4]); CE(v[2], v[6]);
;     CE(v[2], v[4]); CE(v[1], v[5]); CE(v[3], v[7]); CE(v[3], v[5]);
;     CE(v[1], v[2]); CE(v[3], v[4]); CE(v[5], v[6]); CE(v[8], v[9]);
;     CE(v[10], v[11]); CE(v[8], v[10]); CE(v[9], v[11]); CE(v[9], v[10]);
;     CE(v[12], v[13]); CE(v[14], v[15]); CE(v[12], v[14]); CE(v[13], v[15]);
;     CE(v[13], v[14]); CE(v[8], v[12]); CE(v[10], v[14]); CE(v[10], v[12]);
;     CE(v[9], v[13]); CE(v[11], v[15]); CE(v[11], v[13]); CE(v[9], v[10]);
;     CE(v[11], v[12]); CE(v[13], v[14]); CE(v[0], v[8]); CE(v[4], v[12]);
;     CE(v[4], v[8]); CE(v[2], v[10]); CE(v[6], v[14]); CE(v[6], v[10]);
;     CE(v[2], v[4]); CE(v[6], v[8]); CE(v[10], v[12]); CE(v[1], v[9]);
;     CE(v[5], v[13]); CE(v[5], v[9]); CE(v[3], v[11]); CE(v[7], v[15]);
;     CE(v[7], v[11]); CE(v[3], v[5]); CE(v[7], v[9]); CE(v[11], v[13]);
;     CE(v[1], v[2]); CE(v[3], v[4]); CE(v[5], v[6]); CE(v[7], v[8]);
;     CE(v[9], v[10]); CE(v[11], v[12]); CE(v[13], v[14]);
; }
; __device__ __forceinline__ void merge_top16(float (&v)[16], const float (&nw)[16]) {
;     v[0] = fmaxf(v[0], nw[15]); v[1] = fmaxf(v[1], nw[14]); v[2] = fmaxf(v[2], nw[13]); v[3] = fmaxf(v[3], nw[12]); v[4] = fmaxf(v[4], nw[11]); v[5] = fmaxf(v[5], nw[10]); v[6] = fmaxf(v[6], nw[9]); v[7] = fmaxf(v[7], nw[8]); v[8] = fmaxf(v[8], nw[7]); v[9] = fmaxf(v[9], nw[6]); v[10] = fmaxf(v[10], nw[5]); v[11] = fmaxf(v[11], nw[4]); v[12] = fmaxf(v[12], nw[3]); v[13] = fmaxf(v[13], nw[2]); v[14] = fmaxf(v[14], nw[1]); v[15] = fmaxf(v[15], nw[0]);
;     CE(v[0], v[8]); CE(v[1], v[9]); CE(v[2], v[10]); CE(v[3], v[11]);
;     CE(v[4], v[12]); CE(v[5], v[13]); CE(v[6], v[14]); CE(v[7], v[15]);
;     CE(v[0], v[4]); CE(v[1], v[5]); CE(v[2], v[6]); CE(v[3], v[7]);
;     CE(v[8], v[12]); CE(v[9], v[13]); CE(v[10], v[14]); CE(v[11], v[15]);
;     CE(v[0], v[2]); CE(v[1], v[3]); CE(v[4], v[6]); CE(v[5], v[7]);
;     CE(v[8], v[10]); CE(v[9], v[11]); CE(v[12], v[14]); CE(v[13], v[15]);
;     CE(v[0], v[1]); CE(v[2], v[3]); CE(v[4], v[5]); CE(v[6], v[7]);
;     CE(v[8], v[9]); CE(v[10], v[11]); CE(v[12], v[13]); CE(v[14], v[15]);
; }
	v_min_f32_e32 v34, v0, v1
	v_max_f32_e32 v32, v0, v1
	v_min_f32_e32 v37, v2, v3
	v_max_f32_e32 v33, v2, v3
	v_min_f32_e32 v41, v4, v5
	v_max_f32_e32 v39, v4, v5
	v_min_f32_e32 v44, v6, v7
	v_max_f32_e32 v40, v6, v7
	ds_read_b128 v[0:3], v95
	ds_read_b128 v[4:7], v94
	s_waitcnt lgkmcnt(0)
	v_min_f32_e32 v47, v0, v1
	v_min_f32_e32 v48, v2, v3
	v_min_f32_e32 v50, v4, v5
	v_min_f32_e32 v51, v6, v7
	v_max_f32_e32 v0, v0, v1
	v_max_f32_e32 v1, v2, v3
	v_max_f32_e32 v4, v4, v5
	v_max_f32_e32 v5, v6, v7
	v_min_f32_e32 v38, v34, v37
	v_min_f32_e32 v45, v41, v44
	v_min_f32_e32 v49, v47, v48
	v_max_f32_e32 v34, v34, v37
	v_min_f32_e32 v35, v32, v33
	v_max_f32_e32 v37, v41, v44
	v_min_f32_e32 v41, v39, v40
	v_max_f32_e32 v47, v47, v48
	v_min_f32_e32 v2, v0, v1
	v_max_f32_e32 v48, v50, v51
	v_min_f32_e32 v6, v4, v5
	v_min_f32_e32 v52, v50, v51
	v_max_f32_e32 v36, v34, v35
	v_max_f32_e32 v42, v37, v41
	v_max_f32_e32 v3, v47, v2
	v_max_f32_e32 v7, v48, v6
	v_min_f32_e32 v46, v38, v45
	v_min_f32_e32 v53, v49, v52
	v_max_f32_e32 v38, v38, v45
	v_min_f32_e32 v43, v36, v42
	v_min_f32_e32 v34, v34, v35
	v_min_f32_e32 v35, v37, v41
	v_max_f32_e32 v45, v49, v52
	v_min_f32_e32 v49, v3, v7
	v_min_f32_e32 v2, v47, v2
	v_min_f32_e32 v6, v48, v6
	v_max_f32_e32 v44, v38, v43
	v_max_f32_e32 v37, v34, v35
	v_max_f32_e32 v32, v32, v33
	v_max_f32_e32 v33, v39, v40
	v_max_f32_e32 v47, v2, v6
	v_max_f32_e32 v0, v0, v1
	v_max_f32_e32 v1, v4, v5
	v_min_f32_e32 v38, v38, v43
	v_min_f32_e32 v34, v34, v35
	v_min_f32_e32 v43, v45, v49
	v_min_f32_e32 v2, v2, v6
	v_min_f32_e32 v39, v32, v33
	v_min_f32_e32 v4, v0, v1
	v_max_f32_e32 v35, v38, v34
	v_max_f32_e32 v6, v43, v2
	v_min_f32_e32 v34, v38, v34
	v_min_f32_e32 v2, v43, v2
	v_min_f32_e32 v40, v37, v39
	v_max_f32_e32 v50, v45, v49
	v_min_f32_e32 v5, v47, v4
	v_min_f32_e32 v38, v34, v2
	v_max_f32_e32 v2, v34, v2
	v_max_f32_e32 v34, v36, v42
	v_max_f32_e32 v36, v37, v39
	v_max_f32_e32 v3, v3, v7
	v_max_f32_e32 v4, v47, v4
	v_max_f32_e32 v41, v44, v40
	v_max_f32_e32 v48, v50, v5
	v_min_f32_e32 v37, v34, v36
	v_min_f32_e32 v7, v3, v4
	v_max_f32_e32 v54, v46, v53
	v_min_f32_e32 v51, v41, v48
	v_min_f32_e32 v39, v37, v7
	v_min_f32_e32 v40, v44, v40
	v_min_f32_e32 v5, v50, v5
	v_min_f32_e32 v52, v54, v51
	v_min_f32_e32 v45, v35, v6
	v_min_f32_e32 v42, v2, v39
	v_min_f32_e32 v44, v40, v5
	v_max_f32_e32 v34, v34, v36
	v_max_f32_e32 v3, v3, v4
	v_max_f32_e32 v32, v32, v33
	v_max_f32_e32 v0, v0, v1
	v_min_f32_e32 v49, v52, v45
	v_max_f32_e32 v45, v52, v45
	v_min_f32_e32 v47, v42, v44
	v_max_f32_e32 v6, v35, v6
	v_min_f32_e32 v4, v34, v3
	v_max_f32_e32 v5, v40, v5
	v_min_f32_e32 v1, v32, v0
	v_min_f32_e32 v43, v49, v38
	v_max_f32_e32 v38, v49, v38
	v_min_f32_e32 v49, v45, v47
	v_max_f32_e32 v45, v45, v47
	v_max_f32_e32 v47, v54, v51
	v_min_f32_e32 v35, v6, v4
	v_max_f32_e32 v2, v2, v39
	v_min_f32_e32 v33, v5, v1
	v_min_f32_e32 v36, v47, v35
	v_max_f32_e32 v35, v47, v35
	v_min_f32_e32 v39, v2, v33
	v_min_f32_e32 v40, v35, v39
	v_max_f32_e32 v35, v35, v39
	v_max_f32_e32 v39, v41, v48
	v_max_f32_e32 v4, v6, v4
	v_min_f32_e32 v6, v39, v4
	v_max_f32_e32 v2, v2, v33
	v_min_f32_e32 v33, v6, v2
	v_max_f32_e32 v2, v6, v2
	v_max_f32_e32 v6, v37, v7
	v_max_f32_e32 v1, v5, v1
	v_max_f32_e32 v42, v42, v44
	v_max_f32_e32 v4, v39, v4
	v_min_f32_e32 v5, v6, v1
	v_max_f32_e32 v3, v34, v3
	v_max_f32_e32 v1, v6, v1
	v_min_f32_e32 v27, v12, v8
	v_min_f32_e32 v28, v10, v16
	v_min_f32_e32 v29, v9, v19
	v_min_f32_e32 v30, v20, v22
	v_min_f32_e32 v31, v21, v23
	v_min_f32_e32 v44, v36, v42
	v_max_f32_e32 v36, v36, v42
	v_min_f32_e32 v7, v4, v5
	v_max_f32_e32 v4, v4, v5
	v_min_f32_e32 v5, v3, v1
	v_max_f32_e32 v1, v3, v1
	v_min_f32_e32 v3, v46, v53
	v_max3_f32 v3, v17, v14, v3
	v_max_f32_e32 v6, v24, v43
	v_max3_f32 v11, v11, v13, v38
	v_max_f32_e32 v13, v25, v49
	v_max3_f32 v14, v15, v18, v45
	v_max_f32_e32 v15, v26, v44
	v_max3_f32 v8, v12, v8, v36
	v_max_f32_e32 v12, v27, v40
	v_max3_f32 v10, v10, v16, v35
	v_max_f32_e32 v16, v28, v33
	v_max3_f32 v2, v9, v19, v2
	v_max_f32_e32 v7, v29, v7
	v_max3_f32 v4, v20, v22, v4
	v_max_f32_e32 v5, v30, v5
	v_max3_f32 v1, v21, v23, v1
	v_max3_f32 v0, v31, v32, v0
	v_max_f32_e32 v9, v3, v10
	v_min_f32_e32 v3, v3, v10
	v_max_f32_e32 v10, v6, v16
	v_min_f32_e32 v6, v6, v16
	v_max_f32_e32 v16, v11, v2
	v_min_f32_e32 v2, v11, v2
	v_max_f32_e32 v11, v13, v7
	v_min_f32_e32 v7, v13, v7
	v_max_f32_e32 v13, v14, v4
	v_min_f32_e32 v4, v14, v4
	v_max_f32_e32 v14, v15, v5
	v_min_f32_e32 v5, v15, v5
	v_max_f32_e32 v15, v8, v1
	v_min_f32_e32 v1, v8, v1
	v_max_f32_e32 v8, v12, v0
	v_min_f32_e32 v0, v12, v0
	v_max_f32_e32 v12, v9, v13
	v_min_f32_e32 v9, v9, v13
	v_max_f32_e32 v13, v10, v14
	v_min_f32_e32 v10, v10, v14
	v_max_f32_e32 v14, v16, v15
	v_min_f32_e32 v15, v16, v15
	v_max_f32_e32 v16, v11, v8
	v_min_f32_e32 v8, v11, v8
	v_max_f32_e32 v11, v3, v4
	v_min_f32_e32 v3, v3, v4
	v_max_f32_e32 v4, v6, v5
	v_min_f32_e32 v5, v6, v5
	v_max_f32_e32 v6, v2, v1
	v_min_f32_e32 v1, v2, v1
	v_max_f32_e32 v2, v7, v0
	v_min_f32_e32 v0, v7, v0
	v_max_f32_e32 v17, v12, v14
	v_min_f32_e32 v12, v12, v14
	v_max_f32_e32 v14, v13, v16
	v_min_f32_e32 v13, v13, v16
	v_max_f32_e32 v16, v9, v15
	v_min_f32_e32 v9, v9, v15
	v_max_f32_e32 v15, v10, v8
	v_min_f32_e32 v8, v10, v8
	v_max_f32_e32 v10, v11, v6
	v_min_f32_e32 v11, v11, v6
	v_max_f32_e32 v18, v4, v2
	v_min_f32_e32 v19, v4, v2
	v_max_f32_e32 v20, v3, v1
	v_min_f32_e32 v21, v3, v1
	v_max_f32_e32 v22, v5, v0
	v_min_f32_e32 v23, v5, v0
	ds_read_b128 v[0:3], v104
	ds_read_b128 v[4:7], v103
	v_min_f32_e32 v24, v17, v14
	v_min_f32_e32 v25, v12, v13
	v_min_f32_e32 v26, v16, v15
	s_waitcnt lgkmcnt(0)
; #define PG8_LAS __attribute__((address_space(3)))
; #define CE(a, b) do { const float hi_ = fmaxf(a, b), lo_ = fminf(a, b); a = hi_; b = lo_; } while (0)
; #define RT_BAR() do { asm volatile("s_waitcnt lgkmcnt(0)" ::: "memory"); __builtin_amdgcn_s_barrier(); asm volatile("" ::: "memory"); } while (0)
; __device__ __forceinline__ void merge_top16(float (&v)[16], const float (&nw)[16]) {
;     v[0] = fmaxf(v[0], nw[15]); v[1] = fmaxf(v[1], nw[14]); v[2] = fmaxf(v[2], nw[13]); v[3] = fmaxf(v[3], nw[12]); v[4] = fmaxf(v[4], nw[11]); v[5] = fmaxf(v[5], nw[10]); v[6] = fmaxf(v[6], nw[9]); v[7] = fmaxf(v[7], nw[8]); v[8] = fmaxf(v[8], nw[7]); v[9] = fmaxf(v[9], nw[6]); v[10] = fmaxf(v[10], nw[5]); v[11] = fmaxf(v[11], nw[4]); v[12] = fmaxf(v[12], nw[3]); v[13] = fmaxf(v[13], nw[2]); v[14] = fmaxf(v[14], nw[1]); v[15] = fmaxf(v[15], nw[0]);
;     CE(v[0], v[8]); CE(v[1], v[9]); CE(v[2], v[10]); CE(v[3], v[11]);
;     CE(v[4], v[12]); CE(v[5], v[13]); CE(v[6], v[14]); CE(v[7], v[15]);
;     CE(v[0], v[4]); CE(v[1], v[5]); CE(v[2], v[6]); CE(v[3], v[7]);
;     CE(v[8], v[12]); CE(v[9], v[13]); CE(v[10], v[14]); CE(v[11], v[15]);
;     CE(v[0], v[2]); CE(v[1], v[3]); CE(v[4], v[6]); CE(v[5], v[7]);
;     CE(v[8], v[10]); CE(v[9], v[11]); CE(v[12], v[14]); CE(v[13], v[15]);
;     CE(v[0], v[1]); CE(v[2], v[3]); CE(v[4], v[5]); CE(v[6], v[7]);
;     CE(v[8], v[9]); CE(v[10], v[11]); CE(v[12], v[13]); CE(v[14], v[15]);
; }
;     __device__ __forceinline__ void fused(f32x4 (&acc)[2][2][4][2], const Unit& u, int wr, int wc, int fr, int fq, PG8_LAS unsigned char* lds, int wid, int lane) const {
;     ...
;                 } else merge_top16(run, nw);
;             }
;             RT_BAR();
;             if (half == 1) {
; #pragma unroll
;                 for (int i = 0; i < 4; ++i) *(PG8_LAS f32x4*)(tile + row * 16 + 4 * i) = (f32x4){run[4 * i], run[4 * i + 1], run[4 * i + 2], run[4 * i + 3]};
	v_min_f32_e32 v34, v0, v1
	v_max_f32_e32 v32, v0, v1
	v_min_f32_e32 v37, v2, v3
	v_max_f32_e32 v33, v2, v3
	v_min_f32_e32 v41, v4, v5
	v_max_f32_e32 v39, v4, v5
	v_min_f32_e32 v44, v6, v7
	v_max_f32_e32 v40, v6, v7
	ds_read_b128 v[0:3], v100
	ds_read_b128 v[4:7], v98
	s_waitcnt lgkmcnt(0)
	v_min_f32_e32 v47, v0, v1
	v_min_f32_e32 v48, v2, v3
	v_min_f32_e32 v50, v4, v5
	v_min_f32_e32 v51, v6, v7
	v_max_f32_e32 v0, v0, v1
	v_max_f32_e32 v1, v2, v3
	v_max_f32_e32 v4, v4, v5
	v_max_f32_e32 v5, v6, v7
	v_min_f32_e32 v38, v34, v37
	v_min_f32_e32 v45, v41, v44
	v_min_f32_e32 v49, v47, v48
	v_max_f32_e32 v34, v34, v37
	v_min_f32_e32 v35, v32, v33
	v_max_f32_e32 v37, v41, v44
	v_min_f32_e32 v41, v39, v40
	v_max_f32_e32 v47, v47, v48
	v_min_f32_e32 v2, v0, v1
	v_max_f32_e32 v48, v50, v51
	v_min_f32_e32 v6, v4, v5
	v_min_f32_e32 v52, v50, v51
	v_max_f32_e32 v36, v34, v35
	v_max_f32_e32 v42, v37, v41
	v_max_f32_e32 v3, v47, v2
	v_max_f32_e32 v7, v48, v6
	v_min_f32_e32 v46, v38, v45
	v_min_f32_e32 v53, v49, v52
	v_max_f32_e32 v38, v38, v45
	v_min_f32_e32 v43, v36, v42
	v_min_f32_e32 v34, v34, v35
	v_min_f32_e32 v35, v37, v41
	v_max_f32_e32 v45, v49, v52
	v_min_f32_e32 v49, v3, v7
	v_min_f32_e32 v2, v47, v2
	v_min_f32_e32 v6, v48, v6
	v_max_f32_e32 v44, v38, v43
	v_max_f32_e32 v37, v34, v35
	v_max_f32_e32 v32, v32, v33
	v_max_f32_e32 v33, v39, v40
	v_max_f32_e32 v47, v2, v6
	v_max_f32_e32 v0, v0, v1
	v_max_f32_e32 v1, v4, v5
	v_min_f32_e32 v38, v38, v43
	v_min_f32_e32 v34, v34, v35
	v_min_f32_e32 v43, v45, v49
	v_min_f32_e32 v2, v2, v6
	v_min_f32_e32 v39, v32, v33
	v_min_f32_e32 v4, v0, v1
	v_max_f32_e32 v35, v38, v34
	v_max_f32_e32 v6, v43, v2
	v_min_f32_e32 v34, v38, v34
	v_min_f32_e32 v2, v43, v2
	v_min_f32_e32 v40, v37, v39
	v_max_f32_e32 v50, v45, v49
	v_min_f32_e32 v5, v47, v4
	v_min_f32_e32 v38, v34, v2
	v_max_f32_e32 v2, v34, v2
	v_max_f32_e32 v34, v36, v42
	v_max_f32_e32 v36, v37, v39
	v_max_f32_e32 v3, v3, v7
	v_max_f32_e32 v4, v47, v4
	v_max_f32_e32 v41, v44, v40
	v_max_f32_e32 v48, v50, v5
	v_min_f32_e32 v37, v34, v36
	v_min_f32_e32 v7, v3, v4
	v_max_f32_e32 v54, v46, v53
	v_min_f32_e32 v51, v41, v48
	v_min_f32_e32 v39, v37, v7
	v_min_f32_e32 v40, v44, v40
	v_min_f32_e32 v5, v50, v5
	v_min_f32_e32 v52, v54, v51
	v_min_f32_e32 v45, v35, v6
	v_min_f32_e32 v42, v2, v39
	v_min_f32_e32 v44, v40, v5
	v_max_f32_e32 v34, v34, v36
	v_max_f32_e32 v3, v3, v4
	v_max_f32_e32 v32, v32, v33
	v_max_f32_e32 v0, v0, v1
	v_min_f32_e32 v49, v52, v45
	v_max_f32_e32 v45, v52, v45
	v_min_f32_e32 v47, v42, v44
	v_max_f32_e32 v6, v35, v6
	v_min_f32_e32 v4, v34, v3
	v_max_f32_e32 v5, v40, v5
	v_min_f32_e32 v1, v32, v0
	v_min_f32_e32 v43, v49, v38
	v_max_f32_e32 v38, v49, v38
	v_min_f32_e32 v49, v45, v47
	v_max_f32_e32 v45, v45, v47
	v_max_f32_e32 v47, v54, v51
	v_min_f32_e32 v35, v6, v4
	v_max_f32_e32 v2, v2, v39
	v_min_f32_e32 v33, v5, v1
	v_min_f32_e32 v36, v47, v35
	v_max_f32_e32 v35, v47, v35
	v_min_f32_e32 v39, v2, v33
	v_min_f32_e32 v40, v35, v39
	v_max_f32_e32 v35, v35, v39
	v_max_f32_e32 v39, v41, v48
	v_max_f32_e32 v4, v6, v4
	v_min_f32_e32 v6, v39, v4
	v_max_f32_e32 v2, v2, v33
	v_min_f32_e32 v33, v6, v2
	v_max_f32_e32 v2, v6, v2
	v_max_f32_e32 v6, v37, v7
	v_max_f32_e32 v1, v5, v1
	v_max_f32_e32 v42, v42, v44
	v_max_f32_e32 v4, v39, v4
	v_min_f32_e32 v5, v6, v1
	v_max_f32_e32 v3, v34, v3
	v_max_f32_e32 v1, v6, v1
	v_min_f32_e32 v27, v9, v8
	v_min_f32_e32 v28, v10, v18
	v_min_f32_e32 v29, v11, v19
	v_min_f32_e32 v30, v20, v22
	v_min_f32_e32 v31, v21, v23
	v_min_f32_e32 v44, v36, v42
	v_max_f32_e32 v36, v36, v42
	v_min_f32_e32 v7, v4, v5
	v_max_f32_e32 v4, v4, v5
	v_min_f32_e32 v5, v3, v1
	v_max_f32_e32 v1, v3, v1
	v_min_f32_e32 v3, v46, v53
	v_max3_f32 v3, v17, v14, v3
	v_max_f32_e32 v6, v24, v43
	v_max3_f32 v12, v12, v13, v38
	v_max_f32_e32 v13, v25, v49
	v_max3_f32 v14, v16, v15, v45
	v_max_f32_e32 v15, v26, v44
	v_max3_f32 v8, v9, v8, v36
	v_max_f32_e32 v9, v27, v40
	v_max3_f32 v10, v10, v18, v35
	v_max_f32_e32 v16, v28, v33
	v_max3_f32 v2, v11, v19, v2
	v_max_f32_e32 v7, v29, v7
	v_max3_f32 v4, v20, v22, v4
	v_max_f32_e32 v5, v30, v5
	v_max3_f32 v1, v21, v23, v1
	v_max3_f32 v0, v31, v32, v0
	v_max_f32_e32 v11, v3, v10
	v_min_f32_e32 v3, v3, v10
	v_max_f32_e32 v10, v6, v16
	v_min_f32_e32 v6, v6, v16
	v_max_f32_e32 v16, v12, v2
	v_min_f32_e32 v2, v12, v2
	v_max_f32_e32 v12, v13, v7
	v_min_f32_e32 v7, v13, v7
	v_max_f32_e32 v13, v14, v4
	v_min_f32_e32 v4, v14, v4
	v_max_f32_e32 v14, v15, v5
	v_min_f32_e32 v5, v15, v5
	v_max_f32_e32 v15, v8, v1
	v_min_f32_e32 v1, v8, v1
	v_max_f32_e32 v8, v9, v0
	v_min_f32_e32 v0, v9, v0
	v_max_f32_e32 v9, v11, v13
	v_min_f32_e32 v11, v11, v13
	v_max_f32_e32 v13, v10, v14
	v_min_f32_e32 v10, v10, v14
	v_max_f32_e32 v14, v16, v15
	v_min_f32_e32 v15, v16, v15
	v_max_f32_e32 v16, v12, v8
	v_min_f32_e32 v8, v12, v8
	v_max_f32_e32 v12, v3, v4
	v_min_f32_e32 v3, v3, v4
	v_max_f32_e32 v4, v6, v5
	v_min_f32_e32 v5, v6, v5
	v_max_f32_e32 v6, v2, v1
	v_min_f32_e32 v1, v2, v1
	v_max_f32_e32 v2, v7, v0
	v_min_f32_e32 v0, v7, v0
	s_waitcnt lgkmcnt(0)
	s_barrier
	s_waitcnt vmcnt(0)
	ds_write_b128 v241, v[224:227]
	ds_write_b128 v241, v[228:231] offset:16
	ds_write_b128 v241, v[232:235] offset:32
	ds_write_b128 v241, v[236:239] offset:48
	v_max_f32_e32 v7, v9, v14
	v_min_f32_e32 v9, v9, v14
	v_max_f32_e32 v14, v13, v16
	v_min_f32_e32 v16, v13, v16
	v_max_f32_e32 v17, v11, v15
	v_min_f32_e32 v11, v11, v15
	v_max_f32_e32 v18, v10, v8
	v_min_f32_e32 v19, v10, v8
	v_max_f32_e32 v20, v12, v6
	v_min_f32_e32 v21, v12, v6
	v_max_f32_e32 v6, v4, v2
	v_min_f32_e32 v2, v4, v2
	v_max_f32_e32 v22, v3, v1
	v_min_f32_e32 v3, v3, v1
	v_max_f32_e32 v1, v5, v0
	v_min_f32_e32 v23, v5, v0
	v_max_f32_e32 v12, v7, v14
	v_min_f32_e32 v13, v7, v14
	v_max_f32_e32 v14, v9, v16
	v_min_f32_e32 v15, v9, v16
	v_max_f32_e32 v8, v17, v18
	v_min_f32_e32 v9, v17, v18
	v_max_f32_e32 v10, v11, v19
	v_min_f32_e32 v11, v11, v19
	v_max_f32_e32 v4, v20, v6
	v_min_f32_e32 v5, v20, v6
	v_max_f32_e32 v6, v21, v2
	v_min_f32_e32 v7, v21, v2
	v_max_f32_e32 v0, v22, v1
	v_min_f32_e32 v1, v22, v1
	v_max_f32_e32 v2, v3, v23
	v_min_f32_e32 v3, v3, v23
	s_cbranch_vccnz .LBB0_586
	ds_write_b128 v97, v[12:15]
	ds_write_b128 v97, v[8:11] offset:16
	ds_write_b128 v97, v[4:7] offset:32
	ds_write_b128 v97, v[0:3] offset:48

; #define PG8_LAS __attribute__((address_space(3)))
;     __device__ __forceinline__ void fused(f32x4 (&acc)[2][2][4][2], const Unit& u, int wr, int wc, int fr, int fq, PG8_LAS unsigned char* lds, int wid, int lane) const {
;     ...
;         if (half == 0) {
;             PG8_LAS int* idxl = (PG8_LAS int*)(lds + 65536) + row * 32;
;             float v0[16], v1[16];
; #pragma unroll
;             for (int q = 0; q < 16; ++q) { const unsigned b0 = __float_as_uint(top0[q]), b1 = __float_as_uint(top1[q]);
;                 v0[q] = __uint_as_float(b0 & ~127u); v1[q] = __uint_as_float(b1 & ~127u); idxl[q] = (int)(b0 & 127u); idxl[16 + q] = (int)(b1 & 127u); }
;             float best[16];
;             { float cv[16]; cv[0] = __uint_as_float((__float_as_uint(v0[0] + v1[0]) & ~255u) | 0u); cv[1] = __uint_as_float((__float_as_uint(v0[0] + v1[1]) & ~255u) | 1u); cv[2] = __uint_as_float((__float_as_uint(v0[0] + v1[2]) & ~255u) | 2u); cv[3] = __uint_as_float((__float_as_uint(v0[0] + v1[3]) & ~255u) | 3u); cv[4] = __uint_as_float((__float_as_uint(v0[0] + v1[4]) & ~255u) | 4u); cv[5] = __uint_as_float((__float_as_uint(v0[0] + v1[5]) & ~255u) | 5u); cv[6] = __uint_as_float((__float_as_uint(v0[0] + v1[6]) & ~255u) | 6u); cv[7] = __uint_as_float((__float_as_uint(v0[0] + v1[7]) & ~255u) | 7u); cv[8] = __uint_as_float((__float_as_uint(v0[0] + v1[8]) & ~255u) | 8u); cv[9] = __uint_as_float((__float_as_uint(v0[0] + v1[9]) & ~255u) | 9u); cv[10] = __uint_as_float((__float_as_uint(v0[0] + v1[10]) & ~255u) | 10u); cv[11] = __uint_as_float((__float_as_uint(v0[0] + v1[11]) & ~255u) | 11u); cv[12] = __uint_as_float((__float_as_uint(v0[0] + v1[12]) & ~255u) | 12u); cv[13] = __uint_as_float((__float_as_uint(v0[0] + v1[13]) & ~255u) | 13u); cv[14] = __uint_as_float((__float_as_uint(v0[0] + v1[14]) & ~255u) | 14u); cv[15] = __uint_as_float((__float_as_uint(v0[0] + v1[15]) & ~255u) | 15u); sort16_desc(cv);
; #pragma unroll
;               for (int q = 0; q < 16; ++q) best[q] = cv[q]; }
.LBB0_588:
	s_waitcnt lgkmcnt(0)
	s_barrier
	s_and_b64 vcc, exec, s[4:5]
	s_cbranch_vccnz .LBB0_590
	v_lshl_add_u32 v16, v128, 7, 0
	v_add_u32_e32 v16, 0x10000, v16
	v_and_b32_e32 v17, 0xffffff80, v12
	v_and_b32_e32 v18, 0xffffff80, v13
	v_and_b32_e32 v21, 0x7f, v77
	v_and_b32_e32 v20, 0x7f, v76
	v_and_b32_e32 v13, 0x7f, v13
	v_and_b32_e32 v12, 0x7f, v12
	v_and_b32_e32 v26, 0xffffff80, v14
	v_and_b32_e32 v28, 0xffffff80, v15
	v_and_b32_e32 v23, 0x7f, v79
	v_and_b32_e32 v22, 0x7f, v78
	v_and_b32_e32 v15, 0x7f, v15
	v_and_b32_e32 v14, 0x7f, v14
	ds_write_b128 v16, v[20:23]
	ds_write_b128 v16, v[12:15] offset:64
	v_and_b32_e32 v21, 0xffffff80, v8
	v_and_b32_e32 v23, 0xffffff80, v9
	v_and_b32_e32 v13, 0x7f, v73
	v_and_b32_e32 v12, 0x7f, v72
	v_and_b32_e32 v9, 0x7f, v9
	v_and_b32_e32 v8, 0x7f, v8
	v_and_b32_e32 v30, 0xffffff80, v10
	v_and_b32_e32 v32, 0xffffff80, v11
	v_and_b32_e32 v15, 0x7f, v75
	v_and_b32_e32 v14, 0x7f, v74
	v_and_b32_e32 v11, 0x7f, v11
	v_and_b32_e32 v10, 0x7f, v10
	v_and_b32_e32 v19, 0xffffff80, v76
	ds_write_b128 v16, v[12:15] offset:16
	ds_write_b128 v16, v[8:11] offset:80
	v_and_b32_e32 v13, 0xffffff80, v4
	v_and_b32_e32 v15, 0xffffff80, v5
	v_and_b32_e32 v9, 0x7f, v69
	v_and_b32_e32 v8, 0x7f, v68
	v_and_b32_e32 v5, 0x7f, v5
	v_and_b32_e32 v4, 0x7f, v4
	v_and_b32_e32 v34, 0xffffff80, v6
	v_and_b32_e32 v36, 0xffffff80, v7
	v_and_b32_e32 v11, 0x7f, v71
	v_and_b32_e32 v10, 0x7f, v70
	v_and_b32_e32 v7, 0x7f, v7
	v_and_b32_e32 v6, 0x7f, v6
	ds_write_b128 v16, v[8:11] offset:32
	ds_write_b128 v16, v[4:7] offset:96
	v_and_b32_e32 v5, 0x7f, v65
	v_and_b32_e32 v4, 0x7f, v64
	v_and_b32_e32 v41, 0xffffff80, v2
	v_and_b32_e32 v42, 0xffffff80, v3
	v_and_b32_e32 v7, 0x7f, v67
	v_and_b32_e32 v6, 0x7f, v66
	v_and_b32_e32 v11, 0x7f, v3
	v_and_b32_e32 v10, 0x7f, v2
	v_add_f32_e32 v2, v19, v17
	s_movk_i32 s4, 0xff00
	v_add_f32_e32 v3, v19, v18
	v_and_b32_e32 v24, 0xffffff80, v77
	ds_write_b128 v16, v[4:7] offset:48
	v_and_b32_e32 v2, 0xffffff00, v2
	v_and_or_b32 v3, v3, s4, 1
	v_add_f32_e32 v4, v19, v26
	v_add_f32_e32 v5, v19, v28
	v_and_b32_e32 v40, 0xffffff80, v1
	v_and_b32_e32 v9, 0x7f, v1
	v_and_b32_e32 v8, 0x7f, v0
	v_and_or_b32 v4, v4, s4, 2
	v_and_or_b32 v5, v5, s4, 3
	v_add_f32_e32 v48, v24, v17
	v_add_f32_e32 v49, v24, v18
	ds_write_b128 v16, v[8:11] offset:112
	v_add_f32_e32 v6, v19, v21
	v_add_f32_e32 v7, v19, v23
	v_add_f32_e32 v11, v19, v15
	v_add_f32_e32 v15, v19, v36
	v_add_f32_e32 v36, v19, v40
	v_max_f32_e32 v40, v2, v3
	v_min_f32_e32 v2, v2, v3
	v_max_f32_e32 v3, v5, v5
	v_and_or_b32 v48, v48, s4, 16
	v_and_or_b32 v49, v49, s4, 17
	v_add_f32_e32 v50, v24, v26
	v_add_f32_e32 v51, v24, v28
	v_and_or_b32 v6, v6, s4, 4
	v_and_or_b32 v7, v7, s4, 5
	v_add_f32_e32 v8, v19, v30
	v_add_f32_e32 v9, v19, v32
	v_max_f32_e32 v5, v4, v3
	v_min_f32_e32 v3, v4, v3
	v_and_or_b32 v50, v50, s4, 18
	v_and_or_b32 v51, v51, s4, 19
	v_and_or_b32 v8, v8, s4, 6
	v_and_or_b32 v9, v9, s4, 7
	v_max_f32_e32 v4, v40, v5
	v_min_f32_e32 v5, v40, v5
	v_max_f32_e32 v40, v2, v3
	v_add_f32_e32 v52, v24, v21
	v_add_f32_e32 v23, v24, v23
	v_add_f32_e32 v30, v24, v30
	v_add_f32_e32 v24, v24, v32
	v_max_f32_e32 v58, v48, v49
	v_min_f32_e32 v48, v48, v49
	v_max_f32_e32 v49, v51, v51
	v_min_f32_e32 v2, v2, v3
	v_max_f32_e32 v3, v40, v5
	v_min_f32_e32 v5, v40, v5
	v_max_f32_e32 v40, v6, v7
	v_min_f32_e32 v6, v6, v7
	v_max_f32_e32 v7, v9, v9
	v_and_or_b32 v52, v52, s4, 20
	v_and_or_b32 v23, v23, s4, 21
	v_and_or_b32 v30, v30, s4, 22
	v_and_or_b32 v24, v24, s4, 23
	v_max_f32_e32 v51, v50, v49
	v_min_f32_e32 v49, v50, v49
	v_max_f32_e32 v9, v8, v7
	v_min_f32_e32 v7, v8, v7
	v_max_f32_e32 v50, v58, v51
	v_min_f32_e32 v51, v58, v51
	v_max_f32_e32 v58, v48, v49
	v_max_f32_e32 v8, v40, v9
	v_min_f32_e32 v9, v40, v9
	v_max_f32_e32 v40, v6, v7
	v_min_f32_e32 v48, v48, v49
	v_max_f32_e32 v49, v58, v51
	v_min_f32_e32 v51, v58, v51
	v_max_f32_e32 v58, v52, v23
	v_min_f32_e32 v23, v52, v23
	v_max_f32_e32 v52, v30, v24
	v_min_f32_e32 v24, v30, v24
	v_min_f32_e32 v6, v6, v7
	v_max_f32_e32 v7, v40, v9
	v_min_f32_e32 v9, v40, v9
	v_max_f32_e32 v30, v58, v52
	v_min_f32_e32 v52, v58, v52
	v_max_f32_e32 v58, v23, v24
	v_max_f32_e32 v40, v4, v8
	v_min_f32_e32 v4, v4, v8
	v_max_f32_e32 v8, v5, v9
	v_min_f32_e32 v23, v23, v24
	v_max_f32_e32 v24, v58, v52
	v_min_f32_e32 v52, v58, v52
	v_and_b32_e32 v25, 0xffffff80, v78
	v_add_f32_e32 v10, v19, v13
	v_min_f32_e32 v5, v5, v9
	v_max_f32_e32 v9, v8, v4
	v_min_f32_e32 v4, v8, v4
	v_max_f32_e32 v8, v3, v7
	v_min_f32_e32 v3, v3, v7
	v_max_f32_e32 v7, v2, v6
	v_max_f32_e32 v58, v50, v30
	v_min_f32_e32 v30, v50, v30
	v_max_f32_e32 v50, v51, v52
	v_and_or_b32 v10, v10, s4, 8
	v_and_or_b32 v11, v11, s4, 9
	v_add_f32_e32 v13, v19, v34
	v_min_f32_e32 v2, v2, v6
	v_max_f32_e32 v6, v7, v3
	v_min_f32_e32 v3, v7, v3
	v_add_f32_e32 v32, v25, v17
	v_add_f32_e32 v53, v25, v18
	v_min_f32_e32 v51, v51, v52
	v_max_f32_e32 v52, v50, v30
	v_min_f32_e32 v30, v50, v30
	v_max_f32_e32 v50, v49, v24
	v_min_f32_e32 v24, v49, v24
	v_max_f32_e32 v49, v48, v23
	v_and_or_b32 v13, v13, s4, 10
	v_and_or_b32 v15, v15, s4, 11
	v_max_f32_e32 v7, v8, v9
	v_min_f32_e32 v8, v8, v9
	v_max_f32_e32 v9, v6, v4
	v_min_f32_e32 v4, v6, v4
	v_max_f32_e32 v6, v3, v5
	v_min_f32_e32 v3, v3, v5
	v_max_f32_e32 v5, v11, v11
	v_and_or_b32 v32, v32, s4, 32
	v_and_or_b32 v53, v53, s4, 33
	v_add_f32_e32 v54, v25, v26
	v_add_f32_e32 v55, v25, v28
	v_min_f32_e32 v23, v48, v23
	v_max_f32_e32 v48, v49, v24
	v_min_f32_e32 v24, v49, v24
	v_and_b32_e32 v27, 0xffffff80, v79
	v_and_b32_e32 v38, 0xffffff80, v0
	v_max_f32_e32 v11, v10, v5
	v_min_f32_e32 v5, v10, v5
	v_max_f32_e32 v10, v15, v15
; #define CE(a, b) do { const float hi_ = fmaxf(a, b), lo_ = fminf(a, b); a = hi_; b = lo_; } while (0)
; __device__ __forceinline__ void sort16_desc(float (&v)[16]) {
;     CE(v[0], v[1]); CE(v[2], v[3]); CE(v[0], v[2]); CE(v[1], v[3]);
;     CE(v[1], v[2]); CE(v[4], v[5]); CE(v[6], v[7]); CE(v[4], v[6]);
;     CE(v[5], v[7]); CE(v[5], v[6]); CE(v[0], v[4]); CE(v[2], v[6]);
;     CE(v[2], v[4]); CE(v[1], v[5]); CE(v[3], v[7]); CE(v[3], v[5]);
;     CE(v[1], v[2]); CE(v[3], v[4]); CE(v[5], v[6]); CE(v[8], v[9]);
;     CE(v[10], v[11]); CE(v[8], v[10]); CE(v[9], v[11]); CE(v[9], v[10]);
;     CE(v[12], v[13]); CE(v[14], v[15]); CE(v[12], v[14]); CE(v[13], v[15]);
;     CE(v[13], v[14]); CE(v[8], v[12]); CE(v[10], v[14]); CE(v[10], v[12]);
;     CE(v[9], v[13]); CE(v[11], v[15]); CE(v[11], v[13]); CE(v[9], v[10]);
;     CE(v[11], v[12]); CE(v[13], v[14]); CE(v[0], v[8]); CE(v[4], v[12]);
;     CE(v[4], v[8]); CE(v[2], v[10]); CE(v[6], v[14]); CE(v[6], v[10]);
;     CE(v[2], v[4]); CE(v[6], v[8]); CE(v[10], v[12]); CE(v[1], v[9]);
;     CE(v[5], v[13]); CE(v[5], v[9]); CE(v[3], v[11]); CE(v[7], v[15]);
;     CE(v[7], v[11]); CE(v[3], v[5]); CE(v[7], v[9]); CE(v[11], v[13]);
;     CE(v[1], v[2]); CE(v[3], v[4]); CE(v[5], v[6]); CE(v[7], v[8]);
;     CE(v[9], v[10]); CE(v[11], v[12]); CE(v[13], v[14]);
; }
	v_and_or_b32 v54, v54, s4, 34
	v_and_or_b32 v55, v55, s4, 35
	v_max_f32_e32 v49, v50, v52
	v_min_f32_e32 v50, v50, v52
	v_max_f32_e32 v52, v48, v30
	v_min_f32_e32 v30, v48, v30
	v_max_f32_e32 v48, v24, v51
	v_min_f32_e32 v24, v24, v51
	v_max_f32_e32 v51, v53, v53
	v_add_f32_e32 v34, v19, v38
	v_max_f32_e32 v15, v13, v10
	v_min_f32_e32 v10, v13, v10
	v_add_f32_e32 v21, v25, v21
	v_add_f32_e32 v25, v27, v17
	v_max_f32_e32 v53, v32, v51
	v_min_f32_e32 v32, v32, v51
	v_max_f32_e32 v51, v55, v55
	v_and_or_b32 v34, v34, s4, 12
	v_and_or_b32 v36, v36, s4, 13
	v_add_f32_e32 v38, v19, v41
	v_add_f32_e32 v19, v19, v42
	v_max_f32_e32 v13, v11, v15
	v_min_f32_e32 v11, v11, v15
	v_max_f32_e32 v15, v5, v10
	v_and_or_b32 v21, v21, s4, 36
	v_and_or_b32 v25, v25, s4, 48
	v_add_f32_e32 v56, v27, v18
	v_add_f32_e32 v57, v27, v26
	v_max_f32_e32 v55, v54, v51
	v_min_f32_e32 v51, v54, v51
	v_and_or_b32 v38, v38, s4, 14
	v_and_or_b32 v19, v19, s4, 15
	v_min_f32_e32 v5, v5, v10
	v_max_f32_e32 v10, v15, v11
	v_min_f32_e32 v11, v15, v11
	v_max_f32_e32 v15, v36, v36
	v_and_or_b32 v56, v56, s4, 49
	v_and_or_b32 v57, v57, s4, 50
	v_max_f32_e32 v54, v53, v55
	v_min_f32_e32 v53, v53, v55
	v_max_f32_e32 v55, v32, v51
	v_max_f32_e32 v36, v34, v15
	v_min_f32_e32 v15, v34, v15
	v_max_f32_e32 v34, v38, v38
	v_min_f32_e32 v32, v32, v51
	v_max_f32_e32 v51, v55, v53
	v_min_f32_e32 v53, v55, v53
	v_max_f32_e32 v55, v21, v25
	v_min_f32_e32 v21, v21, v25
	v_max_f32_e32 v25, v57, v57
	v_max_f32_e32 v38, v34, v19
	v_min_f32_e32 v19, v34, v19
	v_max_f32_e32 v57, v56, v25
	v_min_f32_e32 v25, v56, v25
	v_max_f32_e32 v34, v36, v38
	v_min_f32_e32 v36, v36, v38
	v_max_f32_e32 v38, v15, v19
	v_max_f32_e32 v56, v55, v57
	v_min_f32_e32 v55, v55, v57
	v_max_f32_e32 v57, v21, v25
	v_min_f32_e32 v15, v15, v19
	v_max_f32_e32 v19, v38, v36
	v_min_f32_e32 v36, v38, v36
	v_min_f32_e32 v21, v21, v25
	v_max_f32_e32 v25, v57, v55
	v_min_f32_e32 v55, v57, v55
	v_max_f32_e32 v38, v13, v34
	v_min_f32_e32 v13, v13, v34
	v_max_f32_e32 v34, v11, v36
	v_max_f32_e32 v57, v54, v56
	v_min_f32_e32 v54, v54, v56
	v_max_f32_e32 v56, v53, v55
	v_min_f32_e32 v11, v11, v36
	v_max_f32_e32 v36, v34, v13
	v_min_f32_e32 v13, v34, v13
	v_max_f32_e32 v34, v10, v19
	v_min_f32_e32 v10, v10, v19
	v_max_f32_e32 v19, v5, v15
	v_min_f32_e32 v53, v53, v55
	v_max_f32_e32 v55, v56, v54
	v_min_f32_e32 v54, v56, v54
	v_max_f32_e32 v56, v51, v25
	v_min_f32_e32 v25, v51, v25
	v_max_f32_e32 v51, v32, v21
	v_min_f32_e32 v5, v5, v15
	v_max_f32_e32 v15, v19, v10
	v_min_f32_e32 v21, v32, v21
	v_max_f32_e32 v32, v51, v25
	v_min_f32_e32 v10, v19, v10
	v_max_f32_e32 v19, v34, v36
	v_min_f32_e32 v34, v34, v36
	v_max_f32_e32 v36, v15, v13
	v_min_f32_e32 v13, v15, v13
	v_min_f32_e32 v25, v51, v25
	v_max_f32_e32 v51, v56, v55
	v_min_f32_e32 v55, v56, v55
	v_max_f32_e32 v56, v32, v54
	v_min_f32_e32 v32, v32, v54
	v_max_f32_e32 v15, v10, v11
	v_min_f32_e32 v10, v10, v11
	v_min_f32_e32 v11, v40, v38
	v_max_f32_e32 v41, v4, v13
	v_max_f32_e32 v54, v25, v53
	v_min_f32_e32 v25, v25, v53
	v_min_f32_e32 v53, v58, v57
	v_max_f32_e32 v59, v30, v32
	v_min_f32_e32 v4, v4, v13
	v_max_f32_e32 v13, v41, v11
	v_min_f32_e32 v11, v41, v11
	v_max_f32_e32 v41, v8, v34
	v_min_f32_e32 v8, v8, v34
	v_max_f32_e32 v34, v3, v10
	v_min_f32_e32 v30, v30, v32
	v_max_f32_e32 v32, v59, v53
	v_min_f32_e32 v53, v59, v53
	v_max_f32_e32 v59, v50, v55
	v_min_f32_e32 v50, v50, v55
	v_max_f32_e32 v55, v24, v25
	v_min_f32_e32 v3, v3, v10
	v_max_f32_e32 v10, v34, v8
	v_min_f32_e32 v8, v34, v8
	v_min_f32_e32 v24, v24, v25
	v_max_f32_e32 v25, v55, v50
	v_min_f32_e32 v50, v55, v50
	v_max_f32_e32 v34, v41, v13
	v_min_f32_e32 v13, v41, v13
	v_max_f32_e32 v41, v10, v11
	v_min_f32_e32 v10, v10, v11
	v_max_f32_e32 v11, v8, v4
	v_min_f32_e32 v4, v8, v4
	v_max_f32_e32 v8, v7, v19
	v_min_f32_e32 v7, v7, v19
	v_max_f32_e32 v19, v6, v15
	v_max_f32_e32 v55, v59, v32
	v_min_f32_e32 v32, v59, v32
	v_max_f32_e32 v59, v25, v53
	v_min_f32_e32 v25, v25, v53
	v_max_f32_e32 v53, v50, v30
	v_min_f32_e32 v30, v50, v30
	v_max_f32_e32 v50, v49, v51
	v_min_f32_e32 v49, v49, v51
	v_max_f32_e32 v51, v48, v54
	v_min_f32_e32 v6, v6, v15
	v_max_f32_e32 v15, v19, v7
	v_min_f32_e32 v7, v19, v7
	v_max_f32_e32 v19, v9, v36
	v_min_f32_e32 v9, v9, v36
	v_max_f32_e32 v36, v2, v5
	v_min_f32_e32 v48, v48, v54
	v_max_f32_e32 v54, v51, v49
	v_min_f32_e32 v49, v51, v49
	v_max_f32_e32 v51, v52, v56
	v_min_f32_e32 v52, v52, v56
	v_max_f32_e32 v56, v23, v21
	v_min_f32_e32 v2, v2, v5
	v_max_f32_e32 v5, v36, v9
	v_min_f32_e32 v9, v36, v9
	v_max_f32_e32 v36, v19, v15
	v_min_f32_e32 v21, v23, v21
	v_max_f32_e32 v23, v56, v52
	v_min_f32_e32 v52, v56, v52
	v_and_b32_e32 v20, 0xffffff80, v72
	v_min_f32_e32 v15, v19, v15
	v_max_f32_e32 v19, v5, v7
	v_min_f32_e32 v5, v5, v7
	v_max_f32_e32 v7, v9, v6
	v_min_f32_e32 v6, v9, v6
	v_min_f32_e32 v9, v8, v34
	v_min_f32_e32 v42, v36, v13
	v_max_f32_e32 v56, v51, v54
	v_min_f32_e32 v51, v51, v54
	v_max_f32_e32 v54, v23, v49
	v_min_f32_e32 v23, v23, v49
	v_max_f32_e32 v49, v52, v48
	v_min_f32_e32 v48, v52, v48
	v_and_b32_e32 v39, 0xffffff80, v65
	v_min_f32_e32 v65, v48, v24
	v_max3_f32 v9, v9, v48, v24
	v_max3_f32 v24, v42, v49, v30
	v_add_f32_e32 v27, v27, v28
	v_add_f32_e32 v28, v20, v17
	v_add_f32_e32 v42, v20, v18
	v_add_f32_e32 v20, v20, v26
	v_and_b32_e32 v22, 0xffffff80, v73
	v_and_or_b32 v27, v27, s4, 51
	v_and_or_b32 v28, v28, s4, 64
	v_and_b32_e32 v42, 0xffffff00, v42
	v_and_b32_e32 v20, 0xffffff00, v20
	v_and_b32_e32 v29, 0xffffff80, v74
	v_and_b32_e32 v31, 0xffffff80, v75
	v_and_b32_e32 v33, 0xffffff80, v70
	v_and_b32_e32 v35, 0xffffff80, v71
	v_and_b32_e32 v37, 0xffffff80, v64
;     __device__ __forceinline__ void fused(f32x4 (&acc)[2][2][4][2], const Unit& u, int wr, int wc, int fr, int fq, PG8_LAS unsigned char* lds, int wid, int lane) const {
;     ...
;             { float cv[16]; cv[0] = __uint_as_float((__float_as_uint(v0[0] + v1[0]) & ~255u) | 0u); cv[1] = __uint_as_float((__float_as_uint(v0[0] + v1[1]) & ~255u) | 1u); cv[2] = __uint_as_float((__float_as_uint(v0[0] + v1[2]) & ~255u) | 2u); cv[3] = __uint_as_float((__float_as_uint(v0[0] + v1[3]) & ~255u) | 3u); cv[4] = __uint_as_float((__float_as_uint(v0[0] + v1[4]) & ~255u) | 4u); cv[5] = __uint_as_float((__float_as_uint(v0[0] + v1[5]) & ~255u) | 5u); cv[6] = __uint_as_float((__float_as_uint(v0[0] + v1[6]) & ~255u) | 6u); cv[7] = __uint_as_float((__float_as_uint(v0[0] + v1[7]) & ~255u) | 7u); cv[8] = __uint_as_float((__float_as_uint(v0[0] + v1[8]) & ~255u) | 8u); cv[9] = __uint_as_float((__float_as_uint(v0[0] + v1[9]) & ~255u) | 9u); cv[10] = __uint_as_float((__float_as_uint(v0[0] + v1[10]) & ~255u) | 10u); cv[11] = __uint_as_float((__float_as_uint(v0[0] + v1[11]) & ~255u) | 11u); cv[12] = __uint_as_float((__float_as_uint(v0[0] + v1[12]) & ~255u) | 12u); cv[13] = __uint_as_float((__float_as_uint(v0[0] + v1[13]) & ~255u) | 13u); cv[14] = __uint_as_float((__float_as_uint(v0[0] + v1[14]) & ~255u) | 14u); cv[15] = __uint_as_float((__float_as_uint(v0[0] + v1[15]) & ~255u) | 15u); sort16_desc(cv);
; #pragma unroll
;               for (int q = 0; q < 16; ++q) best[q] = cv[q]; }
	v_min_f32_e32 v43, v15, v41
	v_min_f32_e32 v44, v19, v10
	v_min_f32_e32 v62, v54, v25
	v_or_b32_e32 v42, 0x41, v42
	v_or_b32_e32 v20, 0x42, v20
	v_add_f32_e32 v26, v22, v17
	v_add_f32_e32 v22, v22, v18
	v_min_f32_e32 v63, v23, v53
	v_max3_f32 v23, v43, v23, v53
	v_max3_f32 v10, v19, v10, v62
	v_max3_f32 v19, v44, v54, v25
	v_and_b32_e32 v26, 0xffffff00, v26
	v_and_b32_e32 v22, 0xffffff00, v22
	v_add_f32_e32 v43, v29, v17
	v_add_f32_e32 v29, v29, v18
	v_add_f32_e32 v44, v31, v17
	v_add_f32_e32 v18, v31, v18
	v_add_f32_e32 v31, v33, v17
	v_add_f32_e32 v33, v35, v17
	v_add_f32_e32 v35, v37, v17
	v_add_f32_e32 v37, v39, v17
	v_max_f32_e32 v39, v27, v28
	v_min_f32_e32 v27, v27, v28
	v_max_f32_e32 v28, v42, v42
	v_or_b32_e32 v26, 0x50, v26
	v_or_b32_e32 v22, 0x51, v22
	v_and_b32_e32 v43, 0xffffff00, v43
	v_and_b32_e32 v29, 0xffffff00, v29
	v_max_f32_e32 v42, v28, v20
	v_min_f32_e32 v20, v28, v20
	v_or_b32_e32 v43, 0x60, v43
	v_or_b32_e32 v29, 0x61, v29
	v_max_f32_e32 v28, v39, v42
	v_min_f32_e32 v39, v39, v42
	v_max_f32_e32 v42, v27, v20
	v_min_f32_e32 v20, v27, v20
	v_max_f32_e32 v27, v42, v39
	v_min_f32_e32 v39, v42, v39
	v_max_f32_e32 v42, v26, v22
	v_min_f32_e32 v22, v26, v22
	v_max_f32_e32 v26, v29, v29
	v_max_f32_e32 v29, v43, v43
	v_max_f32_e32 v43, v29, v26
	v_min_f32_e32 v26, v29, v26
	v_max_f32_e32 v29, v42, v43
	v_min_f32_e32 v42, v42, v43
	v_max_f32_e32 v43, v22, v26
	v_and_b32_e32 v12, 0xffffff80, v68
	v_and_b32_e32 v14, 0xffffff80, v69
	v_min_f32_e32 v22, v22, v26
	v_max_f32_e32 v26, v43, v42
	v_min_f32_e32 v42, v43, v42
	v_add_f32_e32 v12, v12, v17
	v_add_f32_e32 v14, v14, v17
	v_max_f32_e32 v43, v28, v29
	v_min_f32_e32 v28, v28, v29
	v_max_f32_e32 v29, v39, v42
	v_and_b32_e32 v44, 0xffffff00, v44
	v_and_b32_e32 v18, 0xffffff00, v18
	v_and_b32_e32 v12, 0xffffff00, v12
	v_and_b32_e32 v14, 0xffffff00, v14
	v_min_f32_e32 v39, v39, v42
	v_max_f32_e32 v42, v29, v28
	v_min_f32_e32 v28, v29, v28
	v_max_f32_e32 v29, v27, v26
	v_min_f32_e32 v26, v27, v26
	v_max_f32_e32 v27, v20, v22
	v_or_b32_e32 v44, 0x70, v44
	v_or_b32_e32 v18, 0x71, v18
	v_or_b32_e32 v12, 0x80, v12
	v_or_b32_e32 v14, 0x90, v14
	v_min_f32_e32 v20, v20, v22
	v_max_f32_e32 v22, v27, v26
	v_min_f32_e32 v26, v27, v26
	v_and_b32_e32 v31, 0xffffff00, v31
	v_and_b32_e32 v33, 0xffffff00, v33
	v_max_f32_e32 v27, v29, v42
	v_min_f32_e32 v29, v29, v42
	v_max_f32_e32 v42, v22, v28
	v_min_f32_e32 v22, v22, v28
	v_max_f32_e32 v28, v26, v39
	v_min_f32_e32 v26, v26, v39
	v_max_f32_e32 v39, v44, v44
	v_or_b32_e32 v31, 0xa0, v31
	v_or_b32_e32 v33, 0xb0, v33
	v_and_b32_e32 v35, 0xffffff00, v35
	v_and_b32_e32 v37, 0xffffff00, v37
	v_max_f32_e32 v44, v39, v18
	v_min_f32_e32 v18, v39, v18
	v_max_f32_e32 v39, v12, v14
	v_min_f32_e32 v12, v12, v14
	v_or_b32_e32 v35, 0xc0, v35
	v_or_b32_e32 v37, 0xd0, v37
	v_max_f32_e32 v14, v44, v39
	v_min_f32_e32 v39, v44, v39
	v_max_f32_e32 v44, v18, v12
	v_min_f32_e32 v12, v18, v12
	v_max_f32_e32 v18, v44, v39
	v_min_f32_e32 v39, v44, v39
	v_max_f32_e32 v44, v31, v33
	v_min_f32_e32 v31, v31, v33
	v_max_f32_e32 v33, v37, v37
	v_max_f32_e32 v37, v35, v33
	v_min_f32_e32 v33, v35, v33
	v_max_f32_e32 v35, v44, v37
	v_min_f32_e32 v37, v44, v37
	v_max_f32_e32 v44, v31, v33
	v_min_f32_e32 v31, v31, v33
	v_max_f32_e32 v33, v44, v37
	v_min_f32_e32 v37, v44, v37
	v_max_f32_e32 v44, v14, v35
	v_min_f32_e32 v14, v14, v35
	v_max_f32_e32 v35, v39, v37
	v_min_f32_e32 v37, v39, v37
	v_max_f32_e32 v39, v35, v14
	v_min_f32_e32 v14, v35, v14
	v_max_f32_e32 v35, v18, v33
	v_min_f32_e32 v18, v18, v33
	v_max_f32_e32 v33, v12, v31
	v_min_f32_e32 v12, v12, v31
	v_max_f32_e32 v31, v33, v18
	v_min_f32_e32 v45, v5, v11
	v_min_f32_e32 v61, v51, v59
	v_min_f32_e32 v18, v33, v18
	v_max_f32_e32 v33, v35, v39
	v_min_f32_e32 v35, v35, v39
	v_max_f32_e32 v39, v31, v14
	v_min_f32_e32 v14, v31, v14
	v_max3_f32 v5, v5, v11, v61
	v_max3_f32 v11, v45, v51, v59
	v_max_f32_e32 v31, v18, v37
	v_min_f32_e32 v18, v18, v37
	v_min_f32_e32 v37, v43, v44
	v_max_f32_e32 v45, v22, v14
	v_min_f32_e32 v14, v22, v14
	v_max_f32_e32 v22, v45, v37
	v_min_f32_e32 v37, v45, v37
	v_max_f32_e32 v45, v29, v35
	v_min_f32_e32 v29, v29, v35
	v_max_f32_e32 v35, v26, v18
	v_min_f32_e32 v46, v7, v4
	v_min_f32_e32 v47, v6, v3
	v_min_f32_e32 v52, v50, v55
	v_min_f32_e32 v60, v56, v32
	v_min_f32_e32 v64, v49, v30
	v_min_f32_e32 v18, v26, v18
	v_max_f32_e32 v26, v35, v29
	v_min_f32_e32 v29, v35, v29
	v_max3_f32 v21, v40, v38, v21
	v_max3_f32 v8, v8, v34, v65
	v_max3_f32 v13, v36, v13, v64
	v_max3_f32 v15, v15, v41, v63
	v_max3_f32 v4, v7, v4, v60
	v_max3_f32 v7, v46, v56, v32
	v_max3_f32 v3, v6, v3, v52
	v_max3_f32 v6, v47, v50, v55
	v_max3_f32 v2, v2, v58, v57
	v_max_f32_e32 v35, v45, v22
	v_min_f32_e32 v22, v45, v22
	v_max_f32_e32 v45, v26, v37
	v_min_f32_e32 v26, v26, v37
	v_max_f32_e32 v37, v29, v14
	v_min_f32_e32 v14, v29, v14
	v_max_f32_e32 v29, v27, v33
	v_min_f32_e32 v27, v27, v33
	v_max_f32_e32 v33, v28, v31
	v_max_f32_e32 v25, v21, v19
	v_min_f32_e32 v19, v21, v19
	v_max_f32_e32 v21, v8, v5
	v_min_f32_e32 v5, v8, v5
	v_max_f32_e32 v8, v9, v11
	v_min_f32_e32 v9, v9, v11
	v_max_f32_e32 v11, v13, v4
	v_min_f32_e32 v4, v13, v4
	v_max_f32_e32 v13, v24, v7
	v_min_f32_e32 v7, v24, v7
	v_max_f32_e32 v24, v15, v3
	v_min_f32_e32 v3, v15, v3
	v_max_f32_e32 v15, v23, v6
	v_min_f32_e32 v6, v23, v6
	v_max_f32_e32 v23, v10, v2
	v_min_f32_e32 v2, v10, v2
	v_min_f32_e32 v28, v28, v31
	v_max_f32_e32 v31, v33, v27
	v_min_f32_e32 v27, v33, v27
	v_max_f32_e32 v33, v42, v39
	v_min_f32_e32 v39, v42, v39
	v_max_f32_e32 v42, v20, v12
	v_max_f32_e32 v10, v25, v13
	v_min_f32_e32 v13, v25, v13
	v_max_f32_e32 v25, v21, v24
	v_min_f32_e32 v21, v21, v24
; #define CE(a, b) do { const float hi_ = fmaxf(a, b), lo_ = fminf(a, b); a = hi_; b = lo_; } while (0)
; __device__ __forceinline__ void merge_top16(float (&v)[16], const float (&nw)[16]) {
;     v[0] = fmaxf(v[0], nw[15]); v[1] = fmaxf(v[1], nw[14]); v[2] = fmaxf(v[2], nw[13]); v[3] = fmaxf(v[3], nw[12]); v[4] = fmaxf(v[4], nw[11]); v[5] = fmaxf(v[5], nw[10]); v[6] = fmaxf(v[6], nw[9]); v[7] = fmaxf(v[7], nw[8]); v[8] = fmaxf(v[8], nw[7]); v[9] = fmaxf(v[9], nw[6]); v[10] = fmaxf(v[10], nw[5]); v[11] = fmaxf(v[11], nw[4]); v[12] = fmaxf(v[12], nw[3]); v[13] = fmaxf(v[13], nw[2]); v[14] = fmaxf(v[14], nw[1]); v[15] = fmaxf(v[15], nw[0]);
;     CE(v[0], v[8]); CE(v[1], v[9]); CE(v[2], v[10]); CE(v[3], v[11]);
;     CE(v[4], v[12]); CE(v[5], v[13]); CE(v[6], v[14]); CE(v[7], v[15]);
;     CE(v[0], v[4]); CE(v[1], v[5]); CE(v[2], v[6]); CE(v[3], v[7]);
;     CE(v[8], v[12]); CE(v[9], v[13]); CE(v[10], v[14]); CE(v[11], v[15]);
;     CE(v[0], v[2]); CE(v[1], v[3]); CE(v[4], v[6]); CE(v[5], v[7]);
;     CE(v[8], v[10]); CE(v[9], v[11]); CE(v[12], v[14]); CE(v[13], v[15]);
;     CE(v[0], v[1]); CE(v[2], v[3]); CE(v[4], v[5]); CE(v[6], v[7]);
;     CE(v[8], v[9]); CE(v[10], v[11]); CE(v[12], v[13]); CE(v[14], v[15]);
; }
;     __device__ __forceinline__ void fused(f32x4 (&acc)[2][2][4][2], const Unit& u, int wr, int wc, int fr, int fq, PG8_LAS unsigned char* lds, int wid, int lane) const {
;     ...
;             { float cv[16]; cv[0] = __uint_as_float((__float_as_uint(v0[14] + v1[0]) & ~255u) | 224u); cv[1] = __uint_as_float((__float_as_uint(v0[15] + v1[0]) & ~255u) | 240u); cv[2] = -INFINITY; cv[3] = -INFINITY; cv[4] = -INFINITY; cv[5] = -INFINITY; cv[6] = -INFINITY; cv[7] = -INFINITY; cv[8] = -INFINITY; cv[9] = -INFINITY; cv[10] = -INFINITY; cv[11] = -INFINITY; cv[12] = -INFINITY; cv[13] = -INFINITY; cv[14] = -INFINITY; cv[15] = -INFINITY; sort16_desc(cv); merge_top16(best, cv); }
;             float sc[16], sum = 0.f;
; #pragma unroll
;             for (int q = 0; q < 16; ++q) { sc[q] = __uint_as_float(__float_as_uint(best[q]) & ~255u); }
;             const float smax = sc[0];
; #pragma unroll
;             for (int q = 0; q < 16; ++q) { sc[q] = __builtin_amdgcn_exp2f((sc[q] - smax) * 1.4426950408889634f); }
	v_max_f32_e32 v24, v8, v15
	v_min_f32_e32 v8, v8, v15
	v_max_f32_e32 v15, v11, v23
	v_min_f32_e32 v11, v11, v23
	v_max_f32_e32 v23, v19, v7
	v_min_f32_e32 v7, v19, v7
	v_max_f32_e32 v19, v5, v3
	v_min_f32_e32 v3, v5, v3
	v_max_f32_e32 v5, v9, v6
	v_min_f32_e32 v6, v9, v6
	v_max_f32_e32 v9, v4, v2
	v_min_f32_e32 v2, v4, v2
	v_min_f32_e32 v12, v20, v12
	v_max_f32_e32 v20, v42, v39
	v_min_f32_e32 v39, v42, v39
	v_and_b32_e32 v1, 0xffffff80, v66
	v_and_b32_e32 v0, 0xffffff80, v67
	v_max_f32_e32 v4, v10, v24
	v_min_f32_e32 v10, v10, v24
	v_max_f32_e32 v24, v25, v15
	v_min_f32_e32 v15, v25, v15
	v_max_f32_e32 v25, v13, v8
	v_min_f32_e32 v8, v13, v8
	v_max_f32_e32 v13, v21, v11
	v_min_f32_e32 v11, v21, v11
	v_max_f32_e32 v21, v23, v5
	v_min_f32_e32 v5, v23, v5
	v_max_f32_e32 v23, v19, v9
	v_min_f32_e32 v9, v19, v9
	v_max_f32_e32 v19, v7, v6
	v_min_f32_e32 v6, v7, v6
	v_max_f32_e32 v7, v3, v2
	v_min_f32_e32 v2, v3, v2
	v_max_f32_e32 v42, v33, v31
	v_min_f32_e32 v31, v33, v31
	v_max_f32_e32 v33, v20, v27
	v_min_f32_e32 v20, v20, v27
	v_max_f32_e32 v27, v39, v28
	v_min_f32_e32 v28, v39, v28
	v_min_f32_e32 v3, v4, v24
	v_min_f32_e32 v30, v10, v15
	v_min_f32_e32 v32, v25, v13
	v_min_f32_e32 v34, v8, v11
	v_min_f32_e32 v36, v21, v23
	v_min_f32_e32 v38, v5, v9
	v_min_f32_e32 v40, v19, v7
	v_min_f32_e32 v41, v6, v2
	v_max_f32_e32 v39, v29, v35
	v_min_f32_e32 v29, v29, v35
	v_max_f32_e32 v35, v42, v22
	v_min_f32_e32 v22, v42, v22
	v_max_f32_e32 v42, v31, v45
	v_min_f32_e32 v31, v31, v45
	v_max_f32_e32 v45, v33, v26
	v_min_f32_e32 v26, v33, v26
	v_max_f32_e32 v33, v20, v37
	v_min_f32_e32 v20, v20, v37
	v_max_f32_e32 v37, v27, v14
	v_min_f32_e32 v14, v27, v14
	v_max_f32_e32 v27, v28, v18
	v_min_f32_e32 v18, v28, v18
	v_add_f32_e32 v1, v1, v17
	v_add_f32_e32 v0, v0, v17
	v_max3_f32 v4, v4, v24, v12
	v_max_f32_e32 v3, v3, v18
	v_max3_f32 v10, v10, v15, v27
	v_max_f32_e32 v12, v30, v14
	v_max3_f32 v13, v25, v13, v37
	v_max_f32_e32 v14, v32, v20
	v_max3_f32 v8, v8, v11, v33
	v_max_f32_e32 v11, v34, v26
	v_max3_f32 v15, v21, v23, v45
	v_max_f32_e32 v18, v36, v31
	v_max3_f32 v5, v5, v9, v42
	v_max_f32_e32 v9, v38, v22
	v_max3_f32 v7, v19, v7, v35
	v_max_f32_e32 v19, v40, v29
	v_max3_f32 v2, v6, v2, v39
	v_max3_f32 v6, v41, v43, v44
	v_and_b32_e32 v1, 0xffffff00, v1
	v_and_b32_e32 v0, 0xffffff00, v0
	v_max_f32_e32 v20, v4, v15
	v_min_f32_e32 v4, v4, v15
	v_max_f32_e32 v15, v3, v18
	v_min_f32_e32 v3, v3, v18
	v_max_f32_e32 v18, v10, v5
	v_min_f32_e32 v5, v10, v5
	v_max_f32_e32 v10, v12, v9
	v_min_f32_e32 v9, v12, v9
	v_max_f32_e32 v12, v13, v7
	v_min_f32_e32 v7, v13, v7
	v_max_f32_e32 v13, v14, v19
	v_min_f32_e32 v14, v14, v19
	v_max_f32_e32 v19, v8, v2
	v_min_f32_e32 v2, v8, v2
	v_max_f32_e32 v8, v11, v6
	v_min_f32_e32 v6, v11, v6
	v_or_b32_e32 v1, 0xe0, v1
	v_or_b32_e32 v0, 0xf0, v0
	v_max_f32_e32 v11, v20, v12
	v_min_f32_e32 v12, v20, v12
	v_max_f32_e32 v20, v15, v13
	v_min_f32_e32 v13, v15, v13
	v_max_f32_e32 v15, v18, v19
	v_min_f32_e32 v18, v18, v19
	v_max_f32_e32 v19, v10, v8
	v_min_f32_e32 v8, v10, v8
	v_max_f32_e32 v10, v4, v7
	v_min_f32_e32 v4, v4, v7
	v_max_f32_e32 v7, v3, v14
	v_min_f32_e32 v3, v3, v14
	v_max_f32_e32 v14, v5, v2
	v_min_f32_e32 v2, v5, v2
	v_max_f32_e32 v5, v9, v6
	v_min_f32_e32 v6, v9, v6
	v_max_f32_e32 v9, v11, v15
	v_min_f32_e32 v11, v11, v15
	v_max_f32_e32 v15, v20, v19
	v_min_f32_e32 v19, v20, v19
	v_max_f32_e32 v20, v12, v18
	v_min_f32_e32 v12, v12, v18
	v_max_f32_e32 v18, v13, v8
	v_min_f32_e32 v8, v13, v8
	v_max_f32_e32 v13, v10, v14
	v_min_f32_e32 v10, v10, v14
	v_max_f32_e32 v14, v7, v5
	v_min_f32_e32 v5, v7, v5
	v_max_f32_e32 v7, v4, v2
	v_min_f32_e32 v2, v4, v2
	v_max_f32_e32 v4, v3, v6
	v_min_f32_e32 v3, v3, v6
	v_max_f32_e32 v17, v1, v0
	v_min_f32_e32 v0, v1, v0
	v_min_f32_e32 v6, v9, v15
	v_min_f32_e32 v21, v11, v19
	v_min_f32_e32 v22, v20, v18
	v_min_f32_e32 v23, v12, v8
	v_min_f32_e32 v24, v13, v14
	v_min_f32_e32 v25, v10, v5
	v_min_f32_e32 v26, v7, v4
	v_min_f32_e32 v27, v2, v3
	s_mov_b32 s4, 0xff800000
	v_max_f32_e32 v0, 0xff800000, v0
	v_max3_f32 v1, v9, v15, s4
	v_max_f32_e32 v6, 0xff800000, v6
	v_max3_f32 v9, v11, v19, s4
	v_max_f32_e32 v11, 0xff800000, v21
	v_max3_f32 v15, v20, v18, s4
	v_max_f32_e32 v18, 0xff800000, v22
	v_max3_f32 v8, v12, v8, s4
	v_max_f32_e32 v12, 0xff800000, v23
	v_max3_f32 v13, v13, v14, s4
	v_max_f32_e32 v14, 0xff800000, v24
	v_max3_f32 v5, v10, v5, s4
	v_max_f32_e32 v10, 0xff800000, v25
	v_max3_f32 v4, v7, v4, s4
	v_max_f32_e32 v7, 0xff800000, v26
	v_max3_f32 v0, v2, v3, v0
	v_max3_f32 v2, v27, v17, s4
	v_max_f32_e32 v3, v1, v13
	v_min_f32_e32 v1, v1, v13
	v_max_f32_e32 v13, v6, v14
	v_min_f32_e32 v6, v6, v14
	v_max_f32_e32 v14, v9, v5
	v_min_f32_e32 v5, v9, v5
	v_max_f32_e32 v9, v11, v10
	v_min_f32_e32 v10, v11, v10
	v_max_f32_e32 v11, v15, v4
	v_min_f32_e32 v4, v15, v4
	v_max_f32_e32 v15, v18, v7
	v_max_f32_e32 v17, v8, v0
	v_min_f32_e32 v0, v8, v0
	v_max_f32_e32 v8, v12, v2
	v_min_f32_e32 v2, v12, v2
	v_max_f32_e32 v12, v3, v11
	v_min_f32_e32 v3, v3, v11
	v_max_f32_e32 v11, v13, v15
	v_min_f32_e32 v13, v13, v15
	v_max_f32_e32 v15, v14, v17
	v_min_f32_e32 v14, v14, v17
	v_max_f32_e32 v17, v9, v8
	v_min_f32_e32 v8, v9, v8
	v_max_f32_e32 v9, v1, v4
	v_min_f32_e32 v24, v1, v4
	v_max_f32_e32 v27, v5, v0
	v_min_f32_e32 v28, v5, v0
	v_max_f32_e32 v29, v10, v2
	v_min_f32_e32 v30, v10, v2
	v_max_f32_e32 v0, v12, v15
	v_min_f32_e32 v1, v12, v15
	v_max_f32_e32 v2, v11, v17
	v_min_f32_e32 v4, v11, v17
	v_min_f32_e32 v7, v18, v7
	v_max_f32_e32 v33, v0, v2
	v_min_f32_e32 v34, v0, v2
	v_min_f32_e32 v36, v1, v4
	v_max_f32_e32 v25, v6, v7
	v_min_f32_e32 v26, v6, v7
	v_max_f32_e32 v35, v1, v4
	v_lshrrev_b32_e32 v0, 2, v33
	v_lshrrev_b32_e32 v2, 2, v34
	v_lshrrev_b32_e32 v6, 2, v36
	v_max_f32_e32 v17, v3, v14
	v_min_f32_e32 v31, v3, v14
	v_and_b32_e32 v0, 60, v0
	v_and_b32_e32 v1, 15, v33
	v_and_b32_e32 v2, 60, v2
	v_and_b32_e32 v3, 15, v34
	v_lshrrev_b32_e32 v4, 2, v35
	v_and_b32_e32 v5, 15, v35
	v_and_b32_e32 v6, 60, v6
	v_and_b32_e32 v7, 15, v36
	s_waitcnt lgkmcnt(0)
; #define RT_PK(q_) (ex[q_] | (int)((__float_as_uint(usc[ex[q_]]) >> 23) << 14))
;     __device__ __forceinline__ void fused(f32x4 (&acc)[2][2][4][2], const Unit& u, int wr, int wc, int fr, int fq, PG8_LAS unsigned char* lds, int wid, int lane) const {
;     ...
;             for (int q = 0; q < 16; ++q) { sc[q] = __uint_as_float(__float_as_uint(best[q]) & ~255u); }
;             const float smax = sc[0];
; #pragma unroll
;             for (int q = 0; q < 16; ++q) { sc[q] = __builtin_amdgcn_exp2f((sc[q] - smax) * 1.4426950408889634f); }
; #pragma unroll
;             for (int q = 0; q < 16; ++q) sum += sc[q];
;             const float rs = 1.0f / sum;
;             asm volatile("s_waitcnt lgkmcnt(0)" ::: "memory");
;             int ex[16];
; #pragma unroll
;             for (int q = 0; q < 16; ++q) { const unsigned cid = __float_as_uint(best[q]) & 255u; ex[q] = idxl[cid >> 4] * 128 + idxl[16 + (cid & 15u)]; }
;             const size_t o = ((size_t)u.pn * 16384 + (size_t)(u.pm * BM + row)) * 16;
;             typedef int i32x4 __attribute__((ext_vector_type(4)));
; #pragma unroll
;             for (int i = 0; i < 4; ++i) {
;     ...
;                 *(i32x4*)(eidx + o + 4 * i) = (i32x4){RT_PK(4 * i), RT_PK(4 * i + 1), RT_PK(4 * i + 2), RT_PK(4 * i + 3)};
;                 *(f32x4*)(egate + o + 4 * i) = (f32x4){sc[4 * i] * rs * vsc[ex[4 * i]], sc[4 * i + 1] * rs * vsc[ex[4 * i + 1]], sc[4 * i + 2] * rs * vsc[ex[4 * i + 2]], sc[4 * i + 3] * rs * vsc[ex[4 * i + 3]]};
	v_add_u32_e32 v0, v16, v0
	v_lshl_add_u32 v1, v1, 2, v16
	v_add_u32_e32 v2, v16, v2
	v_lshl_add_u32 v3, v3, 2, v16
	v_and_b32_e32 v4, 60, v4
	v_lshl_add_u32 v5, v5, 2, v16
	v_add_u32_e32 v6, v16, v6
	v_lshl_add_u32 v7, v7, 2, v16
	v_add_u32_e32 v4, v16, v4
	ds_read_b32 v0, v0
	ds_read_b32 v1, v1 offset:64
	ds_read_b32 v2, v2
	ds_read_b32 v3, v3 offset:64
	ds_read_b32 v10, v4
	ds_read_b32 v5, v5 offset:64
	ds_read_b32 v6, v6
	ds_read_b32 v7, v7 offset:64
	s_waitcnt lgkmcnt(0)
	v_lshl_add_u32 v0, v0, 7, v1
	v_ashrrev_i32_e32 v1, 31, v0
	v_lshl_add_u32 v4, v2, 7, v3
	v_lshlrev_b64 v[14:15], 3, v[0:1]
	v_lshl_add_u32 v10, v10, 7, v5
	v_lshl_add_u32 v12, v6, 7, v7
	v_lshl_add_u64 v[2:3], s[8:9], 0, v[14:15]
	v_ashrrev_i32_e32 v5, 31, v4
	v_max_f32_e32 v32, v13, v8
	v_min_f32_e32 v8, v13, v8
	v_mov_b32_e32 v243, 0x18000
	v_lshl_add_u32 v242, v0, 1, v243
	ds_read_u16 v170, v242
	v_lshlrev_b64 v[18:19], 3, v[4:5]
	v_ashrrev_i32_e32 v11, 31, v10
	v_ashrrev_i32_e32 v13, 31, v12
	v_lshl_add_u64 v[2:3], s[8:9], 0, v[18:19]
	v_lshlrev_b64 v[20:21], 3, v[10:11]
	v_lshlrev_b64 v[22:23], 3, v[12:13]
	v_lshl_add_u64 v[6:7], s[8:9], 0, v[20:21]
	v_lshl_add_u32 v242, v4, 1, v243
	ds_read_u16 v172, v242
	v_lshl_add_u32 v242, v10, 1, v243
	ds_read_u16 v174, v242
	v_lshl_add_u64 v[2:3], s[8:9], 0, v[22:23]
	v_lshl_add_u32 v242, v12, 1, v243
	ds_read_u16 v176, v242
	v_min_f32_e32 v2, v9, v27
	v_min_f32_e32 v6, v25, v29
	v_max_f32_e32 v43, v2, v6
	v_min_f32_e32 v44, v2, v6
	v_and_b32_e32 v2, 0xffffff00, v34
	v_and_b32_e32 v51, 0xffffff00, v33
	v_max_f32_e32 v37, v9, v27
	v_max_f32_e32 v3, v25, v29
	v_sub_f32_e32 v2, v2, v51
	v_min_f32_e32 v9, v24, v28
	v_min_f32_e32 v25, v26, v30
	v_max_f32_e32 v41, v37, v3
	v_min_f32_e32 v42, v37, v3
	v_and_b32_e32 v3, 0xffffff00, v35
	v_mul_f32_e32 v2, 0x3fb8aa3b, v2
	v_max_f32_e32 v47, v9, v25
	v_min_f32_e32 v48, v9, v25
	v_exp_f32_e32 v25, v2
	v_sub_f32_e32 v2, v3, v51
	v_and_b32_e32 v6, 0xffffff00, v36
	v_mul_f32_e32 v2, 0x3fb8aa3b, v2
	v_max_f32_e32 v7, v24, v28
	v_max_f32_e32 v24, v26, v30
	v_max_f32_e32 v38, v17, v32
	v_exp_f32_e32 v26, v2
	v_sub_f32_e32 v2, v6, v51
	v_max_f32_e32 v45, v7, v24
	v_min_f32_e32 v46, v7, v24
	v_and_b32_e32 v7, 0xffffff00, v38
	v_mul_f32_e32 v2, 0x3fb8aa3b, v2
	v_min_f32_e32 v17, v17, v32
	v_exp_f32_e32 v27, v2
	v_sub_f32_e32 v2, v7, v51
	v_max_f32_e32 v39, v31, v8
	v_min_f32_e32 v40, v31, v8
	v_and_b32_e32 v8, 0xffffff00, v17
	v_mul_f32_e32 v2, 0x3fb8aa3b, v2
	v_exp_f32_e32 v28, v2
	v_sub_f32_e32 v2, v8, v51
	v_and_b32_e32 v9, 0xffffff00, v39
	v_mul_f32_e32 v2, 0x3fb8aa3b, v2
	v_exp_f32_e32 v29, v2
	v_sub_f32_e32 v2, v9, v51
	v_and_b32_e32 v31, 0xffffff00, v40
	v_mul_f32_e32 v2, 0x3fb8aa3b, v2
	v_exp_f32_e32 v30, v2
	v_sub_f32_e32 v2, v31, v51
	v_and_b32_e32 v32, 0xffffff00, v41
	v_mul_f32_e32 v2, 0x3fb8aa3b, v2
	v_exp_f32_e32 v31, v2
	v_sub_f32_e32 v2, v32, v51
	v_and_b32_e32 v34, 0xffffff00, v42
	v_mul_f32_e32 v2, 0x3fb8aa3b, v2
	v_exp_f32_e32 v6, v2
	v_sub_f32_e32 v2, v34, v51
	v_and_b32_e32 v35, 0xffffff00, v43
	v_mul_f32_e32 v2, 0x3fb8aa3b, v2
	v_exp_f32_e32 v7, v2
	v_sub_f32_e32 v2, v35, v51
	v_mul_f32_e32 v2, 0x3fb8aa3b, v2
	v_exp_f32_e32 v8, v2
	v_lshl_or_b32 v2, s18, 8, v128
	v_ashrrev_i32_e32 v3, 31, v2
	s_lshl_b64 s[4:5], s[16:17], 18
	v_lshl_add_u64 v[32:33], v[2:3], 4, s[4:5]
	s_mov_b32 s4, 0x7fc000
	v_sub_f32_e32 v24, v51, v51
	v_mul_f32_e32 v24, 0x3fb8aa3b, v24
	v_exp_f32_e32 v24, v24
	s_waitcnt vmcnt(0)
	s_waitcnt lgkmcnt(0)
	v_and_b32_e32 v1, 0xff, v170
	v_lshrrev_b32_e32 v171, 8, v170
	v_lshlrev_b32_e32 v171, 23, v171
	v_lshl_or_b32 v2, v1, 14, v0
	v_and_b32_e32 v36, 0xffffff00, v44
	v_and_b32_e32 v37, 0xffffff00, v45
	v_and_b32_e32 v49, 0xffffff00, v46
	v_and_b32_e32 v50, 0xffffff00, v47
	v_and_b32_e32 v52, 0xffffff00, v48
	s_waitcnt lgkmcnt(0)
	v_and_b32_e32 v0, 0xff, v172
	v_lshrrev_b32_e32 v173, 8, v172
	v_lshlrev_b32_e32 v173, 23, v173
	v_lshl_or_b32 v3, v0, 14, v4
	s_waitcnt lgkmcnt(0)
	v_and_b32_e32 v0, 0xff, v174
	v_lshrrev_b32_e32 v175, 8, v174
	v_lshlrev_b32_e32 v175, 23, v175
	v_lshl_or_b32 v4, v0, 14, v10
	s_waitcnt lgkmcnt(0)
	v_and_b32_e32 v0, 0xff, v176
	v_lshrrev_b32_e32 v177, 8, v176
	v_lshlrev_b32_e32 v177, 23, v177
	v_lshl_or_b32 v5, v0, 14, v12
	v_lshlrev_b64 v[12:13], 2, v[32:33]
	v_lshl_add_u64 v[0:1], s[12:13], 0, v[12:13]
	s_nop 0
	v_readfirstlane_b32 s98, v0
	v_readfirstlane_b32 s99, v1
	v_lshrrev_b32_e32 v202, 6, v128
	v_and_b32_e32 v203, 63, v128
	v_lshlrev_b32_e32 v202, 13, v202
	v_lshl_or_b32 v204, v203, 6, v202
	v_lshl_or_b32 v205, v203, 4, v202
	v_lshlrev_b32_e32 v203, 4, v203
	ds_write_b128 v204, v[2:5]
	v_lshrrev_b32_e32 v32, 2, v40
	v_add_f32_e32 v10, 0, v24
	v_add_f32_e32 v10, v25, v10
	v_add_f32_e32 v10, v26, v10
	v_add_f32_e32 v10, v27, v10
	v_sub_f32_e32 v2, v36, v51
	v_add_f32_e32 v10, v28, v10
	v_mul_f32_e32 v2, 0x3fb8aa3b, v2
	v_add_f32_e32 v10, v29, v10
	v_exp_f32_e32 v9, v2
	v_sub_f32_e32 v2, v37, v51
	v_add_f32_e32 v10, v30, v10
	v_mul_f32_e32 v2, 0x3fb8aa3b, v2
	v_sub_f32_e32 v3, v49, v51
	v_add_f32_e32 v10, v31, v10
	v_exp_f32_e32 v2, v2
	v_mul_f32_e32 v3, 0x3fb8aa3b, v3
	v_sub_f32_e32 v4, v50, v51
	v_add_f32_e32 v10, v6, v10
	v_exp_f32_e32 v3, v3
	v_mul_f32_e32 v4, 0x3fb8aa3b, v4
	v_sub_f32_e32 v5, v52, v51
	v_add_f32_e32 v10, v7, v10
	v_exp_f32_e32 v4, v4
	v_mul_f32_e32 v5, 0x3fb8aa3b, v5
	v_add_f32_e32 v10, v8, v10
	v_exp_f32_e32 v5, v5
	v_add_f32_e32 v10, v9, v10
	v_add_f32_e32 v10, v2, v10
	v_lshrrev_b32_e32 v11, 2, v38
	v_lshrrev_b32_e32 v15, 2, v17
	v_add_f32_e32 v10, v3, v10
	v_and_b32_e32 v11, 60, v11
	v_and_b32_e32 v14, 15, v38
	v_and_b32_e32 v15, 60, v15
	v_and_b32_e32 v17, 15, v17
	v_lshrrev_b32_e32 v22, 2, v39
	v_and_b32_e32 v23, 15, v39
	v_and_b32_e32 v33, 15, v40
	v_add_f32_e32 v10, v4, v10
	v_add_u32_e32 v11, v16, v11
	v_lshl_add_u32 v14, v14, 2, v16
	v_add_u32_e32 v15, v16, v15
	v_lshl_add_u32 v17, v17, 2, v16
	v_and_b32_e32 v22, 60, v22
	v_lshl_add_u32 v23, v23, 2, v16
	v_and_b32_e32 v32, 60, v32
	v_lshl_add_u32 v33, v33, 2, v16
	v_add_f32_e32 v10, v5, v10
	v_add_u32_e32 v22, v16, v22
	v_add_u32_e32 v32, v16, v32
	ds_read_b32 v11, v11
	ds_read_b32 v14, v14 offset:64
	ds_read_b32 v15, v15
	ds_read_b32 v17, v17 offset:64
	ds_read_b32 v34, v22
	ds_read_b32 v23, v23 offset:64
	ds_read_b32 v35, v32
	ds_read_b32 v33, v33 offset:64
	s_waitcnt lgkmcnt(6)
; #define RT_PK(q_) (ex[q_] | (int)((__float_as_uint(usc[ex[q_]]) >> 23) << 14))
;     __device__ __forceinline__ void fused(f32x4 (&acc)[2][2][4][2], const Unit& u, int wr, int wc, int fr, int fq, PG8_LAS unsigned char* lds, int wid, int lane) const {
;     ...
;             const float rs = 1.0f / sum;
;             asm volatile("s_waitcnt lgkmcnt(0)" ::: "memory");
;             int ex[16];
; #pragma unroll
;             for (int q = 0; q < 16; ++q) { const unsigned cid = __float_as_uint(best[q]) & 255u; ex[q] = idxl[cid >> 4] * 128 + idxl[16 + (cid & 15u)]; }
;             const size_t o = ((size_t)u.pn * 16384 + (size_t)(u.pm * BM + row)) * 16;
;             typedef int i32x4 __attribute__((ext_vector_type(4)));
; #pragma unroll
;             for (int i = 0; i < 4; ++i) {
;     ...
;                 *(i32x4*)(eidx + o + 4 * i) = (i32x4){RT_PK(4 * i), RT_PK(4 * i + 1), RT_PK(4 * i + 2), RT_PK(4 * i + 3)};
;                 *(f32x4*)(egate + o + 4 * i) = (f32x4){sc[4 * i] * rs * vsc[ex[4 * i]], sc[4 * i + 1] * rs * vsc[ex[4 * i + 1]], sc[4 * i + 2] * rs * vsc[ex[4 * i + 2]], sc[4 * i + 3] * rs * vsc[ex[4 * i + 3]]};
	v_lshl_add_u32 v14, v11, 7, v14
	v_div_scale_f32 v11, s[16:17], v10, v10, 1.0
	v_rcp_f32_e32 v36, v11
	s_waitcnt lgkmcnt(4)
	v_lshl_add_u32 v22, v15, 7, v17
	s_waitcnt lgkmcnt(2)
	v_lshl_add_u32 v32, v34, 7, v23
	s_waitcnt lgkmcnt(0)
	v_lshl_add_u32 v34, v35, 7, v33
	v_fma_f32 v15, -v11, v36, 1.0
	v_fmac_f32_e32 v36, v15, v36
	v_div_scale_f32 v15, vcc, 1.0, v10, 1.0
	v_mul_f32_e32 v17, v15, v36
	v_fma_f32 v23, -v11, v17, v15
	v_fmac_f32_e32 v17, v23, v36
	v_fma_f32 v11, -v11, v17, v15
	v_div_fmas_f32 v11, v11, v36, v17
	v_div_fixup_f32 v10, v11, v10, 1.0
	v_pk_mul_f32 v[24:25], v[24:25], v[10:11] op_sel_hi:[1,0]
	v_pk_mul_f32 v[26:27], v[26:27], v[10:11] op_sel_hi:[1,0]
	v_ashrrev_i32_e32 v15, 31, v14
	v_ashrrev_i32_e32 v33, 31, v32
	v_lshl_add_u64 v[12:13], s[10:11], 0, v[12:13]
	s_nop 0
	v_readfirstlane_b32 s100, v12
	v_readfirstlane_b32 s101, v13
	v_ashrrev_i32_e32 v23, 31, v22
	v_lshlrev_b64 v[36:37], 3, v[32:33]
	v_lshl_add_u64 v[38:39], s[8:9], 0, v[36:37]
	v_ashrrev_i32_e32 v35, 31, v34
	v_mul_f32_e32 v18, v24, v171
	v_mul_f32_e32 v19, v25, v173
	v_lshlrev_b64 v[24:25], 3, v[14:15]
	v_mul_f32_e32 v20, v26, v175
	v_mul_f32_e32 v21, v27, v177
	ds_write_b128 v204, v[18:21] offset:4096
	v_lshlrev_b64 v[26:27], 3, v[22:23]
	s_nop 0
	v_lshl_add_u64 v[18:19], s[8:9], 0, v[24:25]
	v_lshl_add_u64 v[20:21], s[8:9], 0, v[26:27]
	v_lshl_add_u32 v242, v14, 1, v243
	ds_read_u16 v178, v242
	v_lshl_add_u32 v242, v22, 1, v243
	ds_read_u16 v180, v242
	v_lshl_add_u32 v242, v32, 1, v243
	ds_read_u16 v182, v242
	v_lshlrev_b64 v[38:39], 3, v[34:35]
	v_lshl_add_u64 v[18:19], s[8:9], 0, v[38:39]
	v_lshl_add_u32 v242, v34, 1, v243
	ds_read_u16 v184, v242
	s_waitcnt vmcnt(3)
	s_waitcnt lgkmcnt(0)
	v_and_b32_e32 v11, 0xff, v178
	v_lshrrev_b32_e32 v179, 8, v178
	v_lshlrev_b32_e32 v179, 23, v179
	v_lshl_or_b32 v18, v11, 14, v14
	s_waitcnt vmcnt(2)
	s_waitcnt lgkmcnt(0)
	v_and_b32_e32 v11, 0xff, v180
	v_lshrrev_b32_e32 v181, 8, v180
	v_lshlrev_b32_e32 v181, 23, v181
	v_lshl_or_b32 v19, v11, 14, v22
	s_waitcnt vmcnt(1)
	s_waitcnt lgkmcnt(0)
	v_and_b32_e32 v11, 0xff, v182
	v_lshrrev_b32_e32 v183, 8, v182
	v_lshlrev_b32_e32 v183, 23, v183
	v_lshl_or_b32 v20, v11, 14, v32
	s_waitcnt vmcnt(0)
	s_waitcnt lgkmcnt(0)
	v_and_b32_e32 v11, 0xff, v184
	v_lshrrev_b32_e32 v185, 8, v184
	v_lshlrev_b32_e32 v185, 23, v185
	v_lshl_or_b32 v21, v11, 14, v34
	ds_write_b128 v204, v[18:21] offset:16
	v_lshrrev_b32_e32 v11, 2, v41
	v_lshrrev_b32_e32 v15, 2, v42
	v_lshrrev_b32_e32 v18, 2, v43
	v_lshrrev_b32_e32 v20, 2, v44
	v_and_b32_e32 v11, 60, v11
	v_and_b32_e32 v14, 15, v41
	v_and_b32_e32 v15, 60, v15
	v_and_b32_e32 v17, 15, v42
	v_and_b32_e32 v18, 60, v18
	v_and_b32_e32 v19, 15, v43
	v_and_b32_e32 v20, 60, v20
	v_and_b32_e32 v21, 15, v44
	v_add_u32_e32 v11, v16, v11
	v_lshl_add_u32 v14, v14, 2, v16
	v_add_u32_e32 v15, v16, v15
	v_lshl_add_u32 v17, v17, 2, v16
	v_add_u32_e32 v18, v16, v18
	v_lshl_add_u32 v19, v19, 2, v16
	v_add_u32_e32 v20, v16, v20
	v_lshl_add_u32 v21, v21, 2, v16
	ds_read_b32 v11, v11
	ds_read_b32 v14, v14 offset:64
	ds_read_b32 v15, v15
	ds_read_b32 v17, v17 offset:64
	ds_read_b32 v18, v18
	ds_read_b32 v19, v19 offset:64
	ds_read_b32 v20, v20
	ds_read_b32 v21, v21 offset:64
	s_waitcnt lgkmcnt(6)
	v_lshl_add_u32 v14, v11, 7, v14
	s_waitcnt lgkmcnt(4)
	v_lshl_add_u32 v22, v15, 7, v17
	s_waitcnt lgkmcnt(2)
	v_lshl_add_u32 v32, v18, 7, v19
	v_pk_mul_f32 v[18:19], v[28:29], v[10:11] op_sel_hi:[1,0]
	s_waitcnt lgkmcnt(0)
	v_lshl_add_u32 v34, v20, 7, v21
	v_pk_mul_f32 v[20:21], v[30:31], v[10:11] op_sel_hi:[1,0]
	v_ashrrev_i32_e32 v15, 31, v14
	v_ashrrev_i32_e32 v33, 31, v32
	v_ashrrev_i32_e32 v23, 31, v22
	v_lshlrev_b64 v[28:29], 3, v[32:33]
	v_lshl_add_u64 v[30:31], s[8:9], 0, v[28:29]
	v_ashrrev_i32_e32 v35, 31, v34
	v_mul_f32_e32 v20, v20, v183
	v_mul_f32_e32 v21, v21, v185
	v_mul_f32_e32 v18, v18, v179
	v_mul_f32_e32 v19, v19, v181
	v_lshlrev_b64 v[24:25], 3, v[14:15]
	ds_write_b128 v204, v[18:21] offset:4112
	v_lshlrev_b64 v[26:27], 3, v[22:23]
	s_nop 0
	v_lshl_add_u64 v[18:19], s[8:9], 0, v[24:25]
	v_lshl_add_u64 v[20:21], s[8:9], 0, v[26:27]
	v_lshl_add_u32 v242, v14, 1, v243
	ds_read_u16 v186, v242
	v_lshl_add_u32 v242, v22, 1, v243
	ds_read_u16 v188, v242
	v_lshl_add_u32 v242, v32, 1, v243
	ds_read_u16 v190, v242
	v_lshlrev_b64 v[30:31], 3, v[34:35]
	v_lshl_add_u64 v[18:19], s[8:9], 0, v[30:31]
	v_lshl_add_u32 v242, v34, 1, v243
	ds_read_u16 v192, v242
	s_waitcnt vmcnt(3)
	s_waitcnt lgkmcnt(0)
; #define RT_PK(q_) (ex[q_] | (int)((__float_as_uint(usc[ex[q_]]) >> 23) << 14))
;     __device__ __forceinline__ void fused(f32x4 (&acc)[2][2][4][2], const Unit& u, int wr, int wc, int fr, int fq, PG8_LAS unsigned char* lds, int wid, int lane) const {
;     ...
;             for (int q = 0; q < 16; ++q) { const unsigned cid = __float_as_uint(best[q]) & 255u; ex[q] = idxl[cid >> 4] * 128 + idxl[16 + (cid & 15u)]; }
;             const size_t o = ((size_t)u.pn * 16384 + (size_t)(u.pm * BM + row)) * 16;
;             typedef int i32x4 __attribute__((ext_vector_type(4)));
; #pragma unroll
;             for (int i = 0; i < 4; ++i) {
;     ...
;                 *(i32x4*)(eidx + o + 4 * i) = (i32x4){RT_PK(4 * i), RT_PK(4 * i + 1), RT_PK(4 * i + 2), RT_PK(4 * i + 3)};
;                 *(f32x4*)(egate + o + 4 * i) = (f32x4){sc[4 * i] * rs * vsc[ex[4 * i]], sc[4 * i + 1] * rs * vsc[ex[4 * i + 1]], sc[4 * i + 2] * rs * vsc[ex[4 * i + 2]], sc[4 * i + 3] * rs * vsc[ex[4 * i + 3]]};
	v_and_b32_e32 v11, 0xff, v186
	v_lshrrev_b32_e32 v187, 8, v186
	v_lshlrev_b32_e32 v187, 23, v187
	v_lshl_or_b32 v18, v11, 14, v14
	s_waitcnt vmcnt(2)
	s_waitcnt lgkmcnt(0)
	v_and_b32_e32 v11, 0xff, v188
	v_lshrrev_b32_e32 v189, 8, v188
	v_lshlrev_b32_e32 v189, 23, v189
	v_lshl_or_b32 v19, v11, 14, v22
	s_waitcnt vmcnt(1)
	s_waitcnt lgkmcnt(0)
	v_and_b32_e32 v11, 0xff, v190
	v_lshrrev_b32_e32 v191, 8, v190
	v_lshlrev_b32_e32 v191, 23, v191
	v_lshl_or_b32 v20, v11, 14, v32
	s_waitcnt vmcnt(0)
	s_waitcnt lgkmcnt(0)
	v_and_b32_e32 v11, 0xff, v192
	v_lshrrev_b32_e32 v193, 8, v192
	v_lshlrev_b32_e32 v193, 23, v193
	v_lshl_or_b32 v21, v11, 14, v34
	ds_write_b128 v204, v[18:21] offset:32
	v_lshrrev_b32_e32 v11, 2, v45
	v_lshrrev_b32_e32 v15, 2, v46
	v_lshrrev_b32_e32 v18, 2, v47
	v_lshrrev_b32_e32 v20, 2, v48
	v_and_b32_e32 v11, 60, v11
	v_and_b32_e32 v14, 15, v45
	v_and_b32_e32 v15, 60, v15
	v_and_b32_e32 v17, 15, v46
	v_and_b32_e32 v18, 60, v18
	v_and_b32_e32 v19, 15, v47
	v_and_b32_e32 v20, 60, v20
	v_add_u32_e32 v11, v16, v11
	v_lshl_add_u32 v14, v14, 2, v16
	v_add_u32_e32 v15, v16, v15
	v_lshl_add_u32 v17, v17, 2, v16
	v_add_u32_e32 v18, v16, v18
	v_lshl_add_u32 v19, v19, 2, v16
	v_add_u32_e32 v20, v16, v20
	v_and_b32_e32 v21, 15, v48
	v_lshl_add_u32 v16, v21, 2, v16
	ds_read_b32 v11, v11
	ds_read_b32 v14, v14 offset:64
	ds_read_b32 v15, v15
	ds_read_b32 v17, v17 offset:64
	ds_read_b32 v18, v18
	ds_read_b32 v19, v19 offset:64
	ds_read_b32 v20, v20
	ds_read_b32 v21, v16 offset:64
	s_waitcnt lgkmcnt(6)
	v_lshl_add_u32 v14, v11, 7, v14
	s_waitcnt lgkmcnt(4)
	v_lshl_add_u32 v16, v15, 7, v17
	s_waitcnt lgkmcnt(2)
	v_lshl_add_u32 v18, v18, 7, v19
	v_pk_mul_f32 v[6:7], v[6:7], v[10:11] op_sel_hi:[1,0]
	v_pk_mul_f32 v[8:9], v[8:9], v[10:11] op_sel_hi:[1,0]
	v_ashrrev_i32_e32 v15, 31, v14
	v_ashrrev_i32_e32 v19, 31, v18
	s_waitcnt lgkmcnt(0)
	v_lshl_add_u32 v20, v20, 7, v21
	v_lshlrev_b64 v[22:23], 3, v[14:15]
	v_ashrrev_i32_e32 v17, 31, v16
	v_ashrrev_i32_e32 v21, 31, v20
	v_mul_f32_e32 v8, v8, v191
	v_mul_f32_e32 v9, v9, v193
	v_mul_f32_e32 v6, v6, v187
	v_mul_f32_e32 v7, v7, v189
	v_lshlrev_b64 v[26:27], 3, v[18:19]
	ds_write_b128 v204, v[6:9] offset:4128
	v_lshlrev_b64 v[24:25], 3, v[16:17]
	v_lshl_add_u64 v[28:29], s[8:9], 0, v[26:27]
	v_lshl_add_u64 v[6:7], s[8:9], 0, v[22:23]
	v_lshl_add_u64 v[8:9], s[8:9], 0, v[24:25]
	v_lshl_add_u32 v242, v14, 1, v243
	ds_read_u16 v194, v242
	v_lshl_add_u32 v242, v16, 1, v243
	ds_read_u16 v196, v242
	v_lshl_add_u32 v242, v18, 1, v243
	ds_read_u16 v198, v242
	v_lshlrev_b64 v[28:29], 3, v[20:21]
	v_lshl_add_u64 v[6:7], s[8:9], 0, v[28:29]
	v_lshl_add_u32 v242, v20, 1, v243
	ds_read_u16 v200, v242
	s_waitcnt vmcnt(3)
	s_waitcnt lgkmcnt(0)
	v_and_b32_e32 v6, 0xff, v194
	v_lshrrev_b32_e32 v195, 8, v194
	v_lshlrev_b32_e32 v195, 23, v195
	s_waitcnt vmcnt(2)
	s_waitcnt lgkmcnt(0)
	v_and_b32_e32 v7, 0xff, v196
	v_lshrrev_b32_e32 v197, 8, v196
	v_lshlrev_b32_e32 v197, 23, v197
	s_waitcnt vmcnt(1)
	s_waitcnt lgkmcnt(0)
	v_and_b32_e32 v8, 0xff, v198
	v_lshrrev_b32_e32 v199, 8, v198
	v_lshlrev_b32_e32 v199, 23, v199
	v_lshl_or_b32 v6, v6, 14, v14
	v_lshl_or_b32 v7, v7, 14, v16
	s_waitcnt vmcnt(0)
	s_waitcnt lgkmcnt(0)
	v_and_b32_e32 v9, 0xff, v200
	v_lshrrev_b32_e32 v201, 8, v200
	v_lshlrev_b32_e32 v201, 23, v201
	v_lshl_or_b32 v8, v8, 14, v18
	v_lshl_or_b32 v9, v9, 14, v20
	ds_write_b128 v204, v[6:9] offset:48
	v_pk_mul_f32 v[0:1], v[2:3], v[10:11] op_sel_hi:[1,0]
	v_pk_mul_f32 v[2:3], v[4:5], v[10:11] op_sel_hi:[1,0]
	v_mul_f32_e32 v0, v0, v195
	v_mul_f32_e32 v1, v1, v197
	v_mul_f32_e32 v2, v2, v199
	v_mul_f32_e32 v3, v3, v201
	ds_write_b128 v204, v[0:3] offset:4144
	s_waitcnt lgkmcnt(0)
	ds_read_b128 v[140:143], v205
	ds_read_b128 v[144:147], v205 offset:1024
	ds_read_b128 v[148:151], v205 offset:2048
	ds_read_b128 v[152:155], v205 offset:3072
	ds_read_b128 v[156:159], v205 offset:4096
	ds_read_b128 v[160:163], v205 offset:5120
	ds_read_b128 v[164:167], v205 offset:6144
	ds_read_b128 v[206:209], v205 offset:7168
	s_waitcnt lgkmcnt(0)
	global_store_dwordx4 v203, v[140:143], s[98:99]
	global_store_dwordx4 v203, v[144:147], s[98:99] offset:1024
	global_store_dwordx4 v203, v[148:151], s[98:99] offset:2048
	global_store_dwordx4 v203, v[152:155], s[98:99] offset:3072
	global_store_dwordx4 v203, v[156:159], s[100:101]
	global_store_dwordx4 v203, v[160:163], s[100:101] offset:1024
	global_store_dwordx4 v203, v[164:167], s[100:101] offset:2048
	global_store_dwordx4 v203, v[206:209], s[100:101] offset:3072

; #define PG8_LAS __attribute__((address_space(3)))
; #define RT_BAR() do { asm volatile("s_waitcnt lgkmcnt(0)" ::: "memory"); __builtin_amdgcn_s_barrier(); asm volatile("" ::: "memory"); } while (0)
;     __device__ __forceinline__ void fused(f32x4 (&acc)[2][2][4][2], const Unit& u, int wr, int wc, int fr, int fq, PG8_LAS unsigned char* lds, int wid, int lane) const {
;     ...
;                         const int rw = ai * HALF + wr * 64 + m * 16 + fr, g = 8 * wc + 4 * n + fq, col = 32 * wc + 16 * n + 4 * fq;
;                         const f32x4 v = acc[ai][bj][m][n]; f32x4 p;
; #pragma unroll
;                         for (int e = 0; e < 4; ++e) p[e] = __uint_as_float((__float_as_uint(v[e]) & ~127u) | (unsigned)(col + e));
;                         *(PG8_LAS f32x4*)(tile + rw * 128 + ((g ^ fr) << 2)) = p;
;                     }
;             RT_BAR();
;             float run[16];
; #pragma unroll
;             for (int grp = 0; grp < 4; ++grp) {
;                 float nw[16];
; #pragma unroll
;                 for (int i = 0; i < 4; ++i) { const int g = half * 16 + grp * 4 + i; const f32x4 v = *(const PG8_LAS f32x4*)(tile + row * 128 + ((g ^ (row & 15)) << 2));
;                     nw[4 * i] = v[0]; nw[4 * i + 1] = v[1]; nw[4 * i + 2] = v[2]; nw[4 * i + 3] = v[3]; }
;                 sort16_desc(nw);
;                 if (grp == 0) {
; #pragma unroll
;                     for (int q = 0; q < 16; ++q) run[q] = nw[q];
;                 } else merge_top16(run, nw);
.LBB0_602:
	s_movk_i32 s3, 0xff80
	v_and_or_b32 v60, v60, s3, v129
	v_and_or_b32 v61, v61, s98, v224
	v_and_or_b32 v62, v62, s98, v225
	v_and_or_b32 v63, v63, s98, v226
	v_and_or_b32 v56, v56, s3, v124
	v_and_or_b32 v57, v57, s98, v227
	v_and_or_b32 v58, v58, s98, v228
	v_and_or_b32 v59, v59, s98, v229
	v_and_or_b32 v52, v52, s3, v129
	v_and_or_b32 v53, v53, s98, v224
	v_and_or_b32 v54, v54, s98, v225
	v_and_or_b32 v55, v55, s98, v226
	v_and_or_b32 v48, v48, s3, v124
	v_and_or_b32 v49, v49, s98, v227
	v_and_or_b32 v50, v50, s98, v228
	v_and_or_b32 v51, v51, s98, v229
	v_and_or_b32 v44, v44, s3, v129
	v_and_or_b32 v45, v45, s98, v224
	v_and_or_b32 v46, v46, s98, v225
	v_and_or_b32 v47, v47, s98, v226
	v_and_or_b32 v40, v40, s3, v124
	v_and_or_b32 v41, v41, s98, v227
	v_and_or_b32 v42, v42, s98, v228
	v_and_or_b32 v43, v43, s98, v229
	v_and_or_b32 v36, v36, s3, v129
	v_and_or_b32 v37, v37, s98, v224
	v_and_or_b32 v38, v38, s98, v225
	v_and_or_b32 v39, v39, s98, v226
	v_and_or_b32 v32, v32, s3, v124
	v_and_or_b32 v33, v33, s98, v227
	v_and_or_b32 v34, v34, s98, v228
	v_and_or_b32 v35, v35, s98, v229
	v_and_or_b32 v28, v28, s3, v129
	v_and_or_b32 v29, v29, s98, v224
	v_and_or_b32 v30, v30, s98, v225
	v_and_or_b32 v31, v31, s98, v226
	v_and_or_b32 v24, v24, s3, v124
	v_and_or_b32 v25, v25, s98, v227
	v_and_or_b32 v26, v26, s98, v228
	v_and_or_b32 v27, v27, s98, v229
	v_and_or_b32 v20, v20, s3, v129
	v_and_or_b32 v21, v21, s98, v224
	v_and_or_b32 v22, v22, s98, v225
	v_and_or_b32 v23, v23, s98, v226
	v_and_or_b32 v16, v16, s3, v124
	v_and_or_b32 v17, v17, s98, v227
	v_and_or_b32 v18, v18, s98, v228
	v_and_or_b32 v19, v19, s98, v229
	v_and_or_b32 v12, v12, s3, v129
	v_and_or_b32 v13, v13, s98, v224
	v_and_or_b32 v14, v14, s98, v225
	v_and_or_b32 v15, v15, s98, v226
	v_and_or_b32 v8, v8, s3, v124
	v_and_or_b32 v9, v9, s98, v227
	v_and_or_b32 v10, v10, s98, v228
	v_and_or_b32 v11, v11, s98, v229
	v_and_or_b32 v4, v4, s3, v129
	v_and_or_b32 v5, v5, s98, v224
	v_and_or_b32 v6, v6, s98, v225
	v_and_or_b32 v7, v7, s98, v226
	v_and_or_b32 v0, v0, s3, v124
	v_and_or_b32 v1, v1, s98, v227
	v_and_or_b32 v2, v2, s98, v228
	v_and_or_b32 v3, v3, s98, v229
	s_waitcnt lgkmcnt(0)
	s_barrier
	ds_write_b128 v125, v[60:63]
	ds_write_b128 v120, v[56:59]
	ds_write_b128 v125, v[52:55] offset:8192
	ds_write_b128 v120, v[48:51] offset:8192
	ds_write_b128 v125, v[44:47] offset:16384
	ds_write_b128 v120, v[40:43] offset:16384
	ds_write_b128 v125, v[36:39] offset:24576
	ds_write_b128 v120, v[32:35] offset:24576
	ds_write_b128 v92, v[28:31]
	ds_write_b128 v88, v[24:27]
	ds_write_b128 v84, v[20:23]
	ds_write_b128 v82, v[16:19]
	ds_write_b128 v85, v[12:15]
	ds_write_b128 v86, v[8:11]
	ds_write_b128 v90, v[4:7]
	ds_write_b128 v91, v[0:3]
	s_waitcnt lgkmcnt(0)
	s_barrier
	s_lshr_b32 s98, s61, 2
	v_lshlrev_b32_e32 v240, 6, v128
	s_lshl_b32 s98, s98, 14
	v_add_u32_e32 v240, s98, v240
	v_add_u32_e32 v241, 0x18000, v240
	v_add_u32_e32 v240, 0x19100000, v240
	global_load_dwordx4 v[224:227], v240, s[30:31]
	global_load_dwordx4 v[228:231], v240, s[30:31] offset:16
	global_load_dwordx4 v[232:235], v240, s[30:31] offset:32
	global_load_dwordx4 v[236:239], v240, s[30:31] offset:48
	ds_read_b128 v[0:3], v93
	ds_read_b128 v[4:7], v89
	s_and_b64 vcc, exec, s[4:5]
	s_waitcnt lgkmcnt(0)
	v_min_f32_e32 v10, v0, v1
	v_max_f32_e32 v8, v0, v1
	v_min_f32_e32 v13, v2, v3
	v_max_f32_e32 v9, v2, v3
	v_min_f32_e32 v17, v4, v5
	v_max_f32_e32 v15, v4, v5
	v_min_f32_e32 v20, v6, v7
	v_max_f32_e32 v16, v6, v7
	ds_read_b128 v[0:3], v81
	ds_read_b128 v[4:7], v80
	s_waitcnt lgkmcnt(0)
	v_min_f32_e32 v23, v0, v1
	v_min_f32_e32 v24, v2, v3
	v_min_f32_e32 v26, v4, v5
	v_min_f32_e32 v27, v6, v7
	v_max_f32_e32 v0, v0, v1
	v_max_f32_e32 v1, v2, v3
	v_max_f32_e32 v4, v4, v5
	v_max_f32_e32 v5, v6, v7
	v_min_f32_e32 v14, v10, v13
	v_min_f32_e32 v21, v17, v20
	v_min_f32_e32 v25, v23, v24
	v_max_f32_e32 v10, v10, v13
	v_min_f32_e32 v11, v8, v9
	v_max_f32_e32 v13, v17, v20
	v_min_f32_e32 v17, v15, v16
	v_max_f32_e32 v23, v23, v24
	v_min_f32_e32 v2, v0, v1
	v_max_f32_e32 v24, v26, v27
	v_min_f32_e32 v6, v4, v5
	v_min_f32_e32 v28, v26, v27
	v_max_f32_e32 v12, v10, v11
	v_max_f32_e32 v18, v13, v17
	v_max_f32_e32 v3, v23, v2
	v_max_f32_e32 v7, v24, v6
	v_min_f32_e32 v22, v14, v21
	v_min_f32_e32 v29, v25, v28
	v_max_f32_e32 v14, v14, v21
	v_min_f32_e32 v19, v12, v18
	v_min_f32_e32 v10, v10, v11
	v_min_f32_e32 v11, v13, v17
	v_max_f32_e32 v21, v25, v28
	v_min_f32_e32 v25, v3, v7
	v_min_f32_e32 v2, v23, v2
	v_min_f32_e32 v6, v24, v6
	v_max_f32_e32 v20, v14, v19
	v_max_f32_e32 v13, v10, v11
	v_max_f32_e32 v8, v8, v9
	v_max_f32_e32 v9, v15, v16
	v_max_f32_e32 v23, v2, v6
	v_max_f32_e32 v0, v0, v1
	v_max_f32_e32 v1, v4, v5
	v_min_f32_e32 v14, v14, v19
	v_min_f32_e32 v10, v10, v11
	v_min_f32_e32 v19, v21, v25
	v_min_f32_e32 v2, v2, v6
	v_min_f32_e32 v15, v8, v9
	v_min_f32_e32 v4, v0, v1
	v_max_f32_e32 v11, v14, v10
	v_max_f32_e32 v6, v19, v2
	v_min_f32_e32 v10, v14, v10
	v_min_f32_e32 v2, v19, v2
	v_min_f32_e32 v5, v23, v4
	v_min_f32_e32 v14, v10, v2
	v_max_f32_e32 v2, v10, v2
	v_max_f32_e32 v10, v12, v18
	v_max_f32_e32 v12, v13, v15
	v_max_f32_e32 v3, v3, v7
	v_max_f32_e32 v4, v23, v4
	v_min_f32_e32 v16, v13, v15
	v_max_f32_e32 v26, v21, v25
	v_min_f32_e32 v13, v10, v12
	v_min_f32_e32 v7, v3, v4
	v_max_f32_e32 v10, v10, v12
	v_max_f32_e32 v3, v3, v4
	v_max_f32_e32 v17, v20, v16
	v_max_f32_e32 v24, v26, v5
	v_min_f32_e32 v21, v11, v6
	v_min_f32_e32 v16, v20, v16
	v_min_f32_e32 v5, v26, v5
	v_max_f32_e32 v6, v11, v6
	v_min_f32_e32 v4, v10, v3
	v_max_f32_e32 v8, v8, v9
	v_max_f32_e32 v9, v0, v1
	v_max_f32_e32 v30, v22, v29
	v_min_f32_e32 v27, v17, v24
	v_min_f32_e32 v15, v13, v7
	v_min_f32_e32 v20, v16, v5
	v_min_f32_e32 v11, v6, v4
	v_max_f32_e32 v5, v16, v5
	v_min_f32_e32 v0, v8, v9
	v_max_f32_e32 v17, v17, v24
	v_max_f32_e32 v4, v6, v4
	v_min_f32_e32 v28, v30, v27
	v_min_f32_e32 v18, v2, v15
	v_max_f32_e32 v27, v30, v27
	v_max_f32_e32 v2, v2, v15
	v_min_f32_e32 v1, v5, v0
	v_min_f32_e32 v24, v17, v4
	v_max_f32_e32 v17, v17, v4
	v_max_f32_e32 v4, v13, v7
	v_max_f32_e32 v5, v5, v0
	v_min_f32_e32 v12, v27, v11
	v_max_f32_e32 v11, v27, v11
	v_min_f32_e32 v15, v2, v1
	v_max_f32_e32 v27, v2, v1
	v_min_f32_e32 v13, v4, v5
	v_max_f32_e32 v10, v10, v3
	ds_read_b128 v[0:3], v99
	v_max_f32_e32 v31, v4, v5
	ds_read_b128 v[4:7], v96
	v_min_f32_e32 v22, v22, v29
	v_min_f32_e32 v25, v28, v21
	s_waitcnt lgkmcnt(0)
; #define PG8_LAS __attribute__((address_space(3)))
; #define CE(a, b) do { const float hi_ = fmaxf(a, b), lo_ = fminf(a, b); a = hi_; b = lo_; } while (0)
; __device__ __forceinline__ void sort16_desc(float (&v)[16]) {
;     CE(v[0], v[1]); CE(v[2], v[3]); CE(v[0], v[2]); CE(v[1], v[3]);
;     CE(v[1], v[2]); CE(v[4], v[5]); CE(v[6], v[7]); CE(v[4], v[6]);
;     CE(v[5], v[7]); CE(v[5], v[6]); CE(v[0], v[4]); CE(v[2], v[6]);
;     CE(v[2], v[4]); CE(v[1], v[5]); CE(v[3], v[7]); CE(v[3], v[5]);
;     CE(v[1], v[2]); CE(v[3], v[4]); CE(v[5], v[6]); CE(v[8], v[9]);
;     CE(v[10], v[11]); CE(v[8], v[10]); CE(v[9], v[11]); CE(v[9], v[10]);
;     CE(v[12], v[13]); CE(v[14], v[15]); CE(v[12], v[14]); CE(v[13], v[15]);
;     CE(v[13], v[14]); CE(v[8], v[12]); CE(v[10], v[14]); CE(v[10], v[12]);
;     CE(v[9], v[13]); CE(v[11], v[15]); CE(v[11], v[13]); CE(v[9], v[10]);
;     CE(v[11], v[12]); CE(v[13], v[14]); CE(v[0], v[8]); CE(v[4], v[12]);
;     CE(v[4], v[8]); CE(v[2], v[10]); CE(v[6], v[14]); CE(v[6], v[10]);
;     CE(v[2], v[4]); CE(v[6], v[8]); CE(v[10], v[12]); CE(v[1], v[9]);
;     CE(v[5], v[13]); CE(v[5], v[9]); CE(v[3], v[11]); CE(v[7], v[15]);
;     CE(v[7], v[11]); CE(v[3], v[5]); CE(v[7], v[9]); CE(v[11], v[13]);
;     CE(v[1], v[2]); CE(v[3], v[4]); CE(v[5], v[6]); CE(v[7], v[8]);
;     CE(v[9], v[10]); CE(v[11], v[12]); CE(v[13], v[14]);
; }
; __device__ __forceinline__ void merge_top16(float (&v)[16], const float (&nw)[16]) {
;     __device__ __forceinline__ void fused(f32x4 (&acc)[2][2][4][2], const Unit& u, int wr, int wc, int fr, int fq, PG8_LAS unsigned char* lds, int wid, int lane) const {
;     ...
;             for (int grp = 0; grp < 4; ++grp) {
;                 float nw[16];
; #pragma unroll
;                 for (int i = 0; i < 4; ++i) { const int g = half * 16 + grp * 4 + i; const f32x4 v = *(const PG8_LAS f32x4*)(tile + row * 128 + ((g ^ (row & 15)) << 2));
;                     nw[4 * i] = v[0]; nw[4 * i + 1] = v[1]; nw[4 * i + 2] = v[2]; nw[4 * i + 3] = v[3]; }
;                 sort16_desc(nw);
;                 if (grp == 0) {
; #pragma unroll
;                     for (int q = 0; q < 16; ++q) run[q] = nw[q];
;                 } else merge_top16(run, nw);
	v_min_f32_e32 v34, v0, v1
	v_max_f32_e32 v29, v0, v1
	v_min_f32_e32 v37, v2, v3
	v_max_f32_e32 v33, v2, v3
	v_min_f32_e32 v41, v4, v5
	v_max_f32_e32 v39, v4, v5
	v_min_f32_e32 v44, v6, v7
	v_max_f32_e32 v40, v6, v7
	ds_read_b128 v[0:3], v87
	ds_read_b128 v[4:7], v83
	s_waitcnt lgkmcnt(0)
	v_min_f32_e32 v47, v0, v1
	v_min_f32_e32 v48, v2, v3
	v_min_f32_e32 v50, v4, v5
	v_min_f32_e32 v51, v6, v7
	v_max_f32_e32 v0, v0, v1
	v_max_f32_e32 v1, v2, v3
	v_max_f32_e32 v4, v4, v5
	v_max_f32_e32 v5, v6, v7
	v_min_f32_e32 v38, v34, v37
	v_min_f32_e32 v45, v41, v44
	v_min_f32_e32 v49, v47, v48
	v_max_f32_e32 v34, v34, v37
	v_min_f32_e32 v35, v29, v33
	v_max_f32_e32 v37, v41, v44
	v_min_f32_e32 v41, v39, v40
	v_max_f32_e32 v47, v47, v48
	v_min_f32_e32 v2, v0, v1
	v_max_f32_e32 v48, v50, v51
	v_min_f32_e32 v6, v4, v5
	v_min_f32_e32 v52, v50, v51
	v_max_f32_e32 v36, v34, v35
	v_max_f32_e32 v42, v37, v41
	v_max_f32_e32 v3, v47, v2
	v_max_f32_e32 v7, v48, v6
	v_min_f32_e32 v46, v38, v45
	v_min_f32_e32 v53, v49, v52
	v_max_f32_e32 v38, v38, v45
	v_min_f32_e32 v43, v36, v42
	v_min_f32_e32 v34, v34, v35
	v_min_f32_e32 v35, v37, v41
	v_max_f32_e32 v45, v49, v52
	v_min_f32_e32 v49, v3, v7
	v_min_f32_e32 v2, v47, v2
	v_min_f32_e32 v6, v48, v6
	v_max_f32_e32 v44, v38, v43
	v_max_f32_e32 v37, v34, v35
	v_max_f32_e32 v29, v29, v33
	v_max_f32_e32 v33, v39, v40
	v_max_f32_e32 v47, v2, v6
	v_max_f32_e32 v0, v0, v1
	v_max_f32_e32 v1, v4, v5
	v_min_f32_e32 v38, v38, v43
	v_min_f32_e32 v34, v34, v35
	v_min_f32_e32 v43, v45, v49
	v_min_f32_e32 v2, v2, v6
	v_min_f32_e32 v39, v29, v33
	v_min_f32_e32 v4, v0, v1
	v_max_f32_e32 v35, v38, v34
	v_max_f32_e32 v6, v43, v2
	v_min_f32_e32 v34, v38, v34
	v_min_f32_e32 v2, v43, v2
	v_min_f32_e32 v40, v37, v39
	v_max_f32_e32 v50, v45, v49
	v_min_f32_e32 v5, v47, v4
	v_min_f32_e32 v38, v34, v2
	v_max_f32_e32 v2, v34, v2
	v_max_f32_e32 v34, v36, v42
	v_max_f32_e32 v36, v37, v39
	v_max_f32_e32 v3, v3, v7
	v_max_f32_e32 v4, v47, v4
	v_max_f32_e32 v41, v44, v40
	v_max_f32_e32 v48, v50, v5
	v_min_f32_e32 v37, v34, v36
	v_min_f32_e32 v7, v3, v4
	v_min_f32_e32 v40, v44, v40
	v_min_f32_e32 v5, v50, v5
	v_max_f32_e32 v34, v34, v36
	v_max_f32_e32 v3, v3, v4
	v_max_f32_e32 v29, v29, v33
	v_max_f32_e32 v0, v0, v1
	v_max_f32_e32 v54, v46, v53
	v_min_f32_e32 v51, v41, v48
	v_min_f32_e32 v45, v35, v6
	v_min_f32_e32 v39, v37, v7
	v_min_f32_e32 v44, v40, v5
	v_max_f32_e32 v6, v35, v6
	v_min_f32_e32 v4, v34, v3
	v_max_f32_e32 v5, v40, v5
	v_min_f32_e32 v1, v29, v0
	v_min_f32_e32 v52, v54, v51
	v_min_f32_e32 v42, v2, v39
	v_max_f32_e32 v51, v54, v51
	v_min_f32_e32 v35, v6, v4
	v_max_f32_e32 v2, v2, v39
	v_min_f32_e32 v33, v5, v1
	v_max_f32_e32 v41, v41, v48
	v_max_f32_e32 v4, v6, v4
	v_max_f32_e32 v7, v37, v7
	v_max_f32_e32 v1, v5, v1
	v_max_f32_e32 v21, v28, v21
	v_min_f32_e32 v23, v18, v20
	v_max_f32_e32 v18, v18, v20
	v_min_f32_e32 v49, v52, v45
	v_max_f32_e32 v45, v52, v45
	v_min_f32_e32 v47, v42, v44
	v_min_f32_e32 v36, v51, v35
	v_max_f32_e32 v42, v42, v44
	v_max_f32_e32 v35, v51, v35
	v_min_f32_e32 v39, v2, v33
	v_min_f32_e32 v6, v41, v4
	v_max_f32_e32 v2, v2, v33
	v_max_f32_e32 v4, v41, v4
	v_min_f32_e32 v5, v7, v1
	v_max_f32_e32 v3, v34, v3
	v_max_f32_e32 v1, v7, v1
	v_min_f32_e32 v19, v25, v14
	v_min_f32_e32 v26, v21, v23
	v_min_f32_e32 v20, v12, v18
	v_min_f32_e32 v16, v11, v15
	v_min_f32_e32 v28, v24, v27
	v_min_f32_e32 v30, v17, v13
	v_min_f32_e32 v32, v10, v31
	v_min_f32_e32 v43, v49, v38
	v_min_f32_e32 v50, v45, v47
	v_min_f32_e32 v44, v36, v42
	v_min_f32_e32 v40, v35, v39
	v_min_f32_e32 v33, v6, v2
	v_min_f32_e32 v37, v4, v5
	v_min_f32_e32 v7, v3, v1
	v_min_f32_e32 v34, v46, v53
	v_max3_f32 v8, v8, v9, v34
	v_max3_f32 v9, v10, v31, v43
	v_max3_f32 v10, v32, v49, v38
	v_max3_f32 v13, v17, v13, v50
	v_max3_f32 v17, v30, v45, v47
	v_max3_f32 v24, v24, v27, v44
	v_max3_f32 v27, v28, v36, v42
	v_max3_f32 v11, v11, v15, v40
	v_max3_f32 v15, v16, v35, v39
	v_max3_f32 v12, v12, v18, v33
	v_max3_f32 v2, v20, v6, v2
	v_max3_f32 v6, v21, v23, v37
	v_max3_f32 v4, v26, v4, v5
	v_max3_f32 v5, v25, v14, v7
	v_max3_f32 v1, v19, v3, v1
	v_max3_f32 v0, v22, v29, v0
	v_max_f32_e32 v3, v8, v15
	v_min_f32_e32 v7, v8, v15
	v_max_f32_e32 v8, v9, v12
	v_min_f32_e32 v9, v9, v12
	v_max_f32_e32 v12, v10, v2
	v_min_f32_e32 v2, v10, v2
	v_max_f32_e32 v10, v13, v6
	v_min_f32_e32 v6, v13, v6
	v_max_f32_e32 v13, v17, v4
	v_min_f32_e32 v4, v17, v4
	v_max_f32_e32 v14, v24, v5
	v_min_f32_e32 v5, v24, v5
	v_max_f32_e32 v15, v27, v1
	v_min_f32_e32 v1, v27, v1
	v_max_f32_e32 v16, v11, v0
	v_min_f32_e32 v0, v11, v0
	v_max_f32_e32 v11, v3, v13
	v_min_f32_e32 v3, v3, v13
	v_max_f32_e32 v13, v8, v14
	v_min_f32_e32 v8, v8, v14
	v_max_f32_e32 v14, v12, v15
	v_min_f32_e32 v12, v12, v15
	v_max_f32_e32 v15, v10, v16
	v_min_f32_e32 v10, v10, v16
	v_max_f32_e32 v16, v7, v4
	v_min_f32_e32 v4, v7, v4
	v_max_f32_e32 v7, v9, v5
	v_min_f32_e32 v5, v9, v5
	v_max_f32_e32 v9, v2, v1
	v_min_f32_e32 v1, v2, v1
	v_max_f32_e32 v2, v6, v0
	v_min_f32_e32 v0, v6, v0
	v_max_f32_e32 v17, v11, v14
	v_min_f32_e32 v11, v11, v14
	v_max_f32_e32 v14, v13, v15
	v_min_f32_e32 v13, v13, v15
	v_max_f32_e32 v15, v3, v12
	v_min_f32_e32 v12, v3, v12
	v_max_f32_e32 v18, v8, v10
	v_min_f32_e32 v8, v8, v10
	v_max_f32_e32 v10, v16, v9
	v_min_f32_e32 v9, v16, v9
	v_max_f32_e32 v16, v7, v2
	v_min_f32_e32 v19, v7, v2
	v_max_f32_e32 v20, v4, v1
	v_min_f32_e32 v21, v4, v1
	v_max_f32_e32 v22, v5, v0
	v_min_f32_e32 v23, v5, v0
	ds_read_b128 v[0:3], v102
	ds_read_b128 v[4:7], v101
	v_min_f32_e32 v24, v17, v14
	v_min_f32_e32 v25, v11, v13
	v_min_f32_e32 v26, v15, v18
	s_waitcnt lgkmcnt(0)
; #define PG8_LAS __attribute__((address_space(3)))
; #define CE(a, b) do { const float hi_ = fmaxf(a, b), lo_ = fminf(a, b); a = hi_; b = lo_; } while (0)
; __device__ __forceinline__ void merge_top16(float (&v)[16], const float (&nw)[16]) {
;     v[0] = fmaxf(v[0], nw[15]); v[1] = fmaxf(v[1], nw[14]); v[2] = fmaxf(v[2], nw[13]); v[3] = fmaxf(v[3], nw[12]); v[4] = fmaxf(v[4], nw[11]); v[5] = fmaxf(v[5], nw[10]); v[6] = fmaxf(v[6], nw[9]); v[7] = fmaxf(v[7], nw[8]); v[8] = fmaxf(v[8], nw[7]); v[9] = fmaxf(v[9], nw[6]); v[10] = fmaxf(v[10], nw[5]); v[11] = fmaxf(v[11], nw[4]); v[12] = fmaxf(v[12], nw[3]); v[13] = fmaxf(v[13], nw[2]); v[14] = fmaxf(v[14], nw[1]); v[15] = fmaxf(v[15], nw[0]);
;     CE(v[0], v[8]); CE(v[1], v[9]); CE(v[2], v[10]); CE(v[3], v[11]);
;     CE(v[4], v[12]); CE(v[5], v[13]); CE(v[6], v[14]); CE(v[7], v[15]);
;     CE(v[0], v[4]); CE(v[1], v[5]); CE(v[2], v[6]); CE(v[3], v[7]);
;     CE(v[8], v[12]); CE(v[9], v[13]); CE(v[10], v[14]); CE(v[11], v[15]);
;     CE(v[0], v[2]); CE(v[1], v[3]); CE(v[4], v[6]); CE(v[5], v[7]);
;     CE(v[8], v[10]); CE(v[9], v[11]); CE(v[12], v[14]); CE(v[13], v[15]);
;     CE(v[0], v[1]); CE(v[2], v[3]); CE(v[4], v[5]); CE(v[6], v[7]);
;     CE(v[8], v[9]); CE(v[10], v[11]); CE(v[12], v[13]); CE(v[14], v[15]);
; }
;     __device__ __forceinline__ void fused(f32x4 (&acc)[2][2][4][2], const Unit& u, int wr, int wc, int fr, int fq, PG8_LAS unsigned char* lds, int wid, int lane) const {
;     ...
;             for (int grp = 0; grp < 4; ++grp) {
;                 float nw[16];
; #pragma unroll
;                 for (int i = 0; i < 4; ++i) { const int g = half * 16 + grp * 4 + i; const f32x4 v = *(const PG8_LAS f32x4*)(tile + row * 128 + ((g ^ (row & 15)) << 2));
;                     nw[4 * i] = v[0]; nw[4 * i + 1] = v[1]; nw[4 * i + 2] = v[2]; nw[4 * i + 3] = v[3]; }
;                 sort16_desc(nw);
;                 if (grp == 0) {
; #pragma unroll
;                     for (int q = 0; q < 16; ++q) run[q] = nw[q];
;                 } else merge_top16(run, nw);
	v_min_f32_e32 v34, v0, v1
	v_max_f32_e32 v32, v0, v1
	v_min_f32_e32 v37, v2, v3
	v_max_f32_e32 v33, v2, v3
	v_min_f32_e32 v41, v4, v5
	v_max_f32_e32 v39, v4, v5
	v_min_f32_e32 v44, v6, v7
	v_max_f32_e32 v40, v6, v7
	ds_read_b128 v[0:3], v95
	ds_read_b128 v[4:7], v94
	s_waitcnt lgkmcnt(0)
	v_min_f32_e32 v47, v0, v1
	v_min_f32_e32 v48, v2, v3
	v_min_f32_e32 v50, v4, v5
	v_min_f32_e32 v51, v6, v7
	v_max_f32_e32 v0, v0, v1
	v_max_f32_e32 v1, v2, v3
	v_max_f32_e32 v4, v4, v5
	v_max_f32_e32 v5, v6, v7
	v_min_f32_e32 v38, v34, v37
	v_min_f32_e32 v45, v41, v44
	v_min_f32_e32 v49, v47, v48
	v_max_f32_e32 v34, v34, v37
	v_min_f32_e32 v35, v32, v33
	v_max_f32_e32 v37, v41, v44
	v_min_f32_e32 v41, v39, v40
	v_max_f32_e32 v47, v47, v48
	v_min_f32_e32 v2, v0, v1
	v_max_f32_e32 v48, v50, v51
	v_min_f32_e32 v6, v4, v5
	v_min_f32_e32 v52, v50, v51
	v_max_f32_e32 v36, v34, v35
	v_max_f32_e32 v42, v37, v41
	v_max_f32_e32 v3, v47, v2
	v_max_f32_e32 v7, v48, v6
	v_min_f32_e32 v46, v38, v45
	v_min_f32_e32 v53, v49, v52
	v_max_f32_e32 v38, v38, v45
	v_min_f32_e32 v43, v36, v42
	v_min_f32_e32 v34, v34, v35
	v_min_f32_e32 v35, v37, v41
	v_max_f32_e32 v45, v49, v52
	v_min_f32_e32 v49, v3, v7
	v_min_f32_e32 v2, v47, v2
	v_min_f32_e32 v6, v48, v6
	v_max_f32_e32 v44, v38, v43
	v_max_f32_e32 v37, v34, v35
	v_max_f32_e32 v32, v32, v33
	v_max_f32_e32 v33, v39, v40
	v_max_f32_e32 v47, v2, v6
	v_max_f32_e32 v0, v0, v1
	v_max_f32_e32 v1, v4, v5
	v_min_f32_e32 v38, v38, v43
	v_min_f32_e32 v34, v34, v35
	v_min_f32_e32 v43, v45, v49
	v_min_f32_e32 v2, v2, v6
	v_min_f32_e32 v39, v32, v33
	v_min_f32_e32 v4, v0, v1
	v_max_f32_e32 v35, v38, v34
	v_max_f32_e32 v6, v43, v2
	v_min_f32_e32 v34, v38, v34
	v_min_f32_e32 v2, v43, v2
	v_min_f32_e32 v40, v37, v39
	v_max_f32_e32 v50, v45, v49
	v_min_f32_e32 v5, v47, v4
	v_min_f32_e32 v38, v34, v2
	v_max_f32_e32 v2, v34, v2
	v_max_f32_e32 v34, v36, v42
	v_max_f32_e32 v36, v37, v39
	v_max_f32_e32 v3, v3, v7
	v_max_f32_e32 v4, v47, v4
	v_max_f32_e32 v41, v44, v40
	v_max_f32_e32 v48, v50, v5
	v_min_f32_e32 v37, v34, v36
	v_min_f32_e32 v7, v3, v4
	v_max_f32_e32 v54, v46, v53
	v_min_f32_e32 v51, v41, v48
	v_min_f32_e32 v39, v37, v7
	v_min_f32_e32 v40, v44, v40
	v_min_f32_e32 v5, v50, v5
	v_min_f32_e32 v52, v54, v51
	v_min_f32_e32 v45, v35, v6
	v_min_f32_e32 v42, v2, v39
	v_min_f32_e32 v44, v40, v5
	v_max_f32_e32 v34, v34, v36
	v_max_f32_e32 v3, v3, v4
	v_max_f32_e32 v32, v32, v33
	v_max_f32_e32 v0, v0, v1
	v_min_f32_e32 v49, v52, v45
	v_max_f32_e32 v45, v52, v45
	v_min_f32_e32 v47, v42, v44
	v_max_f32_e32 v6, v35, v6
	v_min_f32_e32 v4, v34, v3
	v_max_f32_e32 v5, v40, v5
	v_min_f32_e32 v1, v32, v0
	v_min_f32_e32 v43, v49, v38
	v_max_f32_e32 v38, v49, v38
	v_min_f32_e32 v49, v45, v47
	v_max_f32_e32 v45, v45, v47
	v_max_f32_e32 v47, v54, v51
	v_min_f32_e32 v35, v6, v4
	v_max_f32_e32 v2, v2, v39
	v_min_f32_e32 v33, v5, v1
	v_min_f32_e32 v36, v47, v35
	v_max_f32_e32 v35, v47, v35
	v_min_f32_e32 v39, v2, v33
	v_min_f32_e32 v40, v35, v39
	v_max_f32_e32 v35, v35, v39
	v_max_f32_e32 v39, v41, v48
	v_max_f32_e32 v4, v6, v4
	v_min_f32_e32 v6, v39, v4
	v_max_f32_e32 v2, v2, v33
	v_min_f32_e32 v33, v6, v2
	v_max_f32_e32 v2, v6, v2
	v_max_f32_e32 v6, v37, v7
	v_max_f32_e32 v1, v5, v1
	v_max_f32_e32 v42, v42, v44
	v_max_f32_e32 v4, v39, v4
	v_min_f32_e32 v5, v6, v1
	v_max_f32_e32 v3, v34, v3
	v_max_f32_e32 v1, v6, v1
	v_min_f32_e32 v27, v12, v8
	v_min_f32_e32 v28, v10, v16
	v_min_f32_e32 v29, v9, v19
	v_min_f32_e32 v30, v20, v22
	v_min_f32_e32 v31, v21, v23
	v_min_f32_e32 v44, v36, v42
	v_max_f32_e32 v36, v36, v42
	v_min_f32_e32 v7, v4, v5
	v_max_f32_e32 v4, v4, v5
	v_min_f32_e32 v5, v3, v1
	v_max_f32_e32 v1, v3, v1
	v_min_f32_e32 v3, v46, v53
	v_max3_f32 v3, v17, v14, v3
	v_max_f32_e32 v6, v24, v43
	v_max3_f32 v11, v11, v13, v38
	v_max_f32_e32 v13, v25, v49
	v_max3_f32 v14, v15, v18, v45
	v_max_f32_e32 v15, v26, v44
	v_max3_f32 v8, v12, v8, v36
	v_max_f32_e32 v12, v27, v40
	v_max3_f32 v10, v10, v16, v35
	v_max_f32_e32 v16, v28, v33
	v_max3_f32 v2, v9, v19, v2
	v_max_f32_e32 v7, v29, v7
	v_max3_f32 v4, v20, v22, v4
	v_max_f32_e32 v5, v30, v5
	v_max3_f32 v1, v21, v23, v1
	v_max3_f32 v0, v31, v32, v0
	v_max_f32_e32 v9, v3, v10
	v_min_f32_e32 v3, v3, v10
	v_max_f32_e32 v10, v6, v16
	v_min_f32_e32 v6, v6, v16
	v_max_f32_e32 v16, v11, v2
	v_min_f32_e32 v2, v11, v2
	v_max_f32_e32 v11, v13, v7
	v_min_f32_e32 v7, v13, v7
	v_max_f32_e32 v13, v14, v4
	v_min_f32_e32 v4, v14, v4
	v_max_f32_e32 v14, v15, v5
	v_min_f32_e32 v5, v15, v5
	v_max_f32_e32 v15, v8, v1
	v_min_f32_e32 v1, v8, v1
	v_max_f32_e32 v8, v12, v0
	v_min_f32_e32 v0, v12, v0
	v_max_f32_e32 v12, v9, v13
	v_min_f32_e32 v9, v9, v13
	v_max_f32_e32 v13, v10, v14
	v_min_f32_e32 v10, v10, v14
	v_max_f32_e32 v14, v16, v15
	v_min_f32_e32 v15, v16, v15
	v_max_f32_e32 v16, v11, v8
	v_min_f32_e32 v8, v11, v8
	v_max_f32_e32 v11, v3, v4
	v_min_f32_e32 v3, v3, v4
	v_max_f32_e32 v4, v6, v5
	v_min_f32_e32 v5, v6, v5
	v_max_f32_e32 v6, v2, v1
	v_min_f32_e32 v1, v2, v1
	v_max_f32_e32 v2, v7, v0
	v_min_f32_e32 v0, v7, v0
	v_max_f32_e32 v17, v12, v14
	v_min_f32_e32 v12, v12, v14
	v_max_f32_e32 v14, v13, v16
	v_min_f32_e32 v13, v13, v16
	v_max_f32_e32 v16, v9, v15
	v_min_f32_e32 v9, v9, v15
	v_max_f32_e32 v15, v10, v8
	v_min_f32_e32 v8, v10, v8
	v_max_f32_e32 v10, v11, v6
	v_min_f32_e32 v11, v11, v6
	v_max_f32_e32 v18, v4, v2
	v_min_f32_e32 v19, v4, v2
	v_max_f32_e32 v20, v3, v1
	v_min_f32_e32 v21, v3, v1
	v_max_f32_e32 v22, v5, v0
	v_min_f32_e32 v23, v5, v0
	ds_read_b128 v[0:3], v104
	ds_read_b128 v[4:7], v103
	v_min_f32_e32 v24, v17, v14
	v_min_f32_e32 v25, v12, v13
	v_min_f32_e32 v26, v16, v15
	s_waitcnt lgkmcnt(0)
; #define PG8_LAS __attribute__((address_space(3)))
; #define RT_BAR() do { asm volatile("s_waitcnt lgkmcnt(0)" ::: "memory"); __builtin_amdgcn_s_barrier(); asm volatile("" ::: "memory"); } while (0)
;     __device__ __forceinline__ void fused(f32x4 (&acc)[2][2][4][2], const Unit& u, int wr, int wc, int fr, int fq, PG8_LAS unsigned char* lds, int wid, int lane) const {
;     ...
;             for (int grp = 0; grp < 4; ++grp) {
;                 float nw[16];
; #pragma unroll
;                 for (int i = 0; i < 4; ++i) { const int g = half * 16 + grp * 4 + i; const f32x4 v = *(const PG8_LAS f32x4*)(tile + row * 128 + ((g ^ (row & 15)) << 2));
;                     nw[4 * i] = v[0]; nw[4 * i + 1] = v[1]; nw[4 * i + 2] = v[2]; nw[4 * i + 3] = v[3]; }
;                 sort16_desc(nw);
;                 if (grp == 0) {
; #pragma unroll
;                     for (int q = 0; q < 16; ++q) run[q] = nw[q];
;                 } else merge_top16(run, nw);
;             }
;             RT_BAR();
;             if (half == 1) {
; #pragma unroll
;                 for (int i = 0; i < 4; ++i) *(PG8_LAS f32x4*)(tile + row * 16 + 4 * i) = (f32x4){run[4 * i], run[4 * i + 1], run[4 * i + 2], run[4 * i + 3]};
;             }
;             RT_BAR();
	v_min_f32_e32 v34, v0, v1
	v_max_f32_e32 v32, v0, v1
	v_min_f32_e32 v37, v2, v3
	v_max_f32_e32 v33, v2, v3
	v_min_f32_e32 v41, v4, v5
	v_max_f32_e32 v39, v4, v5
	v_min_f32_e32 v44, v6, v7
	v_max_f32_e32 v40, v6, v7
	ds_read_b128 v[0:3], v100
	ds_read_b128 v[4:7], v98
	s_waitcnt lgkmcnt(0)
	v_min_f32_e32 v47, v0, v1
	v_min_f32_e32 v48, v2, v3
	v_min_f32_e32 v50, v4, v5
	v_min_f32_e32 v51, v6, v7
	v_max_f32_e32 v0, v0, v1
	v_max_f32_e32 v1, v2, v3
	v_max_f32_e32 v4, v4, v5
	v_max_f32_e32 v5, v6, v7
	v_min_f32_e32 v38, v34, v37
	v_min_f32_e32 v45, v41, v44
	v_min_f32_e32 v49, v47, v48
	v_max_f32_e32 v34, v34, v37
	v_min_f32_e32 v35, v32, v33
	v_max_f32_e32 v37, v41, v44
	v_min_f32_e32 v41, v39, v40
	v_max_f32_e32 v47, v47, v48
	v_min_f32_e32 v2, v0, v1
	v_max_f32_e32 v48, v50, v51
	v_min_f32_e32 v6, v4, v5
	v_min_f32_e32 v52, v50, v51
	v_max_f32_e32 v36, v34, v35
	v_max_f32_e32 v42, v37, v41
	v_max_f32_e32 v3, v47, v2
	v_max_f32_e32 v7, v48, v6
	v_min_f32_e32 v46, v38, v45
	v_min_f32_e32 v53, v49, v52
	v_max_f32_e32 v38, v38, v45
	v_min_f32_e32 v43, v36, v42
	v_min_f32_e32 v34, v34, v35
	v_min_f32_e32 v35, v37, v41
	v_max_f32_e32 v45, v49, v52
	v_min_f32_e32 v49, v3, v7
	v_min_f32_e32 v2, v47, v2
	v_min_f32_e32 v6, v48, v6
	v_max_f32_e32 v44, v38, v43
	v_max_f32_e32 v37, v34, v35
	v_max_f32_e32 v32, v32, v33
	v_max_f32_e32 v33, v39, v40
	v_max_f32_e32 v47, v2, v6
	v_max_f32_e32 v0, v0, v1
	v_max_f32_e32 v1, v4, v5
	v_min_f32_e32 v38, v38, v43
	v_min_f32_e32 v34, v34, v35
	v_min_f32_e32 v43, v45, v49
	v_min_f32_e32 v2, v2, v6
	v_min_f32_e32 v39, v32, v33
	v_min_f32_e32 v4, v0, v1
	v_max_f32_e32 v35, v38, v34
	v_max_f32_e32 v6, v43, v2
	v_min_f32_e32 v34, v38, v34
	v_min_f32_e32 v2, v43, v2
	v_min_f32_e32 v40, v37, v39
	v_max_f32_e32 v50, v45, v49
	v_min_f32_e32 v5, v47, v4
	v_min_f32_e32 v38, v34, v2
	v_max_f32_e32 v2, v34, v2
	v_max_f32_e32 v34, v36, v42
	v_max_f32_e32 v36, v37, v39
	v_max_f32_e32 v3, v3, v7
	v_max_f32_e32 v4, v47, v4
	v_max_f32_e32 v41, v44, v40
	v_max_f32_e32 v48, v50, v5
	v_min_f32_e32 v37, v34, v36
	v_min_f32_e32 v7, v3, v4
	v_max_f32_e32 v54, v46, v53
	v_min_f32_e32 v51, v41, v48
	v_min_f32_e32 v39, v37, v7
	v_min_f32_e32 v40, v44, v40
	v_min_f32_e32 v5, v50, v5
	v_min_f32_e32 v52, v54, v51
	v_min_f32_e32 v45, v35, v6
	v_min_f32_e32 v42, v2, v39
	v_min_f32_e32 v44, v40, v5
	v_max_f32_e32 v34, v34, v36
	v_max_f32_e32 v3, v3, v4
	v_max_f32_e32 v32, v32, v33
	v_max_f32_e32 v0, v0, v1
	v_min_f32_e32 v49, v52, v45
	v_max_f32_e32 v45, v52, v45
	v_min_f32_e32 v47, v42, v44
	v_max_f32_e32 v6, v35, v6
	v_min_f32_e32 v4, v34, v3
	v_max_f32_e32 v5, v40, v5
	v_min_f32_e32 v1, v32, v0
	v_min_f32_e32 v43, v49, v38
	v_max_f32_e32 v38, v49, v38
	v_min_f32_e32 v49, v45, v47
	v_max_f32_e32 v45, v45, v47
	v_max_f32_e32 v47, v54, v51
	v_min_f32_e32 v35, v6, v4
	v_max_f32_e32 v2, v2, v39
	v_min_f32_e32 v33, v5, v1
	v_min_f32_e32 v36, v47, v35
	v_max_f32_e32 v35, v47, v35
	v_min_f32_e32 v39, v2, v33
	v_min_f32_e32 v40, v35, v39
	v_max_f32_e32 v35, v35, v39
	v_max_f32_e32 v39, v41, v48
	v_max_f32_e32 v4, v6, v4
	v_min_f32_e32 v6, v39, v4
	v_max_f32_e32 v2, v2, v33
	v_min_f32_e32 v33, v6, v2
	v_max_f32_e32 v2, v6, v2
	v_max_f32_e32 v6, v37, v7
	v_max_f32_e32 v1, v5, v1
	v_max_f32_e32 v42, v42, v44
	v_max_f32_e32 v4, v39, v4
	v_min_f32_e32 v5, v6, v1
	v_max_f32_e32 v3, v34, v3
	v_max_f32_e32 v1, v6, v1
	v_min_f32_e32 v27, v9, v8
	v_min_f32_e32 v28, v10, v18
	v_min_f32_e32 v29, v11, v19
	v_min_f32_e32 v30, v20, v22
	v_min_f32_e32 v31, v21, v23
	v_min_f32_e32 v44, v36, v42
	v_max_f32_e32 v36, v36, v42
	v_min_f32_e32 v7, v4, v5
	v_max_f32_e32 v4, v4, v5
	v_min_f32_e32 v5, v3, v1
	v_max_f32_e32 v1, v3, v1
	v_min_f32_e32 v3, v46, v53
	v_max3_f32 v3, v17, v14, v3
	v_max_f32_e32 v6, v24, v43
	v_max3_f32 v12, v12, v13, v38
	v_max_f32_e32 v13, v25, v49
	v_max3_f32 v14, v16, v15, v45
	v_max_f32_e32 v15, v26, v44
	v_max3_f32 v8, v9, v8, v36
	v_max_f32_e32 v9, v27, v40
	v_max3_f32 v10, v10, v18, v35
	v_max_f32_e32 v16, v28, v33
	v_max3_f32 v2, v11, v19, v2
	v_max_f32_e32 v7, v29, v7
	v_max3_f32 v4, v20, v22, v4
	v_max_f32_e32 v5, v30, v5
	v_max3_f32 v1, v21, v23, v1
	v_max3_f32 v0, v31, v32, v0
	v_max_f32_e32 v11, v3, v10
	v_min_f32_e32 v3, v3, v10
	v_max_f32_e32 v10, v6, v16
	v_min_f32_e32 v6, v6, v16
	v_max_f32_e32 v16, v12, v2
	v_min_f32_e32 v2, v12, v2
	v_max_f32_e32 v12, v13, v7
	v_min_f32_e32 v7, v13, v7
	v_max_f32_e32 v13, v14, v4
	v_min_f32_e32 v4, v14, v4
	v_max_f32_e32 v14, v15, v5
	v_min_f32_e32 v5, v15, v5
	v_max_f32_e32 v15, v8, v1
	v_min_f32_e32 v1, v8, v1
	v_max_f32_e32 v8, v9, v0
	v_min_f32_e32 v0, v9, v0
	v_max_f32_e32 v9, v11, v13
	v_min_f32_e32 v11, v11, v13
	v_max_f32_e32 v13, v10, v14
	v_min_f32_e32 v10, v10, v14
	v_max_f32_e32 v14, v16, v15
	v_min_f32_e32 v15, v16, v15
	v_max_f32_e32 v16, v12, v8
	v_min_f32_e32 v8, v12, v8
	v_max_f32_e32 v12, v3, v4
	v_min_f32_e32 v3, v3, v4
	v_max_f32_e32 v4, v6, v5
	v_min_f32_e32 v5, v6, v5
	v_max_f32_e32 v6, v2, v1
	v_min_f32_e32 v1, v2, v1
	v_max_f32_e32 v2, v7, v0
	v_min_f32_e32 v0, v7, v0
	s_waitcnt lgkmcnt(0)
	s_barrier
	s_waitcnt vmcnt(0)
	ds_write_b128 v241, v[224:227]
	ds_write_b128 v241, v[228:231] offset:16
	ds_write_b128 v241, v[232:235] offset:32
	ds_write_b128 v241, v[236:239] offset:48
	v_max_f32_e32 v7, v9, v14
	v_min_f32_e32 v9, v9, v14
	v_max_f32_e32 v14, v13, v16
	v_min_f32_e32 v16, v13, v16
	v_max_f32_e32 v17, v11, v15
	v_min_f32_e32 v11, v11, v15
	v_max_f32_e32 v18, v10, v8
	v_min_f32_e32 v19, v10, v8
	v_max_f32_e32 v20, v12, v6
	v_min_f32_e32 v21, v12, v6
	v_max_f32_e32 v6, v4, v2
	v_min_f32_e32 v2, v4, v2
	v_max_f32_e32 v22, v3, v1
	v_min_f32_e32 v3, v3, v1
	v_max_f32_e32 v1, v5, v0
	v_min_f32_e32 v23, v5, v0
	v_max_f32_e32 v12, v7, v14
	v_min_f32_e32 v13, v7, v14
	v_max_f32_e32 v14, v9, v16
	v_min_f32_e32 v15, v9, v16
	v_max_f32_e32 v8, v17, v18
	v_min_f32_e32 v9, v17, v18
	v_max_f32_e32 v10, v11, v19
	v_min_f32_e32 v11, v11, v19
	v_max_f32_e32 v4, v20, v6
	v_min_f32_e32 v5, v20, v6
	v_max_f32_e32 v6, v21, v2
	v_min_f32_e32 v7, v21, v2
	v_max_f32_e32 v0, v22, v1
	v_min_f32_e32 v1, v22, v1
	v_max_f32_e32 v2, v3, v23
	v_min_f32_e32 v3, v3, v23
	s_cbranch_vccnz .LBB0_604
	ds_write_b128 v97, v[12:15]
	ds_write_b128 v97, v[8:11] offset:16
	ds_write_b128 v97, v[4:7] offset:32
	ds_write_b128 v97, v[0:3] offset:48

; #define PG8_LAS __attribute__((address_space(3)))
;     __device__ __forceinline__ void fused(f32x4 (&acc)[2][2][4][2], const Unit& u, int wr, int wc, int fr, int fq, PG8_LAS unsigned char* lds, int wid, int lane) const {
;     ...
;         if (half == 0) {
;             PG8_LAS int* idxl = (PG8_LAS int*)(lds + 65536) + row * 32;
;             float v0[16], v1[16];
; #pragma unroll
;             for (int q = 0; q < 16; ++q) { const unsigned b0 = __float_as_uint(top0[q]), b1 = __float_as_uint(top1[q]);
;                 v0[q] = __uint_as_float(b0 & ~127u); v1[q] = __uint_as_float(b1 & ~127u); idxl[q] = (int)(b0 & 127u); idxl[16 + q] = (int)(b1 & 127u); }
;             float best[16];
;             { float cv[16]; cv[0] = __uint_as_float((__float_as_uint(v0[0] + v1[0]) & ~255u) | 0u); cv[1] = __uint_as_float((__float_as_uint(v0[0] + v1[1]) & ~255u) | 1u); cv[2] = __uint_as_float((__float_as_uint(v0[0] + v1[2]) & ~255u) | 2u); cv[3] = __uint_as_float((__float_as_uint(v0[0] + v1[3]) & ~255u) | 3u); cv[4] = __uint_as_float((__float_as_uint(v0[0] + v1[4]) & ~255u) | 4u); cv[5] = __uint_as_float((__float_as_uint(v0[0] + v1[5]) & ~255u) | 5u); cv[6] = __uint_as_float((__float_as_uint(v0[0] + v1[6]) & ~255u) | 6u); cv[7] = __uint_as_float((__float_as_uint(v0[0] + v1[7]) & ~255u) | 7u); cv[8] = __uint_as_float((__float_as_uint(v0[0] + v1[8]) & ~255u) | 8u); cv[9] = __uint_as_float((__float_as_uint(v0[0] + v1[9]) & ~255u) | 9u); cv[10] = __uint_as_float((__float_as_uint(v0[0] + v1[10]) & ~255u) | 10u); cv[11] = __uint_as_float((__float_as_uint(v0[0] + v1[11]) & ~255u) | 11u); cv[12] = __uint_as_float((__float_as_uint(v0[0] + v1[12]) & ~255u) | 12u); cv[13] = __uint_as_float((__float_as_uint(v0[0] + v1[13]) & ~255u) | 13u); cv[14] = __uint_as_float((__float_as_uint(v0[0] + v1[14]) & ~255u) | 14u); cv[15] = __uint_as_float((__float_as_uint(v0[0] + v1[15]) & ~255u) | 15u); sort16_desc(cv);
; #pragma unroll
;               for (int q = 0; q < 16; ++q) best[q] = cv[q]; }
.LBB0_606:
	s_waitcnt lgkmcnt(0)
	s_barrier
	s_and_b64 vcc, exec, s[4:5]
	s_cbranch_vccnz .LBB0_608
	v_lshl_add_u32 v16, v128, 7, 0
	v_add_u32_e32 v16, 0x10000, v16
	v_and_b32_e32 v17, 0xffffff80, v12
	v_and_b32_e32 v18, 0xffffff80, v13
	v_and_b32_e32 v21, 0x7f, v77
	v_and_b32_e32 v20, 0x7f, v76
	v_and_b32_e32 v13, 0x7f, v13
	v_and_b32_e32 v12, 0x7f, v12
	v_and_b32_e32 v26, 0xffffff80, v14
	v_and_b32_e32 v28, 0xffffff80, v15
	v_and_b32_e32 v23, 0x7f, v79
	v_and_b32_e32 v22, 0x7f, v78
	v_and_b32_e32 v15, 0x7f, v15
	v_and_b32_e32 v14, 0x7f, v14
	ds_write_b128 v16, v[20:23]
	ds_write_b128 v16, v[12:15] offset:64
	v_and_b32_e32 v21, 0xffffff80, v8
	v_and_b32_e32 v23, 0xffffff80, v9
	v_and_b32_e32 v13, 0x7f, v73
	v_and_b32_e32 v12, 0x7f, v72
	v_and_b32_e32 v9, 0x7f, v9
	v_and_b32_e32 v8, 0x7f, v8
	v_and_b32_e32 v30, 0xffffff80, v10
	v_and_b32_e32 v32, 0xffffff80, v11
	v_and_b32_e32 v15, 0x7f, v75
	v_and_b32_e32 v14, 0x7f, v74
	v_and_b32_e32 v11, 0x7f, v11
	v_and_b32_e32 v10, 0x7f, v10
	v_and_b32_e32 v19, 0xffffff80, v76
	ds_write_b128 v16, v[12:15] offset:16
	ds_write_b128 v16, v[8:11] offset:80
	v_and_b32_e32 v13, 0xffffff80, v4
	v_and_b32_e32 v15, 0xffffff80, v5
	v_and_b32_e32 v9, 0x7f, v69
	v_and_b32_e32 v8, 0x7f, v68
	v_and_b32_e32 v5, 0x7f, v5
	v_and_b32_e32 v4, 0x7f, v4
	v_and_b32_e32 v34, 0xffffff80, v6
	v_and_b32_e32 v36, 0xffffff80, v7
	v_and_b32_e32 v11, 0x7f, v71
	v_and_b32_e32 v10, 0x7f, v70
	v_and_b32_e32 v7, 0x7f, v7
	v_and_b32_e32 v6, 0x7f, v6
	ds_write_b128 v16, v[8:11] offset:32
	ds_write_b128 v16, v[4:7] offset:96
	v_and_b32_e32 v5, 0x7f, v65
	v_and_b32_e32 v4, 0x7f, v64
	v_and_b32_e32 v41, 0xffffff80, v2
	v_and_b32_e32 v42, 0xffffff80, v3
	v_and_b32_e32 v7, 0x7f, v67
	v_and_b32_e32 v6, 0x7f, v66
	v_and_b32_e32 v11, 0x7f, v3
	v_and_b32_e32 v10, 0x7f, v2
	v_add_f32_e32 v2, v19, v17
	s_movk_i32 s3, 0xff00
	v_add_f32_e32 v3, v19, v18
	v_and_b32_e32 v24, 0xffffff80, v77
	ds_write_b128 v16, v[4:7] offset:48
	v_and_b32_e32 v2, 0xffffff00, v2
	v_and_or_b32 v3, v3, s3, 1
	v_add_f32_e32 v4, v19, v26
	v_add_f32_e32 v5, v19, v28
	v_and_b32_e32 v40, 0xffffff80, v1
	v_and_b32_e32 v9, 0x7f, v1
	v_and_b32_e32 v8, 0x7f, v0
	v_and_or_b32 v4, v4, s3, 2
	v_and_or_b32 v5, v5, s3, 3
	v_add_f32_e32 v48, v24, v17
	v_add_f32_e32 v49, v24, v18
	ds_write_b128 v16, v[8:11] offset:112
	v_add_f32_e32 v6, v19, v21
	v_add_f32_e32 v7, v19, v23
	v_add_f32_e32 v11, v19, v15
	v_add_f32_e32 v15, v19, v36
	v_add_f32_e32 v36, v19, v40
	v_max_f32_e32 v40, v2, v3
	v_min_f32_e32 v2, v2, v3
	v_max_f32_e32 v3, v5, v5
	v_and_or_b32 v48, v48, s3, 16
	v_and_or_b32 v49, v49, s3, 17
	v_add_f32_e32 v50, v24, v26
	v_add_f32_e32 v51, v24, v28
	v_and_or_b32 v6, v6, s3, 4
	v_and_or_b32 v7, v7, s3, 5
	v_add_f32_e32 v8, v19, v30
	v_add_f32_e32 v9, v19, v32
	v_max_f32_e32 v5, v4, v3
	v_min_f32_e32 v3, v4, v3
	v_and_or_b32 v50, v50, s3, 18
	v_and_or_b32 v51, v51, s3, 19
	v_and_or_b32 v8, v8, s3, 6
	v_and_or_b32 v9, v9, s3, 7
	v_max_f32_e32 v4, v40, v5
	v_min_f32_e32 v5, v40, v5
	v_max_f32_e32 v40, v2, v3
	v_add_f32_e32 v52, v24, v21
	v_add_f32_e32 v23, v24, v23
	v_add_f32_e32 v30, v24, v30
	v_add_f32_e32 v24, v24, v32
	v_max_f32_e32 v58, v48, v49
	v_min_f32_e32 v48, v48, v49
	v_max_f32_e32 v49, v51, v51
	v_min_f32_e32 v2, v2, v3
	v_max_f32_e32 v3, v40, v5
	v_min_f32_e32 v5, v40, v5
	v_max_f32_e32 v40, v6, v7
	v_min_f32_e32 v6, v6, v7
	v_max_f32_e32 v7, v9, v9
	v_and_or_b32 v52, v52, s3, 20
	v_and_or_b32 v23, v23, s3, 21
	v_and_or_b32 v30, v30, s3, 22
	v_and_or_b32 v24, v24, s3, 23
	v_max_f32_e32 v51, v50, v49
	v_min_f32_e32 v49, v50, v49
	v_max_f32_e32 v9, v8, v7
	v_min_f32_e32 v7, v8, v7
	v_max_f32_e32 v50, v58, v51
	v_min_f32_e32 v51, v58, v51
	v_max_f32_e32 v58, v48, v49
	v_max_f32_e32 v8, v40, v9
	v_min_f32_e32 v9, v40, v9
	v_max_f32_e32 v40, v6, v7
	v_min_f32_e32 v48, v48, v49
	v_max_f32_e32 v49, v58, v51
	v_min_f32_e32 v51, v58, v51
	v_max_f32_e32 v58, v52, v23
	v_min_f32_e32 v23, v52, v23
	v_max_f32_e32 v52, v30, v24
	v_min_f32_e32 v24, v30, v24
	v_min_f32_e32 v6, v6, v7
	v_max_f32_e32 v7, v40, v9
	v_min_f32_e32 v9, v40, v9
	v_max_f32_e32 v30, v58, v52
	v_min_f32_e32 v52, v58, v52
	v_max_f32_e32 v58, v23, v24
	v_max_f32_e32 v40, v4, v8
	v_min_f32_e32 v4, v4, v8
	v_max_f32_e32 v8, v5, v9
	v_min_f32_e32 v23, v23, v24
	v_max_f32_e32 v24, v58, v52
	v_min_f32_e32 v52, v58, v52
	v_and_b32_e32 v25, 0xffffff80, v78
	v_add_f32_e32 v10, v19, v13
	v_min_f32_e32 v5, v5, v9
	v_max_f32_e32 v9, v8, v4
	v_min_f32_e32 v4, v8, v4
	v_max_f32_e32 v8, v3, v7
	v_min_f32_e32 v3, v3, v7
	v_max_f32_e32 v7, v2, v6
	v_max_f32_e32 v58, v50, v30
	v_min_f32_e32 v30, v50, v30
	v_max_f32_e32 v50, v51, v52
	v_and_or_b32 v10, v10, s3, 8
	v_and_or_b32 v11, v11, s3, 9
	v_add_f32_e32 v13, v19, v34
	v_min_f32_e32 v2, v2, v6
	v_max_f32_e32 v6, v7, v3
	v_min_f32_e32 v3, v7, v3
	v_add_f32_e32 v32, v25, v17
	v_add_f32_e32 v53, v25, v18
	v_min_f32_e32 v51, v51, v52
	v_max_f32_e32 v52, v50, v30
	v_min_f32_e32 v30, v50, v30
	v_max_f32_e32 v50, v49, v24
	v_min_f32_e32 v24, v49, v24
	v_max_f32_e32 v49, v48, v23
	v_and_or_b32 v13, v13, s3, 10
	v_and_or_b32 v15, v15, s3, 11
	v_max_f32_e32 v7, v8, v9
	v_min_f32_e32 v8, v8, v9
	v_max_f32_e32 v9, v6, v4
	v_min_f32_e32 v4, v6, v4
	v_max_f32_e32 v6, v3, v5
	v_min_f32_e32 v3, v3, v5
	v_max_f32_e32 v5, v11, v11
	v_and_or_b32 v32, v32, s3, 32
	v_and_or_b32 v53, v53, s3, 33
	v_add_f32_e32 v54, v25, v26
	v_add_f32_e32 v55, v25, v28
	v_min_f32_e32 v23, v48, v23
	v_max_f32_e32 v48, v49, v24
	v_min_f32_e32 v24, v49, v24
	v_and_b32_e32 v27, 0xffffff80, v79
	v_and_b32_e32 v38, 0xffffff80, v0
	v_max_f32_e32 v11, v10, v5
	v_min_f32_e32 v5, v10, v5
	v_max_f32_e32 v10, v15, v15
; #define CE(a, b) do { const float hi_ = fmaxf(a, b), lo_ = fminf(a, b); a = hi_; b = lo_; } while (0)
; __device__ __forceinline__ void sort16_desc(float (&v)[16]) {
;     CE(v[0], v[1]); CE(v[2], v[3]); CE(v[0], v[2]); CE(v[1], v[3]);
;     CE(v[1], v[2]); CE(v[4], v[5]); CE(v[6], v[7]); CE(v[4], v[6]);
;     CE(v[5], v[7]); CE(v[5], v[6]); CE(v[0], v[4]); CE(v[2], v[6]);
;     CE(v[2], v[4]); CE(v[1], v[5]); CE(v[3], v[7]); CE(v[3], v[5]);
;     CE(v[1], v[2]); CE(v[3], v[4]); CE(v[5], v[6]); CE(v[8], v[9]);
;     CE(v[10], v[11]); CE(v[8], v[10]); CE(v[9], v[11]); CE(v[9], v[10]);
;     CE(v[12], v[13]); CE(v[14], v[15]); CE(v[12], v[14]); CE(v[13], v[15]);
;     CE(v[13], v[14]); CE(v[8], v[12]); CE(v[10], v[14]); CE(v[10], v[12]);
;     CE(v[9], v[13]); CE(v[11], v[15]); CE(v[11], v[13]); CE(v[9], v[10]);
;     CE(v[11], v[12]); CE(v[13], v[14]); CE(v[0], v[8]); CE(v[4], v[12]);
;     CE(v[4], v[8]); CE(v[2], v[10]); CE(v[6], v[14]); CE(v[6], v[10]);
;     CE(v[2], v[4]); CE(v[6], v[8]); CE(v[10], v[12]); CE(v[1], v[9]);
;     CE(v[5], v[13]); CE(v[5], v[9]); CE(v[3], v[11]); CE(v[7], v[15]);
;     CE(v[7], v[11]); CE(v[3], v[5]); CE(v[7], v[9]); CE(v[11], v[13]);
;     CE(v[1], v[2]); CE(v[3], v[4]); CE(v[5], v[6]); CE(v[7], v[8]);
;     CE(v[9], v[10]); CE(v[11], v[12]); CE(v[13], v[14]);
; }
	v_and_or_b32 v54, v54, s3, 34
	v_and_or_b32 v55, v55, s3, 35
	v_max_f32_e32 v49, v50, v52
	v_min_f32_e32 v50, v50, v52
	v_max_f32_e32 v52, v48, v30
	v_min_f32_e32 v30, v48, v30
	v_max_f32_e32 v48, v24, v51
	v_min_f32_e32 v24, v24, v51
	v_max_f32_e32 v51, v53, v53
	v_add_f32_e32 v34, v19, v38
	v_max_f32_e32 v15, v13, v10
	v_min_f32_e32 v10, v13, v10
	v_add_f32_e32 v21, v25, v21
	v_add_f32_e32 v25, v27, v17
	v_max_f32_e32 v53, v32, v51
	v_min_f32_e32 v32, v32, v51
	v_max_f32_e32 v51, v55, v55
	v_and_or_b32 v34, v34, s3, 12
	v_and_or_b32 v36, v36, s3, 13
	v_add_f32_e32 v38, v19, v41
	v_add_f32_e32 v19, v19, v42
	v_max_f32_e32 v13, v11, v15
	v_min_f32_e32 v11, v11, v15
	v_max_f32_e32 v15, v5, v10
	v_and_or_b32 v21, v21, s3, 36
	v_and_or_b32 v25, v25, s3, 48
	v_add_f32_e32 v56, v27, v18
	v_add_f32_e32 v57, v27, v26
	v_max_f32_e32 v55, v54, v51
	v_min_f32_e32 v51, v54, v51
	v_and_or_b32 v38, v38, s3, 14
	v_and_or_b32 v19, v19, s3, 15
	v_min_f32_e32 v5, v5, v10
	v_max_f32_e32 v10, v15, v11
	v_min_f32_e32 v11, v15, v11
	v_max_f32_e32 v15, v36, v36
	v_and_or_b32 v56, v56, s3, 49
	v_and_or_b32 v57, v57, s3, 50
	v_max_f32_e32 v54, v53, v55
	v_min_f32_e32 v53, v53, v55
	v_max_f32_e32 v55, v32, v51
	v_max_f32_e32 v36, v34, v15
	v_min_f32_e32 v15, v34, v15
	v_max_f32_e32 v34, v38, v38
	v_min_f32_e32 v32, v32, v51
	v_max_f32_e32 v51, v55, v53
	v_min_f32_e32 v53, v55, v53
	v_max_f32_e32 v55, v21, v25
	v_min_f32_e32 v21, v21, v25
	v_max_f32_e32 v25, v57, v57
	v_max_f32_e32 v38, v34, v19
	v_min_f32_e32 v19, v34, v19
	v_max_f32_e32 v57, v56, v25
	v_min_f32_e32 v25, v56, v25
	v_max_f32_e32 v34, v36, v38
	v_min_f32_e32 v36, v36, v38
	v_max_f32_e32 v38, v15, v19
	v_max_f32_e32 v56, v55, v57
	v_min_f32_e32 v55, v55, v57
	v_max_f32_e32 v57, v21, v25
	v_min_f32_e32 v15, v15, v19
	v_max_f32_e32 v19, v38, v36
	v_min_f32_e32 v36, v38, v36
	v_min_f32_e32 v21, v21, v25
	v_max_f32_e32 v25, v57, v55
	v_min_f32_e32 v55, v57, v55
	v_max_f32_e32 v38, v13, v34
	v_min_f32_e32 v13, v13, v34
	v_max_f32_e32 v34, v11, v36
	v_max_f32_e32 v57, v54, v56
	v_min_f32_e32 v54, v54, v56
	v_max_f32_e32 v56, v53, v55
	v_min_f32_e32 v11, v11, v36
	v_max_f32_e32 v36, v34, v13
	v_min_f32_e32 v13, v34, v13
	v_max_f32_e32 v34, v10, v19
	v_min_f32_e32 v10, v10, v19
	v_max_f32_e32 v19, v5, v15
	v_min_f32_e32 v53, v53, v55
	v_max_f32_e32 v55, v56, v54
	v_min_f32_e32 v54, v56, v54
	v_max_f32_e32 v56, v51, v25
	v_min_f32_e32 v25, v51, v25
	v_max_f32_e32 v51, v32, v21
	v_min_f32_e32 v5, v5, v15
	v_max_f32_e32 v15, v19, v10
	v_min_f32_e32 v21, v32, v21
	v_max_f32_e32 v32, v51, v25
	v_min_f32_e32 v10, v19, v10
	v_max_f32_e32 v19, v34, v36
	v_min_f32_e32 v34, v34, v36
	v_max_f32_e32 v36, v15, v13
	v_min_f32_e32 v13, v15, v13
	v_min_f32_e32 v25, v51, v25
	v_max_f32_e32 v51, v56, v55
	v_min_f32_e32 v55, v56, v55
	v_max_f32_e32 v56, v32, v54
	v_min_f32_e32 v32, v32, v54
	v_max_f32_e32 v15, v10, v11
	v_min_f32_e32 v10, v10, v11
	v_min_f32_e32 v11, v40, v38
	v_max_f32_e32 v41, v4, v13
	v_max_f32_e32 v54, v25, v53
	v_min_f32_e32 v25, v25, v53
	v_min_f32_e32 v53, v58, v57
	v_max_f32_e32 v59, v30, v32
	v_min_f32_e32 v4, v4, v13
	v_max_f32_e32 v13, v41, v11
	v_min_f32_e32 v11, v41, v11
	v_max_f32_e32 v41, v8, v34
	v_min_f32_e32 v8, v8, v34
	v_max_f32_e32 v34, v3, v10
	v_min_f32_e32 v30, v30, v32
	v_max_f32_e32 v32, v59, v53
	v_min_f32_e32 v53, v59, v53
	v_max_f32_e32 v59, v50, v55
	v_min_f32_e32 v50, v50, v55
	v_max_f32_e32 v55, v24, v25
	v_min_f32_e32 v3, v3, v10
	v_max_f32_e32 v10, v34, v8
	v_min_f32_e32 v8, v34, v8
	v_min_f32_e32 v24, v24, v25
	v_max_f32_e32 v25, v55, v50
	v_min_f32_e32 v50, v55, v50
	v_max_f32_e32 v34, v41, v13
	v_min_f32_e32 v13, v41, v13
	v_max_f32_e32 v41, v10, v11
	v_min_f32_e32 v10, v10, v11
	v_max_f32_e32 v11, v8, v4
	v_min_f32_e32 v4, v8, v4
	v_max_f32_e32 v8, v7, v19
	v_min_f32_e32 v7, v7, v19
	v_max_f32_e32 v19, v6, v15
	v_max_f32_e32 v55, v59, v32
	v_min_f32_e32 v32, v59, v32
	v_max_f32_e32 v59, v25, v53
	v_min_f32_e32 v25, v25, v53
	v_max_f32_e32 v53, v50, v30
	v_min_f32_e32 v30, v50, v30
	v_max_f32_e32 v50, v49, v51
	v_min_f32_e32 v49, v49, v51
	v_max_f32_e32 v51, v48, v54
	v_min_f32_e32 v6, v6, v15
	v_max_f32_e32 v15, v19, v7
	v_min_f32_e32 v7, v19, v7
	v_max_f32_e32 v19, v9, v36
	v_min_f32_e32 v9, v9, v36
	v_max_f32_e32 v36, v2, v5
	v_min_f32_e32 v48, v48, v54
	v_max_f32_e32 v54, v51, v49
	v_min_f32_e32 v49, v51, v49
	v_max_f32_e32 v51, v52, v56
	v_min_f32_e32 v52, v52, v56
	v_max_f32_e32 v56, v23, v21
	v_min_f32_e32 v2, v2, v5
	v_max_f32_e32 v5, v36, v9
	v_min_f32_e32 v9, v36, v9
	v_max_f32_e32 v36, v19, v15
	v_min_f32_e32 v21, v23, v21
	v_max_f32_e32 v23, v56, v52
	v_min_f32_e32 v52, v56, v52
	v_and_b32_e32 v20, 0xffffff80, v72
	v_min_f32_e32 v15, v19, v15
	v_max_f32_e32 v19, v5, v7
	v_min_f32_e32 v5, v5, v7
	v_max_f32_e32 v7, v9, v6
	v_min_f32_e32 v6, v9, v6
	v_min_f32_e32 v9, v8, v34
	v_min_f32_e32 v42, v36, v13
	v_max_f32_e32 v56, v51, v54
	v_min_f32_e32 v51, v51, v54
	v_max_f32_e32 v54, v23, v49
	v_min_f32_e32 v23, v23, v49
	v_max_f32_e32 v49, v52, v48
	v_min_f32_e32 v48, v52, v48
	v_and_b32_e32 v39, 0xffffff80, v65
	v_min_f32_e32 v65, v48, v24
	v_max3_f32 v9, v9, v48, v24
	v_max3_f32 v24, v42, v49, v30
	v_add_f32_e32 v27, v27, v28
	v_add_f32_e32 v28, v20, v17
	v_add_f32_e32 v42, v20, v18
	v_add_f32_e32 v20, v20, v26
	v_and_b32_e32 v22, 0xffffff80, v73
	v_and_or_b32 v27, v27, s3, 51
	v_and_or_b32 v28, v28, s3, 64
	v_and_b32_e32 v42, 0xffffff00, v42
	v_and_b32_e32 v20, 0xffffff00, v20
	v_and_b32_e32 v29, 0xffffff80, v74
	v_and_b32_e32 v31, 0xffffff80, v75
	v_and_b32_e32 v33, 0xffffff80, v70
	v_and_b32_e32 v35, 0xffffff80, v71
	v_and_b32_e32 v37, 0xffffff80, v64
;     __device__ __forceinline__ void fused(f32x4 (&acc)[2][2][4][2], const Unit& u, int wr, int wc, int fr, int fq, PG8_LAS unsigned char* lds, int wid, int lane) const {
;     ...
;             { float cv[16]; cv[0] = __uint_as_float((__float_as_uint(v0[0] + v1[0]) & ~255u) | 0u); cv[1] = __uint_as_float((__float_as_uint(v0[0] + v1[1]) & ~255u) | 1u); cv[2] = __uint_as_float((__float_as_uint(v0[0] + v1[2]) & ~255u) | 2u); cv[3] = __uint_as_float((__float_as_uint(v0[0] + v1[3]) & ~255u) | 3u); cv[4] = __uint_as_float((__float_as_uint(v0[0] + v1[4]) & ~255u) | 4u); cv[5] = __uint_as_float((__float_as_uint(v0[0] + v1[5]) & ~255u) | 5u); cv[6] = __uint_as_float((__float_as_uint(v0[0] + v1[6]) & ~255u) | 6u); cv[7] = __uint_as_float((__float_as_uint(v0[0] + v1[7]) & ~255u) | 7u); cv[8] = __uint_as_float((__float_as_uint(v0[0] + v1[8]) & ~255u) | 8u); cv[9] = __uint_as_float((__float_as_uint(v0[0] + v1[9]) & ~255u) | 9u); cv[10] = __uint_as_float((__float_as_uint(v0[0] + v1[10]) & ~255u) | 10u); cv[11] = __uint_as_float((__float_as_uint(v0[0] + v1[11]) & ~255u) | 11u); cv[12] = __uint_as_float((__float_as_uint(v0[0] + v1[12]) & ~255u) | 12u); cv[13] = __uint_as_float((__float_as_uint(v0[0] + v1[13]) & ~255u) | 13u); cv[14] = __uint_as_float((__float_as_uint(v0[0] + v1[14]) & ~255u) | 14u); cv[15] = __uint_as_float((__float_as_uint(v0[0] + v1[15]) & ~255u) | 15u); sort16_desc(cv);
; #pragma unroll
;               for (int q = 0; q < 16; ++q) best[q] = cv[q]; }
	v_min_f32_e32 v43, v15, v41
	v_min_f32_e32 v44, v19, v10
	v_min_f32_e32 v62, v54, v25
	v_or_b32_e32 v42, 0x41, v42
	v_or_b32_e32 v20, 0x42, v20
	v_add_f32_e32 v26, v22, v17
	v_add_f32_e32 v22, v22, v18
	v_min_f32_e32 v63, v23, v53
	v_max3_f32 v23, v43, v23, v53
	v_max3_f32 v10, v19, v10, v62
	v_max3_f32 v19, v44, v54, v25
	v_and_b32_e32 v26, 0xffffff00, v26
	v_and_b32_e32 v22, 0xffffff00, v22
	v_add_f32_e32 v43, v29, v17
	v_add_f32_e32 v29, v29, v18
	v_add_f32_e32 v44, v31, v17
	v_add_f32_e32 v18, v31, v18
	v_add_f32_e32 v31, v33, v17
	v_add_f32_e32 v33, v35, v17
	v_add_f32_e32 v35, v37, v17
	v_add_f32_e32 v37, v39, v17
	v_max_f32_e32 v39, v27, v28
	v_min_f32_e32 v27, v27, v28
	v_max_f32_e32 v28, v42, v42
	v_or_b32_e32 v26, 0x50, v26
	v_or_b32_e32 v22, 0x51, v22
	v_and_b32_e32 v43, 0xffffff00, v43
	v_and_b32_e32 v29, 0xffffff00, v29
	v_max_f32_e32 v42, v28, v20
	v_min_f32_e32 v20, v28, v20
	v_or_b32_e32 v43, 0x60, v43
	v_or_b32_e32 v29, 0x61, v29
	v_max_f32_e32 v28, v39, v42
	v_min_f32_e32 v39, v39, v42
	v_max_f32_e32 v42, v27, v20
	v_min_f32_e32 v20, v27, v20
	v_max_f32_e32 v27, v42, v39
	v_min_f32_e32 v39, v42, v39
	v_max_f32_e32 v42, v26, v22
	v_min_f32_e32 v22, v26, v22
	v_max_f32_e32 v26, v29, v29
	v_max_f32_e32 v29, v43, v43
	v_max_f32_e32 v43, v29, v26
	v_min_f32_e32 v26, v29, v26
	v_max_f32_e32 v29, v42, v43
	v_min_f32_e32 v42, v42, v43
	v_max_f32_e32 v43, v22, v26
	v_and_b32_e32 v12, 0xffffff80, v68
	v_and_b32_e32 v14, 0xffffff80, v69
	v_min_f32_e32 v22, v22, v26
	v_max_f32_e32 v26, v43, v42
	v_min_f32_e32 v42, v43, v42
	v_add_f32_e32 v12, v12, v17
	v_add_f32_e32 v14, v14, v17
	v_max_f32_e32 v43, v28, v29
	v_min_f32_e32 v28, v28, v29
	v_max_f32_e32 v29, v39, v42
	v_and_b32_e32 v44, 0xffffff00, v44
	v_and_b32_e32 v18, 0xffffff00, v18
	v_and_b32_e32 v12, 0xffffff00, v12
	v_and_b32_e32 v14, 0xffffff00, v14
	v_min_f32_e32 v39, v39, v42
	v_max_f32_e32 v42, v29, v28
	v_min_f32_e32 v28, v29, v28
	v_max_f32_e32 v29, v27, v26
	v_min_f32_e32 v26, v27, v26
	v_max_f32_e32 v27, v20, v22
	v_or_b32_e32 v44, 0x70, v44
	v_or_b32_e32 v18, 0x71, v18
	v_or_b32_e32 v12, 0x80, v12
	v_or_b32_e32 v14, 0x90, v14
	v_min_f32_e32 v20, v20, v22
	v_max_f32_e32 v22, v27, v26
	v_min_f32_e32 v26, v27, v26
	v_and_b32_e32 v31, 0xffffff00, v31
	v_and_b32_e32 v33, 0xffffff00, v33
	v_max_f32_e32 v27, v29, v42
	v_min_f32_e32 v29, v29, v42
	v_max_f32_e32 v42, v22, v28
	v_min_f32_e32 v22, v22, v28
	v_max_f32_e32 v28, v26, v39
	v_min_f32_e32 v26, v26, v39
	v_max_f32_e32 v39, v44, v44
	v_or_b32_e32 v31, 0xa0, v31
	v_or_b32_e32 v33, 0xb0, v33
	v_and_b32_e32 v35, 0xffffff00, v35
	v_and_b32_e32 v37, 0xffffff00, v37
	v_max_f32_e32 v44, v39, v18
	v_min_f32_e32 v18, v39, v18
	v_max_f32_e32 v39, v12, v14
	v_min_f32_e32 v12, v12, v14
	v_or_b32_e32 v35, 0xc0, v35
	v_or_b32_e32 v37, 0xd0, v37
	v_max_f32_e32 v14, v44, v39
	v_min_f32_e32 v39, v44, v39
	v_max_f32_e32 v44, v18, v12
	v_min_f32_e32 v12, v18, v12
	v_max_f32_e32 v18, v44, v39
	v_min_f32_e32 v39, v44, v39
	v_max_f32_e32 v44, v31, v33
	v_min_f32_e32 v31, v31, v33
	v_max_f32_e32 v33, v37, v37
	v_max_f32_e32 v37, v35, v33
	v_min_f32_e32 v33, v35, v33
	v_max_f32_e32 v35, v44, v37
	v_min_f32_e32 v37, v44, v37
	v_max_f32_e32 v44, v31, v33
	v_min_f32_e32 v31, v31, v33
	v_max_f32_e32 v33, v44, v37
	v_min_f32_e32 v37, v44, v37
	v_max_f32_e32 v44, v14, v35
	v_min_f32_e32 v14, v14, v35
	v_max_f32_e32 v35, v39, v37
	v_min_f32_e32 v37, v39, v37
	v_max_f32_e32 v39, v35, v14
	v_min_f32_e32 v14, v35, v14
	v_max_f32_e32 v35, v18, v33
	v_min_f32_e32 v18, v18, v33
	v_max_f32_e32 v33, v12, v31
	v_min_f32_e32 v12, v12, v31
	v_max_f32_e32 v31, v33, v18
	v_min_f32_e32 v45, v5, v11
	v_min_f32_e32 v61, v51, v59
	v_min_f32_e32 v18, v33, v18
	v_max_f32_e32 v33, v35, v39
	v_min_f32_e32 v35, v35, v39
	v_max_f32_e32 v39, v31, v14
	v_min_f32_e32 v14, v31, v14
	v_max3_f32 v5, v5, v11, v61
	v_max3_f32 v11, v45, v51, v59
	v_max_f32_e32 v31, v18, v37
	v_min_f32_e32 v18, v18, v37
	v_min_f32_e32 v37, v43, v44
	v_max_f32_e32 v45, v22, v14
	v_min_f32_e32 v14, v22, v14
	v_max_f32_e32 v22, v45, v37
	v_min_f32_e32 v37, v45, v37
	v_max_f32_e32 v45, v29, v35
	v_min_f32_e32 v29, v29, v35
	v_max_f32_e32 v35, v26, v18
	v_min_f32_e32 v46, v7, v4
	v_min_f32_e32 v47, v6, v3
	v_min_f32_e32 v52, v50, v55
	v_min_f32_e32 v60, v56, v32
	v_min_f32_e32 v64, v49, v30
	v_min_f32_e32 v18, v26, v18
	v_max_f32_e32 v26, v35, v29
	v_min_f32_e32 v29, v35, v29
	v_max3_f32 v21, v40, v38, v21
	v_max3_f32 v8, v8, v34, v65
	v_max3_f32 v13, v36, v13, v64
	v_max3_f32 v15, v15, v41, v63
	v_max3_f32 v4, v7, v4, v60
	v_max3_f32 v7, v46, v56, v32
	v_max3_f32 v3, v6, v3, v52
	v_max3_f32 v6, v47, v50, v55
	v_max3_f32 v2, v2, v58, v57
	v_max_f32_e32 v35, v45, v22
	v_min_f32_e32 v22, v45, v22
	v_max_f32_e32 v45, v26, v37
	v_min_f32_e32 v26, v26, v37
	v_max_f32_e32 v37, v29, v14
	v_min_f32_e32 v14, v29, v14
	v_max_f32_e32 v29, v27, v33
	v_min_f32_e32 v27, v27, v33
	v_max_f32_e32 v33, v28, v31
	v_max_f32_e32 v25, v21, v19
	v_min_f32_e32 v19, v21, v19
	v_max_f32_e32 v21, v8, v5
	v_min_f32_e32 v5, v8, v5
	v_max_f32_e32 v8, v9, v11
	v_min_f32_e32 v9, v9, v11
	v_max_f32_e32 v11, v13, v4
	v_min_f32_e32 v4, v13, v4
	v_max_f32_e32 v13, v24, v7
	v_min_f32_e32 v7, v24, v7
	v_max_f32_e32 v24, v15, v3
	v_min_f32_e32 v3, v15, v3
	v_max_f32_e32 v15, v23, v6
	v_min_f32_e32 v6, v23, v6
	v_max_f32_e32 v23, v10, v2
	v_min_f32_e32 v2, v10, v2
	v_min_f32_e32 v28, v28, v31
	v_max_f32_e32 v31, v33, v27
	v_min_f32_e32 v27, v33, v27
	v_max_f32_e32 v33, v42, v39
	v_min_f32_e32 v39, v42, v39
	v_max_f32_e32 v42, v20, v12
	v_max_f32_e32 v10, v25, v13
	v_min_f32_e32 v13, v25, v13
	v_max_f32_e32 v25, v21, v24
	v_min_f32_e32 v21, v21, v24
; #define CE(a, b) do { const float hi_ = fmaxf(a, b), lo_ = fminf(a, b); a = hi_; b = lo_; } while (0)
; __device__ __forceinline__ void merge_top16(float (&v)[16], const float (&nw)[16]) {
;     v[0] = fmaxf(v[0], nw[15]); v[1] = fmaxf(v[1], nw[14]); v[2] = fmaxf(v[2], nw[13]); v[3] = fmaxf(v[3], nw[12]); v[4] = fmaxf(v[4], nw[11]); v[5] = fmaxf(v[5], nw[10]); v[6] = fmaxf(v[6], nw[9]); v[7] = fmaxf(v[7], nw[8]); v[8] = fmaxf(v[8], nw[7]); v[9] = fmaxf(v[9], nw[6]); v[10] = fmaxf(v[10], nw[5]); v[11] = fmaxf(v[11], nw[4]); v[12] = fmaxf(v[12], nw[3]); v[13] = fmaxf(v[13], nw[2]); v[14] = fmaxf(v[14], nw[1]); v[15] = fmaxf(v[15], nw[0]);
;     CE(v[0], v[8]); CE(v[1], v[9]); CE(v[2], v[10]); CE(v[3], v[11]);
;     CE(v[4], v[12]); CE(v[5], v[13]); CE(v[6], v[14]); CE(v[7], v[15]);
;     CE(v[0], v[4]); CE(v[1], v[5]); CE(v[2], v[6]); CE(v[3], v[7]);
;     CE(v[8], v[12]); CE(v[9], v[13]); CE(v[10], v[14]); CE(v[11], v[15]);
;     CE(v[0], v[2]); CE(v[1], v[3]); CE(v[4], v[6]); CE(v[5], v[7]);
;     CE(v[8], v[10]); CE(v[9], v[11]); CE(v[12], v[14]); CE(v[13], v[15]);
;     CE(v[0], v[1]); CE(v[2], v[3]); CE(v[4], v[5]); CE(v[6], v[7]);
;     CE(v[8], v[9]); CE(v[10], v[11]); CE(v[12], v[13]); CE(v[14], v[15]);
; }
;     __device__ __forceinline__ void fused(f32x4 (&acc)[2][2][4][2], const Unit& u, int wr, int wc, int fr, int fq, PG8_LAS unsigned char* lds, int wid, int lane) const {
;     ...
;             { float cv[16]; cv[0] = __uint_as_float((__float_as_uint(v0[14] + v1[0]) & ~255u) | 224u); cv[1] = __uint_as_float((__float_as_uint(v0[15] + v1[0]) & ~255u) | 240u); cv[2] = -INFINITY; cv[3] = -INFINITY; cv[4] = -INFINITY; cv[5] = -INFINITY; cv[6] = -INFINITY; cv[7] = -INFINITY; cv[8] = -INFINITY; cv[9] = -INFINITY; cv[10] = -INFINITY; cv[11] = -INFINITY; cv[12] = -INFINITY; cv[13] = -INFINITY; cv[14] = -INFINITY; cv[15] = -INFINITY; sort16_desc(cv); merge_top16(best, cv); }
;             float sc[16], sum = 0.f;
; #pragma unroll
;             for (int q = 0; q < 16; ++q) { sc[q] = __uint_as_float(__float_as_uint(best[q]) & ~255u); }
;             const float smax = sc[0];
; #pragma unroll
;             for (int q = 0; q < 16; ++q) { sc[q] = __builtin_amdgcn_exp2f((sc[q] - smax) * 1.4426950408889634f); }
	v_max_f32_e32 v24, v8, v15
	v_min_f32_e32 v8, v8, v15
	v_max_f32_e32 v15, v11, v23
	v_min_f32_e32 v11, v11, v23
	v_max_f32_e32 v23, v19, v7
	v_min_f32_e32 v7, v19, v7
	v_max_f32_e32 v19, v5, v3
	v_min_f32_e32 v3, v5, v3
	v_max_f32_e32 v5, v9, v6
	v_min_f32_e32 v6, v9, v6
	v_max_f32_e32 v9, v4, v2
	v_min_f32_e32 v2, v4, v2
	v_min_f32_e32 v12, v20, v12
	v_max_f32_e32 v20, v42, v39
	v_min_f32_e32 v39, v42, v39
	v_and_b32_e32 v1, 0xffffff80, v66
	v_and_b32_e32 v0, 0xffffff80, v67
	v_max_f32_e32 v4, v10, v24
	v_min_f32_e32 v10, v10, v24
	v_max_f32_e32 v24, v25, v15
	v_min_f32_e32 v15, v25, v15
	v_max_f32_e32 v25, v13, v8
	v_min_f32_e32 v8, v13, v8
	v_max_f32_e32 v13, v21, v11
	v_min_f32_e32 v11, v21, v11
	v_max_f32_e32 v21, v23, v5
	v_min_f32_e32 v5, v23, v5
	v_max_f32_e32 v23, v19, v9
	v_min_f32_e32 v9, v19, v9
	v_max_f32_e32 v19, v7, v6
	v_min_f32_e32 v6, v7, v6
	v_max_f32_e32 v7, v3, v2
	v_min_f32_e32 v2, v3, v2
	v_max_f32_e32 v42, v33, v31
	v_min_f32_e32 v31, v33, v31
	v_max_f32_e32 v33, v20, v27
	v_min_f32_e32 v20, v20, v27
	v_max_f32_e32 v27, v39, v28
	v_min_f32_e32 v28, v39, v28
	v_min_f32_e32 v3, v4, v24
	v_min_f32_e32 v30, v10, v15
	v_min_f32_e32 v32, v25, v13
	v_min_f32_e32 v34, v8, v11
	v_min_f32_e32 v36, v21, v23
	v_min_f32_e32 v38, v5, v9
	v_min_f32_e32 v40, v19, v7
	v_min_f32_e32 v41, v6, v2
	v_max_f32_e32 v39, v29, v35
	v_min_f32_e32 v29, v29, v35
	v_max_f32_e32 v35, v42, v22
	v_min_f32_e32 v22, v42, v22
	v_max_f32_e32 v42, v31, v45
	v_min_f32_e32 v31, v31, v45
	v_max_f32_e32 v45, v33, v26
	v_min_f32_e32 v26, v33, v26
	v_max_f32_e32 v33, v20, v37
	v_min_f32_e32 v20, v20, v37
	v_max_f32_e32 v37, v27, v14
	v_min_f32_e32 v14, v27, v14
	v_max_f32_e32 v27, v28, v18
	v_min_f32_e32 v18, v28, v18
	v_add_f32_e32 v1, v1, v17
	v_add_f32_e32 v0, v0, v17
	v_max3_f32 v4, v4, v24, v12
	v_max_f32_e32 v3, v3, v18
	v_max3_f32 v10, v10, v15, v27
	v_max_f32_e32 v12, v30, v14
	v_max3_f32 v13, v25, v13, v37
	v_max_f32_e32 v14, v32, v20
	v_max3_f32 v8, v8, v11, v33
	v_max_f32_e32 v11, v34, v26
	v_max3_f32 v15, v21, v23, v45
	v_max_f32_e32 v18, v36, v31
	v_max3_f32 v5, v5, v9, v42
	v_max_f32_e32 v9, v38, v22
	v_max3_f32 v7, v19, v7, v35
	v_max_f32_e32 v19, v40, v29
	v_max3_f32 v2, v6, v2, v39
	v_max3_f32 v6, v41, v43, v44
	v_and_b32_e32 v1, 0xffffff00, v1
	v_and_b32_e32 v0, 0xffffff00, v0
	v_max_f32_e32 v20, v4, v15
	v_min_f32_e32 v4, v4, v15
	v_max_f32_e32 v15, v3, v18
	v_min_f32_e32 v3, v3, v18
	v_max_f32_e32 v18, v10, v5
	v_min_f32_e32 v5, v10, v5
	v_max_f32_e32 v10, v12, v9
	v_min_f32_e32 v9, v12, v9
	v_max_f32_e32 v12, v13, v7
	v_min_f32_e32 v7, v13, v7
	v_max_f32_e32 v13, v14, v19
	v_min_f32_e32 v14, v14, v19
	v_max_f32_e32 v19, v8, v2
	v_min_f32_e32 v2, v8, v2
	v_max_f32_e32 v8, v11, v6
	v_min_f32_e32 v6, v11, v6
	v_or_b32_e32 v1, 0xe0, v1
	v_or_b32_e32 v0, 0xf0, v0
	v_max_f32_e32 v11, v20, v12
	v_min_f32_e32 v12, v20, v12
	v_max_f32_e32 v20, v15, v13
	v_min_f32_e32 v13, v15, v13
	v_max_f32_e32 v15, v18, v19
	v_min_f32_e32 v18, v18, v19
	v_max_f32_e32 v19, v10, v8
	v_min_f32_e32 v8, v10, v8
	v_max_f32_e32 v10, v4, v7
	v_min_f32_e32 v4, v4, v7
	v_max_f32_e32 v7, v3, v14
	v_min_f32_e32 v3, v3, v14
	v_max_f32_e32 v14, v5, v2
	v_min_f32_e32 v2, v5, v2
	v_max_f32_e32 v5, v9, v6
	v_min_f32_e32 v6, v9, v6
	v_max_f32_e32 v9, v11, v15
	v_min_f32_e32 v11, v11, v15
	v_max_f32_e32 v15, v20, v19
	v_min_f32_e32 v19, v20, v19
	v_max_f32_e32 v20, v12, v18
	v_min_f32_e32 v12, v12, v18
	v_max_f32_e32 v18, v13, v8
	v_min_f32_e32 v8, v13, v8
	v_max_f32_e32 v13, v10, v14
	v_min_f32_e32 v10, v10, v14
	v_max_f32_e32 v14, v7, v5
	v_min_f32_e32 v5, v7, v5
	v_max_f32_e32 v7, v4, v2
	v_min_f32_e32 v2, v4, v2
	v_max_f32_e32 v4, v3, v6
	v_min_f32_e32 v3, v3, v6
	v_max_f32_e32 v17, v1, v0
	v_min_f32_e32 v0, v1, v0
	v_min_f32_e32 v6, v9, v15
	v_min_f32_e32 v21, v11, v19
	v_min_f32_e32 v22, v20, v18
	v_min_f32_e32 v23, v12, v8
	v_min_f32_e32 v24, v13, v14
	v_min_f32_e32 v25, v10, v5
	v_min_f32_e32 v26, v7, v4
	v_min_f32_e32 v27, v2, v3
	s_mov_b32 s3, 0xff800000
	v_max_f32_e32 v0, 0xff800000, v0
	v_max3_f32 v1, v9, v15, s3
	v_max_f32_e32 v6, 0xff800000, v6
	v_max3_f32 v9, v11, v19, s3
	v_max_f32_e32 v11, 0xff800000, v21
	v_max3_f32 v15, v20, v18, s3
	v_max_f32_e32 v18, 0xff800000, v22
	v_max3_f32 v8, v12, v8, s3
	v_max_f32_e32 v12, 0xff800000, v23
	v_max3_f32 v13, v13, v14, s3
	v_max_f32_e32 v14, 0xff800000, v24
	v_max3_f32 v5, v10, v5, s3
	v_max_f32_e32 v10, 0xff800000, v25
	v_max3_f32 v4, v7, v4, s3
	v_max_f32_e32 v7, 0xff800000, v26
	v_max3_f32 v0, v2, v3, v0
	v_max3_f32 v2, v27, v17, s3
	v_max_f32_e32 v3, v1, v13
	v_min_f32_e32 v1, v1, v13
	v_max_f32_e32 v13, v6, v14
	v_min_f32_e32 v6, v6, v14
	v_max_f32_e32 v14, v9, v5
	v_min_f32_e32 v5, v9, v5
	v_max_f32_e32 v9, v11, v10
	v_min_f32_e32 v10, v11, v10
	v_max_f32_e32 v11, v15, v4
	v_min_f32_e32 v4, v15, v4
	v_max_f32_e32 v15, v18, v7
	v_max_f32_e32 v17, v8, v0
	v_min_f32_e32 v0, v8, v0
	v_max_f32_e32 v8, v12, v2
	v_min_f32_e32 v2, v12, v2
	v_max_f32_e32 v12, v3, v11
	v_min_f32_e32 v3, v3, v11
	v_max_f32_e32 v11, v13, v15
	v_min_f32_e32 v13, v13, v15
	v_max_f32_e32 v15, v14, v17
	v_min_f32_e32 v14, v14, v17
	v_max_f32_e32 v17, v9, v8
	v_min_f32_e32 v8, v9, v8
	v_max_f32_e32 v9, v1, v4
	v_min_f32_e32 v24, v1, v4
	v_max_f32_e32 v27, v5, v0
	v_min_f32_e32 v28, v5, v0
	v_max_f32_e32 v29, v10, v2
	v_min_f32_e32 v30, v10, v2
	v_max_f32_e32 v0, v12, v15
	v_min_f32_e32 v1, v12, v15
	v_max_f32_e32 v2, v11, v17
	v_min_f32_e32 v4, v11, v17
	v_min_f32_e32 v7, v18, v7
	v_max_f32_e32 v33, v0, v2
	v_min_f32_e32 v34, v0, v2
	v_min_f32_e32 v36, v1, v4
	v_max_f32_e32 v25, v6, v7
	v_min_f32_e32 v26, v6, v7
	v_max_f32_e32 v35, v1, v4
	v_lshrrev_b32_e32 v0, 2, v33
	v_lshrrev_b32_e32 v2, 2, v34
	v_lshrrev_b32_e32 v6, 2, v36
	v_max_f32_e32 v17, v3, v14
	v_min_f32_e32 v31, v3, v14
	v_and_b32_e32 v0, 60, v0
	v_and_b32_e32 v1, 15, v33
	v_and_b32_e32 v2, 60, v2
	v_and_b32_e32 v3, 15, v34
	v_lshrrev_b32_e32 v4, 2, v35
	v_and_b32_e32 v5, 15, v35
	v_and_b32_e32 v6, 60, v6
	v_and_b32_e32 v7, 15, v36
	s_waitcnt lgkmcnt(0)
; #define RT_PK(q_) (ex[q_] | (int)((__float_as_uint(usc[ex[q_]]) >> 23) << 14))
;     __device__ __forceinline__ void fused(f32x4 (&acc)[2][2][4][2], const Unit& u, int wr, int wc, int fr, int fq, PG8_LAS unsigned char* lds, int wid, int lane) const {
;     ...
;             for (int q = 0; q < 16; ++q) { sc[q] = __uint_as_float(__float_as_uint(best[q]) & ~255u); }
;             const float smax = sc[0];
; #pragma unroll
;             for (int q = 0; q < 16; ++q) { sc[q] = __builtin_amdgcn_exp2f((sc[q] - smax) * 1.4426950408889634f); }
; #pragma unroll
;             for (int q = 0; q < 16; ++q) sum += sc[q];
;             const float rs = 1.0f / sum;
;             asm volatile("s_waitcnt lgkmcnt(0)" ::: "memory");
;             int ex[16];
; #pragma unroll
;             for (int q = 0; q < 16; ++q) { const unsigned cid = __float_as_uint(best[q]) & 255u; ex[q] = idxl[cid >> 4] * 128 + idxl[16 + (cid & 15u)]; }
;             const size_t o = ((size_t)u.pn * 16384 + (size_t)(u.pm * BM + row)) * 16;
;             typedef int i32x4 __attribute__((ext_vector_type(4)));
; #pragma unroll
;             for (int i = 0; i < 4; ++i) {
;     ...
;                 *(i32x4*)(eidx + o + 4 * i) = (i32x4){RT_PK(4 * i), RT_PK(4 * i + 1), RT_PK(4 * i + 2), RT_PK(4 * i + 3)};
;                 *(f32x4*)(egate + o + 4 * i) = (f32x4){sc[4 * i] * rs * vsc[ex[4 * i]], sc[4 * i + 1] * rs * vsc[ex[4 * i + 1]], sc[4 * i + 2] * rs * vsc[ex[4 * i + 2]], sc[4 * i + 3] * rs * vsc[ex[4 * i + 3]]};
	v_add_u32_e32 v0, v16, v0
	v_lshl_add_u32 v1, v1, 2, v16
	v_add_u32_e32 v2, v16, v2
	v_lshl_add_u32 v3, v3, 2, v16
	v_and_b32_e32 v4, 60, v4
	v_lshl_add_u32 v5, v5, 2, v16
	v_add_u32_e32 v6, v16, v6
	v_lshl_add_u32 v7, v7, 2, v16
	v_add_u32_e32 v4, v16, v4
	ds_read_b32 v0, v0
	ds_read_b32 v1, v1 offset:64
	ds_read_b32 v2, v2
	ds_read_b32 v3, v3 offset:64
	ds_read_b32 v10, v4
	ds_read_b32 v5, v5 offset:64
	ds_read_b32 v6, v6
	ds_read_b32 v7, v7 offset:64
	s_waitcnt lgkmcnt(0)
	v_lshl_add_u32 v0, v0, 7, v1
	v_ashrrev_i32_e32 v1, 31, v0
	v_lshl_add_u32 v4, v2, 7, v3
	v_lshlrev_b64 v[14:15], 3, v[0:1]
	v_lshl_add_u32 v10, v10, 7, v5
	v_lshl_add_u32 v12, v6, 7, v7
	v_lshl_add_u64 v[2:3], s[8:9], 0, v[14:15]
	v_ashrrev_i32_e32 v5, 31, v4
	v_max_f32_e32 v32, v13, v8
	v_min_f32_e32 v8, v13, v8
	v_mov_b32_e32 v243, 0x18000
	v_lshl_add_u32 v242, v0, 1, v243
	ds_read_u16 v170, v242
	v_lshlrev_b64 v[18:19], 3, v[4:5]
	v_ashrrev_i32_e32 v11, 31, v10
	v_ashrrev_i32_e32 v13, 31, v12
	v_lshl_add_u64 v[2:3], s[8:9], 0, v[18:19]
	v_lshlrev_b64 v[20:21], 3, v[10:11]
	v_lshlrev_b64 v[22:23], 3, v[12:13]
	v_lshl_add_u64 v[6:7], s[8:9], 0, v[20:21]
	v_lshl_add_u32 v242, v4, 1, v243
	ds_read_u16 v172, v242
	v_lshl_add_u32 v242, v10, 1, v243
	ds_read_u16 v174, v242
	v_lshl_add_u64 v[2:3], s[8:9], 0, v[22:23]
	v_lshl_add_u32 v242, v12, 1, v243
	ds_read_u16 v176, v242
	v_min_f32_e32 v2, v9, v27
	v_min_f32_e32 v6, v25, v29
	v_max_f32_e32 v43, v2, v6
	v_min_f32_e32 v44, v2, v6
	v_and_b32_e32 v2, 0xffffff00, v34
	v_and_b32_e32 v51, 0xffffff00, v33
	v_max_f32_e32 v37, v9, v27
	v_max_f32_e32 v3, v25, v29
	v_sub_f32_e32 v2, v2, v51
	v_min_f32_e32 v9, v24, v28
	v_min_f32_e32 v25, v26, v30
	v_max_f32_e32 v41, v37, v3
	v_min_f32_e32 v42, v37, v3
	v_and_b32_e32 v3, 0xffffff00, v35
	v_mul_f32_e32 v2, 0x3fb8aa3b, v2
	v_max_f32_e32 v47, v9, v25
	v_min_f32_e32 v48, v9, v25
	v_exp_f32_e32 v25, v2
	v_sub_f32_e32 v2, v3, v51
	v_and_b32_e32 v6, 0xffffff00, v36
	v_mul_f32_e32 v2, 0x3fb8aa3b, v2
	v_max_f32_e32 v7, v24, v28
	v_max_f32_e32 v24, v26, v30
	v_max_f32_e32 v38, v17, v32
	v_exp_f32_e32 v26, v2
	v_sub_f32_e32 v2, v6, v51
	v_max_f32_e32 v45, v7, v24
	v_min_f32_e32 v46, v7, v24
	v_and_b32_e32 v7, 0xffffff00, v38
	v_mul_f32_e32 v2, 0x3fb8aa3b, v2
	v_min_f32_e32 v17, v17, v32
	v_exp_f32_e32 v27, v2
	v_sub_f32_e32 v2, v7, v51
	v_max_f32_e32 v39, v31, v8
	v_min_f32_e32 v40, v31, v8
	v_and_b32_e32 v8, 0xffffff00, v17
	v_mul_f32_e32 v2, 0x3fb8aa3b, v2
	v_exp_f32_e32 v28, v2
	v_sub_f32_e32 v2, v8, v51
	v_and_b32_e32 v9, 0xffffff00, v39
	v_mul_f32_e32 v2, 0x3fb8aa3b, v2
	v_exp_f32_e32 v29, v2
	v_sub_f32_e32 v2, v9, v51
	v_and_b32_e32 v31, 0xffffff00, v40
	v_mul_f32_e32 v2, 0x3fb8aa3b, v2
	v_exp_f32_e32 v30, v2
	v_sub_f32_e32 v2, v31, v51
	v_and_b32_e32 v32, 0xffffff00, v41
	v_mul_f32_e32 v2, 0x3fb8aa3b, v2
	v_exp_f32_e32 v31, v2
	v_sub_f32_e32 v2, v32, v51
	v_and_b32_e32 v34, 0xffffff00, v42
	v_mul_f32_e32 v2, 0x3fb8aa3b, v2
	v_exp_f32_e32 v6, v2
	v_sub_f32_e32 v2, v34, v51
	v_and_b32_e32 v35, 0xffffff00, v43
	v_mul_f32_e32 v2, 0x3fb8aa3b, v2
	v_exp_f32_e32 v7, v2
	v_sub_f32_e32 v2, v35, v51
	v_mul_f32_e32 v2, 0x3fb8aa3b, v2
	v_exp_f32_e32 v8, v2
	v_lshl_or_b32 v2, s18, 8, v128
	v_ashrrev_i32_e32 v3, 31, v2
	s_lshl_b64 s[4:5], s[16:17], 18
	s_mov_b32 s3, 0x7fc000
	v_lshl_add_u64 v[32:33], v[2:3], 4, s[4:5]
	v_sub_f32_e32 v24, v51, v51
	v_mul_f32_e32 v24, 0x3fb8aa3b, v24
	v_exp_f32_e32 v24, v24
	s_waitcnt vmcnt(0)
	s_waitcnt lgkmcnt(0)
	v_and_b32_e32 v1, 0xff, v170
	v_lshrrev_b32_e32 v171, 8, v170
	v_lshlrev_b32_e32 v171, 23, v171
	v_lshl_or_b32 v2, v1, 14, v0
	v_and_b32_e32 v36, 0xffffff00, v44
	v_and_b32_e32 v37, 0xffffff00, v45
	v_and_b32_e32 v49, 0xffffff00, v46
	v_and_b32_e32 v50, 0xffffff00, v47
	v_and_b32_e32 v52, 0xffffff00, v48
	s_waitcnt lgkmcnt(0)
	v_and_b32_e32 v0, 0xff, v172
	v_lshrrev_b32_e32 v173, 8, v172
	v_lshlrev_b32_e32 v173, 23, v173
	v_lshl_or_b32 v3, v0, 14, v4
	s_waitcnt lgkmcnt(0)
	v_and_b32_e32 v0, 0xff, v174
	v_lshrrev_b32_e32 v175, 8, v174
	v_lshlrev_b32_e32 v175, 23, v175
	v_lshl_or_b32 v4, v0, 14, v10
	s_waitcnt lgkmcnt(0)
	v_and_b32_e32 v0, 0xff, v176
	v_lshrrev_b32_e32 v177, 8, v176
	v_lshlrev_b32_e32 v177, 23, v177
	v_lshl_or_b32 v5, v0, 14, v12
	v_lshlrev_b64 v[12:13], 2, v[32:33]
	v_lshl_add_u64 v[0:1], s[12:13], 0, v[12:13]
	s_nop 0
	v_readfirstlane_b32 s98, v0
	v_readfirstlane_b32 s99, v1
	v_lshrrev_b32_e32 v202, 6, v128
	v_and_b32_e32 v203, 63, v128
	v_lshlrev_b32_e32 v202, 13, v202
	v_lshl_or_b32 v204, v203, 6, v202
	v_lshl_or_b32 v205, v203, 4, v202
	v_lshlrev_b32_e32 v203, 4, v203
	ds_write_b128 v204, v[2:5]
	v_lshrrev_b32_e32 v32, 2, v40
	v_add_f32_e32 v10, 0, v24
	v_add_f32_e32 v10, v25, v10
	v_add_f32_e32 v10, v26, v10
	v_add_f32_e32 v10, v27, v10
	v_sub_f32_e32 v2, v36, v51
	v_add_f32_e32 v10, v28, v10
	v_mul_f32_e32 v2, 0x3fb8aa3b, v2
	v_add_f32_e32 v10, v29, v10
	v_exp_f32_e32 v9, v2
	v_sub_f32_e32 v2, v37, v51
	v_add_f32_e32 v10, v30, v10
	v_mul_f32_e32 v2, 0x3fb8aa3b, v2
	v_sub_f32_e32 v3, v49, v51
	v_add_f32_e32 v10, v31, v10
	v_exp_f32_e32 v2, v2
	v_mul_f32_e32 v3, 0x3fb8aa3b, v3
	v_sub_f32_e32 v4, v50, v51
	v_add_f32_e32 v10, v6, v10
	v_exp_f32_e32 v3, v3
	v_mul_f32_e32 v4, 0x3fb8aa3b, v4
	v_sub_f32_e32 v5, v52, v51
	v_add_f32_e32 v10, v7, v10
	v_exp_f32_e32 v4, v4
	v_mul_f32_e32 v5, 0x3fb8aa3b, v5
	v_add_f32_e32 v10, v8, v10
	v_exp_f32_e32 v5, v5
	v_add_f32_e32 v10, v9, v10
	v_add_f32_e32 v10, v2, v10
	v_lshrrev_b32_e32 v11, 2, v38
	v_lshrrev_b32_e32 v15, 2, v17
	v_add_f32_e32 v10, v3, v10
	v_and_b32_e32 v11, 60, v11
	v_and_b32_e32 v14, 15, v38
	v_and_b32_e32 v15, 60, v15
	v_and_b32_e32 v17, 15, v17
	v_lshrrev_b32_e32 v22, 2, v39
	v_and_b32_e32 v23, 15, v39
	v_and_b32_e32 v33, 15, v40
	v_add_f32_e32 v10, v4, v10
	v_add_u32_e32 v11, v16, v11
	v_lshl_add_u32 v14, v14, 2, v16
	v_add_u32_e32 v15, v16, v15
	v_lshl_add_u32 v17, v17, 2, v16
	v_and_b32_e32 v22, 60, v22
	v_lshl_add_u32 v23, v23, 2, v16
	v_and_b32_e32 v32, 60, v32
	v_lshl_add_u32 v33, v33, 2, v16
	v_add_f32_e32 v10, v5, v10
	v_add_u32_e32 v22, v16, v22
	v_add_u32_e32 v32, v16, v32
	ds_read_b32 v11, v11
	ds_read_b32 v14, v14 offset:64
	ds_read_b32 v15, v15
	ds_read_b32 v17, v17 offset:64
	ds_read_b32 v34, v22
	ds_read_b32 v23, v23 offset:64
	ds_read_b32 v35, v32
	ds_read_b32 v33, v33 offset:64
	s_waitcnt lgkmcnt(6)
; #define RT_PK(q_) (ex[q_] | (int)((__float_as_uint(usc[ex[q_]]) >> 23) << 14))
;     __device__ __forceinline__ void fused(f32x4 (&acc)[2][2][4][2], const Unit& u, int wr, int wc, int fr, int fq, PG8_LAS unsigned char* lds, int wid, int lane) const {
;     ...
;             const float rs = 1.0f / sum;
;             asm volatile("s_waitcnt lgkmcnt(0)" ::: "memory");
;             int ex[16];
; #pragma unroll
;             for (int q = 0; q < 16; ++q) { const unsigned cid = __float_as_uint(best[q]) & 255u; ex[q] = idxl[cid >> 4] * 128 + idxl[16 + (cid & 15u)]; }
;             const size_t o = ((size_t)u.pn * 16384 + (size_t)(u.pm * BM + row)) * 16;
;             typedef int i32x4 __attribute__((ext_vector_type(4)));
; #pragma unroll
;             for (int i = 0; i < 4; ++i) {
;     ...
;                 *(i32x4*)(eidx + o + 4 * i) = (i32x4){RT_PK(4 * i), RT_PK(4 * i + 1), RT_PK(4 * i + 2), RT_PK(4 * i + 3)};
;                 *(f32x4*)(egate + o + 4 * i) = (f32x4){sc[4 * i] * rs * vsc[ex[4 * i]], sc[4 * i + 1] * rs * vsc[ex[4 * i + 1]], sc[4 * i + 2] * rs * vsc[ex[4 * i + 2]], sc[4 * i + 3] * rs * vsc[ex[4 * i + 3]]};
	v_lshl_add_u32 v14, v11, 7, v14
	v_div_scale_f32 v11, s[4:5], v10, v10, 1.0
	v_rcp_f32_e32 v36, v11
	s_waitcnt lgkmcnt(4)
	v_lshl_add_u32 v22, v15, 7, v17
	s_waitcnt lgkmcnt(2)
	v_lshl_add_u32 v32, v34, 7, v23
	s_waitcnt lgkmcnt(0)
	v_lshl_add_u32 v34, v35, 7, v33
	v_fma_f32 v15, -v11, v36, 1.0
	v_fmac_f32_e32 v36, v15, v36
	v_div_scale_f32 v15, vcc, 1.0, v10, 1.0
	v_mul_f32_e32 v17, v15, v36
	v_fma_f32 v23, -v11, v17, v15
	v_fmac_f32_e32 v17, v23, v36
	v_fma_f32 v11, -v11, v17, v15
	v_div_fmas_f32 v11, v11, v36, v17
	v_div_fixup_f32 v10, v11, v10, 1.0
	v_pk_mul_f32 v[24:25], v[24:25], v[10:11] op_sel_hi:[1,0]
	v_pk_mul_f32 v[26:27], v[26:27], v[10:11] op_sel_hi:[1,0]
	v_ashrrev_i32_e32 v15, 31, v14
	v_ashrrev_i32_e32 v33, 31, v32
	v_lshl_add_u64 v[12:13], s[10:11], 0, v[12:13]
	s_nop 0
	v_readfirstlane_b32 s100, v12
	v_readfirstlane_b32 s101, v13
	v_ashrrev_i32_e32 v23, 31, v22
	v_lshlrev_b64 v[36:37], 3, v[32:33]
	v_lshl_add_u64 v[38:39], s[8:9], 0, v[36:37]
	v_ashrrev_i32_e32 v35, 31, v34
	v_mul_f32_e32 v18, v24, v171
	v_mul_f32_e32 v19, v25, v173
	v_lshlrev_b64 v[24:25], 3, v[14:15]
	v_mul_f32_e32 v20, v26, v175
	v_mul_f32_e32 v21, v27, v177
	ds_write_b128 v204, v[18:21] offset:4096
	v_lshlrev_b64 v[26:27], 3, v[22:23]
	s_nop 0
	v_lshl_add_u64 v[18:19], s[8:9], 0, v[24:25]
	v_lshl_add_u64 v[20:21], s[8:9], 0, v[26:27]
	v_lshl_add_u32 v242, v14, 1, v243
	ds_read_u16 v178, v242
	v_lshl_add_u32 v242, v22, 1, v243
	ds_read_u16 v180, v242
	v_lshl_add_u32 v242, v32, 1, v243
	ds_read_u16 v182, v242
	v_lshlrev_b64 v[38:39], 3, v[34:35]
	v_lshl_add_u64 v[18:19], s[8:9], 0, v[38:39]
	v_lshl_add_u32 v242, v34, 1, v243
	ds_read_u16 v184, v242
	s_waitcnt vmcnt(3)
	s_waitcnt lgkmcnt(0)
	v_and_b32_e32 v11, 0xff, v178
	v_lshrrev_b32_e32 v179, 8, v178
	v_lshlrev_b32_e32 v179, 23, v179
	v_lshl_or_b32 v18, v11, 14, v14
	s_waitcnt vmcnt(2)
	s_waitcnt lgkmcnt(0)
	v_and_b32_e32 v11, 0xff, v180
	v_lshrrev_b32_e32 v181, 8, v180
	v_lshlrev_b32_e32 v181, 23, v181
	v_lshl_or_b32 v19, v11, 14, v22
	s_waitcnt vmcnt(1)
	s_waitcnt lgkmcnt(0)
	v_and_b32_e32 v11, 0xff, v182
	v_lshrrev_b32_e32 v183, 8, v182
	v_lshlrev_b32_e32 v183, 23, v183
	v_lshl_or_b32 v20, v11, 14, v32
	s_waitcnt vmcnt(0)
	s_waitcnt lgkmcnt(0)
	v_and_b32_e32 v11, 0xff, v184
	v_lshrrev_b32_e32 v185, 8, v184
	v_lshlrev_b32_e32 v185, 23, v185
	v_lshl_or_b32 v21, v11, 14, v34
	ds_write_b128 v204, v[18:21] offset:16
	v_lshrrev_b32_e32 v11, 2, v41
	v_lshrrev_b32_e32 v15, 2, v42
	v_lshrrev_b32_e32 v18, 2, v43
	v_lshrrev_b32_e32 v20, 2, v44
	v_and_b32_e32 v11, 60, v11
	v_and_b32_e32 v14, 15, v41
	v_and_b32_e32 v15, 60, v15
	v_and_b32_e32 v17, 15, v42
	v_and_b32_e32 v18, 60, v18
	v_and_b32_e32 v19, 15, v43
	v_and_b32_e32 v20, 60, v20
	v_and_b32_e32 v21, 15, v44
	v_add_u32_e32 v11, v16, v11
	v_lshl_add_u32 v14, v14, 2, v16
	v_add_u32_e32 v15, v16, v15
	v_lshl_add_u32 v17, v17, 2, v16
	v_add_u32_e32 v18, v16, v18
	v_lshl_add_u32 v19, v19, 2, v16
	v_add_u32_e32 v20, v16, v20
	v_lshl_add_u32 v21, v21, 2, v16
	ds_read_b32 v11, v11
	ds_read_b32 v14, v14 offset:64
	ds_read_b32 v15, v15
	ds_read_b32 v17, v17 offset:64
	ds_read_b32 v18, v18
	ds_read_b32 v19, v19 offset:64
	ds_read_b32 v20, v20
	ds_read_b32 v21, v21 offset:64
	s_waitcnt lgkmcnt(6)
	v_lshl_add_u32 v14, v11, 7, v14
	s_waitcnt lgkmcnt(4)
	v_lshl_add_u32 v22, v15, 7, v17
	s_waitcnt lgkmcnt(2)
	v_lshl_add_u32 v32, v18, 7, v19
	v_pk_mul_f32 v[18:19], v[28:29], v[10:11] op_sel_hi:[1,0]
	s_waitcnt lgkmcnt(0)
	v_lshl_add_u32 v34, v20, 7, v21
	v_pk_mul_f32 v[20:21], v[30:31], v[10:11] op_sel_hi:[1,0]
	v_ashrrev_i32_e32 v15, 31, v14
	v_ashrrev_i32_e32 v33, 31, v32
	v_ashrrev_i32_e32 v23, 31, v22
	v_lshlrev_b64 v[28:29], 3, v[32:33]
	v_lshl_add_u64 v[30:31], s[8:9], 0, v[28:29]
	v_ashrrev_i32_e32 v35, 31, v34
	v_mul_f32_e32 v20, v20, v183
	v_mul_f32_e32 v21, v21, v185
	v_mul_f32_e32 v18, v18, v179
	v_mul_f32_e32 v19, v19, v181
	v_lshlrev_b64 v[24:25], 3, v[14:15]
	ds_write_b128 v204, v[18:21] offset:4112
	v_lshlrev_b64 v[26:27], 3, v[22:23]
	s_nop 0
	v_lshl_add_u64 v[18:19], s[8:9], 0, v[24:25]
	v_lshl_add_u64 v[20:21], s[8:9], 0, v[26:27]
	v_lshl_add_u32 v242, v14, 1, v243
	ds_read_u16 v186, v242
	v_lshl_add_u32 v242, v22, 1, v243
	ds_read_u16 v188, v242
	v_lshl_add_u32 v242, v32, 1, v243
	ds_read_u16 v190, v242
	v_lshlrev_b64 v[30:31], 3, v[34:35]
	v_lshl_add_u64 v[18:19], s[8:9], 0, v[30:31]
	v_lshl_add_u32 v242, v34, 1, v243
	ds_read_u16 v192, v242
	s_waitcnt vmcnt(3)
	s_waitcnt lgkmcnt(0)
; #define RT_PK(q_) (ex[q_] | (int)((__float_as_uint(usc[ex[q_]]) >> 23) << 14))
;     __device__ __forceinline__ void fused(f32x4 (&acc)[2][2][4][2], const Unit& u, int wr, int wc, int fr, int fq, PG8_LAS unsigned char* lds, int wid, int lane) const {
;     ...
;             for (int q = 0; q < 16; ++q) { const unsigned cid = __float_as_uint(best[q]) & 255u; ex[q] = idxl[cid >> 4] * 128 + idxl[16 + (cid & 15u)]; }
;             const size_t o = ((size_t)u.pn * 16384 + (size_t)(u.pm * BM + row)) * 16;
;             typedef int i32x4 __attribute__((ext_vector_type(4)));
; #pragma unroll
;             for (int i = 0; i < 4; ++i) {
;     ...
;                 *(i32x4*)(eidx + o + 4 * i) = (i32x4){RT_PK(4 * i), RT_PK(4 * i + 1), RT_PK(4 * i + 2), RT_PK(4 * i + 3)};
;                 *(f32x4*)(egate + o + 4 * i) = (f32x4){sc[4 * i] * rs * vsc[ex[4 * i]], sc[4 * i + 1] * rs * vsc[ex[4 * i + 1]], sc[4 * i + 2] * rs * vsc[ex[4 * i + 2]], sc[4 * i + 3] * rs * vsc[ex[4 * i + 3]]};
	v_and_b32_e32 v11, 0xff, v186
	v_lshrrev_b32_e32 v187, 8, v186
	v_lshlrev_b32_e32 v187, 23, v187
	v_lshl_or_b32 v18, v11, 14, v14
	s_waitcnt vmcnt(2)
	s_waitcnt lgkmcnt(0)
	v_and_b32_e32 v11, 0xff, v188
	v_lshrrev_b32_e32 v189, 8, v188
	v_lshlrev_b32_e32 v189, 23, v189
	v_lshl_or_b32 v19, v11, 14, v22
	s_waitcnt vmcnt(1)
	s_waitcnt lgkmcnt(0)
	v_and_b32_e32 v11, 0xff, v190
	v_lshrrev_b32_e32 v191, 8, v190
	v_lshlrev_b32_e32 v191, 23, v191
	v_lshl_or_b32 v20, v11, 14, v32
	s_waitcnt vmcnt(0)
	s_waitcnt lgkmcnt(0)
	v_and_b32_e32 v11, 0xff, v192
	v_lshrrev_b32_e32 v193, 8, v192
	v_lshlrev_b32_e32 v193, 23, v193
	v_lshl_or_b32 v21, v11, 14, v34
	ds_write_b128 v204, v[18:21] offset:32
	v_lshrrev_b32_e32 v11, 2, v45
	v_lshrrev_b32_e32 v15, 2, v46
	v_lshrrev_b32_e32 v18, 2, v47
	v_lshrrev_b32_e32 v20, 2, v48
	v_and_b32_e32 v11, 60, v11
	v_and_b32_e32 v14, 15, v45
	v_and_b32_e32 v15, 60, v15
	v_and_b32_e32 v17, 15, v46
	v_and_b32_e32 v18, 60, v18
	v_and_b32_e32 v19, 15, v47
	v_and_b32_e32 v20, 60, v20
	v_add_u32_e32 v11, v16, v11
	v_lshl_add_u32 v14, v14, 2, v16
	v_add_u32_e32 v15, v16, v15
	v_lshl_add_u32 v17, v17, 2, v16
	v_add_u32_e32 v18, v16, v18
	v_lshl_add_u32 v19, v19, 2, v16
	v_add_u32_e32 v20, v16, v20
	v_and_b32_e32 v21, 15, v48
	v_lshl_add_u32 v16, v21, 2, v16
	ds_read_b32 v11, v11
	ds_read_b32 v14, v14 offset:64
	ds_read_b32 v15, v15
	ds_read_b32 v17, v17 offset:64
	ds_read_b32 v18, v18
	ds_read_b32 v19, v19 offset:64
	ds_read_b32 v20, v20
	ds_read_b32 v21, v16 offset:64
	s_waitcnt lgkmcnt(6)
	v_lshl_add_u32 v14, v11, 7, v14
	s_waitcnt lgkmcnt(4)
	v_lshl_add_u32 v16, v15, 7, v17
	s_waitcnt lgkmcnt(2)
	v_lshl_add_u32 v18, v18, 7, v19
	v_pk_mul_f32 v[6:7], v[6:7], v[10:11] op_sel_hi:[1,0]
	v_pk_mul_f32 v[8:9], v[8:9], v[10:11] op_sel_hi:[1,0]
	v_ashrrev_i32_e32 v15, 31, v14
	v_ashrrev_i32_e32 v19, 31, v18
	s_waitcnt lgkmcnt(0)
	v_lshl_add_u32 v20, v20, 7, v21
	v_lshlrev_b64 v[22:23], 3, v[14:15]
	v_ashrrev_i32_e32 v17, 31, v16
	v_ashrrev_i32_e32 v21, 31, v20
	v_mul_f32_e32 v8, v8, v191
	v_mul_f32_e32 v9, v9, v193
	v_mul_f32_e32 v6, v6, v187
	v_mul_f32_e32 v7, v7, v189
	v_lshlrev_b64 v[26:27], 3, v[18:19]
	ds_write_b128 v204, v[6:9] offset:4128
	v_lshlrev_b64 v[24:25], 3, v[16:17]
	v_lshl_add_u64 v[28:29], s[8:9], 0, v[26:27]
	v_lshl_add_u64 v[6:7], s[8:9], 0, v[22:23]
	v_lshl_add_u64 v[8:9], s[8:9], 0, v[24:25]
	v_lshl_add_u32 v242, v14, 1, v243
	ds_read_u16 v194, v242
	v_lshl_add_u32 v242, v16, 1, v243
	ds_read_u16 v196, v242
	v_lshl_add_u32 v242, v18, 1, v243
	ds_read_u16 v198, v242
	v_lshlrev_b64 v[28:29], 3, v[20:21]
	v_lshl_add_u64 v[6:7], s[8:9], 0, v[28:29]
	v_lshl_add_u32 v242, v20, 1, v243
	ds_read_u16 v200, v242
	s_waitcnt vmcnt(3)
	s_waitcnt lgkmcnt(0)
	v_and_b32_e32 v6, 0xff, v194
	v_lshrrev_b32_e32 v195, 8, v194
	v_lshlrev_b32_e32 v195, 23, v195
	s_waitcnt vmcnt(2)
	s_waitcnt lgkmcnt(0)
	v_and_b32_e32 v7, 0xff, v196
	v_lshrrev_b32_e32 v197, 8, v196
	v_lshlrev_b32_e32 v197, 23, v197
	s_waitcnt vmcnt(1)
	s_waitcnt lgkmcnt(0)
	v_and_b32_e32 v8, 0xff, v198
	v_lshrrev_b32_e32 v199, 8, v198
	v_lshlrev_b32_e32 v199, 23, v199
	v_lshl_or_b32 v6, v6, 14, v14
	v_lshl_or_b32 v7, v7, 14, v16
	s_waitcnt vmcnt(0)
	s_waitcnt lgkmcnt(0)
	v_and_b32_e32 v9, 0xff, v200
	v_lshrrev_b32_e32 v201, 8, v200
	v_lshlrev_b32_e32 v201, 23, v201
	v_lshl_or_b32 v8, v8, 14, v18
	v_lshl_or_b32 v9, v9, 14, v20
	ds_write_b128 v204, v[6:9] offset:48
	v_pk_mul_f32 v[0:1], v[2:3], v[10:11] op_sel_hi:[1,0]
	v_pk_mul_f32 v[2:3], v[4:5], v[10:11] op_sel_hi:[1,0]
	v_mul_f32_e32 v0, v0, v195
	v_mul_f32_e32 v1, v1, v197
	v_mul_f32_e32 v2, v2, v199
	v_mul_f32_e32 v3, v3, v201
	ds_write_b128 v204, v[0:3] offset:4144
	s_waitcnt lgkmcnt(0)
	ds_read_b128 v[140:143], v205
	ds_read_b128 v[144:147], v205 offset:1024
	ds_read_b128 v[148:151], v205 offset:2048
	ds_read_b128 v[152:155], v205 offset:3072
	ds_read_b128 v[156:159], v205 offset:4096
	ds_read_b128 v[160:163], v205 offset:5120
	ds_read_b128 v[164:167], v205 offset:6144
	ds_read_b128 v[206:209], v205 offset:7168
	s_waitcnt lgkmcnt(0)
	global_store_dwordx4 v203, v[140:143], s[98:99]
	global_store_dwordx4 v203, v[144:147], s[98:99] offset:1024
	global_store_dwordx4 v203, v[148:151], s[98:99] offset:2048
	global_store_dwordx4 v203, v[152:155], s[98:99] offset:3072
	global_store_dwordx4 v203, v[156:159], s[100:101]
	global_store_dwordx4 v203, v[160:163], s[100:101] offset:1024
	global_store_dwordx4 v203, v[164:167], s[100:101] offset:2048
	global_store_dwordx4 v203, v[206:209], s[100:101] offset:3072

; #define GAS __attribute__((address_space(1)))
; __device__ __forceinline__ void row_to_fp8_2(int lane, const float* xrow0, const float* xrow1, unsigned (&ow0)[4], unsigned (&ow1)[4], float& isc0, float& isc1) {
;     const GAS f32x4* xr0 = (const GAS f32x4*)xrow0 + lane; const GAS f32x4* xr1 = (const GAS f32x4*)xrow1 + lane;
;     f32x4 v0[4], v1[4];
; #pragma unroll
;     for (int j = 0; j < 4; ++j) { v0[j] = __builtin_nontemporal_load(xr0 + 64 * j); v1[j] = __builtin_nontemporal_load(xr1 + 64 * j); }
;     float m0 = 0.f, m1 = 0.f;
; #pragma unroll
;     for (int j = 0; j < 4; ++j) { m0 = fmaxf(m0, fmaxf(fmaxf(fabsf(v0[j].x), fabsf(v0[j].y)), fmaxf(fabsf(v0[j].z), fabsf(v0[j].w)))); m1 = fmaxf(m1, fmaxf(fmaxf(fabsf(v1[j].x), fabsf(v1[j].y)), fmaxf(fabsf(v1[j].z), fabsf(v1[j].w)))); }
; #pragma unroll
;     for (int o = 1; o < 64; o <<= 1) { m0 = fmaxf(m0, __shfl_xor(m0, o)); m1 = fmaxf(m1, __shfl_xor(m1, o)); }
;     int b0 = (int)((__float_as_uint(m0) >> 23) & 255u); b0 = b0 < 16 ? 16 : (b0 > 240 ? 240 : b0);
;     int b1 = (int)((__float_as_uint(m1) >> 23) & 255u); b1 = b1 < 16 ? 16 : (b1 > 240 ? 240 : b1);
;     const float s0 = __uint_as_float((unsigned)(261 - b0) << 23), s1 = __uint_as_float((unsigned)(261 - b1) << 23);
;     isc0 = __uint_as_float((unsigned)(b0 - 7) << 23); isc1 = __uint_as_float((unsigned)(b1 - 7) << 23);
; #pragma unroll
;     for (int j = 0; j < 4; ++j) { int p = __builtin_amdgcn_cvt_pk_fp8_f32(v0[j].x * s0, v0[j].y * s0, 0, false); p = __builtin_amdgcn_cvt_pk_fp8_f32(v0[j].z * s0, v0[j].w * s0, p, true); ow0[j] = (unsigned)p;
; __device__ __forceinline__ void tables_part(LAS unsigned char* lds, int wave, int lane, const float* pu, const float* pv, unsigned char* ws, int gw, int ngw, int wg, int nwg, int r0, int r1, int i0, int i1) {
;     for (int m = r0 + gw; m < r1; m += 2 * ngw) {
;         const int m1 = (m + ngw < r1) ? m + ngw : m;
;         float isc0, isc1; unsigned ow0[4], ow1[4];
;         row_to_fp8_2(lane, pu + (size_t)m * D, pu + (size_t)m1 * D, ow0, ow1, isc0, isc1);
; #pragma unroll
;         for (int j = 0; j < 4; ++j) { *((GAS unsigned*)(ws + WS_UT + (size_t)m * D + j * 256) + lane) = ow0[j]; *((GAS unsigned*)(ws + WS_UT + (size_t)m1 * D + j * 256) + lane) = ow1[j]; }
;         if (lane == 0) { ((float*)(ws + WS_ESC))[m] = isc0; ((float*)(ws + WS_ESC))[m1] = isc1; } }
.LBB0_1175:
	global_load_dwordx4 v[14:17], v[8:9], off offset:-2048 nt
	global_load_dwordx4 v[18:21], v[8:9], off offset:-1024 nt
	global_load_dwordx4 v[22:25], v[8:9], off nt
	global_load_dwordx4 v[26:29], v[8:9], off offset:1024 nt
	s_add_i32 s7, s6, 0x400
	s_cmpk_lt_i32 s6, 0x7c00
	s_cselect_b32 s16, s7, s6
	s_ashr_i32 s17, s16, 31
	s_lshl_b64 s[18:19], s[16:17], 12
	v_lshl_add_u64 v[46:47], v[2:3], 0, s[18:19]
	global_load_dwordx4 v[30:33], v[46:47], off nt
	global_load_dwordx4 v[34:37], v[46:47], off offset:1024 nt
	global_load_dwordx4 v[38:41], v[46:47], off offset:2048 nt
	global_load_dwordx4 v[42:45], v[46:47], off offset:3072 nt
	v_mov_b32_e32 v55, 0
	s_lshl_b64 s[18:19], s[16:17], 10
	s_waitcnt vmcnt(0)
	v_max_f32_e64 v13, |v17|, |v17|
	v_max_f32_e64 v46, |v16|, |v16|
	v_max_f32_e64 v47, |v21|, |v21|
	v_max_f32_e64 v48, |v20|, |v20|
	v_max_f32_e64 v49, |v25|, |v25|
	v_max_f32_e64 v50, |v24|, |v24|
	v_max_f32_e64 v51, |v29|, |v29|
	v_max_f32_e64 v52, |v28|, |v28|
	v_max_f32_e32 v13, v46, v13
	v_max_f32_e32 v46, v48, v47
	v_max_f32_e32 v47, v50, v49
	v_max_f32_e32 v48, v52, v51
	v_max3_f32 v13, |v14|, |v15|, v13
	v_max3_f32 v46, |v18|, |v19|, v46
	v_max3_f32 v47, |v22|, |v23|, v47
	v_max3_f32 v48, |v26|, |v27|, v48
	v_max3_f32 v13, v13, 0, v46
	v_max3_f32 v13, v13, v47, v48
	ds_bpermute_b32 v46, v173, v13
	v_max_f32_e64 v47, |v33|, |v33|
	v_max_f32_e64 v48, |v32|, |v32|
	v_max_f32_e64 v49, |v37|, |v37|
	v_max_f32_e64 v50, |v36|, |v36|
	v_max_f32_e64 v51, |v41|, |v41|
	v_max_f32_e64 v52, |v40|, |v40|
	v_max_f32_e64 v53, |v45|, |v45|
	v_max_f32_e64 v54, |v44|, |v44|
	v_max_f32_e32 v47, v48, v47
	v_max_f32_e32 v48, v50, v49
	v_max_f32_e32 v49, v52, v51
	v_max_f32_e32 v50, v54, v53
	v_max3_f32 v47, |v30|, |v31|, v47
	v_max3_f32 v48, |v34|, |v35|, v48
	v_max3_f32 v49, |v38|, |v39|, v49
	v_max3_f32 v50, |v42|, |v43|, v50
	v_max3_f32 v47, v47, 0, v48
	v_max3_f32 v47, v47, v49, v50
	s_waitcnt lgkmcnt(0)
	v_max_f32_e32 v46, v46, v46
	ds_bpermute_b32 v48, v173, v47
	v_max_f32_e32 v13, v13, v46
	ds_bpermute_b32 v46, v174, v13
	v_mov_b32_e32 v49, 0
	v_mov_b32_e32 v53, 0
	s_waitcnt lgkmcnt(1)
	v_max_f32_e32 v48, v48, v48
	v_max_f32_e32 v47, v47, v48
	s_waitcnt lgkmcnt(0)
	v_max_f32_e32 v46, v46, v46
	ds_bpermute_b32 v48, v174, v47
	v_max_f32_e32 v13, v13, v46
	ds_bpermute_b32 v46, v175, v13
	v_mov_b32_e32 v51, 0
	v_mov_b32_e32 v54, 0
	s_waitcnt lgkmcnt(1)
	v_max_f32_e32 v48, v48, v48
	v_max_f32_e32 v47, v47, v48
	s_waitcnt lgkmcnt(0)
	v_max_f32_e32 v46, v46, v46
	ds_bpermute_b32 v48, v175, v47
	v_max_f32_e32 v13, v13, v46
	ds_bpermute_b32 v46, v176, v13
	v_mov_b32_e32 v50, 0
	v_mov_b32_e32 v52, 0
	s_waitcnt lgkmcnt(1)
	v_max_f32_e32 v48, v48, v48
	v_max_f32_e32 v47, v47, v48
	s_waitcnt lgkmcnt(0)
	v_max_f32_e32 v46, v46, v46
	ds_bpermute_b32 v48, v176, v47
	v_max_f32_e32 v13, v13, v46
	ds_bpermute_b32 v46, v10, v13
	s_waitcnt lgkmcnt(1)
	v_max_f32_e32 v48, v48, v48
	v_max_f32_e32 v47, v47, v48
	s_waitcnt lgkmcnt(0)
	v_max_f32_e32 v46, v46, v46
	ds_bpermute_b32 v48, v10, v47
	v_max_f32_e32 v13, v13, v46
	ds_bpermute_b32 v46, v11, v13
	s_waitcnt lgkmcnt(1)
	v_max_f32_e32 v48, v48, v48
	v_max_f32_e32 v47, v47, v48
	s_waitcnt lgkmcnt(0)
	v_max_f32_e32 v46, v46, v46
	v_max_f32_e32 v13, v13, v46
	ds_bpermute_b32 v46, v11, v47
	v_bfe_u32 v13, v13, 23, 8
	v_med3_u32 v13, v13, 16, v1
	v_lshlrev_b32_e32 v13, 23, v13
	v_sub_u32_e32 v48, 0x82800000, v13
	s_waitcnt lgkmcnt(0)
	v_max_f32_e32 v46, v46, v46
	v_mul_f32_e32 v14, v14, v48
	v_mul_f32_e32 v15, v15, v48
	v_mul_f32_e32 v22, v22, v48
	v_mul_f32_e32 v23, v23, v48
	v_max_f32_e32 v46, v47, v46
	v_cvt_pk_fp8_f32 v49, v14, v15
	v_cvt_pk_fp8_f32 v53, v22, v23
	v_bfe_u32 v14, v46, 23, 8
	v_med3_u32 v14, v14, 16, v1
	v_lshlrev_b32_e32 v14, 23, v14
	v_mul_f32_e32 v18, v18, v48
	v_mul_f32_e32 v19, v19, v48
	v_mul_f32_e32 v24, v24, v48
	v_mul_f32_e32 v25, v25, v48
	v_sub_u32_e32 v15, 0x82800000, v14
	v_cvt_pk_fp8_f32 v51, v18, v19
	v_cvt_pk_fp8_f32 v53, v24, v25 op_sel:[0,0,1]
	v_mul_f32_e32 v24, v38, v15
	v_mul_f32_e32 v25, v39, v15
	v_cvt_pk_fp8_f32 v54, v24, v25
	v_mul_f32_e32 v16, v16, v48
	v_mul_f32_e32 v17, v17, v48
	v_mul_f32_e32 v20, v20, v48
	v_mul_f32_e32 v21, v21, v48
	v_mul_f32_e32 v26, v26, v48
	v_mul_f32_e32 v27, v27, v48
	v_cvt_pk_fp8_f32 v49, v16, v17 op_sel:[0,0,1]
	v_mul_f32_e32 v16, v30, v15
	v_mul_f32_e32 v17, v31, v15
	v_cvt_pk_fp8_f32 v55, v26, v27
	v_cvt_pk_fp8_f32 v51, v20, v21 op_sel:[0,0,1]
	v_mul_f32_e32 v20, v34, v15
	v_mul_f32_e32 v21, v35, v15
	v_mul_f32_e32 v26, v40, v15
	v_cvt_pk_fp8_f32 v50, v16, v17
	v_mul_f32_e32 v16, v41, v15
	v_cvt_pk_fp8_f32 v52, v20, v21
	v_cvt_pk_fp8_f32 v54, v26, v16 op_sel:[0,0,1]
	v_mul_f32_e32 v16, v42, v15
	v_mul_f32_e32 v17, v43, v15
	v_mov_b32_e32 v20, 0
	v_cvt_pk_fp8_f32 v20, v16, v17
	v_mul_f32_e32 v18, v32, v15
	v_mul_f32_e32 v19, v33, v15
	v_mul_f32_e32 v22, v36, v15
	v_mul_f32_e32 v23, v37, v15
	v_cvt_pk_fp8_f32 v50, v18, v19 op_sel:[0,0,1]
	v_mul_f32_e32 v16, v44, v15
	v_mul_f32_e32 v15, v45, v15
	v_cvt_pk_fp8_f32 v20, v16, v15 op_sel:[0,0,1]
	v_lshl_add_u64 v[16:17], s[10:11], 0, v[6:7]
	v_cvt_pk_fp8_f32 v52, v22, v23 op_sel:[0,0,1]
	v_add_co_u32_e32 v16, vcc, 0x15000000, v16
	v_mul_f32_e32 v28, v28, v48
	v_mul_f32_e32 v29, v29, v48
	v_addc_co_u32_e32 v17, vcc, 0, v17, vcc
	v_lshl_add_u64 v[18:19], v[4:5], 0, s[18:19]
	v_cvt_pk_fp8_f32 v55, v28, v29 op_sel:[0,0,1]
	global_store_dword v[16:17], v49, off
	global_store_dword v[18:19], v50, off
	global_store_dword v[16:17], v51, off offset:256
	global_store_dword v[18:19], v52, off offset:256
	global_store_dword v[16:17], v53, off offset:512
	global_store_dword v[18:19], v54, off offset:512
	global_store_dword v[16:17], v55, off offset:768
	global_store_dword v[18:19], v20, off offset:768
	s_and_saveexec_b64 s[18:19], s[4:5]
	s_cbranch_execz .LBB0_1174
	v_mov_b32_e32 v56, s6
	v_mov_b32_e32 v57, s16
	v_lshlrev_b32_e32 v56, 1, v56
	v_lshlrev_b32_e32 v57, 1, v57
	v_add_u32_e32 v56, 0x19100000, v56
	v_add_u32_e32 v57, 0x19100000, v57
	s_lshl_b64 s[16:17], s[16:17], 3
	s_add_u32 s16, s20, s16
	s_addc_u32 s17, s21, s17
	s_add_u32 s24, s10, s22
	v_add_u32_e32 v13, 0xfc800000, v13
	s_addc_u32 s25, s11, s23
	v_add_u32_e32 v14, 0xfc800000, v14
	global_store_dword v12, v13, s[24:25]
	global_store_dword v12, v14, s[16:17]
	v_lshrrev_b32_e32 v58, 23, v13
	v_lshrrev_b32_e32 v59, 23, v14
	global_store_byte v56, v58, s[10:11]
	global_store_byte v57, v59, s[10:11]
	s_branch .LBB0_1174

; #define GAS __attribute__((address_space(1)))
; #define LAS __attribute__((address_space(3)))
; __device__ __forceinline__ void row_to_fp8_2(int lane, const float* xrow0, const float* xrow1, unsigned (&ow0)[4], unsigned (&ow1)[4], float& isc0, float& isc1) {
;     const GAS f32x4* xr0 = (const GAS f32x4*)xrow0 + lane; const GAS f32x4* xr1 = (const GAS f32x4*)xrow1 + lane;
;     f32x4 v0[4], v1[4];
; #pragma unroll
;     for (int j = 0; j < 4; ++j) { v0[j] = __builtin_nontemporal_load(xr0 + 64 * j); v1[j] = __builtin_nontemporal_load(xr1 + 64 * j); }
;     float m0 = 0.f, m1 = 0.f;
; #pragma unroll
;     for (int j = 0; j < 4; ++j) { m0 = fmaxf(m0, fmaxf(fmaxf(fabsf(v0[j].x), fabsf(v0[j].y)), fmaxf(fabsf(v0[j].z), fabsf(v0[j].w)))); m1 = fmaxf(m1, fmaxf(fmaxf(fabsf(v1[j].x), fabsf(v1[j].y)), fmaxf(fabsf(v1[j].z), fabsf(v1[j].w)))); }
; #pragma unroll
;     for (int o = 1; o < 64; o <<= 1) { m0 = fmaxf(m0, __shfl_xor(m0, o)); m1 = fmaxf(m1, __shfl_xor(m1, o)); }
;     int b0 = (int)((__float_as_uint(m0) >> 23) & 255u); b0 = b0 < 16 ? 16 : (b0 > 240 ? 240 : b0);
;     int b1 = (int)((__float_as_uint(m1) >> 23) & 255u); b1 = b1 < 16 ? 16 : (b1 > 240 ? 240 : b1);
;     const float s0 = __uint_as_float((unsigned)(261 - b0) << 23), s1 = __uint_as_float((unsigned)(261 - b1) << 23);
;     isc0 = __uint_as_float((unsigned)(b0 - 7) << 23); isc1 = __uint_as_float((unsigned)(b1 - 7) << 23);
; #pragma unroll
;     for (int j = 0; j < 4; ++j) { int p = __builtin_amdgcn_cvt_pk_fp8_f32(v0[j].x * s0, v0[j].y * s0, 0, false); p = __builtin_amdgcn_cvt_pk_fp8_f32(v0[j].z * s0, v0[j].w * s0, p, true); ow0[j] = (unsigned)p;
; __device__ __forceinline__ void p0_vslice_item(LAS unsigned char* lds, int wave, int tid, const float* vt_l, unsigned char* VS_l, float* vsc_l, int item) {
;     const int lane = tid & 63, e0 = item * 64;
;     __syncthreads();
; #pragma unroll 1
;     for (int i = 0; i < 8; i += 2) { const int er = wave * 8 + i; float isc0, isc1; unsigned ow0[4], ow1[4];
;         row_to_fp8_2(lane, vt_l + (size_t)(e0 + er) * 1024, vt_l + (size_t)(e0 + er + 1) * 1024, ow0, ow1, isc0, isc1);
; #pragma unroll
;         for (int j = 0; j < 4; ++j) { *(LAS unsigned*)(lds + er * 1032 + j * 256 + lane * 4) = ow0[j]; *(LAS unsigned*)(lds + (er + 1) * 1032 + j * 256 + lane * 4) = ow1[j]; }
;         if (lane == 0) { vsc_l[e0 + er] = isc0; vsc_l[e0 + er + 1] = isc1; } }
.LBB0_1182:
	global_load_dwordx4 v[14:17], v[4:5], off offset:-3072 nt
	global_load_dwordx4 v[18:21], v[4:5], off offset:-2048 nt
	global_load_dwordx4 v[22:25], v[4:5], off offset:-1024 nt
	global_load_dwordx4 v[26:29], v[4:5], off nt
	v_add_co_u32_e32 v12, vcc, 0xfffff000, v4
	s_waitcnt vmcnt(2)
	v_max_f32_e64 v46, |v21|, |v21|
	v_addc_co_u32_e32 v13, vcc, -1, v5, vcc
	global_load_dwordx4 v[30:33], v[12:13], off offset:-3072 nt
	global_load_dwordx4 v[34:37], v[12:13], off offset:-2048 nt
	global_load_dwordx4 v[38:41], v[12:13], off offset:-1024 nt
	global_load_dwordx4 v[42:45], v[4:5], off offset:-4096 nt
	v_max_f32_e64 v12, |v17|, |v17|
	v_max_f32_e64 v13, |v16|, |v16|
	v_max_f32_e64 v47, |v20|, |v20|
	s_waitcnt vmcnt(5)
	v_max_f32_e64 v48, |v25|, |v25|
	v_max_f32_e64 v49, |v24|, |v24|
	s_waitcnt vmcnt(4)
	v_max_f32_e64 v50, |v29|, |v29|
	v_max_f32_e64 v51, |v28|, |v28|
	v_max_f32_e32 v12, v13, v12
	v_max_f32_e32 v13, v47, v46
	v_max_f32_e32 v46, v49, v48
	v_max_f32_e32 v47, v51, v50
	v_max3_f32 v12, |v14|, |v15|, v12
	v_max3_f32 v13, |v18|, |v19|, v13
	v_max3_f32 v46, |v22|, |v23|, v46
	v_max3_f32 v47, |v26|, |v27|, v47
	v_max3_f32 v12, v12, 0, v13
	v_max3_f32 v12, v12, v46, v47
	ds_bpermute_b32 v47, v173, v12
	s_waitcnt lgkmcnt(0)
	v_max_f32_e32 v47, v47, v47
	v_max_f32_e32 v12, v12, v47
	ds_bpermute_b32 v47, v174, v12
	s_waitcnt lgkmcnt(0)
	v_max_f32_e32 v47, v47, v47
	v_max_f32_e32 v12, v12, v47
	ds_bpermute_b32 v47, v175, v12
	s_waitcnt lgkmcnt(0)
	v_max_f32_e32 v47, v47, v47
	v_max_f32_e32 v12, v12, v47
	ds_bpermute_b32 v47, v176, v12
	s_waitcnt lgkmcnt(0)
	v_max_f32_e32 v47, v47, v47
	v_max_f32_e32 v12, v12, v47
	ds_bpermute_b32 v47, v10, v12
	s_waitcnt lgkmcnt(0)
	v_max_f32_e32 v47, v47, v47
	v_max_f32_e32 v12, v12, v47
	ds_bpermute_b32 v47, v11, v12
	s_waitcnt lgkmcnt(0)
	v_max_f32_e32 v47, v47, v47
	v_max_f32_e32 v12, v12, v47
	v_bfe_u32 v12, v12, 23, 8
	v_med3_u32 v12, v12, 16, v8
	v_lshlrev_b32_e32 v12, 23, v12
	s_waitcnt vmcnt(3)
	v_max_f32_e64 v48, |v33|, |v33|
	v_max_f32_e64 v49, |v32|, |v32|
	s_waitcnt vmcnt(2)
	v_max_f32_e64 v50, |v37|, |v37|
	v_max_f32_e64 v51, |v36|, |v36|
	s_waitcnt vmcnt(1)
	v_max_f32_e64 v52, |v41|, |v41|
	v_max_f32_e64 v53, |v40|, |v40|
	s_waitcnt vmcnt(0)
	v_max_f32_e64 v54, |v45|, |v45|
	v_max_f32_e64 v55, |v44|, |v44|
	v_max_f32_e32 v48, v49, v48
	v_max_f32_e32 v49, v51, v50
	v_max_f32_e32 v13, v53, v52
	v_max_f32_e32 v50, v55, v54
	v_max3_f32 v48, |v30|, |v31|, v48
	v_max3_f32 v49, |v34|, |v35|, v49
	v_max3_f32 v13, |v38|, |v39|, v13
	v_max3_f32 v50, |v42|, |v43|, v50
	v_max3_f32 v46, v48, 0, v49
	v_max3_f32 v13, v46, v13, v50
	ds_bpermute_b32 v46, v173, v13
	v_mov_b32_e32 v49, 0
	v_mov_b32_e32 v48, 0
	v_mov_b32_e32 v53, 0
	v_mov_b32_e32 v50, 0
	s_waitcnt lgkmcnt(0)
	v_max_f32_e32 v46, v46, v46
	v_max_f32_e32 v13, v13, v46
	ds_bpermute_b32 v46, v174, v13
	v_mov_b32_e32 v51, 0
	v_mov_b32_e32 v52, 0
	v_mov_b32_e32 v54, 0
	s_waitcnt lgkmcnt(0)
	v_max_f32_e32 v46, v46, v46
	v_max_f32_e32 v13, v13, v46
	ds_bpermute_b32 v46, v175, v13
	s_waitcnt lgkmcnt(0)
	v_max_f32_e32 v46, v46, v46
	v_max_f32_e32 v13, v13, v46
	ds_bpermute_b32 v46, v176, v13
	s_waitcnt lgkmcnt(0)
	v_max_f32_e32 v46, v46, v46
	v_max_f32_e32 v13, v13, v46
	ds_bpermute_b32 v46, v10, v13
	s_waitcnt lgkmcnt(0)
	v_max_f32_e32 v46, v46, v46
	v_max_f32_e32 v13, v13, v46
	ds_bpermute_b32 v46, v11, v13
	s_waitcnt lgkmcnt(0)
	v_max_f32_e32 v46, v46, v46
	v_max_f32_e32 v13, v13, v46
	v_bfe_u32 v13, v13, 23, 8
	v_med3_u32 v13, v13, 16, v8
	v_sub_u32_e32 v46, 0x82800000, v12
	v_lshlrev_b32_e32 v13, 23, v13
	v_mul_f32_e32 v14, v14, v46
	v_mul_f32_e32 v15, v15, v46
	v_sub_u32_e32 v47, 0x82800000, v13
	v_cvt_pk_fp8_f32 v49, v14, v15
	v_mul_f32_e32 v14, v30, v47
	v_mul_f32_e32 v15, v31, v47
	v_cvt_pk_fp8_f32 v48, v14, v15
	v_mul_f32_e32 v22, v22, v46
	v_mul_f32_e32 v23, v23, v46
	v_mul_f32_e32 v18, v18, v46
	v_mul_f32_e32 v19, v19, v46
	v_cvt_pk_fp8_f32 v53, v22, v23
	v_mul_f32_e32 v22, v34, v47
	v_mul_f32_e32 v23, v35, v47
	v_mul_f32_e32 v16, v16, v46
	v_mul_f32_e32 v17, v17, v46
	v_cvt_pk_fp8_f32 v51, v18, v19
	v_mul_f32_e32 v18, v32, v47
	v_mul_f32_e32 v19, v33, v47
	v_mul_f32_e32 v30, v36, v47
	v_mul_f32_e32 v31, v37, v47
	v_mul_f32_e32 v32, v38, v47
	v_mul_f32_e32 v33, v39, v47
	v_mul_f32_e32 v36, v42, v47
	v_mul_f32_e32 v37, v43, v47
	v_cvt_pk_fp8_f32 v50, v22, v23
	v_cvt_pk_fp8_f32 v52, v32, v33
	v_cvt_pk_fp8_f32 v54, v36, v37
	v_cvt_pk_fp8_f32 v49, v16, v17 op_sel:[0,0,1]
	v_cvt_pk_fp8_f32 v48, v18, v19 op_sel:[0,0,1]
	v_mul_f32_e32 v16, v26, v46
	v_mul_f32_e32 v17, v27, v46
	v_mov_b32_e32 v18, 0
	v_cvt_pk_fp8_f32 v18, v16, v17
	v_mul_f32_e32 v20, v20, v46
	v_mul_f32_e32 v21, v21, v46
	v_mul_f32_e32 v34, v40, v47
	v_mul_f32_e32 v35, v41, v47
	v_cvt_pk_fp8_f32 v51, v20, v21 op_sel:[0,0,1]
	v_cvt_pk_fp8_f32 v50, v30, v31 op_sel:[0,0,1]
	v_mul_f32_e32 v14, v44, v47
	v_mul_f32_e32 v15, v45, v47
	v_mul_f32_e32 v24, v24, v46
	v_mul_f32_e32 v25, v25, v46
	v_cvt_pk_fp8_f32 v52, v34, v35 op_sel:[0,0,1]
	v_cvt_pk_fp8_f32 v54, v14, v15 op_sel:[0,0,1]
	v_mul_f32_e32 v14, v28, v46
	v_mul_f32_e32 v15, v29, v46
	v_cvt_pk_fp8_f32 v53, v24, v25 op_sel:[0,0,1]
	v_cvt_pk_fp8_f32 v18, v14, v15 op_sel:[0,0,1]
	v_add_u32_e32 v14, 8, v9
	ds_write2st64_b32 v9, v48, v50 offset1:1
	ds_write2st64_b32 v14, v49, v51 offset0:4 offset1:5
	ds_write2st64_b32 v9, v52, v54 offset0:2 offset1:3
	ds_write2st64_b32 v14, v53, v18 offset0:6 offset1:7
	s_and_saveexec_b64 s[16:17], s[4:5]
	s_cbranch_execz .LBB0_1181
	v_add_u32_e32 v14, 0xfc800000, v13
	v_add_u32_e32 v15, 0xfc800000, v12
	global_store_dword v1, v14, s[14:15] offset:-4
	global_store_dword v1, v15, s[14:15] offset:4
	s_sub_u32 s98, s14, s20
	s_sub_u32 s98, s98, 0x2000008
	s_lshr_b32 s98, s98, 2
	s_add_u32 s98, s98, 0x2100001
	v_mov_b32_e32 v56, s98
	v_lshrrev_b32_e32 v58, 23, v14
	v_lshrrev_b32_e32 v59, 23, v15
	global_store_byte v56, v58, s[20:21]
	global_store_byte v56, v59, s[20:21] offset:2
	s_branch .LBB0_1181

; #define PG8_LAS __attribute__((address_space(3)))
; #define RT_BAR() do { asm volatile("s_waitcnt lgkmcnt(0)" ::: "memory"); __builtin_amdgcn_s_barrier(); asm volatile("" ::: "memory"); } while (0)
;     __device__ __forceinline__ void fused(f32x4 (&acc)[2][2][4][2], const Unit& u, int wr, int wc, int fr, int fq, PG8_LAS unsigned char* lds, int wid, int lane) const {
;     ...
;                         const int rw = ai * HALF + wr * 64 + m * 16 + fr, g = 8 * wc + 4 * n + fq, col = 32 * wc + 16 * n + 4 * fq;
;                         const f32x4 v = acc[ai][bj][m][n]; f32x4 p;
; #pragma unroll
;                         for (int e = 0; e < 4; ++e) p[e] = __uint_as_float((__float_as_uint(v[e]) & ~127u) | (unsigned)(col + e));
;                         *(PG8_LAS f32x4*)(tile + rw * 128 + ((g ^ fr) << 2)) = p;
;                     }
;             RT_BAR();
;             float run[16];
; #pragma unroll
;             for (int grp = 0; grp < 4; ++grp) {
;                 float nw[16];
; #pragma unroll
;                 for (int i = 0; i < 4; ++i) { const int g = half * 16 + grp * 4 + i; const f32x4 v = *(const PG8_LAS f32x4*)(tile + row * 128 + ((g ^ (row & 15)) << 2));
;                     nw[4 * i] = v[0]; nw[4 * i + 1] = v[1]; nw[4 * i + 2] = v[2]; nw[4 * i + 3] = v[3]; }
;                 sort16_desc(nw);
;                 if (grp == 0) {
; #pragma unroll
;                     for (int q = 0; q < 16; ++q) run[q] = nw[q];
;                 } else merge_top16(run, nw);
.LBB0_1580:
	s_movk_i32 s19, 0xff80
	v_and_or_b32 v60, v60, s19, v129
	v_and_or_b32 v61, v61, s98, v218
	v_and_or_b32 v62, v62, s98, v219
	v_and_or_b32 v63, v63, s98, v220
	v_and_or_b32 v56, v56, s19, v124
	v_and_or_b32 v57, v57, s98, v221
	v_and_or_b32 v58, v58, s98, v222
	v_and_or_b32 v59, v59, s98, v223
	v_and_or_b32 v52, v52, s19, v129
	v_and_or_b32 v53, v53, s98, v218
	v_and_or_b32 v54, v54, s98, v219
	v_and_or_b32 v55, v55, s98, v220
	v_and_or_b32 v48, v48, s19, v124
	v_and_or_b32 v49, v49, s98, v221
	v_and_or_b32 v50, v50, s98, v222
	v_and_or_b32 v51, v51, s98, v223
	v_and_or_b32 v44, v44, s19, v129
	v_and_or_b32 v45, v45, s98, v218
	v_and_or_b32 v46, v46, s98, v219
	v_and_or_b32 v47, v47, s98, v220
	v_and_or_b32 v40, v40, s19, v124
	v_and_or_b32 v41, v41, s98, v221
	v_and_or_b32 v42, v42, s98, v222
	v_and_or_b32 v43, v43, s98, v223
	v_and_or_b32 v36, v36, s19, v129
	v_and_or_b32 v37, v37, s98, v218
	v_and_or_b32 v38, v38, s98, v219
	v_and_or_b32 v39, v39, s98, v220
	v_and_or_b32 v32, v32, s19, v124
	v_and_or_b32 v33, v33, s98, v221
	v_and_or_b32 v34, v34, s98, v222
	v_and_or_b32 v35, v35, s98, v223
	v_and_or_b32 v28, v28, s19, v129
	v_and_or_b32 v29, v29, s98, v218
	v_and_or_b32 v30, v30, s98, v219
	v_and_or_b32 v31, v31, s98, v220
	v_and_or_b32 v24, v24, s19, v124
	v_and_or_b32 v25, v25, s98, v221
	v_and_or_b32 v26, v26, s98, v222
	v_and_or_b32 v27, v27, s98, v223
	v_and_or_b32 v20, v20, s19, v129
	v_and_or_b32 v21, v21, s98, v218
	v_and_or_b32 v22, v22, s98, v219
	v_and_or_b32 v23, v23, s98, v220
	v_and_or_b32 v16, v16, s19, v124
	v_and_or_b32 v17, v17, s98, v221
	v_and_or_b32 v18, v18, s98, v222
	v_and_or_b32 v19, v19, s98, v223
	v_and_or_b32 v12, v12, s19, v129
	v_and_or_b32 v13, v13, s98, v218
	v_and_or_b32 v14, v14, s98, v219
	v_and_or_b32 v15, v15, s98, v220
	v_and_or_b32 v8, v8, s19, v124
	v_and_or_b32 v9, v9, s98, v221
	v_and_or_b32 v10, v10, s98, v222
	v_and_or_b32 v11, v11, s98, v223
	v_and_or_b32 v4, v4, s19, v129
	v_and_or_b32 v5, v5, s98, v218
	v_and_or_b32 v6, v6, s98, v219
	v_and_or_b32 v7, v7, s98, v220
	v_and_or_b32 v0, v0, s19, v124
	v_and_or_b32 v1, v1, s98, v221
	v_and_or_b32 v2, v2, s98, v222
	v_and_or_b32 v3, v3, s98, v223
	s_waitcnt lgkmcnt(0)
	s_barrier
	ds_write_b128 v125, v[60:63]
	ds_write_b128 v120, v[56:59]
	ds_write_b128 v125, v[52:55] offset:8192
	ds_write_b128 v120, v[48:51] offset:8192
	ds_write_b128 v125, v[44:47] offset:16384
	ds_write_b128 v120, v[40:43] offset:16384
	ds_write_b128 v125, v[36:39] offset:24576
	ds_write_b128 v120, v[32:35] offset:24576
	ds_write_b128 v92, v[28:31]
	ds_write_b128 v88, v[24:27]
	ds_write_b128 v84, v[20:23]
	ds_write_b128 v82, v[16:19]
	ds_write_b128 v85, v[12:15]
	ds_write_b128 v86, v[8:11]
	ds_write_b128 v90, v[4:7]
	ds_write_b128 v91, v[0:3]
	s_waitcnt lgkmcnt(0)
	s_barrier
	s_lshr_b32 s98, s61, 2
	v_lshlrev_b32_e32 v240, 6, v128
	s_lshl_b32 s98, s98, 14
	v_add_u32_e32 v240, s98, v240
	v_add_u32_e32 v241, 0x18000, v240
	v_add_u32_e32 v240, 0x19108000, v240
	global_load_dwordx4 v[224:227], v240, s[30:31]
	global_load_dwordx4 v[228:231], v240, s[30:31] offset:16
	global_load_dwordx4 v[232:235], v240, s[30:31] offset:32
	global_load_dwordx4 v[236:239], v240, s[30:31] offset:48
	ds_read_b128 v[0:3], v93
	ds_read_b128 v[4:7], v89
	s_and_b64 vcc, exec, s[4:5]
	s_waitcnt lgkmcnt(0)
	v_min_f32_e32 v10, v0, v1
	v_max_f32_e32 v8, v0, v1
	v_min_f32_e32 v13, v2, v3
	v_max_f32_e32 v9, v2, v3
	v_min_f32_e32 v17, v4, v5
	v_max_f32_e32 v15, v4, v5
	v_min_f32_e32 v20, v6, v7
	v_max_f32_e32 v16, v6, v7
	ds_read_b128 v[0:3], v81
	ds_read_b128 v[4:7], v80
	s_waitcnt lgkmcnt(0)
	v_min_f32_e32 v23, v0, v1
	v_min_f32_e32 v24, v2, v3
	v_min_f32_e32 v26, v4, v5
	v_min_f32_e32 v27, v6, v7
	v_max_f32_e32 v0, v0, v1
	v_max_f32_e32 v1, v2, v3
	v_max_f32_e32 v4, v4, v5
	v_max_f32_e32 v5, v6, v7
	v_min_f32_e32 v14, v10, v13
	v_min_f32_e32 v21, v17, v20
	v_min_f32_e32 v25, v23, v24
	v_max_f32_e32 v10, v10, v13
	v_min_f32_e32 v11, v8, v9
	v_max_f32_e32 v13, v17, v20
	v_min_f32_e32 v17, v15, v16
	v_max_f32_e32 v23, v23, v24
	v_min_f32_e32 v2, v0, v1
	v_max_f32_e32 v24, v26, v27
	v_min_f32_e32 v6, v4, v5
	v_min_f32_e32 v28, v26, v27
	v_max_f32_e32 v12, v10, v11
	v_max_f32_e32 v18, v13, v17
	v_max_f32_e32 v3, v23, v2
	v_max_f32_e32 v7, v24, v6
	v_min_f32_e32 v22, v14, v21
	v_min_f32_e32 v29, v25, v28
	v_max_f32_e32 v14, v14, v21
	v_min_f32_e32 v19, v12, v18
	v_min_f32_e32 v10, v10, v11
	v_min_f32_e32 v11, v13, v17
	v_max_f32_e32 v21, v25, v28
	v_min_f32_e32 v25, v3, v7
	v_min_f32_e32 v2, v23, v2
	v_min_f32_e32 v6, v24, v6
	v_max_f32_e32 v20, v14, v19
	v_max_f32_e32 v13, v10, v11
	v_max_f32_e32 v8, v8, v9
	v_max_f32_e32 v9, v15, v16
	v_max_f32_e32 v23, v2, v6
	v_max_f32_e32 v0, v0, v1
	v_max_f32_e32 v1, v4, v5
	v_min_f32_e32 v14, v14, v19
	v_min_f32_e32 v10, v10, v11
	v_min_f32_e32 v19, v21, v25
	v_min_f32_e32 v2, v2, v6
	v_min_f32_e32 v15, v8, v9
	v_min_f32_e32 v4, v0, v1
	v_max_f32_e32 v11, v14, v10
	v_max_f32_e32 v6, v19, v2
	v_min_f32_e32 v10, v14, v10
	v_min_f32_e32 v2, v19, v2
	v_min_f32_e32 v5, v23, v4
	v_min_f32_e32 v14, v10, v2
	v_max_f32_e32 v2, v10, v2
	v_max_f32_e32 v10, v12, v18
	v_max_f32_e32 v12, v13, v15
	v_max_f32_e32 v3, v3, v7
	v_max_f32_e32 v4, v23, v4
	v_min_f32_e32 v16, v13, v15
	v_max_f32_e32 v26, v21, v25
	v_min_f32_e32 v13, v10, v12
	v_min_f32_e32 v7, v3, v4
	v_max_f32_e32 v10, v10, v12
	v_max_f32_e32 v3, v3, v4
	v_max_f32_e32 v17, v20, v16
	v_max_f32_e32 v24, v26, v5
	v_min_f32_e32 v21, v11, v6
	v_min_f32_e32 v16, v20, v16
	v_min_f32_e32 v5, v26, v5
	v_max_f32_e32 v6, v11, v6
	v_min_f32_e32 v4, v10, v3
	v_max_f32_e32 v8, v8, v9
	v_max_f32_e32 v9, v0, v1
	v_max_f32_e32 v30, v22, v29
	v_min_f32_e32 v27, v17, v24
	v_min_f32_e32 v15, v13, v7
	v_min_f32_e32 v20, v16, v5
	v_min_f32_e32 v11, v6, v4
	v_max_f32_e32 v5, v16, v5
	v_min_f32_e32 v0, v8, v9
	v_max_f32_e32 v17, v17, v24
	v_max_f32_e32 v4, v6, v4
	v_min_f32_e32 v28, v30, v27
	v_min_f32_e32 v18, v2, v15
	v_max_f32_e32 v27, v30, v27
	v_max_f32_e32 v2, v2, v15
	v_min_f32_e32 v1, v5, v0
	v_min_f32_e32 v24, v17, v4
	v_max_f32_e32 v17, v17, v4
	v_max_f32_e32 v4, v13, v7
	v_max_f32_e32 v5, v5, v0
	v_min_f32_e32 v12, v27, v11
	v_max_f32_e32 v11, v27, v11
	v_min_f32_e32 v15, v2, v1
	v_max_f32_e32 v27, v2, v1
	v_min_f32_e32 v13, v4, v5
	v_max_f32_e32 v10, v10, v3
	ds_read_b128 v[0:3], v99
	v_max_f32_e32 v31, v4, v5
	ds_read_b128 v[4:7], v96
	v_min_f32_e32 v22, v22, v29
	v_min_f32_e32 v25, v28, v21
	s_waitcnt lgkmcnt(0)
; __device__ __forceinline__ void sort16_desc(float (&v)[16]) {
;     CE(v[0], v[1]); CE(v[2], v[3]); CE(v[0], v[2]); CE(v[1], v[3]);
;     CE(v[1], v[2]); CE(v[4], v[5]); CE(v[6], v[7]); CE(v[4], v[6]);
;     CE(v[5], v[7]); CE(v[5], v[6]); CE(v[0], v[4]); CE(v[2], v[6]);
;     CE(v[2], v[4]); CE(v[1], v[5]); CE(v[3], v[7]); CE(v[3], v[5]);
;     CE(v[1], v[2]); CE(v[3], v[4]); CE(v[5], v[6]); CE(v[8], v[9]);
;     CE(v[10], v[11]); CE(v[8], v[10]); CE(v[9], v[11]); CE(v[9], v[10]);
;     CE(v[12], v[13]); CE(v[14], v[15]); CE(v[12], v[14]); CE(v[13], v[15]);
;     CE(v[13], v[14]); CE(v[8], v[12]); CE(v[10], v[14]); CE(v[10], v[12]);
;     CE(v[9], v[13]); CE(v[11], v[15]); CE(v[11], v[13]); CE(v[9], v[10]);
;     CE(v[11], v[12]); CE(v[13], v[14]); CE(v[0], v[8]); CE(v[4], v[12]);
;     CE(v[4], v[8]); CE(v[2], v[10]); CE(v[6], v[14]); CE(v[6], v[10]);
;     CE(v[2], v[4]); CE(v[6], v[8]); CE(v[10], v[12]); CE(v[1], v[9]);
;     CE(v[5], v[13]); CE(v[5], v[9]); CE(v[3], v[11]); CE(v[7], v[15]);
;     CE(v[7], v[11]); CE(v[3], v[5]); CE(v[7], v[9]); CE(v[11], v[13]);
;     CE(v[1], v[2]); CE(v[3], v[4]); CE(v[5], v[6]); CE(v[7], v[8]);
;     CE(v[9], v[10]); CE(v[11], v[12]); CE(v[13], v[14]);
; }
; __device__ __forceinline__ void merge_top16(float (&v)[16], const float (&nw)[16]) {
;     v[0] = fmaxf(v[0], nw[15]); v[1] = fmaxf(v[1], nw[14]); v[2] = fmaxf(v[2], nw[13]); v[3] = fmaxf(v[3], nw[12]); v[4] = fmaxf(v[4], nw[11]); v[5] = fmaxf(v[5], nw[10]); v[6] = fmaxf(v[6], nw[9]); v[7] = fmaxf(v[7], nw[8]); v[8] = fmaxf(v[8], nw[7]); v[9] = fmaxf(v[9], nw[6]); v[10] = fmaxf(v[10], nw[5]); v[11] = fmaxf(v[11], nw[4]); v[12] = fmaxf(v[12], nw[3]); v[13] = fmaxf(v[13], nw[2]); v[14] = fmaxf(v[14], nw[1]); v[15] = fmaxf(v[15], nw[0]);
;     CE(v[0], v[8]); CE(v[1], v[9]); CE(v[2], v[10]); CE(v[3], v[11]);
;     CE(v[4], v[12]); CE(v[5], v[13]); CE(v[6], v[14]); CE(v[7], v[15]);
;     CE(v[0], v[4]); CE(v[1], v[5]); CE(v[2], v[6]); CE(v[3], v[7]);
;     CE(v[8], v[12]); CE(v[9], v[13]); CE(v[10], v[14]); CE(v[11], v[15]);
;     CE(v[0], v[2]); CE(v[1], v[3]); CE(v[4], v[6]); CE(v[5], v[7]);
;     CE(v[8], v[10]); CE(v[9], v[11]); CE(v[12], v[14]); CE(v[13], v[15]);
;     CE(v[0], v[1]); CE(v[2], v[3]); CE(v[4], v[5]); CE(v[6], v[7]);
;     CE(v[8], v[9]); CE(v[10], v[11]); CE(v[12], v[13]); CE(v[14], v[15]);
; }
	v_min_f32_e32 v34, v0, v1
	v_max_f32_e32 v29, v0, v1
	v_min_f32_e32 v37, v2, v3
	v_max_f32_e32 v33, v2, v3
	v_min_f32_e32 v41, v4, v5
	v_max_f32_e32 v39, v4, v5
	v_min_f32_e32 v44, v6, v7
	v_max_f32_e32 v40, v6, v7
	ds_read_b128 v[0:3], v87
	ds_read_b128 v[4:7], v83
	s_waitcnt lgkmcnt(0)
	v_min_f32_e32 v47, v0, v1
	v_min_f32_e32 v48, v2, v3
	v_min_f32_e32 v50, v4, v5
	v_min_f32_e32 v51, v6, v7
	v_max_f32_e32 v0, v0, v1
	v_max_f32_e32 v1, v2, v3
	v_max_f32_e32 v4, v4, v5
	v_max_f32_e32 v5, v6, v7
	v_min_f32_e32 v38, v34, v37
	v_min_f32_e32 v45, v41, v44
	v_min_f32_e32 v49, v47, v48
	v_max_f32_e32 v34, v34, v37
	v_min_f32_e32 v35, v29, v33
	v_max_f32_e32 v37, v41, v44
	v_min_f32_e32 v41, v39, v40
	v_max_f32_e32 v47, v47, v48
	v_min_f32_e32 v2, v0, v1
	v_max_f32_e32 v48, v50, v51
	v_min_f32_e32 v6, v4, v5
	v_min_f32_e32 v52, v50, v51
	v_max_f32_e32 v36, v34, v35
	v_max_f32_e32 v42, v37, v41
	v_max_f32_e32 v3, v47, v2
	v_max_f32_e32 v7, v48, v6
	v_min_f32_e32 v46, v38, v45
	v_min_f32_e32 v53, v49, v52
	v_max_f32_e32 v38, v38, v45
	v_min_f32_e32 v43, v36, v42
	v_min_f32_e32 v34, v34, v35
	v_min_f32_e32 v35, v37, v41
	v_max_f32_e32 v45, v49, v52
	v_min_f32_e32 v49, v3, v7
	v_min_f32_e32 v2, v47, v2
	v_min_f32_e32 v6, v48, v6
	v_max_f32_e32 v44, v38, v43
	v_max_f32_e32 v37, v34, v35
	v_max_f32_e32 v29, v29, v33
	v_max_f32_e32 v33, v39, v40
	v_max_f32_e32 v47, v2, v6
	v_max_f32_e32 v0, v0, v1
	v_max_f32_e32 v1, v4, v5
	v_min_f32_e32 v38, v38, v43
	v_min_f32_e32 v34, v34, v35
	v_min_f32_e32 v43, v45, v49
	v_min_f32_e32 v2, v2, v6
	v_min_f32_e32 v39, v29, v33
	v_min_f32_e32 v4, v0, v1
	v_max_f32_e32 v35, v38, v34
	v_max_f32_e32 v6, v43, v2
	v_min_f32_e32 v34, v38, v34
	v_min_f32_e32 v2, v43, v2
	v_min_f32_e32 v40, v37, v39
	v_max_f32_e32 v50, v45, v49
	v_min_f32_e32 v5, v47, v4
	v_min_f32_e32 v38, v34, v2
	v_max_f32_e32 v2, v34, v2
	v_max_f32_e32 v34, v36, v42
	v_max_f32_e32 v36, v37, v39
	v_max_f32_e32 v3, v3, v7
	v_max_f32_e32 v4, v47, v4
	v_max_f32_e32 v41, v44, v40
	v_max_f32_e32 v48, v50, v5
	v_min_f32_e32 v37, v34, v36
	v_min_f32_e32 v7, v3, v4
	v_min_f32_e32 v40, v44, v40
	v_min_f32_e32 v5, v50, v5
	v_max_f32_e32 v34, v34, v36
	v_max_f32_e32 v3, v3, v4
	v_max_f32_e32 v29, v29, v33
	v_max_f32_e32 v0, v0, v1
	v_max_f32_e32 v54, v46, v53
	v_min_f32_e32 v51, v41, v48
	v_min_f32_e32 v45, v35, v6
	v_min_f32_e32 v39, v37, v7
	v_min_f32_e32 v44, v40, v5
	v_max_f32_e32 v6, v35, v6
	v_min_f32_e32 v4, v34, v3
	v_max_f32_e32 v5, v40, v5
	v_min_f32_e32 v1, v29, v0
	v_min_f32_e32 v52, v54, v51
	v_min_f32_e32 v42, v2, v39
	v_max_f32_e32 v51, v54, v51
	v_min_f32_e32 v35, v6, v4
	v_max_f32_e32 v2, v2, v39
	v_min_f32_e32 v33, v5, v1
	v_max_f32_e32 v41, v41, v48
	v_max_f32_e32 v4, v6, v4
	v_max_f32_e32 v7, v37, v7
	v_max_f32_e32 v1, v5, v1
	v_max_f32_e32 v21, v28, v21
	v_min_f32_e32 v23, v18, v20
	v_max_f32_e32 v18, v18, v20
	v_min_f32_e32 v49, v52, v45
	v_max_f32_e32 v45, v52, v45
	v_min_f32_e32 v47, v42, v44
	v_min_f32_e32 v36, v51, v35
	v_max_f32_e32 v42, v42, v44
	v_max_f32_e32 v35, v51, v35
	v_min_f32_e32 v39, v2, v33
	v_min_f32_e32 v6, v41, v4
	v_max_f32_e32 v2, v2, v33
	v_max_f32_e32 v4, v41, v4
	v_min_f32_e32 v5, v7, v1
	v_max_f32_e32 v3, v34, v3
	v_max_f32_e32 v1, v7, v1
	v_min_f32_e32 v19, v25, v14
	v_min_f32_e32 v26, v21, v23
	v_min_f32_e32 v20, v12, v18
	v_min_f32_e32 v16, v11, v15
	v_min_f32_e32 v28, v24, v27
	v_min_f32_e32 v30, v17, v13
	v_min_f32_e32 v32, v10, v31
	v_min_f32_e32 v43, v49, v38
	v_min_f32_e32 v50, v45, v47
	v_min_f32_e32 v44, v36, v42
	v_min_f32_e32 v40, v35, v39
	v_min_f32_e32 v33, v6, v2
	v_min_f32_e32 v37, v4, v5
	v_min_f32_e32 v7, v3, v1
	v_min_f32_e32 v34, v46, v53
	v_max3_f32 v8, v8, v9, v34
	v_max3_f32 v9, v10, v31, v43
	v_max3_f32 v10, v32, v49, v38
	v_max3_f32 v13, v17, v13, v50
	v_max3_f32 v17, v30, v45, v47
	v_max3_f32 v24, v24, v27, v44
	v_max3_f32 v27, v28, v36, v42
	v_max3_f32 v11, v11, v15, v40
	v_max3_f32 v15, v16, v35, v39
	v_max3_f32 v12, v12, v18, v33
	v_max3_f32 v2, v20, v6, v2
	v_max3_f32 v6, v21, v23, v37
	v_max3_f32 v4, v26, v4, v5
	v_max3_f32 v5, v25, v14, v7
	v_max3_f32 v1, v19, v3, v1
	v_max3_f32 v0, v22, v29, v0
	v_max_f32_e32 v3, v8, v15
	v_min_f32_e32 v7, v8, v15
	v_max_f32_e32 v8, v9, v12
	v_min_f32_e32 v9, v9, v12
	v_max_f32_e32 v12, v10, v2
	v_min_f32_e32 v2, v10, v2
	v_max_f32_e32 v10, v13, v6
	v_min_f32_e32 v6, v13, v6
	v_max_f32_e32 v13, v17, v4
	v_min_f32_e32 v4, v17, v4
	v_max_f32_e32 v14, v24, v5
	v_min_f32_e32 v5, v24, v5
	v_max_f32_e32 v15, v27, v1
	v_min_f32_e32 v1, v27, v1
	v_max_f32_e32 v16, v11, v0
	v_min_f32_e32 v0, v11, v0
	v_max_f32_e32 v11, v3, v13
	v_min_f32_e32 v3, v3, v13
	v_max_f32_e32 v13, v8, v14
	v_min_f32_e32 v8, v8, v14
	v_max_f32_e32 v14, v12, v15
	v_min_f32_e32 v12, v12, v15
	v_max_f32_e32 v15, v10, v16
	v_min_f32_e32 v10, v10, v16
	v_max_f32_e32 v16, v7, v4
	v_min_f32_e32 v4, v7, v4
	v_max_f32_e32 v7, v9, v5
	v_min_f32_e32 v5, v9, v5
	v_max_f32_e32 v9, v2, v1
	v_min_f32_e32 v1, v2, v1
	v_max_f32_e32 v2, v6, v0
	v_min_f32_e32 v0, v6, v0
	v_max_f32_e32 v17, v11, v14
	v_min_f32_e32 v11, v11, v14
	v_max_f32_e32 v14, v13, v15
	v_min_f32_e32 v13, v13, v15
	v_max_f32_e32 v15, v3, v12
	v_min_f32_e32 v12, v3, v12
	v_max_f32_e32 v18, v8, v10
	v_min_f32_e32 v8, v8, v10
	v_max_f32_e32 v10, v16, v9
	v_min_f32_e32 v9, v16, v9
	v_max_f32_e32 v16, v7, v2
	v_min_f32_e32 v19, v7, v2
	v_max_f32_e32 v20, v4, v1
	v_min_f32_e32 v21, v4, v1
	v_max_f32_e32 v22, v5, v0
	v_min_f32_e32 v23, v5, v0
	ds_read_b128 v[0:3], v102
	ds_read_b128 v[4:7], v101
	v_min_f32_e32 v24, v17, v14
	v_min_f32_e32 v25, v11, v13
	v_min_f32_e32 v26, v15, v18
	s_waitcnt lgkmcnt(0)
; __device__ __forceinline__ void sort16_desc(float (&v)[16]) {
;     CE(v[0], v[1]); CE(v[2], v[3]); CE(v[0], v[2]); CE(v[1], v[3]);
;     CE(v[1], v[2]); CE(v[4], v[5]); CE(v[6], v[7]); CE(v[4], v[6]);
;     CE(v[5], v[7]); CE(v[5], v[6]); CE(v[0], v[4]); CE(v[2], v[6]);
;     CE(v[2], v[4]); CE(v[1], v[5]); CE(v[3], v[7]); CE(v[3], v[5]);
;     CE(v[1], v[2]); CE(v[3], v[4]); CE(v[5], v[6]); CE(v[8], v[9]);
;     CE(v[10], v[11]); CE(v[8], v[10]); CE(v[9], v[11]); CE(v[9], v[10]);
;     CE(v[12], v[13]); CE(v[14], v[15]); CE(v[12], v[14]); CE(v[13], v[15]);
;     CE(v[13], v[14]); CE(v[8], v[12]); CE(v[10], v[14]); CE(v[10], v[12]);
;     CE(v[9], v[13]); CE(v[11], v[15]); CE(v[11], v[13]); CE(v[9], v[10]);
;     CE(v[11], v[12]); CE(v[13], v[14]); CE(v[0], v[8]); CE(v[4], v[12]);
;     CE(v[4], v[8]); CE(v[2], v[10]); CE(v[6], v[14]); CE(v[6], v[10]);
;     CE(v[2], v[4]); CE(v[6], v[8]); CE(v[10], v[12]); CE(v[1], v[9]);
;     CE(v[5], v[13]); CE(v[5], v[9]); CE(v[3], v[11]); CE(v[7], v[15]);
;     CE(v[7], v[11]); CE(v[3], v[5]); CE(v[7], v[9]); CE(v[11], v[13]);
;     CE(v[1], v[2]); CE(v[3], v[4]); CE(v[5], v[6]); CE(v[7], v[8]);
;     CE(v[9], v[10]); CE(v[11], v[12]); CE(v[13], v[14]);
; }
; __device__ __forceinline__ void merge_top16(float (&v)[16], const float (&nw)[16]) {
;     v[0] = fmaxf(v[0], nw[15]); v[1] = fmaxf(v[1], nw[14]); v[2] = fmaxf(v[2], nw[13]); v[3] = fmaxf(v[3], nw[12]); v[4] = fmaxf(v[4], nw[11]); v[5] = fmaxf(v[5], nw[10]); v[6] = fmaxf(v[6], nw[9]); v[7] = fmaxf(v[7], nw[8]); v[8] = fmaxf(v[8], nw[7]); v[9] = fmaxf(v[9], nw[6]); v[10] = fmaxf(v[10], nw[5]); v[11] = fmaxf(v[11], nw[4]); v[12] = fmaxf(v[12], nw[3]); v[13] = fmaxf(v[13], nw[2]); v[14] = fmaxf(v[14], nw[1]); v[15] = fmaxf(v[15], nw[0]);
;     CE(v[0], v[8]); CE(v[1], v[9]); CE(v[2], v[10]); CE(v[3], v[11]);
;     CE(v[4], v[12]); CE(v[5], v[13]); CE(v[6], v[14]); CE(v[7], v[15]);
;     CE(v[0], v[4]); CE(v[1], v[5]); CE(v[2], v[6]); CE(v[3], v[7]);
;     CE(v[8], v[12]); CE(v[9], v[13]); CE(v[10], v[14]); CE(v[11], v[15]);
;     CE(v[0], v[2]); CE(v[1], v[3]); CE(v[4], v[6]); CE(v[5], v[7]);
;     CE(v[8], v[10]); CE(v[9], v[11]); CE(v[12], v[14]); CE(v[13], v[15]);
;     CE(v[0], v[1]); CE(v[2], v[3]); CE(v[4], v[5]); CE(v[6], v[7]);
;     CE(v[8], v[9]); CE(v[10], v[11]); CE(v[12], v[13]); CE(v[14], v[15]);
; }
	v_min_f32_e32 v34, v0, v1
	v_max_f32_e32 v32, v0, v1
	v_min_f32_e32 v37, v2, v3
	v_max_f32_e32 v33, v2, v3
	v_min_f32_e32 v41, v4, v5
	v_max_f32_e32 v39, v4, v5
	v_min_f32_e32 v44, v6, v7
	v_max_f32_e32 v40, v6, v7
	ds_read_b128 v[0:3], v95
	ds_read_b128 v[4:7], v94
	s_waitcnt lgkmcnt(0)
	v_min_f32_e32 v47, v0, v1
	v_min_f32_e32 v48, v2, v3
	v_min_f32_e32 v50, v4, v5
	v_min_f32_e32 v51, v6, v7
	v_max_f32_e32 v0, v0, v1
	v_max_f32_e32 v1, v2, v3
	v_max_f32_e32 v4, v4, v5
	v_max_f32_e32 v5, v6, v7
	v_min_f32_e32 v38, v34, v37
	v_min_f32_e32 v45, v41, v44
	v_min_f32_e32 v49, v47, v48
	v_max_f32_e32 v34, v34, v37
	v_min_f32_e32 v35, v32, v33
	v_max_f32_e32 v37, v41, v44
	v_min_f32_e32 v41, v39, v40
	v_max_f32_e32 v47, v47, v48
	v_min_f32_e32 v2, v0, v1
	v_max_f32_e32 v48, v50, v51
	v_min_f32_e32 v6, v4, v5
	v_min_f32_e32 v52, v50, v51
	v_max_f32_e32 v36, v34, v35
	v_max_f32_e32 v42, v37, v41
	v_max_f32_e32 v3, v47, v2
	v_max_f32_e32 v7, v48, v6
	v_min_f32_e32 v46, v38, v45
	v_min_f32_e32 v53, v49, v52
	v_max_f32_e32 v38, v38, v45
	v_min_f32_e32 v43, v36, v42
	v_min_f32_e32 v34, v34, v35
	v_min_f32_e32 v35, v37, v41
	v_max_f32_e32 v45, v49, v52
	v_min_f32_e32 v49, v3, v7
	v_min_f32_e32 v2, v47, v2
	v_min_f32_e32 v6, v48, v6
	v_max_f32_e32 v44, v38, v43
	v_max_f32_e32 v37, v34, v35
	v_max_f32_e32 v32, v32, v33
	v_max_f32_e32 v33, v39, v40
	v_max_f32_e32 v47, v2, v6
	v_max_f32_e32 v0, v0, v1
	v_max_f32_e32 v1, v4, v5
	v_min_f32_e32 v38, v38, v43
	v_min_f32_e32 v34, v34, v35
	v_min_f32_e32 v43, v45, v49
	v_min_f32_e32 v2, v2, v6
	v_min_f32_e32 v39, v32, v33
	v_min_f32_e32 v4, v0, v1
	v_max_f32_e32 v35, v38, v34
	v_max_f32_e32 v6, v43, v2
	v_min_f32_e32 v34, v38, v34
	v_min_f32_e32 v2, v43, v2
	v_min_f32_e32 v40, v37, v39
	v_max_f32_e32 v50, v45, v49
	v_min_f32_e32 v5, v47, v4
	v_min_f32_e32 v38, v34, v2
	v_max_f32_e32 v2, v34, v2
	v_max_f32_e32 v34, v36, v42
	v_max_f32_e32 v36, v37, v39
	v_max_f32_e32 v3, v3, v7
	v_max_f32_e32 v4, v47, v4
	v_max_f32_e32 v41, v44, v40
	v_max_f32_e32 v48, v50, v5
	v_min_f32_e32 v37, v34, v36
	v_min_f32_e32 v7, v3, v4
	v_max_f32_e32 v54, v46, v53
	v_min_f32_e32 v51, v41, v48
	v_min_f32_e32 v39, v37, v7
	v_min_f32_e32 v40, v44, v40
	v_min_f32_e32 v5, v50, v5
	v_min_f32_e32 v52, v54, v51
	v_min_f32_e32 v45, v35, v6
	v_min_f32_e32 v42, v2, v39
	v_min_f32_e32 v44, v40, v5
	v_max_f32_e32 v34, v34, v36
	v_max_f32_e32 v3, v3, v4
	v_max_f32_e32 v32, v32, v33
	v_max_f32_e32 v0, v0, v1
	v_min_f32_e32 v49, v52, v45
	v_max_f32_e32 v45, v52, v45
	v_min_f32_e32 v47, v42, v44
	v_max_f32_e32 v6, v35, v6
	v_min_f32_e32 v4, v34, v3
	v_max_f32_e32 v5, v40, v5
	v_min_f32_e32 v1, v32, v0
	v_min_f32_e32 v43, v49, v38
	v_max_f32_e32 v38, v49, v38
	v_min_f32_e32 v49, v45, v47
	v_max_f32_e32 v45, v45, v47
	v_max_f32_e32 v47, v54, v51
	v_min_f32_e32 v35, v6, v4
	v_max_f32_e32 v2, v2, v39
	v_min_f32_e32 v33, v5, v1
	v_min_f32_e32 v36, v47, v35
	v_max_f32_e32 v35, v47, v35
	v_min_f32_e32 v39, v2, v33
	v_min_f32_e32 v40, v35, v39
	v_max_f32_e32 v35, v35, v39
	v_max_f32_e32 v39, v41, v48
	v_max_f32_e32 v4, v6, v4
	v_min_f32_e32 v6, v39, v4
	v_max_f32_e32 v2, v2, v33
	v_min_f32_e32 v33, v6, v2
	v_max_f32_e32 v2, v6, v2
	v_max_f32_e32 v6, v37, v7
	v_max_f32_e32 v1, v5, v1
	v_max_f32_e32 v42, v42, v44
	v_max_f32_e32 v4, v39, v4
	v_min_f32_e32 v5, v6, v1
	v_max_f32_e32 v3, v34, v3
	v_max_f32_e32 v1, v6, v1
	v_min_f32_e32 v27, v12, v8
	v_min_f32_e32 v28, v10, v16
	v_min_f32_e32 v29, v9, v19
	v_min_f32_e32 v30, v20, v22
	v_min_f32_e32 v31, v21, v23
	v_min_f32_e32 v44, v36, v42
	v_max_f32_e32 v36, v36, v42
	v_min_f32_e32 v7, v4, v5
	v_max_f32_e32 v4, v4, v5
	v_min_f32_e32 v5, v3, v1
	v_max_f32_e32 v1, v3, v1
	v_min_f32_e32 v3, v46, v53
	v_max3_f32 v3, v17, v14, v3
	v_max_f32_e32 v6, v24, v43
	v_max3_f32 v11, v11, v13, v38
	v_max_f32_e32 v13, v25, v49
	v_max3_f32 v14, v15, v18, v45
	v_max_f32_e32 v15, v26, v44
	v_max3_f32 v8, v12, v8, v36
	v_max_f32_e32 v12, v27, v40
	v_max3_f32 v10, v10, v16, v35
	v_max_f32_e32 v16, v28, v33
	v_max3_f32 v2, v9, v19, v2
	v_max_f32_e32 v7, v29, v7
	v_max3_f32 v4, v20, v22, v4
	v_max_f32_e32 v5, v30, v5
	v_max3_f32 v1, v21, v23, v1
	v_max3_f32 v0, v31, v32, v0
	v_max_f32_e32 v9, v3, v10
	v_min_f32_e32 v3, v3, v10
	v_max_f32_e32 v10, v6, v16
	v_min_f32_e32 v6, v6, v16
	v_max_f32_e32 v16, v11, v2
	v_min_f32_e32 v2, v11, v2
	v_max_f32_e32 v11, v13, v7
	v_min_f32_e32 v7, v13, v7
	v_max_f32_e32 v13, v14, v4
	v_min_f32_e32 v4, v14, v4
	v_max_f32_e32 v14, v15, v5
	v_min_f32_e32 v5, v15, v5
	v_max_f32_e32 v15, v8, v1
	v_min_f32_e32 v1, v8, v1
	v_max_f32_e32 v8, v12, v0
	v_min_f32_e32 v0, v12, v0
	v_max_f32_e32 v12, v9, v13
	v_min_f32_e32 v9, v9, v13
	v_max_f32_e32 v13, v10, v14
	v_min_f32_e32 v10, v10, v14
	v_max_f32_e32 v14, v16, v15
	v_min_f32_e32 v15, v16, v15
	v_max_f32_e32 v16, v11, v8
	v_min_f32_e32 v8, v11, v8
	v_max_f32_e32 v11, v3, v4
	v_min_f32_e32 v3, v3, v4
	v_max_f32_e32 v4, v6, v5
	v_min_f32_e32 v5, v6, v5
	v_max_f32_e32 v6, v2, v1
	v_min_f32_e32 v1, v2, v1
	v_max_f32_e32 v2, v7, v0
	v_min_f32_e32 v0, v7, v0
	v_max_f32_e32 v17, v12, v14
	v_min_f32_e32 v12, v12, v14
	v_max_f32_e32 v14, v13, v16
	v_min_f32_e32 v13, v13, v16
	v_max_f32_e32 v16, v9, v15
	v_min_f32_e32 v9, v9, v15
	v_max_f32_e32 v15, v10, v8
	v_min_f32_e32 v8, v10, v8
	v_max_f32_e32 v10, v11, v6
	v_min_f32_e32 v11, v11, v6
	v_max_f32_e32 v18, v4, v2
	v_min_f32_e32 v19, v4, v2
	v_max_f32_e32 v20, v3, v1
	v_min_f32_e32 v21, v3, v1
	v_max_f32_e32 v22, v5, v0
	v_min_f32_e32 v23, v5, v0
	ds_read_b128 v[0:3], v104
	ds_read_b128 v[4:7], v103
	v_min_f32_e32 v24, v17, v14
	v_min_f32_e32 v25, v12, v13
	v_min_f32_e32 v26, v16, v15
	s_waitcnt lgkmcnt(0)
; #define PG8_LAS __attribute__((address_space(3)))
; #define CE(a, b) do { const float hi_ = fmaxf(a, b), lo_ = fminf(a, b); a = hi_; b = lo_; } while (0)
; #define RT_BAR() do { asm volatile("s_waitcnt lgkmcnt(0)" ::: "memory"); __builtin_amdgcn_s_barrier(); asm volatile("" ::: "memory"); } while (0)
; __device__ __forceinline__ void merge_top16(float (&v)[16], const float (&nw)[16]) {
;     v[0] = fmaxf(v[0], nw[15]); v[1] = fmaxf(v[1], nw[14]); v[2] = fmaxf(v[2], nw[13]); v[3] = fmaxf(v[3], nw[12]); v[4] = fmaxf(v[4], nw[11]); v[5] = fmaxf(v[5], nw[10]); v[6] = fmaxf(v[6], nw[9]); v[7] = fmaxf(v[7], nw[8]); v[8] = fmaxf(v[8], nw[7]); v[9] = fmaxf(v[9], nw[6]); v[10] = fmaxf(v[10], nw[5]); v[11] = fmaxf(v[11], nw[4]); v[12] = fmaxf(v[12], nw[3]); v[13] = fmaxf(v[13], nw[2]); v[14] = fmaxf(v[14], nw[1]); v[15] = fmaxf(v[15], nw[0]);
;     CE(v[0], v[8]); CE(v[1], v[9]); CE(v[2], v[10]); CE(v[3], v[11]);
;     CE(v[4], v[12]); CE(v[5], v[13]); CE(v[6], v[14]); CE(v[7], v[15]);
;     CE(v[0], v[4]); CE(v[1], v[5]); CE(v[2], v[6]); CE(v[3], v[7]);
;     CE(v[8], v[12]); CE(v[9], v[13]); CE(v[10], v[14]); CE(v[11], v[15]);
;     CE(v[0], v[2]); CE(v[1], v[3]); CE(v[4], v[6]); CE(v[5], v[7]);
;     CE(v[8], v[10]); CE(v[9], v[11]); CE(v[12], v[14]); CE(v[13], v[15]);
;     CE(v[0], v[1]); CE(v[2], v[3]); CE(v[4], v[5]); CE(v[6], v[7]);
;     CE(v[8], v[9]); CE(v[10], v[11]); CE(v[12], v[13]); CE(v[14], v[15]);
; }
;     __device__ __forceinline__ void fused(f32x4 (&acc)[2][2][4][2], const Unit& u, int wr, int wc, int fr, int fq, PG8_LAS unsigned char* lds, int wid, int lane) const {
;     ...
;             RT_BAR();
;             if (half == 1) {
; #pragma unroll
;                 for (int i = 0; i < 4; ++i) *(PG8_LAS f32x4*)(tile + row * 16 + 4 * i) = (f32x4){run[4 * i], run[4 * i + 1], run[4 * i + 2], run[4 * i + 3]};
;             }
	v_min_f32_e32 v34, v0, v1
	v_max_f32_e32 v32, v0, v1
	v_min_f32_e32 v37, v2, v3
	v_max_f32_e32 v33, v2, v3
	v_min_f32_e32 v41, v4, v5
	v_max_f32_e32 v39, v4, v5
	v_min_f32_e32 v44, v6, v7
	v_max_f32_e32 v40, v6, v7
	ds_read_b128 v[0:3], v100
	ds_read_b128 v[4:7], v98
	s_waitcnt lgkmcnt(0)
	v_min_f32_e32 v47, v0, v1
	v_min_f32_e32 v48, v2, v3
	v_min_f32_e32 v50, v4, v5
	v_min_f32_e32 v51, v6, v7
	v_max_f32_e32 v0, v0, v1
	v_max_f32_e32 v1, v2, v3
	v_max_f32_e32 v4, v4, v5
	v_max_f32_e32 v5, v6, v7
	v_min_f32_e32 v38, v34, v37
	v_min_f32_e32 v45, v41, v44
	v_min_f32_e32 v49, v47, v48
	v_max_f32_e32 v34, v34, v37
	v_min_f32_e32 v35, v32, v33
	v_max_f32_e32 v37, v41, v44
	v_min_f32_e32 v41, v39, v40
	v_max_f32_e32 v47, v47, v48
	v_min_f32_e32 v2, v0, v1
	v_max_f32_e32 v48, v50, v51
	v_min_f32_e32 v6, v4, v5
	v_min_f32_e32 v52, v50, v51
	v_max_f32_e32 v36, v34, v35
	v_max_f32_e32 v42, v37, v41
	v_max_f32_e32 v3, v47, v2
	v_max_f32_e32 v7, v48, v6
	v_min_f32_e32 v46, v38, v45
	v_min_f32_e32 v53, v49, v52
	v_max_f32_e32 v38, v38, v45
	v_min_f32_e32 v43, v36, v42
	v_min_f32_e32 v34, v34, v35
	v_min_f32_e32 v35, v37, v41
	v_max_f32_e32 v45, v49, v52
	v_min_f32_e32 v49, v3, v7
	v_min_f32_e32 v2, v47, v2
	v_min_f32_e32 v6, v48, v6
	v_max_f32_e32 v44, v38, v43
	v_max_f32_e32 v37, v34, v35
	v_max_f32_e32 v32, v32, v33
	v_max_f32_e32 v33, v39, v40
	v_max_f32_e32 v47, v2, v6
	v_max_f32_e32 v0, v0, v1
	v_max_f32_e32 v1, v4, v5
	v_min_f32_e32 v38, v38, v43
	v_min_f32_e32 v34, v34, v35
	v_min_f32_e32 v43, v45, v49
	v_min_f32_e32 v2, v2, v6
	v_min_f32_e32 v39, v32, v33
	v_min_f32_e32 v4, v0, v1
	v_max_f32_e32 v35, v38, v34
	v_max_f32_e32 v6, v43, v2
	v_min_f32_e32 v34, v38, v34
	v_min_f32_e32 v2, v43, v2
	v_min_f32_e32 v40, v37, v39
	v_max_f32_e32 v50, v45, v49
	v_min_f32_e32 v5, v47, v4
	v_min_f32_e32 v38, v34, v2
	v_max_f32_e32 v2, v34, v2
	v_max_f32_e32 v34, v36, v42
	v_max_f32_e32 v36, v37, v39
	v_max_f32_e32 v3, v3, v7
	v_max_f32_e32 v4, v47, v4
	v_max_f32_e32 v41, v44, v40
	v_max_f32_e32 v48, v50, v5
	v_min_f32_e32 v37, v34, v36
	v_min_f32_e32 v7, v3, v4
	v_max_f32_e32 v54, v46, v53
	v_min_f32_e32 v51, v41, v48
	v_min_f32_e32 v39, v37, v7
	v_min_f32_e32 v40, v44, v40
	v_min_f32_e32 v5, v50, v5
	v_min_f32_e32 v52, v54, v51
	v_min_f32_e32 v45, v35, v6
	v_min_f32_e32 v42, v2, v39
	v_min_f32_e32 v44, v40, v5
	v_max_f32_e32 v34, v34, v36
	v_max_f32_e32 v3, v3, v4
	v_max_f32_e32 v32, v32, v33
	v_max_f32_e32 v0, v0, v1
	v_min_f32_e32 v49, v52, v45
	v_max_f32_e32 v45, v52, v45
	v_min_f32_e32 v47, v42, v44
	v_max_f32_e32 v6, v35, v6
	v_min_f32_e32 v4, v34, v3
	v_max_f32_e32 v5, v40, v5
	v_min_f32_e32 v1, v32, v0
	v_min_f32_e32 v43, v49, v38
	v_max_f32_e32 v38, v49, v38
	v_min_f32_e32 v49, v45, v47
	v_max_f32_e32 v45, v45, v47
	v_max_f32_e32 v47, v54, v51
	v_min_f32_e32 v35, v6, v4
	v_max_f32_e32 v2, v2, v39
	v_min_f32_e32 v33, v5, v1
	v_min_f32_e32 v36, v47, v35
	v_max_f32_e32 v35, v47, v35
	v_min_f32_e32 v39, v2, v33
	v_min_f32_e32 v40, v35, v39
	v_max_f32_e32 v35, v35, v39
	v_max_f32_e32 v39, v41, v48
	v_max_f32_e32 v4, v6, v4
	v_min_f32_e32 v6, v39, v4
	v_max_f32_e32 v2, v2, v33
	v_min_f32_e32 v33, v6, v2
	v_max_f32_e32 v2, v6, v2
	v_max_f32_e32 v6, v37, v7
	v_max_f32_e32 v1, v5, v1
	v_max_f32_e32 v42, v42, v44
	v_max_f32_e32 v4, v39, v4
	v_min_f32_e32 v5, v6, v1
	v_max_f32_e32 v3, v34, v3
	v_max_f32_e32 v1, v6, v1
	v_min_f32_e32 v27, v9, v8
	v_min_f32_e32 v28, v10, v18
	v_min_f32_e32 v29, v11, v19
	v_min_f32_e32 v30, v20, v22
	v_min_f32_e32 v31, v21, v23
	v_min_f32_e32 v44, v36, v42
	v_max_f32_e32 v36, v36, v42
	v_min_f32_e32 v7, v4, v5
	v_max_f32_e32 v4, v4, v5
	v_min_f32_e32 v5, v3, v1
	v_max_f32_e32 v1, v3, v1
	v_min_f32_e32 v3, v46, v53
	v_max3_f32 v3, v17, v14, v3
	v_max_f32_e32 v6, v24, v43
	v_max3_f32 v12, v12, v13, v38
	v_max_f32_e32 v13, v25, v49
	v_max3_f32 v14, v16, v15, v45
	v_max_f32_e32 v15, v26, v44
	v_max3_f32 v8, v9, v8, v36
	v_max_f32_e32 v9, v27, v40
	v_max3_f32 v10, v10, v18, v35
	v_max_f32_e32 v16, v28, v33
	v_max3_f32 v2, v11, v19, v2
	v_max_f32_e32 v7, v29, v7
	v_max3_f32 v4, v20, v22, v4
	v_max_f32_e32 v5, v30, v5
	v_max3_f32 v1, v21, v23, v1
	v_max3_f32 v0, v31, v32, v0
	v_max_f32_e32 v11, v3, v10
	v_min_f32_e32 v3, v3, v10
	v_max_f32_e32 v10, v6, v16
	v_min_f32_e32 v6, v6, v16
	v_max_f32_e32 v16, v12, v2
	v_min_f32_e32 v2, v12, v2
	v_max_f32_e32 v12, v13, v7
	v_min_f32_e32 v7, v13, v7
	v_max_f32_e32 v13, v14, v4
	v_min_f32_e32 v4, v14, v4
	v_max_f32_e32 v14, v15, v5
	v_min_f32_e32 v5, v15, v5
	v_max_f32_e32 v15, v8, v1
	v_min_f32_e32 v1, v8, v1
	v_max_f32_e32 v8, v9, v0
	v_min_f32_e32 v0, v9, v0
	v_max_f32_e32 v9, v11, v13
	v_min_f32_e32 v11, v11, v13
	v_max_f32_e32 v13, v10, v14
	v_min_f32_e32 v10, v10, v14
	v_max_f32_e32 v14, v16, v15
	v_min_f32_e32 v15, v16, v15
	v_max_f32_e32 v16, v12, v8
	v_min_f32_e32 v8, v12, v8
	v_max_f32_e32 v12, v3, v4
	v_min_f32_e32 v3, v3, v4
	v_max_f32_e32 v4, v6, v5
	v_min_f32_e32 v5, v6, v5
	v_max_f32_e32 v6, v2, v1
	v_min_f32_e32 v1, v2, v1
	v_max_f32_e32 v2, v7, v0
	v_min_f32_e32 v0, v7, v0
	s_waitcnt lgkmcnt(0)
	s_barrier
	s_waitcnt vmcnt(0)
	ds_write_b128 v241, v[224:227]
	ds_write_b128 v241, v[228:231] offset:16
	ds_write_b128 v241, v[232:235] offset:32
	ds_write_b128 v241, v[236:239] offset:48
	v_max_f32_e32 v7, v9, v14
	v_min_f32_e32 v9, v9, v14
	v_max_f32_e32 v14, v13, v16
	v_min_f32_e32 v16, v13, v16
	v_max_f32_e32 v17, v11, v15
	v_min_f32_e32 v11, v11, v15
	v_max_f32_e32 v18, v10, v8
	v_min_f32_e32 v19, v10, v8
	v_max_f32_e32 v20, v12, v6
	v_min_f32_e32 v21, v12, v6
	v_max_f32_e32 v6, v4, v2
	v_min_f32_e32 v2, v4, v2
	v_max_f32_e32 v22, v3, v1
	v_min_f32_e32 v3, v3, v1
	v_max_f32_e32 v1, v5, v0
	v_min_f32_e32 v23, v5, v0
	v_max_f32_e32 v12, v7, v14
	v_min_f32_e32 v13, v7, v14
	v_max_f32_e32 v14, v9, v16
	v_min_f32_e32 v15, v9, v16
	v_max_f32_e32 v8, v17, v18
	v_min_f32_e32 v9, v17, v18
	v_max_f32_e32 v10, v11, v19
	v_min_f32_e32 v11, v11, v19
	v_max_f32_e32 v4, v20, v6
	v_min_f32_e32 v5, v20, v6
	v_max_f32_e32 v6, v21, v2
	v_min_f32_e32 v7, v21, v2
	v_max_f32_e32 v0, v22, v1
	v_min_f32_e32 v1, v22, v1
	v_max_f32_e32 v2, v3, v23
	v_min_f32_e32 v3, v3, v23
	s_cbranch_vccnz .LBB0_1582
	ds_write_b128 v97, v[12:15]
	ds_write_b128 v97, v[8:11] offset:16
	ds_write_b128 v97, v[4:7] offset:32
	ds_write_b128 v97, v[0:3] offset:48

; #define PG8_LAS __attribute__((address_space(3)))
; #define RT_BAR() do { asm volatile("s_waitcnt lgkmcnt(0)" ::: "memory"); __builtin_amdgcn_s_barrier(); asm volatile("" ::: "memory"); } while (0)
;     __device__ __forceinline__ void fused(f32x4 (&acc)[2][2][4][2], const Unit& u, int wr, int wc, int fr, int fq, PG8_LAS unsigned char* lds, int wid, int lane) const {
;     ...
;         for (int bj = 0; bj < 2; ++bj) {
; #pragma unroll
;             for (int ai = 0; ai < 2; ++ai)
; #pragma unroll
;                 for (int m = 0; m < 4; ++m)
; #pragma unroll
;                     for (int n = 0; n < 2; ++n) {
;                         const int rw = ai * HALF + wr * 64 + m * 16 + fr, g = 8 * wc + 4 * n + fq, col = 32 * wc + 16 * n + 4 * fq;
;                         const f32x4 v = acc[ai][bj][m][n]; f32x4 p;
; #pragma unroll
;                         for (int e = 0; e < 4; ++e) p[e] = __uint_as_float((__float_as_uint(v[e]) & ~127u) | (unsigned)(col + e));
;                         *(PG8_LAS f32x4*)(tile + rw * 128 + ((g ^ fr) << 2)) = p;
;                     }
;             RT_BAR();
;             float run[16];
; #pragma unroll
;             for (int grp = 0; grp < 4; ++grp) {
;                 float nw[16];
; #pragma unroll
;                 for (int i = 0; i < 4; ++i) { const int g = half * 16 + grp * 4 + i; const f32x4 v = *(const PG8_LAS f32x4*)(tile + row * 128 + ((g ^ (row & 15)) << 2));
;                     nw[4 * i] = v[0]; nw[4 * i + 1] = v[1]; nw[4 * i + 2] = v[2]; nw[4 * i + 3] = v[3]; }
;                 sort16_desc(nw);
.LBB0_1598:
	s_movk_i32 s3, 0xff80
	v_and_or_b32 v60, v60, s3, v129
	v_and_or_b32 v61, v61, s98, v224
	v_and_or_b32 v62, v62, s98, v225
	v_and_or_b32 v63, v63, s98, v226
	v_and_or_b32 v56, v56, s3, v124
	v_and_or_b32 v57, v57, s98, v227
	v_and_or_b32 v58, v58, s98, v228
	v_and_or_b32 v59, v59, s98, v229
	v_and_or_b32 v52, v52, s3, v129
	v_and_or_b32 v53, v53, s98, v224
	v_and_or_b32 v54, v54, s98, v225
	v_and_or_b32 v55, v55, s98, v226
	v_and_or_b32 v48, v48, s3, v124
	v_and_or_b32 v49, v49, s98, v227
	v_and_or_b32 v50, v50, s98, v228
	v_and_or_b32 v51, v51, s98, v229
	v_and_or_b32 v44, v44, s3, v129
	v_and_or_b32 v45, v45, s98, v224
	v_and_or_b32 v46, v46, s98, v225
	v_and_or_b32 v47, v47, s98, v226
	v_and_or_b32 v40, v40, s3, v124
	v_and_or_b32 v41, v41, s98, v227
	v_and_or_b32 v42, v42, s98, v228
	v_and_or_b32 v43, v43, s98, v229
	v_and_or_b32 v36, v36, s3, v129
	v_and_or_b32 v37, v37, s98, v224
	v_and_or_b32 v38, v38, s98, v225
	v_and_or_b32 v39, v39, s98, v226
	v_and_or_b32 v32, v32, s3, v124
	v_and_or_b32 v33, v33, s98, v227
	v_and_or_b32 v34, v34, s98, v228
	v_and_or_b32 v35, v35, s98, v229
	v_and_or_b32 v28, v28, s3, v129
	v_and_or_b32 v29, v29, s98, v224
	v_and_or_b32 v30, v30, s98, v225
	v_and_or_b32 v31, v31, s98, v226
	v_and_or_b32 v24, v24, s3, v124
	v_and_or_b32 v25, v25, s98, v227
	v_and_or_b32 v26, v26, s98, v228
	v_and_or_b32 v27, v27, s98, v229
	v_and_or_b32 v20, v20, s3, v129
	v_and_or_b32 v21, v21, s98, v224
	v_and_or_b32 v22, v22, s98, v225
	v_and_or_b32 v23, v23, s98, v226
	v_and_or_b32 v16, v16, s3, v124
	v_and_or_b32 v17, v17, s98, v227
	v_and_or_b32 v18, v18, s98, v228
	v_and_or_b32 v19, v19, s98, v229
	v_and_or_b32 v12, v12, s3, v129
	v_and_or_b32 v13, v13, s98, v224
	v_and_or_b32 v14, v14, s98, v225
	v_and_or_b32 v15, v15, s98, v226
	v_and_or_b32 v8, v8, s3, v124
	v_and_or_b32 v9, v9, s98, v227
	v_and_or_b32 v10, v10, s98, v228
	v_and_or_b32 v11, v11, s98, v229
	v_and_or_b32 v4, v4, s3, v129
	v_and_or_b32 v5, v5, s98, v224
	v_and_or_b32 v6, v6, s98, v225
	v_and_or_b32 v7, v7, s98, v226
	v_and_or_b32 v0, v0, s3, v124
	v_and_or_b32 v1, v1, s98, v227
	v_and_or_b32 v2, v2, s98, v228
	v_and_or_b32 v3, v3, s98, v229
	s_waitcnt lgkmcnt(0)
	s_barrier
	ds_write_b128 v125, v[60:63]
	ds_write_b128 v120, v[56:59]
	ds_write_b128 v125, v[52:55] offset:8192
	ds_write_b128 v120, v[48:51] offset:8192
	ds_write_b128 v125, v[44:47] offset:16384
	ds_write_b128 v120, v[40:43] offset:16384
	ds_write_b128 v125, v[36:39] offset:24576
	ds_write_b128 v120, v[32:35] offset:24576
	ds_write_b128 v92, v[28:31]
	ds_write_b128 v88, v[24:27]
	ds_write_b128 v84, v[20:23]
	ds_write_b128 v82, v[16:19]
	ds_write_b128 v85, v[12:15]
	ds_write_b128 v86, v[8:11]
	ds_write_b128 v90, v[4:7]
	ds_write_b128 v91, v[0:3]
	s_waitcnt lgkmcnt(0)
	s_barrier
	s_lshr_b32 s98, s61, 2
	v_lshlrev_b32_e32 v240, 6, v128
	s_lshl_b32 s98, s98, 14
	v_add_u32_e32 v240, s98, v240
	v_add_u32_e32 v241, 0x18000, v240
	v_add_u32_e32 v240, 0x19108000, v240
	global_load_dwordx4 v[224:227], v240, s[30:31]
	global_load_dwordx4 v[228:231], v240, s[30:31] offset:16
	global_load_dwordx4 v[232:235], v240, s[30:31] offset:32
	global_load_dwordx4 v[236:239], v240, s[30:31] offset:48
	ds_read_b128 v[0:3], v93
	ds_read_b128 v[4:7], v89
	s_and_b64 vcc, exec, s[4:5]
	s_waitcnt lgkmcnt(0)
	v_min_f32_e32 v10, v0, v1
	v_max_f32_e32 v8, v0, v1
	v_min_f32_e32 v13, v2, v3
	v_max_f32_e32 v9, v2, v3
	v_min_f32_e32 v17, v4, v5
	v_max_f32_e32 v15, v4, v5
	v_min_f32_e32 v20, v6, v7
	v_max_f32_e32 v16, v6, v7
	ds_read_b128 v[0:3], v81
	ds_read_b128 v[4:7], v80
	s_waitcnt lgkmcnt(0)
	v_min_f32_e32 v23, v0, v1
	v_min_f32_e32 v24, v2, v3
	v_min_f32_e32 v26, v4, v5
	v_min_f32_e32 v27, v6, v7
	v_max_f32_e32 v0, v0, v1
	v_max_f32_e32 v1, v2, v3
	v_max_f32_e32 v4, v4, v5
	v_max_f32_e32 v5, v6, v7
	v_min_f32_e32 v14, v10, v13
	v_min_f32_e32 v21, v17, v20
	v_min_f32_e32 v25, v23, v24
	v_max_f32_e32 v10, v10, v13
	v_min_f32_e32 v11, v8, v9
	v_max_f32_e32 v13, v17, v20
	v_min_f32_e32 v17, v15, v16
	v_max_f32_e32 v23, v23, v24
	v_min_f32_e32 v2, v0, v1
	v_max_f32_e32 v24, v26, v27
	v_min_f32_e32 v6, v4, v5
	v_min_f32_e32 v28, v26, v27
	v_max_f32_e32 v12, v10, v11
	v_max_f32_e32 v18, v13, v17
	v_max_f32_e32 v3, v23, v2
	v_max_f32_e32 v7, v24, v6
	v_min_f32_e32 v22, v14, v21
	v_min_f32_e32 v29, v25, v28
	v_max_f32_e32 v14, v14, v21
	v_min_f32_e32 v19, v12, v18
	v_min_f32_e32 v10, v10, v11
	v_min_f32_e32 v11, v13, v17
	v_max_f32_e32 v21, v25, v28
	v_min_f32_e32 v25, v3, v7
	v_min_f32_e32 v2, v23, v2
	v_min_f32_e32 v6, v24, v6
	v_max_f32_e32 v20, v14, v19
	v_max_f32_e32 v13, v10, v11
	v_max_f32_e32 v8, v8, v9
	v_max_f32_e32 v9, v15, v16
	v_max_f32_e32 v23, v2, v6
	v_max_f32_e32 v0, v0, v1
	v_max_f32_e32 v1, v4, v5
	v_min_f32_e32 v14, v14, v19
	v_min_f32_e32 v10, v10, v11
	v_min_f32_e32 v19, v21, v25
	v_min_f32_e32 v2, v2, v6
	v_min_f32_e32 v15, v8, v9
	v_min_f32_e32 v4, v0, v1
	v_max_f32_e32 v11, v14, v10
	v_max_f32_e32 v6, v19, v2
	v_min_f32_e32 v10, v14, v10
	v_min_f32_e32 v2, v19, v2
	v_min_f32_e32 v5, v23, v4
	v_min_f32_e32 v14, v10, v2
	v_max_f32_e32 v2, v10, v2
	v_max_f32_e32 v10, v12, v18
	v_max_f32_e32 v12, v13, v15
	v_max_f32_e32 v3, v3, v7
	v_max_f32_e32 v4, v23, v4
	v_min_f32_e32 v16, v13, v15
	v_max_f32_e32 v26, v21, v25
	v_min_f32_e32 v13, v10, v12
	v_min_f32_e32 v7, v3, v4
	v_max_f32_e32 v10, v10, v12
	v_max_f32_e32 v3, v3, v4
	v_max_f32_e32 v17, v20, v16
	v_max_f32_e32 v24, v26, v5
	v_min_f32_e32 v21, v11, v6
	v_min_f32_e32 v16, v20, v16
	v_min_f32_e32 v5, v26, v5
	v_max_f32_e32 v6, v11, v6
	v_min_f32_e32 v4, v10, v3
	v_max_f32_e32 v8, v8, v9
	v_max_f32_e32 v9, v0, v1
	v_max_f32_e32 v30, v22, v29
	v_min_f32_e32 v27, v17, v24
	v_min_f32_e32 v15, v13, v7
	v_min_f32_e32 v20, v16, v5
	v_min_f32_e32 v11, v6, v4
	v_max_f32_e32 v5, v16, v5
	v_min_f32_e32 v0, v8, v9
	v_max_f32_e32 v17, v17, v24
	v_max_f32_e32 v4, v6, v4
	v_min_f32_e32 v28, v30, v27
	v_min_f32_e32 v18, v2, v15
	v_max_f32_e32 v27, v30, v27
	v_max_f32_e32 v2, v2, v15
	v_min_f32_e32 v1, v5, v0
	v_min_f32_e32 v24, v17, v4
	v_max_f32_e32 v17, v17, v4
	v_max_f32_e32 v4, v13, v7
	v_max_f32_e32 v5, v5, v0
	v_min_f32_e32 v12, v27, v11
	v_max_f32_e32 v11, v27, v11
	v_min_f32_e32 v15, v2, v1
	v_max_f32_e32 v27, v2, v1
	v_min_f32_e32 v13, v4, v5
	v_max_f32_e32 v10, v10, v3
	ds_read_b128 v[0:3], v99
	v_max_f32_e32 v31, v4, v5
	ds_read_b128 v[4:7], v96
	v_min_f32_e32 v22, v22, v29
	v_min_f32_e32 v25, v28, v21
	s_waitcnt lgkmcnt(0)
; __device__ __forceinline__ void sort16_desc(float (&v)[16]) {
;     CE(v[0], v[1]); CE(v[2], v[3]); CE(v[0], v[2]); CE(v[1], v[3]);
;     CE(v[1], v[2]); CE(v[4], v[5]); CE(v[6], v[7]); CE(v[4], v[6]);
;     CE(v[5], v[7]); CE(v[5], v[6]); CE(v[0], v[4]); CE(v[2], v[6]);
;     CE(v[2], v[4]); CE(v[1], v[5]); CE(v[3], v[7]); CE(v[3], v[5]);
;     CE(v[1], v[2]); CE(v[3], v[4]); CE(v[5], v[6]); CE(v[8], v[9]);
;     CE(v[10], v[11]); CE(v[8], v[10]); CE(v[9], v[11]); CE(v[9], v[10]);
;     CE(v[12], v[13]); CE(v[14], v[15]); CE(v[12], v[14]); CE(v[13], v[15]);
;     CE(v[13], v[14]); CE(v[8], v[12]); CE(v[10], v[14]); CE(v[10], v[12]);
;     CE(v[9], v[13]); CE(v[11], v[15]); CE(v[11], v[13]); CE(v[9], v[10]);
;     CE(v[11], v[12]); CE(v[13], v[14]); CE(v[0], v[8]); CE(v[4], v[12]);
;     CE(v[4], v[8]); CE(v[2], v[10]); CE(v[6], v[14]); CE(v[6], v[10]);
;     CE(v[2], v[4]); CE(v[6], v[8]); CE(v[10], v[12]); CE(v[1], v[9]);
;     CE(v[5], v[13]); CE(v[5], v[9]); CE(v[3], v[11]); CE(v[7], v[15]);
;     CE(v[7], v[11]); CE(v[3], v[5]); CE(v[7], v[9]); CE(v[11], v[13]);
;     CE(v[1], v[2]); CE(v[3], v[4]); CE(v[5], v[6]); CE(v[7], v[8]);
;     CE(v[9], v[10]); CE(v[11], v[12]); CE(v[13], v[14]);
; }
; __device__ __forceinline__ void merge_top16(float (&v)[16], const float (&nw)[16]) {
;     v[0] = fmaxf(v[0], nw[15]); v[1] = fmaxf(v[1], nw[14]); v[2] = fmaxf(v[2], nw[13]); v[3] = fmaxf(v[3], nw[12]); v[4] = fmaxf(v[4], nw[11]); v[5] = fmaxf(v[5], nw[10]); v[6] = fmaxf(v[6], nw[9]); v[7] = fmaxf(v[7], nw[8]); v[8] = fmaxf(v[8], nw[7]); v[9] = fmaxf(v[9], nw[6]); v[10] = fmaxf(v[10], nw[5]); v[11] = fmaxf(v[11], nw[4]); v[12] = fmaxf(v[12], nw[3]); v[13] = fmaxf(v[13], nw[2]); v[14] = fmaxf(v[14], nw[1]); v[15] = fmaxf(v[15], nw[0]);
;     CE(v[0], v[8]); CE(v[1], v[9]); CE(v[2], v[10]); CE(v[3], v[11]);
;     CE(v[4], v[12]); CE(v[5], v[13]); CE(v[6], v[14]); CE(v[7], v[15]);
;     CE(v[0], v[4]); CE(v[1], v[5]); CE(v[2], v[6]); CE(v[3], v[7]);
;     CE(v[8], v[12]); CE(v[9], v[13]); CE(v[10], v[14]); CE(v[11], v[15]);
;     CE(v[0], v[2]); CE(v[1], v[3]); CE(v[4], v[6]); CE(v[5], v[7]);
;     CE(v[8], v[10]); CE(v[9], v[11]); CE(v[12], v[14]); CE(v[13], v[15]);
;     CE(v[0], v[1]); CE(v[2], v[3]); CE(v[4], v[5]); CE(v[6], v[7]);
;     CE(v[8], v[9]); CE(v[10], v[11]); CE(v[12], v[13]); CE(v[14], v[15]);
; }
	v_min_f32_e32 v34, v0, v1
	v_max_f32_e32 v29, v0, v1
	v_min_f32_e32 v37, v2, v3
	v_max_f32_e32 v33, v2, v3
	v_min_f32_e32 v41, v4, v5
	v_max_f32_e32 v39, v4, v5
	v_min_f32_e32 v44, v6, v7
	v_max_f32_e32 v40, v6, v7
	ds_read_b128 v[0:3], v87
	ds_read_b128 v[4:7], v83
	s_waitcnt lgkmcnt(0)
	v_min_f32_e32 v47, v0, v1
	v_min_f32_e32 v48, v2, v3
	v_min_f32_e32 v50, v4, v5
	v_min_f32_e32 v51, v6, v7
	v_max_f32_e32 v0, v0, v1
	v_max_f32_e32 v1, v2, v3
	v_max_f32_e32 v4, v4, v5
	v_max_f32_e32 v5, v6, v7
	v_min_f32_e32 v38, v34, v37
	v_min_f32_e32 v45, v41, v44
	v_min_f32_e32 v49, v47, v48
	v_max_f32_e32 v34, v34, v37
	v_min_f32_e32 v35, v29, v33
	v_max_f32_e32 v37, v41, v44
	v_min_f32_e32 v41, v39, v40
	v_max_f32_e32 v47, v47, v48
	v_min_f32_e32 v2, v0, v1
	v_max_f32_e32 v48, v50, v51
	v_min_f32_e32 v6, v4, v5
	v_min_f32_e32 v52, v50, v51
	v_max_f32_e32 v36, v34, v35
	v_max_f32_e32 v42, v37, v41
	v_max_f32_e32 v3, v47, v2
	v_max_f32_e32 v7, v48, v6
	v_min_f32_e32 v46, v38, v45
	v_min_f32_e32 v53, v49, v52
	v_max_f32_e32 v38, v38, v45
	v_min_f32_e32 v43, v36, v42
	v_min_f32_e32 v34, v34, v35
	v_min_f32_e32 v35, v37, v41
	v_max_f32_e32 v45, v49, v52
	v_min_f32_e32 v49, v3, v7
	v_min_f32_e32 v2, v47, v2
	v_min_f32_e32 v6, v48, v6
	v_max_f32_e32 v44, v38, v43
	v_max_f32_e32 v37, v34, v35
	v_max_f32_e32 v29, v29, v33
	v_max_f32_e32 v33, v39, v40
	v_max_f32_e32 v47, v2, v6
	v_max_f32_e32 v0, v0, v1
	v_max_f32_e32 v1, v4, v5
	v_min_f32_e32 v38, v38, v43
	v_min_f32_e32 v34, v34, v35
	v_min_f32_e32 v43, v45, v49
	v_min_f32_e32 v2, v2, v6
	v_min_f32_e32 v39, v29, v33
	v_min_f32_e32 v4, v0, v1
	v_max_f32_e32 v35, v38, v34
	v_max_f32_e32 v6, v43, v2
	v_min_f32_e32 v34, v38, v34
	v_min_f32_e32 v2, v43, v2
	v_min_f32_e32 v40, v37, v39
	v_max_f32_e32 v50, v45, v49
	v_min_f32_e32 v5, v47, v4
	v_min_f32_e32 v38, v34, v2
	v_max_f32_e32 v2, v34, v2
	v_max_f32_e32 v34, v36, v42
	v_max_f32_e32 v36, v37, v39
	v_max_f32_e32 v3, v3, v7
	v_max_f32_e32 v4, v47, v4
	v_max_f32_e32 v41, v44, v40
	v_max_f32_e32 v48, v50, v5
	v_min_f32_e32 v37, v34, v36
	v_min_f32_e32 v7, v3, v4
	v_min_f32_e32 v40, v44, v40
	v_min_f32_e32 v5, v50, v5
	v_max_f32_e32 v34, v34, v36
	v_max_f32_e32 v3, v3, v4
	v_max_f32_e32 v29, v29, v33
	v_max_f32_e32 v0, v0, v1
	v_max_f32_e32 v54, v46, v53
	v_min_f32_e32 v51, v41, v48
	v_min_f32_e32 v45, v35, v6
	v_min_f32_e32 v39, v37, v7
	v_min_f32_e32 v44, v40, v5
	v_max_f32_e32 v6, v35, v6
	v_min_f32_e32 v4, v34, v3
	v_max_f32_e32 v5, v40, v5
	v_min_f32_e32 v1, v29, v0
	v_min_f32_e32 v52, v54, v51
	v_min_f32_e32 v42, v2, v39
	v_max_f32_e32 v51, v54, v51
	v_min_f32_e32 v35, v6, v4
	v_max_f32_e32 v2, v2, v39
	v_min_f32_e32 v33, v5, v1
	v_max_f32_e32 v41, v41, v48
	v_max_f32_e32 v4, v6, v4
	v_max_f32_e32 v7, v37, v7
	v_max_f32_e32 v1, v5, v1
	v_max_f32_e32 v21, v28, v21
	v_min_f32_e32 v23, v18, v20
	v_max_f32_e32 v18, v18, v20
	v_min_f32_e32 v49, v52, v45
	v_max_f32_e32 v45, v52, v45
	v_min_f32_e32 v47, v42, v44
	v_min_f32_e32 v36, v51, v35
	v_max_f32_e32 v42, v42, v44
	v_max_f32_e32 v35, v51, v35
	v_min_f32_e32 v39, v2, v33
	v_min_f32_e32 v6, v41, v4
	v_max_f32_e32 v2, v2, v33
	v_max_f32_e32 v4, v41, v4
	v_min_f32_e32 v5, v7, v1
	v_max_f32_e32 v3, v34, v3
	v_max_f32_e32 v1, v7, v1
	v_min_f32_e32 v19, v25, v14
	v_min_f32_e32 v26, v21, v23
	v_min_f32_e32 v20, v12, v18
	v_min_f32_e32 v16, v11, v15
	v_min_f32_e32 v28, v24, v27
	v_min_f32_e32 v30, v17, v13
	v_min_f32_e32 v32, v10, v31
	v_min_f32_e32 v43, v49, v38
	v_min_f32_e32 v50, v45, v47
	v_min_f32_e32 v44, v36, v42
	v_min_f32_e32 v40, v35, v39
	v_min_f32_e32 v33, v6, v2
	v_min_f32_e32 v37, v4, v5
	v_min_f32_e32 v7, v3, v1
	v_min_f32_e32 v34, v46, v53
	v_max3_f32 v8, v8, v9, v34
	v_max3_f32 v9, v10, v31, v43
	v_max3_f32 v10, v32, v49, v38
	v_max3_f32 v13, v17, v13, v50
	v_max3_f32 v17, v30, v45, v47
	v_max3_f32 v24, v24, v27, v44
	v_max3_f32 v27, v28, v36, v42
	v_max3_f32 v11, v11, v15, v40
	v_max3_f32 v15, v16, v35, v39
	v_max3_f32 v12, v12, v18, v33
	v_max3_f32 v2, v20, v6, v2
	v_max3_f32 v6, v21, v23, v37
	v_max3_f32 v4, v26, v4, v5
	v_max3_f32 v5, v25, v14, v7
	v_max3_f32 v1, v19, v3, v1
	v_max3_f32 v0, v22, v29, v0
	v_max_f32_e32 v3, v8, v15
	v_min_f32_e32 v7, v8, v15
	v_max_f32_e32 v8, v9, v12
	v_min_f32_e32 v9, v9, v12
	v_max_f32_e32 v12, v10, v2
	v_min_f32_e32 v2, v10, v2
	v_max_f32_e32 v10, v13, v6
	v_min_f32_e32 v6, v13, v6
	v_max_f32_e32 v13, v17, v4
	v_min_f32_e32 v4, v17, v4
	v_max_f32_e32 v14, v24, v5
	v_min_f32_e32 v5, v24, v5
	v_max_f32_e32 v15, v27, v1
	v_min_f32_e32 v1, v27, v1
	v_max_f32_e32 v16, v11, v0
	v_min_f32_e32 v0, v11, v0
	v_max_f32_e32 v11, v3, v13
	v_min_f32_e32 v3, v3, v13
	v_max_f32_e32 v13, v8, v14
	v_min_f32_e32 v8, v8, v14
	v_max_f32_e32 v14, v12, v15
	v_min_f32_e32 v12, v12, v15
	v_max_f32_e32 v15, v10, v16
	v_min_f32_e32 v10, v10, v16
	v_max_f32_e32 v16, v7, v4
	v_min_f32_e32 v4, v7, v4
	v_max_f32_e32 v7, v9, v5
	v_min_f32_e32 v5, v9, v5
	v_max_f32_e32 v9, v2, v1
	v_min_f32_e32 v1, v2, v1
	v_max_f32_e32 v2, v6, v0
	v_min_f32_e32 v0, v6, v0
	v_max_f32_e32 v17, v11, v14
	v_min_f32_e32 v11, v11, v14
	v_max_f32_e32 v14, v13, v15
	v_min_f32_e32 v13, v13, v15
	v_max_f32_e32 v15, v3, v12
	v_min_f32_e32 v12, v3, v12
	v_max_f32_e32 v18, v8, v10
	v_min_f32_e32 v8, v8, v10
	v_max_f32_e32 v10, v16, v9
	v_min_f32_e32 v9, v16, v9
	v_max_f32_e32 v16, v7, v2
	v_min_f32_e32 v19, v7, v2
	v_max_f32_e32 v20, v4, v1
	v_min_f32_e32 v21, v4, v1
	v_max_f32_e32 v22, v5, v0
	v_min_f32_e32 v23, v5, v0
	ds_read_b128 v[0:3], v102
	ds_read_b128 v[4:7], v101
	v_min_f32_e32 v24, v17, v14
	v_min_f32_e32 v25, v11, v13
	v_min_f32_e32 v26, v15, v18
	s_waitcnt lgkmcnt(0)
; __device__ __forceinline__ void sort16_desc(float (&v)[16]) {
;     CE(v[0], v[1]); CE(v[2], v[3]); CE(v[0], v[2]); CE(v[1], v[3]);
;     CE(v[1], v[2]); CE(v[4], v[5]); CE(v[6], v[7]); CE(v[4], v[6]);
;     CE(v[5], v[7]); CE(v[5], v[6]); CE(v[0], v[4]); CE(v[2], v[6]);
;     CE(v[2], v[4]); CE(v[1], v[5]); CE(v[3], v[7]); CE(v[3], v[5]);
;     CE(v[1], v[2]); CE(v[3], v[4]); CE(v[5], v[6]); CE(v[8], v[9]);
;     CE(v[10], v[11]); CE(v[8], v[10]); CE(v[9], v[11]); CE(v[9], v[10]);
;     CE(v[12], v[13]); CE(v[14], v[15]); CE(v[12], v[14]); CE(v[13], v[15]);
;     CE(v[13], v[14]); CE(v[8], v[12]); CE(v[10], v[14]); CE(v[10], v[12]);
;     CE(v[9], v[13]); CE(v[11], v[15]); CE(v[11], v[13]); CE(v[9], v[10]);
;     CE(v[11], v[12]); CE(v[13], v[14]); CE(v[0], v[8]); CE(v[4], v[12]);
;     CE(v[4], v[8]); CE(v[2], v[10]); CE(v[6], v[14]); CE(v[6], v[10]);
;     CE(v[2], v[4]); CE(v[6], v[8]); CE(v[10], v[12]); CE(v[1], v[9]);
;     CE(v[5], v[13]); CE(v[5], v[9]); CE(v[3], v[11]); CE(v[7], v[15]);
;     CE(v[7], v[11]); CE(v[3], v[5]); CE(v[7], v[9]); CE(v[11], v[13]);
;     CE(v[1], v[2]); CE(v[3], v[4]); CE(v[5], v[6]); CE(v[7], v[8]);
;     CE(v[9], v[10]); CE(v[11], v[12]); CE(v[13], v[14]);
; }
; __device__ __forceinline__ void merge_top16(float (&v)[16], const float (&nw)[16]) {
;     v[0] = fmaxf(v[0], nw[15]); v[1] = fmaxf(v[1], nw[14]); v[2] = fmaxf(v[2], nw[13]); v[3] = fmaxf(v[3], nw[12]); v[4] = fmaxf(v[4], nw[11]); v[5] = fmaxf(v[5], nw[10]); v[6] = fmaxf(v[6], nw[9]); v[7] = fmaxf(v[7], nw[8]); v[8] = fmaxf(v[8], nw[7]); v[9] = fmaxf(v[9], nw[6]); v[10] = fmaxf(v[10], nw[5]); v[11] = fmaxf(v[11], nw[4]); v[12] = fmaxf(v[12], nw[3]); v[13] = fmaxf(v[13], nw[2]); v[14] = fmaxf(v[14], nw[1]); v[15] = fmaxf(v[15], nw[0]);
;     CE(v[0], v[8]); CE(v[1], v[9]); CE(v[2], v[10]); CE(v[3], v[11]);
;     CE(v[4], v[12]); CE(v[5], v[13]); CE(v[6], v[14]); CE(v[7], v[15]);
;     CE(v[0], v[4]); CE(v[1], v[5]); CE(v[2], v[6]); CE(v[3], v[7]);
;     CE(v[8], v[12]); CE(v[9], v[13]); CE(v[10], v[14]); CE(v[11], v[15]);
;     CE(v[0], v[2]); CE(v[1], v[3]); CE(v[4], v[6]); CE(v[5], v[7]);
;     CE(v[8], v[10]); CE(v[9], v[11]); CE(v[12], v[14]); CE(v[13], v[15]);
;     CE(v[0], v[1]); CE(v[2], v[3]); CE(v[4], v[5]); CE(v[6], v[7]);
;     CE(v[8], v[9]); CE(v[10], v[11]); CE(v[12], v[13]); CE(v[14], v[15]);
; }
	v_min_f32_e32 v34, v0, v1
	v_max_f32_e32 v32, v0, v1
	v_min_f32_e32 v37, v2, v3
	v_max_f32_e32 v33, v2, v3
	v_min_f32_e32 v41, v4, v5
	v_max_f32_e32 v39, v4, v5
	v_min_f32_e32 v44, v6, v7
	v_max_f32_e32 v40, v6, v7
	ds_read_b128 v[0:3], v95
	ds_read_b128 v[4:7], v94
	s_waitcnt lgkmcnt(0)
	v_min_f32_e32 v47, v0, v1
	v_min_f32_e32 v48, v2, v3
	v_min_f32_e32 v50, v4, v5
	v_min_f32_e32 v51, v6, v7
	v_max_f32_e32 v0, v0, v1
	v_max_f32_e32 v1, v2, v3
	v_max_f32_e32 v4, v4, v5
	v_max_f32_e32 v5, v6, v7
	v_min_f32_e32 v38, v34, v37
	v_min_f32_e32 v45, v41, v44
	v_min_f32_e32 v49, v47, v48
	v_max_f32_e32 v34, v34, v37
	v_min_f32_e32 v35, v32, v33
	v_max_f32_e32 v37, v41, v44
	v_min_f32_e32 v41, v39, v40
	v_max_f32_e32 v47, v47, v48
	v_min_f32_e32 v2, v0, v1
	v_max_f32_e32 v48, v50, v51
	v_min_f32_e32 v6, v4, v5
	v_min_f32_e32 v52, v50, v51
	v_max_f32_e32 v36, v34, v35
	v_max_f32_e32 v42, v37, v41
	v_max_f32_e32 v3, v47, v2
	v_max_f32_e32 v7, v48, v6
	v_min_f32_e32 v46, v38, v45
	v_min_f32_e32 v53, v49, v52
	v_max_f32_e32 v38, v38, v45
	v_min_f32_e32 v43, v36, v42
	v_min_f32_e32 v34, v34, v35
	v_min_f32_e32 v35, v37, v41
	v_max_f32_e32 v45, v49, v52
	v_min_f32_e32 v49, v3, v7
	v_min_f32_e32 v2, v47, v2
	v_min_f32_e32 v6, v48, v6
	v_max_f32_e32 v44, v38, v43
	v_max_f32_e32 v37, v34, v35
	v_max_f32_e32 v32, v32, v33
	v_max_f32_e32 v33, v39, v40
	v_max_f32_e32 v47, v2, v6
	v_max_f32_e32 v0, v0, v1
	v_max_f32_e32 v1, v4, v5
	v_min_f32_e32 v38, v38, v43
	v_min_f32_e32 v34, v34, v35
	v_min_f32_e32 v43, v45, v49
	v_min_f32_e32 v2, v2, v6
	v_min_f32_e32 v39, v32, v33
	v_min_f32_e32 v4, v0, v1
	v_max_f32_e32 v35, v38, v34
	v_max_f32_e32 v6, v43, v2
	v_min_f32_e32 v34, v38, v34
	v_min_f32_e32 v2, v43, v2
	v_min_f32_e32 v40, v37, v39
	v_max_f32_e32 v50, v45, v49
	v_min_f32_e32 v5, v47, v4
	v_min_f32_e32 v38, v34, v2
	v_max_f32_e32 v2, v34, v2
	v_max_f32_e32 v34, v36, v42
	v_max_f32_e32 v36, v37, v39
	v_max_f32_e32 v3, v3, v7
	v_max_f32_e32 v4, v47, v4
	v_max_f32_e32 v41, v44, v40
	v_max_f32_e32 v48, v50, v5
	v_min_f32_e32 v37, v34, v36
	v_min_f32_e32 v7, v3, v4
	v_max_f32_e32 v54, v46, v53
	v_min_f32_e32 v51, v41, v48
	v_min_f32_e32 v39, v37, v7
	v_min_f32_e32 v40, v44, v40
	v_min_f32_e32 v5, v50, v5
	v_min_f32_e32 v52, v54, v51
	v_min_f32_e32 v45, v35, v6
	v_min_f32_e32 v42, v2, v39
	v_min_f32_e32 v44, v40, v5
	v_max_f32_e32 v34, v34, v36
	v_max_f32_e32 v3, v3, v4
	v_max_f32_e32 v32, v32, v33
	v_max_f32_e32 v0, v0, v1
	v_min_f32_e32 v49, v52, v45
	v_max_f32_e32 v45, v52, v45
	v_min_f32_e32 v47, v42, v44
	v_max_f32_e32 v6, v35, v6
	v_min_f32_e32 v4, v34, v3
	v_max_f32_e32 v5, v40, v5
	v_min_f32_e32 v1, v32, v0
	v_min_f32_e32 v43, v49, v38
	v_max_f32_e32 v38, v49, v38
	v_min_f32_e32 v49, v45, v47
	v_max_f32_e32 v45, v45, v47
	v_max_f32_e32 v47, v54, v51
	v_min_f32_e32 v35, v6, v4
	v_max_f32_e32 v2, v2, v39
	v_min_f32_e32 v33, v5, v1
	v_min_f32_e32 v36, v47, v35
	v_max_f32_e32 v35, v47, v35
	v_min_f32_e32 v39, v2, v33
	v_min_f32_e32 v40, v35, v39
	v_max_f32_e32 v35, v35, v39
	v_max_f32_e32 v39, v41, v48
	v_max_f32_e32 v4, v6, v4
	v_min_f32_e32 v6, v39, v4
	v_max_f32_e32 v2, v2, v33
	v_min_f32_e32 v33, v6, v2
	v_max_f32_e32 v2, v6, v2
	v_max_f32_e32 v6, v37, v7
	v_max_f32_e32 v1, v5, v1
	v_max_f32_e32 v42, v42, v44
	v_max_f32_e32 v4, v39, v4
	v_min_f32_e32 v5, v6, v1
	v_max_f32_e32 v3, v34, v3
	v_max_f32_e32 v1, v6, v1
	v_min_f32_e32 v27, v12, v8
	v_min_f32_e32 v28, v10, v16
	v_min_f32_e32 v29, v9, v19
	v_min_f32_e32 v30, v20, v22
	v_min_f32_e32 v31, v21, v23
	v_min_f32_e32 v44, v36, v42
	v_max_f32_e32 v36, v36, v42
	v_min_f32_e32 v7, v4, v5
	v_max_f32_e32 v4, v4, v5
	v_min_f32_e32 v5, v3, v1
	v_max_f32_e32 v1, v3, v1
	v_min_f32_e32 v3, v46, v53
	v_max3_f32 v3, v17, v14, v3
	v_max_f32_e32 v6, v24, v43
	v_max3_f32 v11, v11, v13, v38
	v_max_f32_e32 v13, v25, v49
	v_max3_f32 v14, v15, v18, v45
	v_max_f32_e32 v15, v26, v44
	v_max3_f32 v8, v12, v8, v36
	v_max_f32_e32 v12, v27, v40
	v_max3_f32 v10, v10, v16, v35
	v_max_f32_e32 v16, v28, v33
	v_max3_f32 v2, v9, v19, v2
	v_max_f32_e32 v7, v29, v7
	v_max3_f32 v4, v20, v22, v4
	v_max_f32_e32 v5, v30, v5
	v_max3_f32 v1, v21, v23, v1
	v_max3_f32 v0, v31, v32, v0
	v_max_f32_e32 v9, v3, v10
	v_min_f32_e32 v3, v3, v10
	v_max_f32_e32 v10, v6, v16
	v_min_f32_e32 v6, v6, v16
	v_max_f32_e32 v16, v11, v2
	v_min_f32_e32 v2, v11, v2
	v_max_f32_e32 v11, v13, v7
	v_min_f32_e32 v7, v13, v7
	v_max_f32_e32 v13, v14, v4
	v_min_f32_e32 v4, v14, v4
	v_max_f32_e32 v14, v15, v5
	v_min_f32_e32 v5, v15, v5
	v_max_f32_e32 v15, v8, v1
	v_min_f32_e32 v1, v8, v1
	v_max_f32_e32 v8, v12, v0
	v_min_f32_e32 v0, v12, v0
	v_max_f32_e32 v12, v9, v13
	v_min_f32_e32 v9, v9, v13
	v_max_f32_e32 v13, v10, v14
	v_min_f32_e32 v10, v10, v14
	v_max_f32_e32 v14, v16, v15
	v_min_f32_e32 v15, v16, v15
	v_max_f32_e32 v16, v11, v8
	v_min_f32_e32 v8, v11, v8
	v_max_f32_e32 v11, v3, v4
	v_min_f32_e32 v3, v3, v4
	v_max_f32_e32 v4, v6, v5
	v_min_f32_e32 v5, v6, v5
	v_max_f32_e32 v6, v2, v1
	v_min_f32_e32 v1, v2, v1
	v_max_f32_e32 v2, v7, v0
	v_min_f32_e32 v0, v7, v0
	v_max_f32_e32 v17, v12, v14
	v_min_f32_e32 v12, v12, v14
	v_max_f32_e32 v14, v13, v16
	v_min_f32_e32 v13, v13, v16
	v_max_f32_e32 v16, v9, v15
	v_min_f32_e32 v9, v9, v15
	v_max_f32_e32 v15, v10, v8
	v_min_f32_e32 v8, v10, v8
	v_max_f32_e32 v10, v11, v6
	v_min_f32_e32 v11, v11, v6
	v_max_f32_e32 v18, v4, v2
	v_min_f32_e32 v19, v4, v2
	v_max_f32_e32 v20, v3, v1
	v_min_f32_e32 v21, v3, v1
	v_max_f32_e32 v22, v5, v0
	v_min_f32_e32 v23, v5, v0
	ds_read_b128 v[0:3], v104
	ds_read_b128 v[4:7], v103
	v_min_f32_e32 v24, v17, v14
	v_min_f32_e32 v25, v12, v13
	v_min_f32_e32 v26, v16, v15
	s_waitcnt lgkmcnt(0)
; #define PG8_LAS __attribute__((address_space(3)))
; #define CE(a, b) do { const float hi_ = fmaxf(a, b), lo_ = fminf(a, b); a = hi_; b = lo_; } while (0)
; #define RT_BAR() do { asm volatile("s_waitcnt lgkmcnt(0)" ::: "memory"); __builtin_amdgcn_s_barrier(); asm volatile("" ::: "memory"); } while (0)
; __device__ __forceinline__ void merge_top16(float (&v)[16], const float (&nw)[16]) {
;     v[0] = fmaxf(v[0], nw[15]); v[1] = fmaxf(v[1], nw[14]); v[2] = fmaxf(v[2], nw[13]); v[3] = fmaxf(v[3], nw[12]); v[4] = fmaxf(v[4], nw[11]); v[5] = fmaxf(v[5], nw[10]); v[6] = fmaxf(v[6], nw[9]); v[7] = fmaxf(v[7], nw[8]); v[8] = fmaxf(v[8], nw[7]); v[9] = fmaxf(v[9], nw[6]); v[10] = fmaxf(v[10], nw[5]); v[11] = fmaxf(v[11], nw[4]); v[12] = fmaxf(v[12], nw[3]); v[13] = fmaxf(v[13], nw[2]); v[14] = fmaxf(v[14], nw[1]); v[15] = fmaxf(v[15], nw[0]);
;     CE(v[0], v[8]); CE(v[1], v[9]); CE(v[2], v[10]); CE(v[3], v[11]);
;     CE(v[4], v[12]); CE(v[5], v[13]); CE(v[6], v[14]); CE(v[7], v[15]);
;     CE(v[0], v[4]); CE(v[1], v[5]); CE(v[2], v[6]); CE(v[3], v[7]);
;     CE(v[8], v[12]); CE(v[9], v[13]); CE(v[10], v[14]); CE(v[11], v[15]);
;     CE(v[0], v[2]); CE(v[1], v[3]); CE(v[4], v[6]); CE(v[5], v[7]);
;     CE(v[8], v[10]); CE(v[9], v[11]); CE(v[12], v[14]); CE(v[13], v[15]);
;     CE(v[0], v[1]); CE(v[2], v[3]); CE(v[4], v[5]); CE(v[6], v[7]);
;     CE(v[8], v[9]); CE(v[10], v[11]); CE(v[12], v[13]); CE(v[14], v[15]);
; }
;     __device__ __forceinline__ void fused(f32x4 (&acc)[2][2][4][2], const Unit& u, int wr, int wc, int fr, int fq, PG8_LAS unsigned char* lds, int wid, int lane) const {
;     ...
;             RT_BAR();
;             if (half == 1) {
; #pragma unroll
;                 for (int i = 0; i < 4; ++i) *(PG8_LAS f32x4*)(tile + row * 16 + 4 * i) = (f32x4){run[4 * i], run[4 * i + 1], run[4 * i + 2], run[4 * i + 3]};
;             }
	v_min_f32_e32 v34, v0, v1
	v_max_f32_e32 v32, v0, v1
	v_min_f32_e32 v37, v2, v3
	v_max_f32_e32 v33, v2, v3
	v_min_f32_e32 v41, v4, v5
	v_max_f32_e32 v39, v4, v5
	v_min_f32_e32 v44, v6, v7
	v_max_f32_e32 v40, v6, v7
	ds_read_b128 v[0:3], v100
	ds_read_b128 v[4:7], v98
	s_waitcnt lgkmcnt(0)
	v_min_f32_e32 v47, v0, v1
	v_min_f32_e32 v48, v2, v3
	v_min_f32_e32 v50, v4, v5
	v_min_f32_e32 v51, v6, v7
	v_max_f32_e32 v0, v0, v1
	v_max_f32_e32 v1, v2, v3
	v_max_f32_e32 v4, v4, v5
	v_max_f32_e32 v5, v6, v7
	v_min_f32_e32 v38, v34, v37
	v_min_f32_e32 v45, v41, v44
	v_min_f32_e32 v49, v47, v48
	v_max_f32_e32 v34, v34, v37
	v_min_f32_e32 v35, v32, v33
	v_max_f32_e32 v37, v41, v44
	v_min_f32_e32 v41, v39, v40
	v_max_f32_e32 v47, v47, v48
	v_min_f32_e32 v2, v0, v1
	v_max_f32_e32 v48, v50, v51
	v_min_f32_e32 v6, v4, v5
	v_min_f32_e32 v52, v50, v51
	v_max_f32_e32 v36, v34, v35
	v_max_f32_e32 v42, v37, v41
	v_max_f32_e32 v3, v47, v2
	v_max_f32_e32 v7, v48, v6
	v_min_f32_e32 v46, v38, v45
	v_min_f32_e32 v53, v49, v52
	v_max_f32_e32 v38, v38, v45
	v_min_f32_e32 v43, v36, v42
	v_min_f32_e32 v34, v34, v35
	v_min_f32_e32 v35, v37, v41
	v_max_f32_e32 v45, v49, v52
	v_min_f32_e32 v49, v3, v7
	v_min_f32_e32 v2, v47, v2
	v_min_f32_e32 v6, v48, v6
	v_max_f32_e32 v44, v38, v43
	v_max_f32_e32 v37, v34, v35
	v_max_f32_e32 v32, v32, v33
	v_max_f32_e32 v33, v39, v40
	v_max_f32_e32 v47, v2, v6
	v_max_f32_e32 v0, v0, v1
	v_max_f32_e32 v1, v4, v5
	v_min_f32_e32 v38, v38, v43
	v_min_f32_e32 v34, v34, v35
	v_min_f32_e32 v43, v45, v49
	v_min_f32_e32 v2, v2, v6
	v_min_f32_e32 v39, v32, v33
	v_min_f32_e32 v4, v0, v1
	v_max_f32_e32 v35, v38, v34
	v_max_f32_e32 v6, v43, v2
	v_min_f32_e32 v34, v38, v34
	v_min_f32_e32 v2, v43, v2
	v_min_f32_e32 v40, v37, v39
	v_max_f32_e32 v50, v45, v49
	v_min_f32_e32 v5, v47, v4
	v_min_f32_e32 v38, v34, v2
	v_max_f32_e32 v2, v34, v2
	v_max_f32_e32 v34, v36, v42
	v_max_f32_e32 v36, v37, v39
	v_max_f32_e32 v3, v3, v7
	v_max_f32_e32 v4, v47, v4
	v_max_f32_e32 v41, v44, v40
	v_max_f32_e32 v48, v50, v5
	v_min_f32_e32 v37, v34, v36
	v_min_f32_e32 v7, v3, v4
	v_max_f32_e32 v54, v46, v53
	v_min_f32_e32 v51, v41, v48
	v_min_f32_e32 v39, v37, v7
	v_min_f32_e32 v40, v44, v40
	v_min_f32_e32 v5, v50, v5
	v_min_f32_e32 v52, v54, v51
	v_min_f32_e32 v45, v35, v6
	v_min_f32_e32 v42, v2, v39
	v_min_f32_e32 v44, v40, v5
	v_max_f32_e32 v34, v34, v36
	v_max_f32_e32 v3, v3, v4
	v_max_f32_e32 v32, v32, v33
	v_max_f32_e32 v0, v0, v1
	v_min_f32_e32 v49, v52, v45
	v_max_f32_e32 v45, v52, v45
	v_min_f32_e32 v47, v42, v44
	v_max_f32_e32 v6, v35, v6
	v_min_f32_e32 v4, v34, v3
	v_max_f32_e32 v5, v40, v5
	v_min_f32_e32 v1, v32, v0
	v_min_f32_e32 v43, v49, v38
	v_max_f32_e32 v38, v49, v38
	v_min_f32_e32 v49, v45, v47
	v_max_f32_e32 v45, v45, v47
	v_max_f32_e32 v47, v54, v51
	v_min_f32_e32 v35, v6, v4
	v_max_f32_e32 v2, v2, v39
	v_min_f32_e32 v33, v5, v1
	v_min_f32_e32 v36, v47, v35
	v_max_f32_e32 v35, v47, v35
	v_min_f32_e32 v39, v2, v33
	v_min_f32_e32 v40, v35, v39
	v_max_f32_e32 v35, v35, v39
	v_max_f32_e32 v39, v41, v48
	v_max_f32_e32 v4, v6, v4
	v_min_f32_e32 v6, v39, v4
	v_max_f32_e32 v2, v2, v33
	v_min_f32_e32 v33, v6, v2
	v_max_f32_e32 v2, v6, v2
	v_max_f32_e32 v6, v37, v7
	v_max_f32_e32 v1, v5, v1
	v_max_f32_e32 v42, v42, v44
	v_max_f32_e32 v4, v39, v4
	v_min_f32_e32 v5, v6, v1
	v_max_f32_e32 v3, v34, v3
	v_max_f32_e32 v1, v6, v1
	v_min_f32_e32 v27, v9, v8
	v_min_f32_e32 v28, v10, v18
	v_min_f32_e32 v29, v11, v19
	v_min_f32_e32 v30, v20, v22
	v_min_f32_e32 v31, v21, v23
	v_min_f32_e32 v44, v36, v42
	v_max_f32_e32 v36, v36, v42
	v_min_f32_e32 v7, v4, v5
	v_max_f32_e32 v4, v4, v5
	v_min_f32_e32 v5, v3, v1
	v_max_f32_e32 v1, v3, v1
	v_min_f32_e32 v3, v46, v53
	v_max3_f32 v3, v17, v14, v3
	v_max_f32_e32 v6, v24, v43
	v_max3_f32 v12, v12, v13, v38
	v_max_f32_e32 v13, v25, v49
	v_max3_f32 v14, v16, v15, v45
	v_max_f32_e32 v15, v26, v44
	v_max3_f32 v8, v9, v8, v36
	v_max_f32_e32 v9, v27, v40
	v_max3_f32 v10, v10, v18, v35
	v_max_f32_e32 v16, v28, v33
	v_max3_f32 v2, v11, v19, v2
	v_max_f32_e32 v7, v29, v7
	v_max3_f32 v4, v20, v22, v4
	v_max_f32_e32 v5, v30, v5
	v_max3_f32 v1, v21, v23, v1
	v_max3_f32 v0, v31, v32, v0
	v_max_f32_e32 v11, v3, v10
	v_min_f32_e32 v3, v3, v10
	v_max_f32_e32 v10, v6, v16
	v_min_f32_e32 v6, v6, v16
	v_max_f32_e32 v16, v12, v2
	v_min_f32_e32 v2, v12, v2
	v_max_f32_e32 v12, v13, v7
	v_min_f32_e32 v7, v13, v7
	v_max_f32_e32 v13, v14, v4
	v_min_f32_e32 v4, v14, v4
	v_max_f32_e32 v14, v15, v5
	v_min_f32_e32 v5, v15, v5
	v_max_f32_e32 v15, v8, v1
	v_min_f32_e32 v1, v8, v1
	v_max_f32_e32 v8, v9, v0
	v_min_f32_e32 v0, v9, v0
	v_max_f32_e32 v9, v11, v13
	v_min_f32_e32 v11, v11, v13
	v_max_f32_e32 v13, v10, v14
	v_min_f32_e32 v10, v10, v14
	v_max_f32_e32 v14, v16, v15
	v_min_f32_e32 v15, v16, v15
	v_max_f32_e32 v16, v12, v8
	v_min_f32_e32 v8, v12, v8
	v_max_f32_e32 v12, v3, v4
	v_min_f32_e32 v3, v3, v4
	v_max_f32_e32 v4, v6, v5
	v_min_f32_e32 v5, v6, v5
	v_max_f32_e32 v6, v2, v1
	v_min_f32_e32 v1, v2, v1
	v_max_f32_e32 v2, v7, v0
	v_min_f32_e32 v0, v7, v0
	s_waitcnt lgkmcnt(0)
	s_barrier
	s_waitcnt vmcnt(0)
	ds_write_b128 v241, v[224:227]
	ds_write_b128 v241, v[228:231] offset:16
	ds_write_b128 v241, v[232:235] offset:32
	ds_write_b128 v241, v[236:239] offset:48
	v_max_f32_e32 v7, v9, v14
	v_min_f32_e32 v9, v9, v14
	v_max_f32_e32 v14, v13, v16
	v_min_f32_e32 v16, v13, v16
	v_max_f32_e32 v17, v11, v15
	v_min_f32_e32 v11, v11, v15
	v_max_f32_e32 v18, v10, v8
	v_min_f32_e32 v19, v10, v8
	v_max_f32_e32 v20, v12, v6
	v_min_f32_e32 v21, v12, v6
	v_max_f32_e32 v6, v4, v2
	v_min_f32_e32 v2, v4, v2
	v_max_f32_e32 v22, v3, v1
	v_min_f32_e32 v3, v3, v1
	v_max_f32_e32 v1, v5, v0
	v_min_f32_e32 v23, v5, v0
	v_max_f32_e32 v12, v7, v14
	v_min_f32_e32 v13, v7, v14
	v_max_f32_e32 v14, v9, v16
	v_min_f32_e32 v15, v9, v16
	v_max_f32_e32 v8, v17, v18
	v_min_f32_e32 v9, v17, v18
	v_max_f32_e32 v10, v11, v19
	v_min_f32_e32 v11, v11, v19
	v_max_f32_e32 v4, v20, v6
	v_min_f32_e32 v5, v20, v6
	v_max_f32_e32 v6, v21, v2
	v_min_f32_e32 v7, v21, v2
	v_max_f32_e32 v0, v22, v1
	v_min_f32_e32 v1, v22, v1
	v_max_f32_e32 v2, v3, v23
	v_min_f32_e32 v3, v3, v23
	s_cbranch_vccnz .LBB0_1600
	ds_write_b128 v97, v[12:15]
	ds_write_b128 v97, v[8:11] offset:16
	ds_write_b128 v97, v[4:7] offset:32
	ds_write_b128 v97, v[0:3] offset:48
